# baseline (speedup 1.0000x reference)
_Z12gemm8_kernelPKDF16_S0_PDF16_S1_:
	s_load_dwordx8 s[4:11], s[0:1], 0x0
	s_and_b32 s12, s2, 7
	s_lshr_b32 s13, s2, 3
	v_lshrrev_b32_e32 v1, 6, v0
	v_and_b32_e32 v28, 63, v0
	v_and_b32_e32 v29, 15, v28
	v_lshrrev_b32_e32 v30, 4, v28
	v_readfirstlane_b32 s14, v1
	v_lshrrev_b32_e32 v2, 3, v0
	v_lshlrev_b32_e32 v2, 11, v2
	v_and_b32_e32 v3, 7, v0
	v_bfe_u32 v4, v0, 4, 3
	v_xor_b32_e32 v3, v3, v4
	v_lshl_or_b32 v2, v3, 4, v2
	v_bfe_u32 v6, v0, 3, 4
	v_lshrrev_b32_e32 v7, 2, v6
	v_lshlrev_b32_e32 v7, 3, v7
	v_and_b32_e32 v4, 3, v6
	v_or_b32_e32 v7, v7, v4
	v_bfe_u32 v4, v0, 7, 1
	v_lshl_or_b32 v7, v4, 2, v7
	v_bfe_u32 v4, v0, 8, 1
	v_lshl_or_b32 v7, v4, 5, v7
	v_lshlrev_b32_e32 v7, 11, v7
	v_lshl_or_b32 v6, v3, 4, v7
	v_add_u32_e32 v7, 0x20000, v6
	v_add_u32_e32 v3, 0x20000, v2
	v_add_u32_e32 v4, 0x40000, v2
	v_add_u32_e32 v5, 0x60000, v2
	v_lshrrev_b32_e32 v31, 1, v29
	v_xor_b32_e32 v31, v30, v31
	v_lshlrev_b32_e32 v31, 4, v31
	v_lshl_or_b32 v31, v29, 7, v31
	s_lshr_b32 s15, s14, 1
	s_and_b32 s36, s14, 1
	s_lshl_b32 s37, s15, 13
	s_lshl_b32 s38, s36, 13
	v_add_u32_e32 v8, s37, v31
	v_add_u32_e32 v9, s38, v31
	v_xor_b32_e32 v10, 64, v8
	v_xor_b32_e32 v11, 64, v9
	v_add_u32_e32 v12, 0xc000, v8
	v_add_u32_e32 v13, 0xc000, v9
	v_add_u32_e32 v14, 0xc000, v10
	v_add_u32_e32 v15, 0xc000, v11
	v_add_u32_e32 v16, 0x18000, v8
	v_add_u32_e32 v17, 0x18000, v9
	v_add_u32_e32 v18, 0x18000, v10
	v_add_u32_e32 v19, 0x18000, v11
	s_lshl_b32 s39, s15, 6
	s_lshl_b32 s40, s36, 7
	v_add_u32_e32 v28, s39, v29
	v_lshl_add_u32 v30, v30, 4, s40
	v_lshl_add_u32 v20, v28, 12, v30
	v_lshl_add_u32 v24, v28, 13, v30
	v_add_u32_e32 v21, 0x10000, v20
	v_add_u32_e32 v25, 0x20000, v24
	v_add_u32_e32 v22, 0x20000, v20
	v_add_u32_e32 v26, 0x40000, v24
	v_add_u32_e32 v23, 0x30000, v20
	v_add_u32_e32 v27, 0x60000, v24
	s_lshl_b32 s14, s14, 10
	s_mov_b32 s50, 0x3d000000
	s_mov_b32 s52, 0xbfb8aa3b
	s_lshr_b32 s41, s12, 1
	s_lshl_b32 s41, s41, 3
	s_and_b32 s42, s13, 7
	s_add_u32 s41, s41, s42
	s_and_b32 s43, s12, 1
	s_lshl_b32 s43, s43, 2
	s_lshr_b32 s44, s13, 3
	s_add_u32 s43, s43, s44
	s_lshl_b32 s45, s12, 2
	s_add_u32 s45, s45, s44
	s_waitcnt lgkmcnt(0)
	s_lshl_b32 s46, s41, 19
	s_add_u32 s16, s4, s46
	s_addc_u32 s17, s5, 0
	s_lshl_b32 s46, s42, 19
	s_add_u32 s46, s46, 0x400000
	s_add_u32 s18, s6, s46
	s_addc_u32 s19, s7, 0
	s_lshl_b32 s46, s43, 19
	s_add_u32 s20, s6, s46
	s_addc_u32 s21, s7, 0
	s_add_u32 s22, s20, 0x40000
	s_addc_u32 s23, s21, 0
	s_lshl_b32 s46, s45, 19
	s_add_u32 s24, s4, s46
	s_addc_u32 s25, s5, 0
	s_add_u32 s26, s24, 0x40000
	s_addc_u32 s27, s25, 0
	s_lshl_b32 s46, s41, 20
	s_lshl_b32 s47, s43, 9
	s_add_u32 s46, s46, s47
	s_add_u32 s32, s8, s46
	s_addc_u32 s33, s9, 0
	s_lshr_b32 s46, s45, 4
	s_lshl_b32 s46, s46, 24
	s_lshl_b32 s47, s42, 21
	s_add_u32 s46, s46, s47
	s_and_b32 s47, s45, 15
	s_lshl_b32 s47, s47, 9
	s_add_u32 s46, s46, s47
	s_add_u32 s34, s10, s46
	s_addc_u32 s35, s11, 0
	s_mov_b64 s[28:29], s[16:17]
	s_mov_b64 s[30:31], s[20:21]
	s_add_u32 m0, s14, 0x0
	s_nop 0
	global_load_lds_dwordx4 v2, s[28:29]
	s_add_u32 m0, s14, 0x2000
	s_nop 0
	global_load_lds_dwordx4 v3, s[28:29]
	s_add_u32 m0, s14, 0x4000
	s_nop 0
	global_load_lds_dwordx4 v4, s[28:29]
	s_add_u32 m0, s14, 0x6000
	s_nop 0
	global_load_lds_dwordx4 v5, s[28:29]
	s_add_u32 m0, s14, 0x8000
	s_nop 0
	global_load_lds_dwordx4 v6, s[30:31]
	s_add_u32 m0, s14, 0xa000
	s_nop 0
	global_load_lds_dwordx4 v7, s[30:31]
	s_add_u32 s28, s28, 0x80
	s_addc_u32 s29, s29, 0
	s_add_u32 s30, s30, 0x80
	s_addc_u32 s31, s31, 0
	s_add_u32 m0, s14, 0xc000
	s_nop 0
	global_load_lds_dwordx4 v2, s[28:29]
	s_add_u32 m0, s14, 0xe000
	s_nop 0
	global_load_lds_dwordx4 v3, s[28:29]
	s_add_u32 m0, s14, 0x10000
	s_nop 0
	global_load_lds_dwordx4 v4, s[28:29]
	s_add_u32 m0, s14, 0x12000
	s_nop 0
	global_load_lds_dwordx4 v5, s[28:29]
	s_add_u32 m0, s14, 0x14000
	s_nop 0
	global_load_lds_dwordx4 v6, s[30:31]
	s_add_u32 m0, s14, 0x16000
	s_nop 0
	global_load_lds_dwordx4 v7, s[30:31]
	s_add_u32 s28, s28, 0x80
	s_addc_u32 s29, s29, 0
	s_add_u32 s30, s30, 0x80
	s_addc_u32 s31, s31, 0
	s_add_u32 m0, s14, 0x18000
	s_nop 0
	global_load_lds_dwordx4 v2, s[28:29]
	s_add_u32 m0, s14, 0x1a000
	s_nop 0
	global_load_lds_dwordx4 v3, s[28:29]
	s_add_u32 m0, s14, 0x1c000
	s_nop 0
	global_load_lds_dwordx4 v4, s[28:29]
	s_add_u32 m0, s14, 0x1e000
	s_nop 0
	global_load_lds_dwordx4 v5, s[28:29]
	s_add_u32 m0, s14, 0x20000
	s_nop 0
	global_load_lds_dwordx4 v6, s[30:31]
	s_add_u32 m0, s14, 0x22000
	s_nop 0
	global_load_lds_dwordx4 v7, s[30:31]
	s_waitcnt vmcnt(12)
	s_barrier
	ds_read_b128 v[96:99], v8
	ds_read_b128 v[112:115], v9 offset:32768
	ds_read_b128 v[116:119], v9 offset:34816
	ds_read_b128 v[120:123], v9 offset:36864
	ds_read_b128 v[124:127], v9 offset:38912
	ds_read_b128 v[100:103], v8 offset:2048
	ds_read_b128 v[104:107], v8 offset:4096
	ds_read_b128 v[108:111], v8 offset:6144
	s_waitcnt lgkmcnt(0)
	v_mfma_f32_16x16x32_f16 v[32:35], v[112:115], v[96:99], 0
	ds_read_b128 v[128:131], v10
	v_mfma_f32_16x16x32_f16 v[36:39], v[116:119], v[96:99], 0
	ds_read_b128 v[144:147], v11 offset:32768
	v_mfma_f32_16x16x32_f16 v[40:43], v[120:123], v[96:99], 0
	ds_read_b128 v[148:151], v11 offset:34816
	v_mfma_f32_16x16x32_f16 v[44:47], v[124:127], v[96:99], 0
	ds_read_b128 v[152:155], v11 offset:36864
	v_mfma_f32_16x16x32_f16 v[48:51], v[112:115], v[100:103], 0
	ds_read_b128 v[156:159], v11 offset:38912
	v_mfma_f32_16x16x32_f16 v[52:55], v[116:119], v[100:103], 0
	ds_read_b128 v[132:135], v10 offset:2048
	v_mfma_f32_16x16x32_f16 v[56:59], v[120:123], v[100:103], 0
	ds_read_b128 v[136:139], v10 offset:4096
	v_mfma_f32_16x16x32_f16 v[60:63], v[124:127], v[100:103], 0
	ds_read_b128 v[140:143], v10 offset:6144
	v_mfma_f32_16x16x32_f16 v[64:67], v[112:115], v[104:107], 0
	v_mfma_f32_16x16x32_f16 v[68:71], v[116:119], v[104:107], 0
	v_mfma_f32_16x16x32_f16 v[72:75], v[120:123], v[104:107], 0
	v_mfma_f32_16x16x32_f16 v[76:79], v[124:127], v[104:107], 0
	v_mfma_f32_16x16x32_f16 v[80:83], v[112:115], v[108:111], 0
	v_mfma_f32_16x16x32_f16 v[84:87], v[116:119], v[108:111], 0
	v_mfma_f32_16x16x32_f16 v[88:91], v[120:123], v[108:111], 0
	v_mfma_f32_16x16x32_f16 v[92:95], v[124:127], v[108:111], 0
	s_waitcnt vmcnt(6) lgkmcnt(0)
	s_barrier
	s_add_u32 s28, s28, 0x80
	s_addc_u32 s29, s29, 0
	s_add_u32 s30, s30, 0x80
	s_addc_u32 s31, s31, 0
	s_waitcnt lgkmcnt(0)
	v_mfma_f32_16x16x32_f16 v[32:35], v[144:147], v[128:131], v[32:35]
	ds_read_b128 v[96:99], v12
	v_mfma_f32_16x16x32_f16 v[36:39], v[148:151], v[128:131], v[36:39]
	ds_read_b128 v[112:115], v13 offset:32768
	v_mfma_f32_16x16x32_f16 v[40:43], v[152:155], v[128:131], v[40:43]
	ds_read_b128 v[116:119], v13 offset:34816
	v_mfma_f32_16x16x32_f16 v[44:47], v[156:159], v[128:131], v[44:47]
	ds_read_b128 v[120:123], v13 offset:36864
	v_mfma_f32_16x16x32_f16 v[48:51], v[144:147], v[132:135], v[48:51]
	ds_read_b128 v[124:127], v13 offset:38912
	v_mfma_f32_16x16x32_f16 v[52:55], v[148:151], v[132:135], v[52:55]
	ds_read_b128 v[100:103], v12 offset:2048
	v_mfma_f32_16x16x32_f16 v[56:59], v[152:155], v[132:135], v[56:59]
	ds_read_b128 v[104:107], v12 offset:4096
	v_mfma_f32_16x16x32_f16 v[60:63], v[156:159], v[132:135], v[60:63]
	ds_read_b128 v[108:111], v12 offset:6144
	v_mfma_f32_16x16x32_f16 v[64:67], v[144:147], v[136:139], v[64:67]
	v_mfma_f32_16x16x32_f16 v[68:71], v[148:151], v[136:139], v[68:71]
	v_mfma_f32_16x16x32_f16 v[72:75], v[152:155], v[136:139], v[72:75]
	s_add_u32 m0, s14, 0x0
	s_nop 0
	global_load_lds_dwordx4 v2, s[28:29]
	v_mfma_f32_16x16x32_f16 v[76:79], v[156:159], v[136:139], v[76:79]
	v_mfma_f32_16x16x32_f16 v[80:83], v[144:147], v[140:143], v[80:83]
	s_add_u32 m0, s14, 0x2000
	s_nop 0
	global_load_lds_dwordx4 v3, s[28:29]
	v_mfma_f32_16x16x32_f16 v[84:87], v[148:151], v[140:143], v[84:87]
	v_mfma_f32_16x16x32_f16 v[88:91], v[152:155], v[140:143], v[88:91]
	s_add_u32 m0, s14, 0x4000
	s_nop 0
	global_load_lds_dwordx4 v4, s[28:29]
	v_mfma_f32_16x16x32_f16 v[92:95], v[156:159], v[140:143], v[92:95]
	s_waitcnt lgkmcnt(0)
	v_mfma_f32_16x16x32_f16 v[32:35], v[112:115], v[96:99], v[32:35]
	ds_read_b128 v[128:131], v14
	v_mfma_f32_16x16x32_f16 v[36:39], v[116:119], v[96:99], v[36:39]
	ds_read_b128 v[144:147], v15 offset:32768
	v_mfma_f32_16x16x32_f16 v[40:43], v[120:123], v[96:99], v[40:43]
	ds_read_b128 v[148:151], v15 offset:34816
	v_mfma_f32_16x16x32_f16 v[44:47], v[124:127], v[96:99], v[44:47]
	ds_read_b128 v[152:155], v15 offset:36864
	v_mfma_f32_16x16x32_f16 v[48:51], v[112:115], v[100:103], v[48:51]
	ds_read_b128 v[156:159], v15 offset:38912
	v_mfma_f32_16x16x32_f16 v[52:55], v[116:119], v[100:103], v[52:55]
	ds_read_b128 v[132:135], v14 offset:2048
	v_mfma_f32_16x16x32_f16 v[56:59], v[120:123], v[100:103], v[56:59]
	ds_read_b128 v[136:139], v14 offset:4096
	v_mfma_f32_16x16x32_f16 v[60:63], v[124:127], v[100:103], v[60:63]
	ds_read_b128 v[140:143], v14 offset:6144
	v_mfma_f32_16x16x32_f16 v[64:67], v[112:115], v[104:107], v[64:67]
	v_mfma_f32_16x16x32_f16 v[68:71], v[116:119], v[104:107], v[68:71]
	v_mfma_f32_16x16x32_f16 v[72:75], v[120:123], v[104:107], v[72:75]
	s_add_u32 m0, s14, 0x6000
	s_nop 0
	global_load_lds_dwordx4 v5, s[28:29]
	v_mfma_f32_16x16x32_f16 v[76:79], v[124:127], v[104:107], v[76:79]
	v_mfma_f32_16x16x32_f16 v[80:83], v[112:115], v[108:111], v[80:83]
	s_add_u32 m0, s14, 0x8000
	s_nop 0
	global_load_lds_dwordx4 v6, s[30:31]
	v_mfma_f32_16x16x32_f16 v[84:87], v[116:119], v[108:111], v[84:87]
	v_mfma_f32_16x16x32_f16 v[88:91], v[120:123], v[108:111], v[88:91]
	s_add_u32 m0, s14, 0xa000
	s_nop 0
	global_load_lds_dwordx4 v7, s[30:31]
	v_mfma_f32_16x16x32_f16 v[92:95], v[124:127], v[108:111], v[92:95]
	s_waitcnt vmcnt(6) lgkmcnt(0)
	s_barrier
	s_add_u32 s28, s28, 0x80
	s_addc_u32 s29, s29, 0
	s_add_u32 s30, s30, 0x80
	s_addc_u32 s31, s31, 0
	s_waitcnt lgkmcnt(0)
	v_mfma_f32_16x16x32_f16 v[32:35], v[144:147], v[128:131], v[32:35]
	ds_read_b128 v[96:99], v16
	v_mfma_f32_16x16x32_f16 v[36:39], v[148:151], v[128:131], v[36:39]
	ds_read_b128 v[112:115], v17 offset:32768
	v_mfma_f32_16x16x32_f16 v[40:43], v[152:155], v[128:131], v[40:43]
	ds_read_b128 v[116:119], v17 offset:34816
	v_mfma_f32_16x16x32_f16 v[44:47], v[156:159], v[128:131], v[44:47]
	ds_read_b128 v[120:123], v17 offset:36864
	v_mfma_f32_16x16x32_f16 v[48:51], v[144:147], v[132:135], v[48:51]
	ds_read_b128 v[124:127], v17 offset:38912
	v_mfma_f32_16x16x32_f16 v[52:55], v[148:151], v[132:135], v[52:55]
	ds_read_b128 v[100:103], v16 offset:2048
	v_mfma_f32_16x16x32_f16 v[56:59], v[152:155], v[132:135], v[56:59]
	ds_read_b128 v[104:107], v16 offset:4096
	v_mfma_f32_16x16x32_f16 v[60:63], v[156:159], v[132:135], v[60:63]
	ds_read_b128 v[108:111], v16 offset:6144
	v_mfma_f32_16x16x32_f16 v[64:67], v[144:147], v[136:139], v[64:67]
	v_mfma_f32_16x16x32_f16 v[68:71], v[148:151], v[136:139], v[68:71]
	v_mfma_f32_16x16x32_f16 v[72:75], v[152:155], v[136:139], v[72:75]
	s_add_u32 m0, s14, 0xc000
	s_nop 0
	global_load_lds_dwordx4 v2, s[28:29]
	v_mfma_f32_16x16x32_f16 v[76:79], v[156:159], v[136:139], v[76:79]
	v_mfma_f32_16x16x32_f16 v[80:83], v[144:147], v[140:143], v[80:83]
	s_add_u32 m0, s14, 0xe000
	s_nop 0
	global_load_lds_dwordx4 v3, s[28:29]
	v_mfma_f32_16x16x32_f16 v[84:87], v[148:151], v[140:143], v[84:87]
	v_mfma_f32_16x16x32_f16 v[88:91], v[152:155], v[140:143], v[88:91]
	s_add_u32 m0, s14, 0x10000
	s_nop 0
	global_load_lds_dwordx4 v4, s[28:29]
	v_mfma_f32_16x16x32_f16 v[92:95], v[156:159], v[140:143], v[92:95]
	s_waitcnt lgkmcnt(0)
	v_mfma_f32_16x16x32_f16 v[32:35], v[112:115], v[96:99], v[32:35]
	ds_read_b128 v[128:131], v18
	v_mfma_f32_16x16x32_f16 v[36:39], v[116:119], v[96:99], v[36:39]
	ds_read_b128 v[144:147], v19 offset:32768
	v_mfma_f32_16x16x32_f16 v[40:43], v[120:123], v[96:99], v[40:43]
	ds_read_b128 v[148:151], v19 offset:34816
	v_mfma_f32_16x16x32_f16 v[44:47], v[124:127], v[96:99], v[44:47]
	ds_read_b128 v[152:155], v19 offset:36864
	v_mfma_f32_16x16x32_f16 v[48:51], v[112:115], v[100:103], v[48:51]
	ds_read_b128 v[156:159], v19 offset:38912
	v_mfma_f32_16x16x32_f16 v[52:55], v[116:119], v[100:103], v[52:55]
	ds_read_b128 v[132:135], v18 offset:2048
	v_mfma_f32_16x16x32_f16 v[56:59], v[120:123], v[100:103], v[56:59]
	ds_read_b128 v[136:139], v18 offset:4096
	v_mfma_f32_16x16x32_f16 v[60:63], v[124:127], v[100:103], v[60:63]
	ds_read_b128 v[140:143], v18 offset:6144
	v_mfma_f32_16x16x32_f16 v[64:67], v[112:115], v[104:107], v[64:67]
	v_mfma_f32_16x16x32_f16 v[68:71], v[116:119], v[104:107], v[68:71]
	v_mfma_f32_16x16x32_f16 v[72:75], v[120:123], v[104:107], v[72:75]
	s_add_u32 m0, s14, 0x12000
	s_nop 0
	global_load_lds_dwordx4 v5, s[28:29]
	v_mfma_f32_16x16x32_f16 v[76:79], v[124:127], v[104:107], v[76:79]
	v_mfma_f32_16x16x32_f16 v[80:83], v[112:115], v[108:111], v[80:83]
	s_add_u32 m0, s14, 0x14000
	s_nop 0
	global_load_lds_dwordx4 v6, s[30:31]
	v_mfma_f32_16x16x32_f16 v[84:87], v[116:119], v[108:111], v[84:87]
	v_mfma_f32_16x16x32_f16 v[88:91], v[120:123], v[108:111], v[88:91]
	s_add_u32 m0, s14, 0x16000
	s_nop 0
	global_load_lds_dwordx4 v7, s[30:31]
	v_mfma_f32_16x16x32_f16 v[92:95], v[124:127], v[108:111], v[92:95]
	s_waitcnt vmcnt(6) lgkmcnt(0)
	s_barrier
	s_add_u32 s28, s28, 0x80
	s_addc_u32 s29, s29, 0
	s_add_u32 s30, s30, 0x80
	s_addc_u32 s31, s31, 0
	s_waitcnt lgkmcnt(0)
	v_mfma_f32_16x16x32_f16 v[32:35], v[144:147], v[128:131], v[32:35]
	ds_read_b128 v[96:99], v8
	v_mfma_f32_16x16x32_f16 v[36:39], v[148:151], v[128:131], v[36:39]
	ds_read_b128 v[112:115], v9 offset:32768
	v_mfma_f32_16x16x32_f16 v[40:43], v[152:155], v[128:131], v[40:43]
	ds_read_b128 v[116:119], v9 offset:34816
	v_mfma_f32_16x16x32_f16 v[44:47], v[156:159], v[128:131], v[44:47]
	ds_read_b128 v[120:123], v9 offset:36864
	v_mfma_f32_16x16x32_f16 v[48:51], v[144:147], v[132:135], v[48:51]
	ds_read_b128 v[124:127], v9 offset:38912
	v_mfma_f32_16x16x32_f16 v[52:55], v[148:151], v[132:135], v[52:55]
	ds_read_b128 v[100:103], v8 offset:2048
	v_mfma_f32_16x16x32_f16 v[56:59], v[152:155], v[132:135], v[56:59]
	ds_read_b128 v[104:107], v8 offset:4096
	v_mfma_f32_16x16x32_f16 v[60:63], v[156:159], v[132:135], v[60:63]
	ds_read_b128 v[108:111], v8 offset:6144
	v_mfma_f32_16x16x32_f16 v[64:67], v[144:147], v[136:139], v[64:67]
	v_mfma_f32_16x16x32_f16 v[68:71], v[148:151], v[136:139], v[68:71]
	v_mfma_f32_16x16x32_f16 v[72:75], v[152:155], v[136:139], v[72:75]
	s_add_u32 m0, s14, 0x18000
	s_nop 0
	global_load_lds_dwordx4 v2, s[28:29]
	v_mfma_f32_16x16x32_f16 v[76:79], v[156:159], v[136:139], v[76:79]
	v_mfma_f32_16x16x32_f16 v[80:83], v[144:147], v[140:143], v[80:83]
	s_add_u32 m0, s14, 0x1a000
	s_nop 0
	global_load_lds_dwordx4 v3, s[28:29]
	v_mfma_f32_16x16x32_f16 v[84:87], v[148:151], v[140:143], v[84:87]
	v_mfma_f32_16x16x32_f16 v[88:91], v[152:155], v[140:143], v[88:91]
	s_add_u32 m0, s14, 0x1c000
	s_nop 0
	global_load_lds_dwordx4 v4, s[28:29]
	v_mfma_f32_16x16x32_f16 v[92:95], v[156:159], v[140:143], v[92:95]
	s_waitcnt lgkmcnt(0)
	v_mfma_f32_16x16x32_f16 v[32:35], v[112:115], v[96:99], v[32:35]
	ds_read_b128 v[128:131], v10
	v_mfma_f32_16x16x32_f16 v[36:39], v[116:119], v[96:99], v[36:39]
	ds_read_b128 v[144:147], v11 offset:32768
	v_mfma_f32_16x16x32_f16 v[40:43], v[120:123], v[96:99], v[40:43]
	ds_read_b128 v[148:151], v11 offset:34816
	v_mfma_f32_16x16x32_f16 v[44:47], v[124:127], v[96:99], v[44:47]
	ds_read_b128 v[152:155], v11 offset:36864
	v_mfma_f32_16x16x32_f16 v[48:51], v[112:115], v[100:103], v[48:51]
	ds_read_b128 v[156:159], v11 offset:38912
	v_mfma_f32_16x16x32_f16 v[52:55], v[116:119], v[100:103], v[52:55]
	ds_read_b128 v[132:135], v10 offset:2048
	v_mfma_f32_16x16x32_f16 v[56:59], v[120:123], v[100:103], v[56:59]
	ds_read_b128 v[136:139], v10 offset:4096
	v_mfma_f32_16x16x32_f16 v[60:63], v[124:127], v[100:103], v[60:63]
	ds_read_b128 v[140:143], v10 offset:6144
	v_mfma_f32_16x16x32_f16 v[64:67], v[112:115], v[104:107], v[64:67]
	v_mfma_f32_16x16x32_f16 v[68:71], v[116:119], v[104:107], v[68:71]
	v_mfma_f32_16x16x32_f16 v[72:75], v[120:123], v[104:107], v[72:75]
	s_add_u32 m0, s14, 0x1e000
	s_nop 0
	global_load_lds_dwordx4 v5, s[28:29]
	v_mfma_f32_16x16x32_f16 v[76:79], v[124:127], v[104:107], v[76:79]
	v_mfma_f32_16x16x32_f16 v[80:83], v[112:115], v[108:111], v[80:83]
	s_add_u32 m0, s14, 0x20000
	s_nop 0
	global_load_lds_dwordx4 v6, s[30:31]
	v_mfma_f32_16x16x32_f16 v[84:87], v[116:119], v[108:111], v[84:87]
	v_mfma_f32_16x16x32_f16 v[88:91], v[120:123], v[108:111], v[88:91]
	s_add_u32 m0, s14, 0x22000
	s_nop 0
	global_load_lds_dwordx4 v7, s[30:31]
	v_mfma_f32_16x16x32_f16 v[92:95], v[124:127], v[108:111], v[92:95]
	s_waitcnt vmcnt(6) lgkmcnt(0)
	s_barrier
	s_add_u32 s28, s28, 0x80
	s_addc_u32 s29, s29, 0
	s_add_u32 s30, s30, 0x80
	s_addc_u32 s31, s31, 0
	s_waitcnt lgkmcnt(0)
	v_mfma_f32_16x16x32_f16 v[32:35], v[144:147], v[128:131], v[32:35]
	ds_read_b128 v[96:99], v12
	v_mfma_f32_16x16x32_f16 v[36:39], v[148:151], v[128:131], v[36:39]
	ds_read_b128 v[112:115], v13 offset:32768
	v_mfma_f32_16x16x32_f16 v[40:43], v[152:155], v[128:131], v[40:43]
	ds_read_b128 v[116:119], v13 offset:34816
	v_mfma_f32_16x16x32_f16 v[44:47], v[156:159], v[128:131], v[44:47]
	ds_read_b128 v[120:123], v13 offset:36864
	v_mfma_f32_16x16x32_f16 v[48:51], v[144:147], v[132:135], v[48:51]
	ds_read_b128 v[124:127], v13 offset:38912
	v_mfma_f32_16x16x32_f16 v[52:55], v[148:151], v[132:135], v[52:55]
	ds_read_b128 v[100:103], v12 offset:2048
	v_mfma_f32_16x16x32_f16 v[56:59], v[152:155], v[132:135], v[56:59]
	ds_read_b128 v[104:107], v12 offset:4096
	v_mfma_f32_16x16x32_f16 v[60:63], v[156:159], v[132:135], v[60:63]
	ds_read_b128 v[108:111], v12 offset:6144
	v_mfma_f32_16x16x32_f16 v[64:67], v[144:147], v[136:139], v[64:67]
	v_mfma_f32_16x16x32_f16 v[68:71], v[148:151], v[136:139], v[68:71]
	v_mfma_f32_16x16x32_f16 v[72:75], v[152:155], v[136:139], v[72:75]
	s_add_u32 m0, s14, 0x0
	s_nop 0
	global_load_lds_dwordx4 v2, s[28:29]
	v_mfma_f32_16x16x32_f16 v[76:79], v[156:159], v[136:139], v[76:79]
	v_mfma_f32_16x16x32_f16 v[80:83], v[144:147], v[140:143], v[80:83]
	s_add_u32 m0, s14, 0x2000
	s_nop 0
	global_load_lds_dwordx4 v3, s[28:29]
	v_mfma_f32_16x16x32_f16 v[84:87], v[148:151], v[140:143], v[84:87]
	v_mfma_f32_16x16x32_f16 v[88:91], v[152:155], v[140:143], v[88:91]
	s_add_u32 m0, s14, 0x4000
	s_nop 0
	global_load_lds_dwordx4 v4, s[28:29]
	v_mfma_f32_16x16x32_f16 v[92:95], v[156:159], v[140:143], v[92:95]
	s_waitcnt lgkmcnt(0)
	v_mfma_f32_16x16x32_f16 v[32:35], v[112:115], v[96:99], v[32:35]
	ds_read_b128 v[128:131], v14
	v_mfma_f32_16x16x32_f16 v[36:39], v[116:119], v[96:99], v[36:39]
	ds_read_b128 v[144:147], v15 offset:32768
	v_mfma_f32_16x16x32_f16 v[40:43], v[120:123], v[96:99], v[40:43]
	ds_read_b128 v[148:151], v15 offset:34816
	v_mfma_f32_16x16x32_f16 v[44:47], v[124:127], v[96:99], v[44:47]
	ds_read_b128 v[152:155], v15 offset:36864
	v_mfma_f32_16x16x32_f16 v[48:51], v[112:115], v[100:103], v[48:51]
	ds_read_b128 v[156:159], v15 offset:38912
	v_mfma_f32_16x16x32_f16 v[52:55], v[116:119], v[100:103], v[52:55]
	ds_read_b128 v[132:135], v14 offset:2048
	v_mfma_f32_16x16x32_f16 v[56:59], v[120:123], v[100:103], v[56:59]
	ds_read_b128 v[136:139], v14 offset:4096
	v_mfma_f32_16x16x32_f16 v[60:63], v[124:127], v[100:103], v[60:63]
	ds_read_b128 v[140:143], v14 offset:6144
	v_mfma_f32_16x16x32_f16 v[64:67], v[112:115], v[104:107], v[64:67]
	v_mfma_f32_16x16x32_f16 v[68:71], v[116:119], v[104:107], v[68:71]
	v_mfma_f32_16x16x32_f16 v[72:75], v[120:123], v[104:107], v[72:75]
	s_add_u32 m0, s14, 0x6000
	s_nop 0
	global_load_lds_dwordx4 v5, s[28:29]
	v_mfma_f32_16x16x32_f16 v[76:79], v[124:127], v[104:107], v[76:79]
	v_mfma_f32_16x16x32_f16 v[80:83], v[112:115], v[108:111], v[80:83]
	s_add_u32 m0, s14, 0x8000
	s_nop 0
	global_load_lds_dwordx4 v6, s[30:31]
	v_mfma_f32_16x16x32_f16 v[84:87], v[116:119], v[108:111], v[84:87]
	v_mfma_f32_16x16x32_f16 v[88:91], v[120:123], v[108:111], v[88:91]
	s_add_u32 m0, s14, 0xa000
	s_nop 0
	global_load_lds_dwordx4 v7, s[30:31]
	v_mfma_f32_16x16x32_f16 v[92:95], v[124:127], v[108:111], v[92:95]
	s_waitcnt vmcnt(6) lgkmcnt(0)
	s_barrier
	s_add_u32 s28, s28, 0x80
	s_addc_u32 s29, s29, 0
	s_add_u32 s30, s30, 0x80
	s_addc_u32 s31, s31, 0
	s_waitcnt lgkmcnt(0)
	v_mfma_f32_16x16x32_f16 v[32:35], v[144:147], v[128:131], v[32:35]
	ds_read_b128 v[96:99], v16
	v_mfma_f32_16x16x32_f16 v[36:39], v[148:151], v[128:131], v[36:39]
	ds_read_b128 v[112:115], v17 offset:32768
	v_mfma_f32_16x16x32_f16 v[40:43], v[152:155], v[128:131], v[40:43]
	ds_read_b128 v[116:119], v17 offset:34816
	v_mfma_f32_16x16x32_f16 v[44:47], v[156:159], v[128:131], v[44:47]
	ds_read_b128 v[120:123], v17 offset:36864
	v_mfma_f32_16x16x32_f16 v[48:51], v[144:147], v[132:135], v[48:51]
	ds_read_b128 v[124:127], v17 offset:38912
	v_mfma_f32_16x16x32_f16 v[52:55], v[148:151], v[132:135], v[52:55]
	ds_read_b128 v[100:103], v16 offset:2048
	v_mfma_f32_16x16x32_f16 v[56:59], v[152:155], v[132:135], v[56:59]
	ds_read_b128 v[104:107], v16 offset:4096
	v_mfma_f32_16x16x32_f16 v[60:63], v[156:159], v[132:135], v[60:63]
	ds_read_b128 v[108:111], v16 offset:6144
	v_mfma_f32_16x16x32_f16 v[64:67], v[144:147], v[136:139], v[64:67]
	v_mfma_f32_16x16x32_f16 v[68:71], v[148:151], v[136:139], v[68:71]
	v_mfma_f32_16x16x32_f16 v[72:75], v[152:155], v[136:139], v[72:75]
	s_add_u32 m0, s14, 0xc000
	s_nop 0
	global_load_lds_dwordx4 v2, s[28:29]
	v_mfma_f32_16x16x32_f16 v[76:79], v[156:159], v[136:139], v[76:79]
	v_mfma_f32_16x16x32_f16 v[80:83], v[144:147], v[140:143], v[80:83]
	s_add_u32 m0, s14, 0xe000
	s_nop 0
	global_load_lds_dwordx4 v3, s[28:29]
	v_mfma_f32_16x16x32_f16 v[84:87], v[148:151], v[140:143], v[84:87]
	v_mfma_f32_16x16x32_f16 v[88:91], v[152:155], v[140:143], v[88:91]
	s_add_u32 m0, s14, 0x10000
	s_nop 0
	global_load_lds_dwordx4 v4, s[28:29]
	v_mfma_f32_16x16x32_f16 v[92:95], v[156:159], v[140:143], v[92:95]
	s_waitcnt lgkmcnt(0)
	v_mfma_f32_16x16x32_f16 v[32:35], v[112:115], v[96:99], v[32:35]
	ds_read_b128 v[128:131], v18
	v_mfma_f32_16x16x32_f16 v[36:39], v[116:119], v[96:99], v[36:39]
	ds_read_b128 v[144:147], v19 offset:32768
	v_mfma_f32_16x16x32_f16 v[40:43], v[120:123], v[96:99], v[40:43]
	ds_read_b128 v[148:151], v19 offset:34816
	v_mfma_f32_16x16x32_f16 v[44:47], v[124:127], v[96:99], v[44:47]
	ds_read_b128 v[152:155], v19 offset:36864
	v_mfma_f32_16x16x32_f16 v[48:51], v[112:115], v[100:103], v[48:51]
	ds_read_b128 v[156:159], v19 offset:38912
	v_mfma_f32_16x16x32_f16 v[52:55], v[116:119], v[100:103], v[52:55]
	ds_read_b128 v[132:135], v18 offset:2048
	v_mfma_f32_16x16x32_f16 v[56:59], v[120:123], v[100:103], v[56:59]
	ds_read_b128 v[136:139], v18 offset:4096
	v_mfma_f32_16x16x32_f16 v[60:63], v[124:127], v[100:103], v[60:63]
	ds_read_b128 v[140:143], v18 offset:6144
	v_mfma_f32_16x16x32_f16 v[64:67], v[112:115], v[104:107], v[64:67]
	v_mfma_f32_16x16x32_f16 v[68:71], v[116:119], v[104:107], v[68:71]
	v_mfma_f32_16x16x32_f16 v[72:75], v[120:123], v[104:107], v[72:75]
	s_add_u32 m0, s14, 0x12000
	s_nop 0
	global_load_lds_dwordx4 v5, s[28:29]
	v_mfma_f32_16x16x32_f16 v[76:79], v[124:127], v[104:107], v[76:79]
	v_mfma_f32_16x16x32_f16 v[80:83], v[112:115], v[108:111], v[80:83]
	s_add_u32 m0, s14, 0x14000
	s_nop 0
	global_load_lds_dwordx4 v6, s[30:31]
	v_mfma_f32_16x16x32_f16 v[84:87], v[116:119], v[108:111], v[84:87]
	v_mfma_f32_16x16x32_f16 v[88:91], v[120:123], v[108:111], v[88:91]
	s_add_u32 m0, s14, 0x16000
	s_nop 0
	global_load_lds_dwordx4 v7, s[30:31]
	v_mfma_f32_16x16x32_f16 v[92:95], v[124:127], v[108:111], v[92:95]
	s_waitcnt vmcnt(6) lgkmcnt(0)
	s_barrier
	s_add_u32 s28, s28, 0x80
	s_addc_u32 s29, s29, 0
	s_add_u32 s30, s30, 0x80
	s_addc_u32 s31, s31, 0
	s_waitcnt lgkmcnt(0)
	v_mfma_f32_16x16x32_f16 v[32:35], v[144:147], v[128:131], v[32:35]
	ds_read_b128 v[96:99], v8
	v_mfma_f32_16x16x32_f16 v[36:39], v[148:151], v[128:131], v[36:39]
	ds_read_b128 v[112:115], v9 offset:32768
	v_mfma_f32_16x16x32_f16 v[40:43], v[152:155], v[128:131], v[40:43]
	ds_read_b128 v[116:119], v9 offset:34816
	v_mfma_f32_16x16x32_f16 v[44:47], v[156:159], v[128:131], v[44:47]
	ds_read_b128 v[120:123], v9 offset:36864
	v_mfma_f32_16x16x32_f16 v[48:51], v[144:147], v[132:135], v[48:51]
	ds_read_b128 v[124:127], v9 offset:38912
	v_mfma_f32_16x16x32_f16 v[52:55], v[148:151], v[132:135], v[52:55]
	ds_read_b128 v[100:103], v8 offset:2048
	v_mfma_f32_16x16x32_f16 v[56:59], v[152:155], v[132:135], v[56:59]
	ds_read_b128 v[104:107], v8 offset:4096
	v_mfma_f32_16x16x32_f16 v[60:63], v[156:159], v[132:135], v[60:63]
	ds_read_b128 v[108:111], v8 offset:6144
	v_mfma_f32_16x16x32_f16 v[64:67], v[144:147], v[136:139], v[64:67]
	v_mfma_f32_16x16x32_f16 v[68:71], v[148:151], v[136:139], v[68:71]
	v_mfma_f32_16x16x32_f16 v[72:75], v[152:155], v[136:139], v[72:75]
	s_add_u32 m0, s14, 0x18000
	s_nop 0
	global_load_lds_dwordx4 v2, s[28:29]
	v_mfma_f32_16x16x32_f16 v[76:79], v[156:159], v[136:139], v[76:79]
	v_mfma_f32_16x16x32_f16 v[80:83], v[144:147], v[140:143], v[80:83]
	s_add_u32 m0, s14, 0x1a000
	s_nop 0
	global_load_lds_dwordx4 v3, s[28:29]
	v_mfma_f32_16x16x32_f16 v[84:87], v[148:151], v[140:143], v[84:87]
	v_mfma_f32_16x16x32_f16 v[88:91], v[152:155], v[140:143], v[88:91]
	s_add_u32 m0, s14, 0x1c000
	s_nop 0
	global_load_lds_dwordx4 v4, s[28:29]
	v_mfma_f32_16x16x32_f16 v[92:95], v[156:159], v[140:143], v[92:95]
	s_waitcnt lgkmcnt(0)
	v_mfma_f32_16x16x32_f16 v[32:35], v[112:115], v[96:99], v[32:35]
	ds_read_b128 v[128:131], v10
	v_mfma_f32_16x16x32_f16 v[36:39], v[116:119], v[96:99], v[36:39]
	ds_read_b128 v[144:147], v11 offset:32768
	v_mfma_f32_16x16x32_f16 v[40:43], v[120:123], v[96:99], v[40:43]
	ds_read_b128 v[148:151], v11 offset:34816
	v_mfma_f32_16x16x32_f16 v[44:47], v[124:127], v[96:99], v[44:47]
	ds_read_b128 v[152:155], v11 offset:36864
	v_mfma_f32_16x16x32_f16 v[48:51], v[112:115], v[100:103], v[48:51]
	ds_read_b128 v[156:159], v11 offset:38912
	v_mfma_f32_16x16x32_f16 v[52:55], v[116:119], v[100:103], v[52:55]
	ds_read_b128 v[132:135], v10 offset:2048
	v_mfma_f32_16x16x32_f16 v[56:59], v[120:123], v[100:103], v[56:59]
	ds_read_b128 v[136:139], v10 offset:4096
	v_mfma_f32_16x16x32_f16 v[60:63], v[124:127], v[100:103], v[60:63]
	ds_read_b128 v[140:143], v10 offset:6144
	v_mfma_f32_16x16x32_f16 v[64:67], v[112:115], v[104:107], v[64:67]
	v_mfma_f32_16x16x32_f16 v[68:71], v[116:119], v[104:107], v[68:71]
	v_mfma_f32_16x16x32_f16 v[72:75], v[120:123], v[104:107], v[72:75]
	s_add_u32 m0, s14, 0x1e000
	s_nop 0
	global_load_lds_dwordx4 v5, s[28:29]
	v_mfma_f32_16x16x32_f16 v[76:79], v[124:127], v[104:107], v[76:79]
	v_mfma_f32_16x16x32_f16 v[80:83], v[112:115], v[108:111], v[80:83]
	s_add_u32 m0, s14, 0x20000
	s_nop 0
	global_load_lds_dwordx4 v6, s[30:31]
	v_mfma_f32_16x16x32_f16 v[84:87], v[116:119], v[108:111], v[84:87]
	v_mfma_f32_16x16x32_f16 v[88:91], v[120:123], v[108:111], v[88:91]
	s_add_u32 m0, s14, 0x22000
	s_nop 0
	global_load_lds_dwordx4 v7, s[30:31]
	v_mfma_f32_16x16x32_f16 v[92:95], v[124:127], v[108:111], v[92:95]
	s_waitcnt vmcnt(6) lgkmcnt(0)
	s_barrier
	s_add_u32 s28, s28, 0x80
	s_addc_u32 s29, s29, 0
	s_add_u32 s30, s30, 0x80
	s_addc_u32 s31, s31, 0
	s_waitcnt lgkmcnt(0)
	v_mfma_f32_16x16x32_f16 v[32:35], v[144:147], v[128:131], v[32:35]
	ds_read_b128 v[96:99], v12
	v_mfma_f32_16x16x32_f16 v[36:39], v[148:151], v[128:131], v[36:39]
	ds_read_b128 v[112:115], v13 offset:32768
	v_mfma_f32_16x16x32_f16 v[40:43], v[152:155], v[128:131], v[40:43]
	ds_read_b128 v[116:119], v13 offset:34816
	v_mfma_f32_16x16x32_f16 v[44:47], v[156:159], v[128:131], v[44:47]
	ds_read_b128 v[120:123], v13 offset:36864
	v_mfma_f32_16x16x32_f16 v[48:51], v[144:147], v[132:135], v[48:51]
	ds_read_b128 v[124:127], v13 offset:38912
	v_mfma_f32_16x16x32_f16 v[52:55], v[148:151], v[132:135], v[52:55]
	ds_read_b128 v[100:103], v12 offset:2048
	v_mfma_f32_16x16x32_f16 v[56:59], v[152:155], v[132:135], v[56:59]
	ds_read_b128 v[104:107], v12 offset:4096
	v_mfma_f32_16x16x32_f16 v[60:63], v[156:159], v[132:135], v[60:63]
	ds_read_b128 v[108:111], v12 offset:6144
	v_mfma_f32_16x16x32_f16 v[64:67], v[144:147], v[136:139], v[64:67]
	v_mfma_f32_16x16x32_f16 v[68:71], v[148:151], v[136:139], v[68:71]
	v_mfma_f32_16x16x32_f16 v[72:75], v[152:155], v[136:139], v[72:75]
	s_add_u32 m0, s14, 0x0
	s_nop 0
	global_load_lds_dwordx4 v2, s[28:29]
	v_mfma_f32_16x16x32_f16 v[76:79], v[156:159], v[136:139], v[76:79]
	v_mfma_f32_16x16x32_f16 v[80:83], v[144:147], v[140:143], v[80:83]
	s_add_u32 m0, s14, 0x2000
	s_nop 0
	global_load_lds_dwordx4 v3, s[28:29]
	v_mfma_f32_16x16x32_f16 v[84:87], v[148:151], v[140:143], v[84:87]
	v_mfma_f32_16x16x32_f16 v[88:91], v[152:155], v[140:143], v[88:91]
	s_add_u32 m0, s14, 0x4000
	s_nop 0
	global_load_lds_dwordx4 v4, s[28:29]
	v_mfma_f32_16x16x32_f16 v[92:95], v[156:159], v[140:143], v[92:95]
	s_waitcnt lgkmcnt(0)
	v_mfma_f32_16x16x32_f16 v[32:35], v[112:115], v[96:99], v[32:35]
	ds_read_b128 v[128:131], v14
	v_mfma_f32_16x16x32_f16 v[36:39], v[116:119], v[96:99], v[36:39]
	ds_read_b128 v[144:147], v15 offset:32768
	v_mfma_f32_16x16x32_f16 v[40:43], v[120:123], v[96:99], v[40:43]
	ds_read_b128 v[148:151], v15 offset:34816
	v_mfma_f32_16x16x32_f16 v[44:47], v[124:127], v[96:99], v[44:47]
	ds_read_b128 v[152:155], v15 offset:36864
	v_mfma_f32_16x16x32_f16 v[48:51], v[112:115], v[100:103], v[48:51]
	ds_read_b128 v[156:159], v15 offset:38912
	v_mfma_f32_16x16x32_f16 v[52:55], v[116:119], v[100:103], v[52:55]
	ds_read_b128 v[132:135], v14 offset:2048
	v_mfma_f32_16x16x32_f16 v[56:59], v[120:123], v[100:103], v[56:59]
	ds_read_b128 v[136:139], v14 offset:4096
	v_mfma_f32_16x16x32_f16 v[60:63], v[124:127], v[100:103], v[60:63]
	ds_read_b128 v[140:143], v14 offset:6144
	v_mfma_f32_16x16x32_f16 v[64:67], v[112:115], v[104:107], v[64:67]
	v_mfma_f32_16x16x32_f16 v[68:71], v[116:119], v[104:107], v[68:71]
	v_mfma_f32_16x16x32_f16 v[72:75], v[120:123], v[104:107], v[72:75]
	s_add_u32 m0, s14, 0x6000
	s_nop 0
	global_load_lds_dwordx4 v5, s[28:29]
	v_mfma_f32_16x16x32_f16 v[76:79], v[124:127], v[104:107], v[76:79]
	v_mfma_f32_16x16x32_f16 v[80:83], v[112:115], v[108:111], v[80:83]
	s_add_u32 m0, s14, 0x8000
	s_nop 0
	global_load_lds_dwordx4 v6, s[30:31]
	v_mfma_f32_16x16x32_f16 v[84:87], v[116:119], v[108:111], v[84:87]
	v_mfma_f32_16x16x32_f16 v[88:91], v[120:123], v[108:111], v[88:91]
	s_add_u32 m0, s14, 0xa000
	s_nop 0
	global_load_lds_dwordx4 v7, s[30:31]
	v_mfma_f32_16x16x32_f16 v[92:95], v[124:127], v[108:111], v[92:95]
	s_waitcnt vmcnt(6) lgkmcnt(0)
	s_barrier
	s_add_u32 s28, s28, 0x80
	s_addc_u32 s29, s29, 0
	s_add_u32 s30, s30, 0x80
	s_addc_u32 s31, s31, 0
	s_waitcnt lgkmcnt(0)
	v_mfma_f32_16x16x32_f16 v[32:35], v[144:147], v[128:131], v[32:35]
	ds_read_b128 v[96:99], v16
	v_mfma_f32_16x16x32_f16 v[36:39], v[148:151], v[128:131], v[36:39]
	ds_read_b128 v[112:115], v17 offset:32768
	v_mfma_f32_16x16x32_f16 v[40:43], v[152:155], v[128:131], v[40:43]
	ds_read_b128 v[116:119], v17 offset:34816
	v_mfma_f32_16x16x32_f16 v[44:47], v[156:159], v[128:131], v[44:47]
	ds_read_b128 v[120:123], v17 offset:36864
	v_mfma_f32_16x16x32_f16 v[48:51], v[144:147], v[132:135], v[48:51]
	ds_read_b128 v[124:127], v17 offset:38912
	v_mfma_f32_16x16x32_f16 v[52:55], v[148:151], v[132:135], v[52:55]
	ds_read_b128 v[100:103], v16 offset:2048
	v_mfma_f32_16x16x32_f16 v[56:59], v[152:155], v[132:135], v[56:59]
	ds_read_b128 v[104:107], v16 offset:4096
	v_mfma_f32_16x16x32_f16 v[60:63], v[156:159], v[132:135], v[60:63]
	ds_read_b128 v[108:111], v16 offset:6144
	v_mfma_f32_16x16x32_f16 v[64:67], v[144:147], v[136:139], v[64:67]
	v_mfma_f32_16x16x32_f16 v[68:71], v[148:151], v[136:139], v[68:71]
	v_mfma_f32_16x16x32_f16 v[72:75], v[152:155], v[136:139], v[72:75]
	s_add_u32 m0, s14, 0xc000
	s_nop 0
	global_load_lds_dwordx4 v2, s[28:29]
	v_mfma_f32_16x16x32_f16 v[76:79], v[156:159], v[136:139], v[76:79]
	v_mfma_f32_16x16x32_f16 v[80:83], v[144:147], v[140:143], v[80:83]
	s_add_u32 m0, s14, 0xe000
	s_nop 0
	global_load_lds_dwordx4 v3, s[28:29]
	v_mfma_f32_16x16x32_f16 v[84:87], v[148:151], v[140:143], v[84:87]
	v_mfma_f32_16x16x32_f16 v[88:91], v[152:155], v[140:143], v[88:91]
	s_add_u32 m0, s14, 0x10000
	s_nop 0
	global_load_lds_dwordx4 v4, s[28:29]
	v_mfma_f32_16x16x32_f16 v[92:95], v[156:159], v[140:143], v[92:95]
	s_waitcnt lgkmcnt(0)
	v_mfma_f32_16x16x32_f16 v[32:35], v[112:115], v[96:99], v[32:35]
	ds_read_b128 v[128:131], v18
	v_mfma_f32_16x16x32_f16 v[36:39], v[116:119], v[96:99], v[36:39]
	ds_read_b128 v[144:147], v19 offset:32768
	v_mfma_f32_16x16x32_f16 v[40:43], v[120:123], v[96:99], v[40:43]
	ds_read_b128 v[148:151], v19 offset:34816
	v_mfma_f32_16x16x32_f16 v[44:47], v[124:127], v[96:99], v[44:47]
	ds_read_b128 v[152:155], v19 offset:36864
	v_mfma_f32_16x16x32_f16 v[48:51], v[112:115], v[100:103], v[48:51]
	ds_read_b128 v[156:159], v19 offset:38912
	v_mfma_f32_16x16x32_f16 v[52:55], v[116:119], v[100:103], v[52:55]
	ds_read_b128 v[132:135], v18 offset:2048
	v_mfma_f32_16x16x32_f16 v[56:59], v[120:123], v[100:103], v[56:59]
	ds_read_b128 v[136:139], v18 offset:4096
	v_mfma_f32_16x16x32_f16 v[60:63], v[124:127], v[100:103], v[60:63]
	ds_read_b128 v[140:143], v18 offset:6144
	v_mfma_f32_16x16x32_f16 v[64:67], v[112:115], v[104:107], v[64:67]
	v_mfma_f32_16x16x32_f16 v[68:71], v[116:119], v[104:107], v[68:71]
	v_mfma_f32_16x16x32_f16 v[72:75], v[120:123], v[104:107], v[72:75]
	s_add_u32 m0, s14, 0x12000
	s_nop 0
	global_load_lds_dwordx4 v5, s[28:29]
	v_mfma_f32_16x16x32_f16 v[76:79], v[124:127], v[104:107], v[76:79]
	v_mfma_f32_16x16x32_f16 v[80:83], v[112:115], v[108:111], v[80:83]
	s_add_u32 m0, s14, 0x14000
	s_nop 0
	global_load_lds_dwordx4 v6, s[30:31]
	v_mfma_f32_16x16x32_f16 v[84:87], v[116:119], v[108:111], v[84:87]
	v_mfma_f32_16x16x32_f16 v[88:91], v[120:123], v[108:111], v[88:91]
	s_add_u32 m0, s14, 0x16000
	s_nop 0
	global_load_lds_dwordx4 v7, s[30:31]
	v_mfma_f32_16x16x32_f16 v[92:95], v[124:127], v[108:111], v[92:95]
	s_waitcnt vmcnt(6) lgkmcnt(0)
	s_barrier
	s_add_u32 s28, s28, 0x80
	s_addc_u32 s29, s29, 0
	s_add_u32 s30, s30, 0x80
	s_addc_u32 s31, s31, 0
	s_waitcnt lgkmcnt(0)
	v_mfma_f32_16x16x32_f16 v[32:35], v[144:147], v[128:131], v[32:35]
	ds_read_b128 v[96:99], v8
	v_mfma_f32_16x16x32_f16 v[36:39], v[148:151], v[128:131], v[36:39]
	ds_read_b128 v[112:115], v9 offset:32768
	v_mfma_f32_16x16x32_f16 v[40:43], v[152:155], v[128:131], v[40:43]
	ds_read_b128 v[116:119], v9 offset:34816
	v_mfma_f32_16x16x32_f16 v[44:47], v[156:159], v[128:131], v[44:47]
	ds_read_b128 v[120:123], v9 offset:36864
	v_mfma_f32_16x16x32_f16 v[48:51], v[144:147], v[132:135], v[48:51]
	ds_read_b128 v[124:127], v9 offset:38912
	v_mfma_f32_16x16x32_f16 v[52:55], v[148:151], v[132:135], v[52:55]
	ds_read_b128 v[100:103], v8 offset:2048
	v_mfma_f32_16x16x32_f16 v[56:59], v[152:155], v[132:135], v[56:59]
	ds_read_b128 v[104:107], v8 offset:4096
	v_mfma_f32_16x16x32_f16 v[60:63], v[156:159], v[132:135], v[60:63]
	ds_read_b128 v[108:111], v8 offset:6144
	v_mfma_f32_16x16x32_f16 v[64:67], v[144:147], v[136:139], v[64:67]
	v_mfma_f32_16x16x32_f16 v[68:71], v[148:151], v[136:139], v[68:71]
	v_mfma_f32_16x16x32_f16 v[72:75], v[152:155], v[136:139], v[72:75]
	s_add_u32 m0, s14, 0x18000
	s_nop 0
	global_load_lds_dwordx4 v2, s[28:29]
	v_mfma_f32_16x16x32_f16 v[76:79], v[156:159], v[136:139], v[76:79]
	v_mfma_f32_16x16x32_f16 v[80:83], v[144:147], v[140:143], v[80:83]
	s_add_u32 m0, s14, 0x1a000
	s_nop 0
	global_load_lds_dwordx4 v3, s[28:29]
	v_mfma_f32_16x16x32_f16 v[84:87], v[148:151], v[140:143], v[84:87]
	v_mfma_f32_16x16x32_f16 v[88:91], v[152:155], v[140:143], v[88:91]
	s_add_u32 m0, s14, 0x1c000
	s_nop 0
	global_load_lds_dwordx4 v4, s[28:29]
	v_mfma_f32_16x16x32_f16 v[92:95], v[156:159], v[140:143], v[92:95]
	s_waitcnt lgkmcnt(0)
	v_mfma_f32_16x16x32_f16 v[32:35], v[112:115], v[96:99], v[32:35]
	ds_read_b128 v[128:131], v10
	v_mfma_f32_16x16x32_f16 v[36:39], v[116:119], v[96:99], v[36:39]
	ds_read_b128 v[144:147], v11 offset:32768
	v_mfma_f32_16x16x32_f16 v[40:43], v[120:123], v[96:99], v[40:43]
	ds_read_b128 v[148:151], v11 offset:34816
	v_mfma_f32_16x16x32_f16 v[44:47], v[124:127], v[96:99], v[44:47]
	ds_read_b128 v[152:155], v11 offset:36864
	v_mfma_f32_16x16x32_f16 v[48:51], v[112:115], v[100:103], v[48:51]
	ds_read_b128 v[156:159], v11 offset:38912
	v_mfma_f32_16x16x32_f16 v[52:55], v[116:119], v[100:103], v[52:55]
	ds_read_b128 v[132:135], v10 offset:2048
	v_mfma_f32_16x16x32_f16 v[56:59], v[120:123], v[100:103], v[56:59]
	ds_read_b128 v[136:139], v10 offset:4096
	v_mfma_f32_16x16x32_f16 v[60:63], v[124:127], v[100:103], v[60:63]
	ds_read_b128 v[140:143], v10 offset:6144
	v_mfma_f32_16x16x32_f16 v[64:67], v[112:115], v[104:107], v[64:67]
	v_mfma_f32_16x16x32_f16 v[68:71], v[116:119], v[104:107], v[68:71]
	v_mfma_f32_16x16x32_f16 v[72:75], v[120:123], v[104:107], v[72:75]
	s_add_u32 m0, s14, 0x1e000
	s_nop 0
	global_load_lds_dwordx4 v5, s[28:29]
	v_mfma_f32_16x16x32_f16 v[76:79], v[124:127], v[104:107], v[76:79]
	v_mfma_f32_16x16x32_f16 v[80:83], v[112:115], v[108:111], v[80:83]
	s_add_u32 m0, s14, 0x20000
	s_nop 0
	global_load_lds_dwordx4 v6, s[30:31]
	v_mfma_f32_16x16x32_f16 v[84:87], v[116:119], v[108:111], v[84:87]
	v_mfma_f32_16x16x32_f16 v[88:91], v[120:123], v[108:111], v[88:91]
	s_add_u32 m0, s14, 0x22000
	s_nop 0
	global_load_lds_dwordx4 v7, s[30:31]
	v_mfma_f32_16x16x32_f16 v[92:95], v[124:127], v[108:111], v[92:95]
	s_waitcnt vmcnt(6) lgkmcnt(0)
	s_barrier
	s_add_u32 s28, s28, 0x80
	s_addc_u32 s29, s29, 0
	s_add_u32 s30, s30, 0x80
	s_addc_u32 s31, s31, 0
	s_waitcnt lgkmcnt(0)
	v_mfma_f32_16x16x32_f16 v[32:35], v[144:147], v[128:131], v[32:35]
	ds_read_b128 v[96:99], v12
	v_mfma_f32_16x16x32_f16 v[36:39], v[148:151], v[128:131], v[36:39]
	ds_read_b128 v[112:115], v13 offset:32768
	v_mfma_f32_16x16x32_f16 v[40:43], v[152:155], v[128:131], v[40:43]
	ds_read_b128 v[116:119], v13 offset:34816
	v_mfma_f32_16x16x32_f16 v[44:47], v[156:159], v[128:131], v[44:47]
	ds_read_b128 v[120:123], v13 offset:36864
	v_mfma_f32_16x16x32_f16 v[48:51], v[144:147], v[132:135], v[48:51]
	ds_read_b128 v[124:127], v13 offset:38912
	v_mfma_f32_16x16x32_f16 v[52:55], v[148:151], v[132:135], v[52:55]
	ds_read_b128 v[100:103], v12 offset:2048
	v_mfma_f32_16x16x32_f16 v[56:59], v[152:155], v[132:135], v[56:59]
	ds_read_b128 v[104:107], v12 offset:4096
	v_mfma_f32_16x16x32_f16 v[60:63], v[156:159], v[132:135], v[60:63]
	ds_read_b128 v[108:111], v12 offset:6144
	v_mfma_f32_16x16x32_f16 v[64:67], v[144:147], v[136:139], v[64:67]
	v_mfma_f32_16x16x32_f16 v[68:71], v[148:151], v[136:139], v[68:71]
	v_mfma_f32_16x16x32_f16 v[72:75], v[152:155], v[136:139], v[72:75]
	s_add_u32 m0, s14, 0x0
	s_nop 0
	global_load_lds_dwordx4 v2, s[28:29]
	v_mfma_f32_16x16x32_f16 v[76:79], v[156:159], v[136:139], v[76:79]
	v_mfma_f32_16x16x32_f16 v[80:83], v[144:147], v[140:143], v[80:83]
	s_add_u32 m0, s14, 0x2000
	s_nop 0
	global_load_lds_dwordx4 v3, s[28:29]
	v_mfma_f32_16x16x32_f16 v[84:87], v[148:151], v[140:143], v[84:87]
	v_mfma_f32_16x16x32_f16 v[88:91], v[152:155], v[140:143], v[88:91]
	s_add_u32 m0, s14, 0x4000
	s_nop 0
	global_load_lds_dwordx4 v4, s[28:29]
	v_mfma_f32_16x16x32_f16 v[92:95], v[156:159], v[140:143], v[92:95]
	s_waitcnt lgkmcnt(0)
	v_mfma_f32_16x16x32_f16 v[32:35], v[112:115], v[96:99], v[32:35]
	ds_read_b128 v[128:131], v14
	v_mfma_f32_16x16x32_f16 v[36:39], v[116:119], v[96:99], v[36:39]
	ds_read_b128 v[144:147], v15 offset:32768
	v_mfma_f32_16x16x32_f16 v[40:43], v[120:123], v[96:99], v[40:43]
	ds_read_b128 v[148:151], v15 offset:34816
	v_mfma_f32_16x16x32_f16 v[44:47], v[124:127], v[96:99], v[44:47]
	ds_read_b128 v[152:155], v15 offset:36864
	v_mfma_f32_16x16x32_f16 v[48:51], v[112:115], v[100:103], v[48:51]
	ds_read_b128 v[156:159], v15 offset:38912
	v_mfma_f32_16x16x32_f16 v[52:55], v[116:119], v[100:103], v[52:55]
	ds_read_b128 v[132:135], v14 offset:2048
	v_mfma_f32_16x16x32_f16 v[56:59], v[120:123], v[100:103], v[56:59]
	ds_read_b128 v[136:139], v14 offset:4096
	v_mfma_f32_16x16x32_f16 v[60:63], v[124:127], v[100:103], v[60:63]
	ds_read_b128 v[140:143], v14 offset:6144
	v_mfma_f32_16x16x32_f16 v[64:67], v[112:115], v[104:107], v[64:67]
	v_mfma_f32_16x16x32_f16 v[68:71], v[116:119], v[104:107], v[68:71]
	v_mfma_f32_16x16x32_f16 v[72:75], v[120:123], v[104:107], v[72:75]
	s_add_u32 m0, s14, 0x6000
	s_nop 0
	global_load_lds_dwordx4 v5, s[28:29]
	v_mfma_f32_16x16x32_f16 v[76:79], v[124:127], v[104:107], v[76:79]
	v_mfma_f32_16x16x32_f16 v[80:83], v[112:115], v[108:111], v[80:83]
	s_add_u32 m0, s14, 0x8000
	s_nop 0
	global_load_lds_dwordx4 v6, s[30:31]
	v_mfma_f32_16x16x32_f16 v[84:87], v[116:119], v[108:111], v[84:87]
	v_mfma_f32_16x16x32_f16 v[88:91], v[120:123], v[108:111], v[88:91]
	s_add_u32 m0, s14, 0xa000
	s_nop 0
	global_load_lds_dwordx4 v7, s[30:31]
	v_mfma_f32_16x16x32_f16 v[92:95], v[124:127], v[108:111], v[92:95]
	s_waitcnt vmcnt(6) lgkmcnt(0)
	s_barrier
	s_add_u32 s28, s28, 0x80
	s_addc_u32 s29, s29, 0
	s_add_u32 s30, s30, 0x80
	s_addc_u32 s31, s31, 0
	s_waitcnt lgkmcnt(0)
	v_mfma_f32_16x16x32_f16 v[32:35], v[144:147], v[128:131], v[32:35]
	ds_read_b128 v[96:99], v16
	v_mfma_f32_16x16x32_f16 v[36:39], v[148:151], v[128:131], v[36:39]
	ds_read_b128 v[112:115], v17 offset:32768
	v_mfma_f32_16x16x32_f16 v[40:43], v[152:155], v[128:131], v[40:43]
	ds_read_b128 v[116:119], v17 offset:34816
	v_mfma_f32_16x16x32_f16 v[44:47], v[156:159], v[128:131], v[44:47]
	ds_read_b128 v[120:123], v17 offset:36864
	v_mfma_f32_16x16x32_f16 v[48:51], v[144:147], v[132:135], v[48:51]
	ds_read_b128 v[124:127], v17 offset:38912
	v_mfma_f32_16x16x32_f16 v[52:55], v[148:151], v[132:135], v[52:55]
	ds_read_b128 v[100:103], v16 offset:2048
	v_mfma_f32_16x16x32_f16 v[56:59], v[152:155], v[132:135], v[56:59]
	ds_read_b128 v[104:107], v16 offset:4096
	v_mfma_f32_16x16x32_f16 v[60:63], v[156:159], v[132:135], v[60:63]
	ds_read_b128 v[108:111], v16 offset:6144
	v_mfma_f32_16x16x32_f16 v[64:67], v[144:147], v[136:139], v[64:67]
	v_mfma_f32_16x16x32_f16 v[68:71], v[148:151], v[136:139], v[68:71]
	v_mfma_f32_16x16x32_f16 v[72:75], v[152:155], v[136:139], v[72:75]
	s_add_u32 m0, s14, 0xc000
	s_nop 0
	global_load_lds_dwordx4 v2, s[28:29]
	v_mfma_f32_16x16x32_f16 v[76:79], v[156:159], v[136:139], v[76:79]
	v_mfma_f32_16x16x32_f16 v[80:83], v[144:147], v[140:143], v[80:83]
	s_add_u32 m0, s14, 0xe000
	s_nop 0
	global_load_lds_dwordx4 v3, s[28:29]
	v_mfma_f32_16x16x32_f16 v[84:87], v[148:151], v[140:143], v[84:87]
	v_mfma_f32_16x16x32_f16 v[88:91], v[152:155], v[140:143], v[88:91]
	s_add_u32 m0, s14, 0x10000
	s_nop 0
	global_load_lds_dwordx4 v4, s[28:29]
	v_mfma_f32_16x16x32_f16 v[92:95], v[156:159], v[140:143], v[92:95]
	s_waitcnt lgkmcnt(0)
	v_mfma_f32_16x16x32_f16 v[32:35], v[112:115], v[96:99], v[32:35]
	ds_read_b128 v[128:131], v18
	v_mfma_f32_16x16x32_f16 v[36:39], v[116:119], v[96:99], v[36:39]
	ds_read_b128 v[144:147], v19 offset:32768
	v_mfma_f32_16x16x32_f16 v[40:43], v[120:123], v[96:99], v[40:43]
	ds_read_b128 v[148:151], v19 offset:34816
	v_mfma_f32_16x16x32_f16 v[44:47], v[124:127], v[96:99], v[44:47]
	ds_read_b128 v[152:155], v19 offset:36864
	v_mfma_f32_16x16x32_f16 v[48:51], v[112:115], v[100:103], v[48:51]
	ds_read_b128 v[156:159], v19 offset:38912
	v_mfma_f32_16x16x32_f16 v[52:55], v[116:119], v[100:103], v[52:55]
	ds_read_b128 v[132:135], v18 offset:2048
	v_mfma_f32_16x16x32_f16 v[56:59], v[120:123], v[100:103], v[56:59]
	ds_read_b128 v[136:139], v18 offset:4096
	v_mfma_f32_16x16x32_f16 v[60:63], v[124:127], v[100:103], v[60:63]
	ds_read_b128 v[140:143], v18 offset:6144
	v_mfma_f32_16x16x32_f16 v[64:67], v[112:115], v[104:107], v[64:67]
	v_mfma_f32_16x16x32_f16 v[68:71], v[116:119], v[104:107], v[68:71]
	v_mfma_f32_16x16x32_f16 v[72:75], v[120:123], v[104:107], v[72:75]
	s_add_u32 m0, s14, 0x12000
	s_nop 0
	global_load_lds_dwordx4 v5, s[28:29]
	v_mfma_f32_16x16x32_f16 v[76:79], v[124:127], v[104:107], v[76:79]
	v_mfma_f32_16x16x32_f16 v[80:83], v[112:115], v[108:111], v[80:83]
	s_add_u32 m0, s14, 0x14000
	s_nop 0
	global_load_lds_dwordx4 v6, s[30:31]
	v_mfma_f32_16x16x32_f16 v[84:87], v[116:119], v[108:111], v[84:87]
	v_mfma_f32_16x16x32_f16 v[88:91], v[120:123], v[108:111], v[88:91]
	s_add_u32 m0, s14, 0x16000
	s_nop 0
	global_load_lds_dwordx4 v7, s[30:31]
	v_mfma_f32_16x16x32_f16 v[92:95], v[124:127], v[108:111], v[92:95]
	s_waitcnt vmcnt(6) lgkmcnt(0)
	s_barrier
	s_add_u32 s28, s28, 0x80
	s_addc_u32 s29, s29, 0
	s_add_u32 s30, s30, 0x80
	s_addc_u32 s31, s31, 0
	s_waitcnt lgkmcnt(0)
	v_mfma_f32_16x16x32_f16 v[32:35], v[144:147], v[128:131], v[32:35]
	ds_read_b128 v[96:99], v8
	v_mfma_f32_16x16x32_f16 v[36:39], v[148:151], v[128:131], v[36:39]
	ds_read_b128 v[112:115], v9 offset:32768
	v_mfma_f32_16x16x32_f16 v[40:43], v[152:155], v[128:131], v[40:43]
	ds_read_b128 v[116:119], v9 offset:34816
	v_mfma_f32_16x16x32_f16 v[44:47], v[156:159], v[128:131], v[44:47]
	ds_read_b128 v[120:123], v9 offset:36864
	v_mfma_f32_16x16x32_f16 v[48:51], v[144:147], v[132:135], v[48:51]
	ds_read_b128 v[124:127], v9 offset:38912
	v_mfma_f32_16x16x32_f16 v[52:55], v[148:151], v[132:135], v[52:55]
	ds_read_b128 v[100:103], v8 offset:2048
	v_mfma_f32_16x16x32_f16 v[56:59], v[152:155], v[132:135], v[56:59]
	ds_read_b128 v[104:107], v8 offset:4096
	v_mfma_f32_16x16x32_f16 v[60:63], v[156:159], v[132:135], v[60:63]
	ds_read_b128 v[108:111], v8 offset:6144
	v_mfma_f32_16x16x32_f16 v[64:67], v[144:147], v[136:139], v[64:67]
	v_mfma_f32_16x16x32_f16 v[68:71], v[148:151], v[136:139], v[68:71]
	v_mfma_f32_16x16x32_f16 v[72:75], v[152:155], v[136:139], v[72:75]
	s_add_u32 m0, s14, 0x18000
	s_nop 0
	global_load_lds_dwordx4 v2, s[28:29]
	v_mfma_f32_16x16x32_f16 v[76:79], v[156:159], v[136:139], v[76:79]
	v_mfma_f32_16x16x32_f16 v[80:83], v[144:147], v[140:143], v[80:83]
	s_add_u32 m0, s14, 0x1a000
	s_nop 0
	global_load_lds_dwordx4 v3, s[28:29]
	v_mfma_f32_16x16x32_f16 v[84:87], v[148:151], v[140:143], v[84:87]
	v_mfma_f32_16x16x32_f16 v[88:91], v[152:155], v[140:143], v[88:91]
	s_add_u32 m0, s14, 0x1c000
	s_nop 0
	global_load_lds_dwordx4 v4, s[28:29]
	v_mfma_f32_16x16x32_f16 v[92:95], v[156:159], v[140:143], v[92:95]
	s_waitcnt lgkmcnt(0)
	v_mfma_f32_16x16x32_f16 v[32:35], v[112:115], v[96:99], v[32:35]
	ds_read_b128 v[128:131], v10
	v_mfma_f32_16x16x32_f16 v[36:39], v[116:119], v[96:99], v[36:39]
	ds_read_b128 v[144:147], v11 offset:32768
	v_mfma_f32_16x16x32_f16 v[40:43], v[120:123], v[96:99], v[40:43]
	ds_read_b128 v[148:151], v11 offset:34816
	v_mfma_f32_16x16x32_f16 v[44:47], v[124:127], v[96:99], v[44:47]
	ds_read_b128 v[152:155], v11 offset:36864
	v_mfma_f32_16x16x32_f16 v[48:51], v[112:115], v[100:103], v[48:51]
	ds_read_b128 v[156:159], v11 offset:38912
	v_mfma_f32_16x16x32_f16 v[52:55], v[116:119], v[100:103], v[52:55]
	ds_read_b128 v[132:135], v10 offset:2048
	v_mfma_f32_16x16x32_f16 v[56:59], v[120:123], v[100:103], v[56:59]
	ds_read_b128 v[136:139], v10 offset:4096
	v_mfma_f32_16x16x32_f16 v[60:63], v[124:127], v[100:103], v[60:63]
	ds_read_b128 v[140:143], v10 offset:6144
	v_mfma_f32_16x16x32_f16 v[64:67], v[112:115], v[104:107], v[64:67]
	v_mfma_f32_16x16x32_f16 v[68:71], v[116:119], v[104:107], v[68:71]
	v_mfma_f32_16x16x32_f16 v[72:75], v[120:123], v[104:107], v[72:75]
	s_add_u32 m0, s14, 0x1e000
	s_nop 0
	global_load_lds_dwordx4 v5, s[28:29]
	v_mfma_f32_16x16x32_f16 v[76:79], v[124:127], v[104:107], v[76:79]
	v_mfma_f32_16x16x32_f16 v[80:83], v[112:115], v[108:111], v[80:83]
	s_add_u32 m0, s14, 0x20000
	s_nop 0
	global_load_lds_dwordx4 v6, s[30:31]
	v_mfma_f32_16x16x32_f16 v[84:87], v[116:119], v[108:111], v[84:87]
	v_mfma_f32_16x16x32_f16 v[88:91], v[120:123], v[108:111], v[88:91]
	s_add_u32 m0, s14, 0x22000
	s_nop 0
	global_load_lds_dwordx4 v7, s[30:31]
	v_mfma_f32_16x16x32_f16 v[92:95], v[124:127], v[108:111], v[92:95]
	s_waitcnt vmcnt(6) lgkmcnt(0)
	s_barrier
	s_add_u32 s28, s28, 0x80
	s_addc_u32 s29, s29, 0
	s_add_u32 s30, s30, 0x80
	s_addc_u32 s31, s31, 0
	s_waitcnt lgkmcnt(0)
	v_mfma_f32_16x16x32_f16 v[32:35], v[144:147], v[128:131], v[32:35]
	ds_read_b128 v[96:99], v12
	v_mfma_f32_16x16x32_f16 v[36:39], v[148:151], v[128:131], v[36:39]
	ds_read_b128 v[112:115], v13 offset:32768
	v_mfma_f32_16x16x32_f16 v[40:43], v[152:155], v[128:131], v[40:43]
	ds_read_b128 v[116:119], v13 offset:34816
	v_mfma_f32_16x16x32_f16 v[44:47], v[156:159], v[128:131], v[44:47]
	ds_read_b128 v[120:123], v13 offset:36864
	v_mfma_f32_16x16x32_f16 v[48:51], v[144:147], v[132:135], v[48:51]
	ds_read_b128 v[124:127], v13 offset:38912
	v_mfma_f32_16x16x32_f16 v[52:55], v[148:151], v[132:135], v[52:55]
	ds_read_b128 v[100:103], v12 offset:2048
	v_mfma_f32_16x16x32_f16 v[56:59], v[152:155], v[132:135], v[56:59]
	ds_read_b128 v[104:107], v12 offset:4096
	v_mfma_f32_16x16x32_f16 v[60:63], v[156:159], v[132:135], v[60:63]
	ds_read_b128 v[108:111], v12 offset:6144
	v_mfma_f32_16x16x32_f16 v[64:67], v[144:147], v[136:139], v[64:67]
	v_mfma_f32_16x16x32_f16 v[68:71], v[148:151], v[136:139], v[68:71]
	v_mfma_f32_16x16x32_f16 v[72:75], v[152:155], v[136:139], v[72:75]
	s_add_u32 m0, s14, 0x0
	s_nop 0
	global_load_lds_dwordx4 v2, s[28:29]
	v_mfma_f32_16x16x32_f16 v[76:79], v[156:159], v[136:139], v[76:79]
	v_mfma_f32_16x16x32_f16 v[80:83], v[144:147], v[140:143], v[80:83]
	s_add_u32 m0, s14, 0x2000
	s_nop 0
	global_load_lds_dwordx4 v3, s[28:29]
	v_mfma_f32_16x16x32_f16 v[84:87], v[148:151], v[140:143], v[84:87]
	v_mfma_f32_16x16x32_f16 v[88:91], v[152:155], v[140:143], v[88:91]
	s_add_u32 m0, s14, 0x4000
	s_nop 0
	global_load_lds_dwordx4 v4, s[28:29]
	v_mfma_f32_16x16x32_f16 v[92:95], v[156:159], v[140:143], v[92:95]
	s_waitcnt lgkmcnt(0)
	v_mfma_f32_16x16x32_f16 v[32:35], v[112:115], v[96:99], v[32:35]
	ds_read_b128 v[128:131], v14
	v_mfma_f32_16x16x32_f16 v[36:39], v[116:119], v[96:99], v[36:39]
	ds_read_b128 v[144:147], v15 offset:32768
	v_mfma_f32_16x16x32_f16 v[40:43], v[120:123], v[96:99], v[40:43]
	ds_read_b128 v[148:151], v15 offset:34816
	v_mfma_f32_16x16x32_f16 v[44:47], v[124:127], v[96:99], v[44:47]
	ds_read_b128 v[152:155], v15 offset:36864
	v_mfma_f32_16x16x32_f16 v[48:51], v[112:115], v[100:103], v[48:51]
	ds_read_b128 v[156:159], v15 offset:38912
	v_mfma_f32_16x16x32_f16 v[52:55], v[116:119], v[100:103], v[52:55]
	ds_read_b128 v[132:135], v14 offset:2048
	v_mfma_f32_16x16x32_f16 v[56:59], v[120:123], v[100:103], v[56:59]
	ds_read_b128 v[136:139], v14 offset:4096
	v_mfma_f32_16x16x32_f16 v[60:63], v[124:127], v[100:103], v[60:63]
	ds_read_b128 v[140:143], v14 offset:6144
	v_mfma_f32_16x16x32_f16 v[64:67], v[112:115], v[104:107], v[64:67]
	v_mfma_f32_16x16x32_f16 v[68:71], v[116:119], v[104:107], v[68:71]
	v_mfma_f32_16x16x32_f16 v[72:75], v[120:123], v[104:107], v[72:75]
	s_add_u32 m0, s14, 0x6000
	s_nop 0
	global_load_lds_dwordx4 v5, s[28:29]
	v_mfma_f32_16x16x32_f16 v[76:79], v[124:127], v[104:107], v[76:79]
	v_mfma_f32_16x16x32_f16 v[80:83], v[112:115], v[108:111], v[80:83]
	s_add_u32 m0, s14, 0x8000
	s_nop 0
	global_load_lds_dwordx4 v6, s[30:31]
	v_mfma_f32_16x16x32_f16 v[84:87], v[116:119], v[108:111], v[84:87]
	v_mfma_f32_16x16x32_f16 v[88:91], v[120:123], v[108:111], v[88:91]
	s_add_u32 m0, s14, 0xa000
	s_nop 0
	global_load_lds_dwordx4 v7, s[30:31]
	v_mfma_f32_16x16x32_f16 v[92:95], v[124:127], v[108:111], v[92:95]
	s_waitcnt vmcnt(6) lgkmcnt(0)
	s_barrier
	s_mov_b64 s[28:29], s[16:17]
	s_mov_b64 s[30:31], s[22:23]
	s_waitcnt lgkmcnt(0)
	v_mfma_f32_16x16x32_f16 v[32:35], v[144:147], v[128:131], v[32:35]
	ds_read_b128 v[96:99], v16
	v_mfma_f32_16x16x32_f16 v[36:39], v[148:151], v[128:131], v[36:39]
	ds_read_b128 v[112:115], v17 offset:32768
	v_mfma_f32_16x16x32_f16 v[40:43], v[152:155], v[128:131], v[40:43]
	ds_read_b128 v[116:119], v17 offset:34816
	v_mfma_f32_16x16x32_f16 v[44:47], v[156:159], v[128:131], v[44:47]
	ds_read_b128 v[120:123], v17 offset:36864
	v_mfma_f32_16x16x32_f16 v[48:51], v[144:147], v[132:135], v[48:51]
	ds_read_b128 v[124:127], v17 offset:38912
	v_mfma_f32_16x16x32_f16 v[52:55], v[148:151], v[132:135], v[52:55]
	ds_read_b128 v[100:103], v16 offset:2048
	v_mfma_f32_16x16x32_f16 v[56:59], v[152:155], v[132:135], v[56:59]
	ds_read_b128 v[104:107], v16 offset:4096
	v_mfma_f32_16x16x32_f16 v[60:63], v[156:159], v[132:135], v[60:63]
	ds_read_b128 v[108:111], v16 offset:6144
	v_mfma_f32_16x16x32_f16 v[64:67], v[144:147], v[136:139], v[64:67]
	v_mfma_f32_16x16x32_f16 v[68:71], v[148:151], v[136:139], v[68:71]
	v_mfma_f32_16x16x32_f16 v[72:75], v[152:155], v[136:139], v[72:75]
	s_add_u32 m0, s14, 0xc000
	s_nop 0
	global_load_lds_dwordx4 v2, s[28:29]
	v_mfma_f32_16x16x32_f16 v[76:79], v[156:159], v[136:139], v[76:79]
	v_mfma_f32_16x16x32_f16 v[80:83], v[144:147], v[140:143], v[80:83]
	s_add_u32 m0, s14, 0xe000
	s_nop 0
	global_load_lds_dwordx4 v3, s[28:29]
	v_mfma_f32_16x16x32_f16 v[84:87], v[148:151], v[140:143], v[84:87]
	v_mfma_f32_16x16x32_f16 v[88:91], v[152:155], v[140:143], v[88:91]
	s_add_u32 m0, s14, 0x10000
	s_nop 0
	global_load_lds_dwordx4 v4, s[28:29]
	v_mfma_f32_16x16x32_f16 v[92:95], v[156:159], v[140:143], v[92:95]
	s_waitcnt lgkmcnt(0)
	v_mfma_f32_16x16x32_f16 v[32:35], v[112:115], v[96:99], v[32:35]
	ds_read_b128 v[128:131], v18
	v_mfma_f32_16x16x32_f16 v[36:39], v[116:119], v[96:99], v[36:39]
	ds_read_b128 v[144:147], v19 offset:32768
	v_mfma_f32_16x16x32_f16 v[40:43], v[120:123], v[96:99], v[40:43]
	ds_read_b128 v[148:151], v19 offset:34816
	v_mfma_f32_16x16x32_f16 v[44:47], v[124:127], v[96:99], v[44:47]
	ds_read_b128 v[152:155], v19 offset:36864
	v_mfma_f32_16x16x32_f16 v[48:51], v[112:115], v[100:103], v[48:51]
	ds_read_b128 v[156:159], v19 offset:38912
	v_mfma_f32_16x16x32_f16 v[52:55], v[116:119], v[100:103], v[52:55]
	ds_read_b128 v[132:135], v18 offset:2048
	v_mfma_f32_16x16x32_f16 v[56:59], v[120:123], v[100:103], v[56:59]
	ds_read_b128 v[136:139], v18 offset:4096
	v_mfma_f32_16x16x32_f16 v[60:63], v[124:127], v[100:103], v[60:63]
	ds_read_b128 v[140:143], v18 offset:6144
	v_mfma_f32_16x16x32_f16 v[64:67], v[112:115], v[104:107], v[64:67]
	v_mfma_f32_16x16x32_f16 v[68:71], v[116:119], v[104:107], v[68:71]
	v_mfma_f32_16x16x32_f16 v[72:75], v[120:123], v[104:107], v[72:75]
	s_add_u32 m0, s14, 0x12000
	s_nop 0
	global_load_lds_dwordx4 v5, s[28:29]
	v_mfma_f32_16x16x32_f16 v[76:79], v[124:127], v[104:107], v[76:79]
	v_mfma_f32_16x16x32_f16 v[80:83], v[112:115], v[108:111], v[80:83]
	s_add_u32 m0, s14, 0x14000
	s_nop 0
	global_load_lds_dwordx4 v6, s[30:31]
	v_mfma_f32_16x16x32_f16 v[84:87], v[116:119], v[108:111], v[84:87]
	v_mfma_f32_16x16x32_f16 v[88:91], v[120:123], v[108:111], v[88:91]
	s_add_u32 m0, s14, 0x16000
	s_nop 0
	global_load_lds_dwordx4 v7, s[30:31]
	v_mfma_f32_16x16x32_f16 v[92:95], v[124:127], v[108:111], v[92:95]
	s_waitcnt vmcnt(6) lgkmcnt(0)
	s_barrier
	s_add_u32 s28, s28, 0x80
	s_addc_u32 s29, s29, 0
	s_add_u32 s30, s30, 0x80
	s_addc_u32 s31, s31, 0
	s_waitcnt lgkmcnt(0)
	v_mfma_f32_16x16x32_f16 v[32:35], v[144:147], v[128:131], v[32:35]
	ds_read_b128 v[96:99], v8
	v_mfma_f32_16x16x32_f16 v[36:39], v[148:151], v[128:131], v[36:39]
	ds_read_b128 v[112:115], v9 offset:32768
	v_mfma_f32_16x16x32_f16 v[40:43], v[152:155], v[128:131], v[40:43]
	ds_read_b128 v[116:119], v9 offset:34816
	v_mfma_f32_16x16x32_f16 v[44:47], v[156:159], v[128:131], v[44:47]
	ds_read_b128 v[120:123], v9 offset:36864
	v_mfma_f32_16x16x32_f16 v[48:51], v[144:147], v[132:135], v[48:51]
	ds_read_b128 v[124:127], v9 offset:38912
	v_mfma_f32_16x16x32_f16 v[52:55], v[148:151], v[132:135], v[52:55]
	ds_read_b128 v[100:103], v8 offset:2048
	v_mfma_f32_16x16x32_f16 v[56:59], v[152:155], v[132:135], v[56:59]
	ds_read_b128 v[104:107], v8 offset:4096
	v_mfma_f32_16x16x32_f16 v[60:63], v[156:159], v[132:135], v[60:63]
	ds_read_b128 v[108:111], v8 offset:6144
	v_mfma_f32_16x16x32_f16 v[64:67], v[144:147], v[136:139], v[64:67]
	v_mfma_f32_16x16x32_f16 v[68:71], v[148:151], v[136:139], v[68:71]
	v_mfma_f32_16x16x32_f16 v[72:75], v[152:155], v[136:139], v[72:75]
	s_add_u32 m0, s14, 0x18000
	s_nop 0
	global_load_lds_dwordx4 v2, s[28:29]
	v_mfma_f32_16x16x32_f16 v[76:79], v[156:159], v[136:139], v[76:79]
	v_mfma_f32_16x16x32_f16 v[80:83], v[144:147], v[140:143], v[80:83]
	s_add_u32 m0, s14, 0x1a000
	s_nop 0
	global_load_lds_dwordx4 v3, s[28:29]
	v_mfma_f32_16x16x32_f16 v[84:87], v[148:151], v[140:143], v[84:87]
	v_mfma_f32_16x16x32_f16 v[88:91], v[152:155], v[140:143], v[88:91]
	s_add_u32 m0, s14, 0x1c000
	s_nop 0
	global_load_lds_dwordx4 v4, s[28:29]
	v_mfma_f32_16x16x32_f16 v[92:95], v[156:159], v[140:143], v[92:95]
	s_waitcnt lgkmcnt(0)
	v_mfma_f32_16x16x32_f16 v[32:35], v[112:115], v[96:99], v[32:35]
	ds_read_b128 v[128:131], v10
	v_mfma_f32_16x16x32_f16 v[36:39], v[116:119], v[96:99], v[36:39]
	ds_read_b128 v[144:147], v11 offset:32768
	v_mfma_f32_16x16x32_f16 v[40:43], v[120:123], v[96:99], v[40:43]
	ds_read_b128 v[148:151], v11 offset:34816
	v_mfma_f32_16x16x32_f16 v[44:47], v[124:127], v[96:99], v[44:47]
	ds_read_b128 v[152:155], v11 offset:36864
	v_mfma_f32_16x16x32_f16 v[48:51], v[112:115], v[100:103], v[48:51]
	ds_read_b128 v[156:159], v11 offset:38912
	v_mfma_f32_16x16x32_f16 v[52:55], v[116:119], v[100:103], v[52:55]
	ds_read_b128 v[132:135], v10 offset:2048
	v_mfma_f32_16x16x32_f16 v[56:59], v[120:123], v[100:103], v[56:59]
	ds_read_b128 v[136:139], v10 offset:4096
	v_mfma_f32_16x16x32_f16 v[60:63], v[124:127], v[100:103], v[60:63]
	ds_read_b128 v[140:143], v10 offset:6144
	v_mfma_f32_16x16x32_f16 v[64:67], v[112:115], v[104:107], v[64:67]
	v_mfma_f32_16x16x32_f16 v[68:71], v[116:119], v[104:107], v[68:71]
	v_mfma_f32_16x16x32_f16 v[72:75], v[120:123], v[104:107], v[72:75]
	s_add_u32 m0, s14, 0x1e000
	s_nop 0
	global_load_lds_dwordx4 v5, s[28:29]
	v_mfma_f32_16x16x32_f16 v[76:79], v[124:127], v[104:107], v[76:79]
	v_mfma_f32_16x16x32_f16 v[80:83], v[112:115], v[108:111], v[80:83]
	s_add_u32 m0, s14, 0x20000
	s_nop 0
	global_load_lds_dwordx4 v6, s[30:31]
	v_mfma_f32_16x16x32_f16 v[84:87], v[116:119], v[108:111], v[84:87]
	v_mfma_f32_16x16x32_f16 v[88:91], v[120:123], v[108:111], v[88:91]
	s_add_u32 m0, s14, 0x22000
	s_nop 0
	global_load_lds_dwordx4 v7, s[30:31]
	v_mfma_f32_16x16x32_f16 v[92:95], v[124:127], v[108:111], v[92:95]
	s_waitcnt vmcnt(6) lgkmcnt(0)
	s_barrier
	s_add_u32 s28, s28, 0x80
	s_addc_u32 s29, s29, 0
	s_add_u32 s30, s30, 0x80
	s_addc_u32 s31, s31, 0
	s_waitcnt lgkmcnt(0)
	v_mfma_f32_16x16x32_f16 v[32:35], v[144:147], v[128:131], v[32:35]
	ds_read_b128 v[96:99], v12
	v_mfma_f32_16x16x32_f16 v[36:39], v[148:151], v[128:131], v[36:39]
	ds_read_b128 v[112:115], v13 offset:32768
	v_mfma_f32_16x16x32_f16 v[40:43], v[152:155], v[128:131], v[40:43]
	ds_read_b128 v[116:119], v13 offset:34816
	v_mfma_f32_16x16x32_f16 v[44:47], v[156:159], v[128:131], v[44:47]
	ds_read_b128 v[120:123], v13 offset:36864
	v_mfma_f32_16x16x32_f16 v[48:51], v[144:147], v[132:135], v[48:51]
	ds_read_b128 v[124:127], v13 offset:38912
	v_mfma_f32_16x16x32_f16 v[52:55], v[148:151], v[132:135], v[52:55]
	ds_read_b128 v[100:103], v12 offset:2048
	v_mfma_f32_16x16x32_f16 v[56:59], v[152:155], v[132:135], v[56:59]
	ds_read_b128 v[104:107], v12 offset:4096
	v_mfma_f32_16x16x32_f16 v[60:63], v[156:159], v[132:135], v[60:63]
	ds_read_b128 v[108:111], v12 offset:6144
	v_mfma_f32_16x16x32_f16 v[64:67], v[144:147], v[136:139], v[64:67]
	v_mfma_f32_16x16x32_f16 v[68:71], v[148:151], v[136:139], v[68:71]
	v_mfma_f32_16x16x32_f16 v[72:75], v[152:155], v[136:139], v[72:75]
	s_add_u32 m0, s14, 0x0
	s_nop 0
	global_load_lds_dwordx4 v2, s[28:29]
	v_mfma_f32_16x16x32_f16 v[76:79], v[156:159], v[136:139], v[76:79]
	v_mfma_f32_16x16x32_f16 v[80:83], v[144:147], v[140:143], v[80:83]
	s_add_u32 m0, s14, 0x2000
	s_nop 0
	global_load_lds_dwordx4 v3, s[28:29]
	v_mfma_f32_16x16x32_f16 v[84:87], v[148:151], v[140:143], v[84:87]
	v_mfma_f32_16x16x32_f16 v[88:91], v[152:155], v[140:143], v[88:91]
	s_add_u32 m0, s14, 0x4000
	s_nop 0
	global_load_lds_dwordx4 v4, s[28:29]
	v_mfma_f32_16x16x32_f16 v[92:95], v[156:159], v[140:143], v[92:95]
	s_nop 7
	s_nop 1
	v_pk_mul_f32 v[160:161], v[32:33], s[50:51] op_sel_hi:[1,0]
	v_pk_mul_f32 v[162:163], v[34:35], s[50:51] op_sel_hi:[1,0]
	v_pk_mul_f32 v[164:165], v[36:37], s[50:51] op_sel_hi:[1,0]
	v_pk_mul_f32 v[166:167], v[38:39], s[50:51] op_sel_hi:[1,0]
	v_pk_mul_f32 v[176:177], v[160:161], s[52:53] op_sel_hi:[1,0]
	v_pk_mul_f32 v[178:179], v[162:163], s[52:53] op_sel_hi:[1,0]
	v_pk_mul_f32 v[180:181], v[164:165], s[52:53] op_sel_hi:[1,0]
	v_pk_mul_f32 v[182:183], v[166:167], s[52:53] op_sel_hi:[1,0]
	v_exp_f32_e32 v176, v176
	v_exp_f32_e32 v177, v177
	v_exp_f32_e32 v178, v178
	v_exp_f32_e32 v179, v179
	v_exp_f32_e32 v180, v180
	v_exp_f32_e32 v181, v181
	v_exp_f32_e32 v182, v182
	v_exp_f32_e32 v183, v183
	v_pk_add_f32 v[176:177], v[176:177], 1.0 op_sel_hi:[1,0]
	v_pk_add_f32 v[178:179], v[178:179], 1.0 op_sel_hi:[1,0]
	v_pk_add_f32 v[180:181], v[180:181], 1.0 op_sel_hi:[1,0]
	v_pk_add_f32 v[182:183], v[182:183], 1.0 op_sel_hi:[1,0]
	v_rcp_f32_e32 v176, v176
	v_rcp_f32_e32 v177, v177
	v_rcp_f32_e32 v178, v178
	v_rcp_f32_e32 v179, v179
	v_rcp_f32_e32 v180, v180
	v_rcp_f32_e32 v181, v181
	v_rcp_f32_e32 v182, v182
	v_rcp_f32_e32 v183, v183
	v_pk_mul_f32 v[160:161], v[160:161], v[176:177]
	v_pk_mul_f32 v[162:163], v[162:163], v[178:179]
	v_pk_mul_f32 v[164:165], v[164:165], v[180:181]
	v_pk_mul_f32 v[166:167], v[166:167], v[182:183]
	v_cvt_pk_f16_f32 v168, v160, v161
	v_cvt_pk_f16_f32 v169, v162, v163
	v_cvt_pk_f16_f32 v170, v164, v165
	v_cvt_pk_f16_f32 v171, v166, v167
	global_store_dwordx4 v20, v[168:171], s[32:33]
	v_pk_mul_f32 v[160:161], v[40:41], s[50:51] op_sel_hi:[1,0]
	v_pk_mul_f32 v[162:163], v[42:43], s[50:51] op_sel_hi:[1,0]
	v_pk_mul_f32 v[164:165], v[44:45], s[50:51] op_sel_hi:[1,0]
	v_pk_mul_f32 v[166:167], v[46:47], s[50:51] op_sel_hi:[1,0]
	v_pk_mul_f32 v[176:177], v[160:161], s[52:53] op_sel_hi:[1,0]
	v_pk_mul_f32 v[178:179], v[162:163], s[52:53] op_sel_hi:[1,0]
	v_pk_mul_f32 v[180:181], v[164:165], s[52:53] op_sel_hi:[1,0]
	v_pk_mul_f32 v[182:183], v[166:167], s[52:53] op_sel_hi:[1,0]
	v_exp_f32_e32 v176, v176
	v_exp_f32_e32 v177, v177
	v_exp_f32_e32 v178, v178
	v_exp_f32_e32 v179, v179
	v_exp_f32_e32 v180, v180
	v_exp_f32_e32 v181, v181
	v_exp_f32_e32 v182, v182
	v_exp_f32_e32 v183, v183
	v_pk_add_f32 v[176:177], v[176:177], 1.0 op_sel_hi:[1,0]
	v_pk_add_f32 v[178:179], v[178:179], 1.0 op_sel_hi:[1,0]
	v_pk_add_f32 v[180:181], v[180:181], 1.0 op_sel_hi:[1,0]
	v_pk_add_f32 v[182:183], v[182:183], 1.0 op_sel_hi:[1,0]
	v_rcp_f32_e32 v176, v176
	v_rcp_f32_e32 v177, v177
	v_rcp_f32_e32 v178, v178
	v_rcp_f32_e32 v179, v179
	v_rcp_f32_e32 v180, v180
	v_rcp_f32_e32 v181, v181
	v_rcp_f32_e32 v182, v182
	v_rcp_f32_e32 v183, v183
	v_pk_mul_f32 v[160:161], v[160:161], v[176:177]
	v_pk_mul_f32 v[162:163], v[162:163], v[178:179]
	v_pk_mul_f32 v[164:165], v[164:165], v[180:181]
	v_pk_mul_f32 v[166:167], v[166:167], v[182:183]
	v_cvt_pk_f16_f32 v172, v160, v161
	v_cvt_pk_f16_f32 v173, v162, v163
	v_cvt_pk_f16_f32 v174, v164, v165
	v_cvt_pk_f16_f32 v175, v166, v167
	global_store_dwordx4 v20, v[172:175], s[32:33] offset:64
	v_pk_mul_f32 v[160:161], v[48:49], s[50:51] op_sel_hi:[1,0]
	v_pk_mul_f32 v[162:163], v[50:51], s[50:51] op_sel_hi:[1,0]
	v_pk_mul_f32 v[164:165], v[52:53], s[50:51] op_sel_hi:[1,0]
	v_pk_mul_f32 v[166:167], v[54:55], s[50:51] op_sel_hi:[1,0]
	v_pk_mul_f32 v[176:177], v[160:161], s[52:53] op_sel_hi:[1,0]
	v_pk_mul_f32 v[178:179], v[162:163], s[52:53] op_sel_hi:[1,0]
	v_pk_mul_f32 v[180:181], v[164:165], s[52:53] op_sel_hi:[1,0]
	v_pk_mul_f32 v[182:183], v[166:167], s[52:53] op_sel_hi:[1,0]
	v_exp_f32_e32 v176, v176
	v_exp_f32_e32 v177, v177
	v_exp_f32_e32 v178, v178
	v_exp_f32_e32 v179, v179
	v_exp_f32_e32 v180, v180
	v_exp_f32_e32 v181, v181
	v_exp_f32_e32 v182, v182
	v_exp_f32_e32 v183, v183
	v_pk_add_f32 v[176:177], v[176:177], 1.0 op_sel_hi:[1,0]
	v_pk_add_f32 v[178:179], v[178:179], 1.0 op_sel_hi:[1,0]
	v_pk_add_f32 v[180:181], v[180:181], 1.0 op_sel_hi:[1,0]
	v_pk_add_f32 v[182:183], v[182:183], 1.0 op_sel_hi:[1,0]
	v_rcp_f32_e32 v176, v176
	v_rcp_f32_e32 v177, v177
	v_rcp_f32_e32 v178, v178
	v_rcp_f32_e32 v179, v179
	v_rcp_f32_e32 v180, v180
	v_rcp_f32_e32 v181, v181
	v_rcp_f32_e32 v182, v182
	v_rcp_f32_e32 v183, v183
	v_pk_mul_f32 v[160:161], v[160:161], v[176:177]
	v_pk_mul_f32 v[162:163], v[162:163], v[178:179]
	v_pk_mul_f32 v[164:165], v[164:165], v[180:181]
	v_pk_mul_f32 v[166:167], v[166:167], v[182:183]
	v_cvt_pk_f16_f32 v168, v160, v161
	v_cvt_pk_f16_f32 v169, v162, v163
	v_cvt_pk_f16_f32 v170, v164, v165
	v_cvt_pk_f16_f32 v171, v166, v167
	global_store_dwordx4 v21, v[168:171], s[32:33]
	v_pk_mul_f32 v[160:161], v[56:57], s[50:51] op_sel_hi:[1,0]
	v_pk_mul_f32 v[162:163], v[58:59], s[50:51] op_sel_hi:[1,0]
	v_pk_mul_f32 v[164:165], v[60:61], s[50:51] op_sel_hi:[1,0]
	v_pk_mul_f32 v[166:167], v[62:63], s[50:51] op_sel_hi:[1,0]
	v_pk_mul_f32 v[176:177], v[160:161], s[52:53] op_sel_hi:[1,0]
	v_pk_mul_f32 v[178:179], v[162:163], s[52:53] op_sel_hi:[1,0]
	v_pk_mul_f32 v[180:181], v[164:165], s[52:53] op_sel_hi:[1,0]
	v_pk_mul_f32 v[182:183], v[166:167], s[52:53] op_sel_hi:[1,0]
	v_exp_f32_e32 v176, v176
	v_exp_f32_e32 v177, v177
	v_exp_f32_e32 v178, v178
	v_exp_f32_e32 v179, v179
	v_exp_f32_e32 v180, v180
	v_exp_f32_e32 v181, v181
	v_exp_f32_e32 v182, v182
	v_exp_f32_e32 v183, v183
	v_pk_add_f32 v[176:177], v[176:177], 1.0 op_sel_hi:[1,0]
	v_pk_add_f32 v[178:179], v[178:179], 1.0 op_sel_hi:[1,0]
	v_pk_add_f32 v[180:181], v[180:181], 1.0 op_sel_hi:[1,0]
	v_pk_add_f32 v[182:183], v[182:183], 1.0 op_sel_hi:[1,0]
	v_rcp_f32_e32 v176, v176
	v_rcp_f32_e32 v177, v177
	v_rcp_f32_e32 v178, v178
	v_rcp_f32_e32 v179, v179
	v_rcp_f32_e32 v180, v180
	v_rcp_f32_e32 v181, v181
	v_rcp_f32_e32 v182, v182
	v_rcp_f32_e32 v183, v183
	v_pk_mul_f32 v[160:161], v[160:161], v[176:177]
	v_pk_mul_f32 v[162:163], v[162:163], v[178:179]
	v_pk_mul_f32 v[164:165], v[164:165], v[180:181]
	v_pk_mul_f32 v[166:167], v[166:167], v[182:183]
	v_cvt_pk_f16_f32 v172, v160, v161
	v_cvt_pk_f16_f32 v173, v162, v163
	v_cvt_pk_f16_f32 v174, v164, v165
	v_cvt_pk_f16_f32 v175, v166, v167
	global_store_dwordx4 v21, v[172:175], s[32:33] offset:64
	v_pk_mul_f32 v[160:161], v[64:65], s[50:51] op_sel_hi:[1,0]
	v_pk_mul_f32 v[162:163], v[66:67], s[50:51] op_sel_hi:[1,0]
	v_pk_mul_f32 v[164:165], v[68:69], s[50:51] op_sel_hi:[1,0]
	v_pk_mul_f32 v[166:167], v[70:71], s[50:51] op_sel_hi:[1,0]
	v_pk_mul_f32 v[176:177], v[160:161], s[52:53] op_sel_hi:[1,0]
	v_pk_mul_f32 v[178:179], v[162:163], s[52:53] op_sel_hi:[1,0]
	v_pk_mul_f32 v[180:181], v[164:165], s[52:53] op_sel_hi:[1,0]
	v_pk_mul_f32 v[182:183], v[166:167], s[52:53] op_sel_hi:[1,0]
	v_exp_f32_e32 v176, v176
	v_exp_f32_e32 v177, v177
	v_exp_f32_e32 v178, v178
	v_exp_f32_e32 v179, v179
	v_exp_f32_e32 v180, v180
	v_exp_f32_e32 v181, v181
	v_exp_f32_e32 v182, v182
	v_exp_f32_e32 v183, v183
	v_pk_add_f32 v[176:177], v[176:177], 1.0 op_sel_hi:[1,0]
	v_pk_add_f32 v[178:179], v[178:179], 1.0 op_sel_hi:[1,0]
	v_pk_add_f32 v[180:181], v[180:181], 1.0 op_sel_hi:[1,0]
	v_pk_add_f32 v[182:183], v[182:183], 1.0 op_sel_hi:[1,0]
	v_rcp_f32_e32 v176, v176
	v_rcp_f32_e32 v177, v177
	v_rcp_f32_e32 v178, v178
	v_rcp_f32_e32 v179, v179
	v_rcp_f32_e32 v180, v180
	v_rcp_f32_e32 v181, v181
	v_rcp_f32_e32 v182, v182
	v_rcp_f32_e32 v183, v183
	v_pk_mul_f32 v[160:161], v[160:161], v[176:177]
	v_pk_mul_f32 v[162:163], v[162:163], v[178:179]
	v_pk_mul_f32 v[164:165], v[164:165], v[180:181]
	v_pk_mul_f32 v[166:167], v[166:167], v[182:183]
	v_cvt_pk_f16_f32 v168, v160, v161
	v_cvt_pk_f16_f32 v169, v162, v163
	v_cvt_pk_f16_f32 v170, v164, v165
	v_cvt_pk_f16_f32 v171, v166, v167
	global_store_dwordx4 v22, v[168:171], s[32:33]
	v_pk_mul_f32 v[160:161], v[72:73], s[50:51] op_sel_hi:[1,0]
	v_pk_mul_f32 v[162:163], v[74:75], s[50:51] op_sel_hi:[1,0]
	v_pk_mul_f32 v[164:165], v[76:77], s[50:51] op_sel_hi:[1,0]
	v_pk_mul_f32 v[166:167], v[78:79], s[50:51] op_sel_hi:[1,0]
	v_pk_mul_f32 v[176:177], v[160:161], s[52:53] op_sel_hi:[1,0]
	v_pk_mul_f32 v[178:179], v[162:163], s[52:53] op_sel_hi:[1,0]
	v_pk_mul_f32 v[180:181], v[164:165], s[52:53] op_sel_hi:[1,0]
	v_pk_mul_f32 v[182:183], v[166:167], s[52:53] op_sel_hi:[1,0]
	v_exp_f32_e32 v176, v176
	v_exp_f32_e32 v177, v177
	v_exp_f32_e32 v178, v178
	v_exp_f32_e32 v179, v179
	v_exp_f32_e32 v180, v180
	v_exp_f32_e32 v181, v181
	v_exp_f32_e32 v182, v182
	v_exp_f32_e32 v183, v183
	v_pk_add_f32 v[176:177], v[176:177], 1.0 op_sel_hi:[1,0]
	v_pk_add_f32 v[178:179], v[178:179], 1.0 op_sel_hi:[1,0]
	v_pk_add_f32 v[180:181], v[180:181], 1.0 op_sel_hi:[1,0]
	v_pk_add_f32 v[182:183], v[182:183], 1.0 op_sel_hi:[1,0]
	v_rcp_f32_e32 v176, v176
	v_rcp_f32_e32 v177, v177
	v_rcp_f32_e32 v178, v178
	v_rcp_f32_e32 v179, v179
	v_rcp_f32_e32 v180, v180
	v_rcp_f32_e32 v181, v181
	v_rcp_f32_e32 v182, v182
	v_rcp_f32_e32 v183, v183
	v_pk_mul_f32 v[160:161], v[160:161], v[176:177]
	v_pk_mul_f32 v[162:163], v[162:163], v[178:179]
	v_pk_mul_f32 v[164:165], v[164:165], v[180:181]
	v_pk_mul_f32 v[166:167], v[166:167], v[182:183]
	v_cvt_pk_f16_f32 v172, v160, v161
	v_cvt_pk_f16_f32 v173, v162, v163
	v_cvt_pk_f16_f32 v174, v164, v165
	v_cvt_pk_f16_f32 v175, v166, v167
	global_store_dwordx4 v22, v[172:175], s[32:33] offset:64
	v_pk_mul_f32 v[160:161], v[80:81], s[50:51] op_sel_hi:[1,0]
	v_pk_mul_f32 v[162:163], v[82:83], s[50:51] op_sel_hi:[1,0]
	v_pk_mul_f32 v[164:165], v[84:85], s[50:51] op_sel_hi:[1,0]
	v_pk_mul_f32 v[166:167], v[86:87], s[50:51] op_sel_hi:[1,0]
	v_pk_mul_f32 v[176:177], v[160:161], s[52:53] op_sel_hi:[1,0]
	v_pk_mul_f32 v[178:179], v[162:163], s[52:53] op_sel_hi:[1,0]
	v_pk_mul_f32 v[180:181], v[164:165], s[52:53] op_sel_hi:[1,0]
	v_pk_mul_f32 v[182:183], v[166:167], s[52:53] op_sel_hi:[1,0]
	v_exp_f32_e32 v176, v176
	v_exp_f32_e32 v177, v177
	v_exp_f32_e32 v178, v178
	v_exp_f32_e32 v179, v179
	v_exp_f32_e32 v180, v180
	v_exp_f32_e32 v181, v181
	v_exp_f32_e32 v182, v182
	v_exp_f32_e32 v183, v183
	v_pk_add_f32 v[176:177], v[176:177], 1.0 op_sel_hi:[1,0]
	v_pk_add_f32 v[178:179], v[178:179], 1.0 op_sel_hi:[1,0]
	v_pk_add_f32 v[180:181], v[180:181], 1.0 op_sel_hi:[1,0]
	v_pk_add_f32 v[182:183], v[182:183], 1.0 op_sel_hi:[1,0]
	v_rcp_f32_e32 v176, v176
	v_rcp_f32_e32 v177, v177
	v_rcp_f32_e32 v178, v178
	v_rcp_f32_e32 v179, v179
	v_rcp_f32_e32 v180, v180
	v_rcp_f32_e32 v181, v181
	v_rcp_f32_e32 v182, v182
	v_rcp_f32_e32 v183, v183
	v_pk_mul_f32 v[160:161], v[160:161], v[176:177]
	v_pk_mul_f32 v[162:163], v[162:163], v[178:179]
	v_pk_mul_f32 v[164:165], v[164:165], v[180:181]
	v_pk_mul_f32 v[166:167], v[166:167], v[182:183]
	v_cvt_pk_f16_f32 v168, v160, v161
	v_cvt_pk_f16_f32 v169, v162, v163
	v_cvt_pk_f16_f32 v170, v164, v165
	v_cvt_pk_f16_f32 v171, v166, v167
	global_store_dwordx4 v23, v[168:171], s[32:33]
	v_pk_mul_f32 v[160:161], v[88:89], s[50:51] op_sel_hi:[1,0]
	v_pk_mul_f32 v[162:163], v[90:91], s[50:51] op_sel_hi:[1,0]
	v_pk_mul_f32 v[164:165], v[92:93], s[50:51] op_sel_hi:[1,0]
	v_pk_mul_f32 v[166:167], v[94:95], s[50:51] op_sel_hi:[1,0]
	v_pk_mul_f32 v[176:177], v[160:161], s[52:53] op_sel_hi:[1,0]
	v_pk_mul_f32 v[178:179], v[162:163], s[52:53] op_sel_hi:[1,0]
	v_pk_mul_f32 v[180:181], v[164:165], s[52:53] op_sel_hi:[1,0]
	v_pk_mul_f32 v[182:183], v[166:167], s[52:53] op_sel_hi:[1,0]
	v_exp_f32_e32 v176, v176
	v_exp_f32_e32 v177, v177
	v_exp_f32_e32 v178, v178
	v_exp_f32_e32 v179, v179
	v_exp_f32_e32 v180, v180
	v_exp_f32_e32 v181, v181
	v_exp_f32_e32 v182, v182
	v_exp_f32_e32 v183, v183
	v_pk_add_f32 v[176:177], v[176:177], 1.0 op_sel_hi:[1,0]
	v_pk_add_f32 v[178:179], v[178:179], 1.0 op_sel_hi:[1,0]
	v_pk_add_f32 v[180:181], v[180:181], 1.0 op_sel_hi:[1,0]
	v_pk_add_f32 v[182:183], v[182:183], 1.0 op_sel_hi:[1,0]
	v_rcp_f32_e32 v176, v176
	v_rcp_f32_e32 v177, v177
	v_rcp_f32_e32 v178, v178
	v_rcp_f32_e32 v179, v179
	v_rcp_f32_e32 v180, v180
	v_rcp_f32_e32 v181, v181
	v_rcp_f32_e32 v182, v182
	v_rcp_f32_e32 v183, v183
	v_pk_mul_f32 v[160:161], v[160:161], v[176:177]
	v_pk_mul_f32 v[162:163], v[162:163], v[178:179]
	v_pk_mul_f32 v[164:165], v[164:165], v[180:181]
	v_pk_mul_f32 v[166:167], v[166:167], v[182:183]
	v_cvt_pk_f16_f32 v172, v160, v161
	v_cvt_pk_f16_f32 v173, v162, v163
	v_cvt_pk_f16_f32 v174, v164, v165
	v_cvt_pk_f16_f32 v175, v166, v167
	global_store_dwordx4 v23, v[172:175], s[32:33] offset:64
	s_waitcnt lgkmcnt(0)
	v_mfma_f32_16x16x32_f16 v[32:35], v[112:115], v[96:99], 0
	ds_read_b128 v[128:131], v14
	v_mfma_f32_16x16x32_f16 v[36:39], v[116:119], v[96:99], 0
	ds_read_b128 v[144:147], v15 offset:32768
	v_mfma_f32_16x16x32_f16 v[40:43], v[120:123], v[96:99], 0
	ds_read_b128 v[148:151], v15 offset:34816
	v_mfma_f32_16x16x32_f16 v[44:47], v[124:127], v[96:99], 0
	ds_read_b128 v[152:155], v15 offset:36864
	v_mfma_f32_16x16x32_f16 v[48:51], v[112:115], v[100:103], 0
	ds_read_b128 v[156:159], v15 offset:38912
	v_mfma_f32_16x16x32_f16 v[52:55], v[116:119], v[100:103], 0
	ds_read_b128 v[132:135], v14 offset:2048
	v_mfma_f32_16x16x32_f16 v[56:59], v[120:123], v[100:103], 0
	ds_read_b128 v[136:139], v14 offset:4096
	v_mfma_f32_16x16x32_f16 v[60:63], v[124:127], v[100:103], 0
	ds_read_b128 v[140:143], v14 offset:6144
	v_mfma_f32_16x16x32_f16 v[64:67], v[112:115], v[104:107], 0
	v_mfma_f32_16x16x32_f16 v[68:71], v[116:119], v[104:107], 0
	v_mfma_f32_16x16x32_f16 v[72:75], v[120:123], v[104:107], 0
	s_add_u32 m0, s14, 0x6000
	s_nop 0
	global_load_lds_dwordx4 v5, s[28:29]
	v_mfma_f32_16x16x32_f16 v[76:79], v[124:127], v[104:107], 0
	v_mfma_f32_16x16x32_f16 v[80:83], v[112:115], v[108:111], 0
	s_add_u32 m0, s14, 0x8000
	s_nop 0
	global_load_lds_dwordx4 v6, s[30:31]
	v_mfma_f32_16x16x32_f16 v[84:87], v[116:119], v[108:111], 0
	v_mfma_f32_16x16x32_f16 v[88:91], v[120:123], v[108:111], 0
	s_add_u32 m0, s14, 0xa000
	s_nop 0
	global_load_lds_dwordx4 v7, s[30:31]
	v_mfma_f32_16x16x32_f16 v[92:95], v[124:127], v[108:111], 0
	s_waitcnt vmcnt(14) lgkmcnt(0)
	s_barrier
	s_add_u32 s28, s28, 0x80
	s_addc_u32 s29, s29, 0
	s_add_u32 s30, s30, 0x80
	s_addc_u32 s31, s31, 0
	s_waitcnt lgkmcnt(0)
	v_mfma_f32_16x16x32_f16 v[32:35], v[144:147], v[128:131], v[32:35]
	ds_read_b128 v[96:99], v16
	v_mfma_f32_16x16x32_f16 v[36:39], v[148:151], v[128:131], v[36:39]
	ds_read_b128 v[112:115], v17 offset:32768
	v_mfma_f32_16x16x32_f16 v[40:43], v[152:155], v[128:131], v[40:43]
	ds_read_b128 v[116:119], v17 offset:34816
	v_mfma_f32_16x16x32_f16 v[44:47], v[156:159], v[128:131], v[44:47]
	ds_read_b128 v[120:123], v17 offset:36864
	v_mfma_f32_16x16x32_f16 v[48:51], v[144:147], v[132:135], v[48:51]
	ds_read_b128 v[124:127], v17 offset:38912
	v_mfma_f32_16x16x32_f16 v[52:55], v[148:151], v[132:135], v[52:55]
	ds_read_b128 v[100:103], v16 offset:2048
	v_mfma_f32_16x16x32_f16 v[56:59], v[152:155], v[132:135], v[56:59]
	ds_read_b128 v[104:107], v16 offset:4096
	v_mfma_f32_16x16x32_f16 v[60:63], v[156:159], v[132:135], v[60:63]
	ds_read_b128 v[108:111], v16 offset:6144
	v_mfma_f32_16x16x32_f16 v[64:67], v[144:147], v[136:139], v[64:67]
	v_mfma_f32_16x16x32_f16 v[68:71], v[148:151], v[136:139], v[68:71]
	v_mfma_f32_16x16x32_f16 v[72:75], v[152:155], v[136:139], v[72:75]
	s_add_u32 m0, s14, 0xc000
	s_nop 0
	global_load_lds_dwordx4 v2, s[28:29]
	v_mfma_f32_16x16x32_f16 v[76:79], v[156:159], v[136:139], v[76:79]
	v_mfma_f32_16x16x32_f16 v[80:83], v[144:147], v[140:143], v[80:83]
	s_add_u32 m0, s14, 0xe000
	s_nop 0
	global_load_lds_dwordx4 v3, s[28:29]
	v_mfma_f32_16x16x32_f16 v[84:87], v[148:151], v[140:143], v[84:87]
	v_mfma_f32_16x16x32_f16 v[88:91], v[152:155], v[140:143], v[88:91]
	s_add_u32 m0, s14, 0x10000
	s_nop 0
	global_load_lds_dwordx4 v4, s[28:29]
	v_mfma_f32_16x16x32_f16 v[92:95], v[156:159], v[140:143], v[92:95]
	s_waitcnt lgkmcnt(0)
	v_mfma_f32_16x16x32_f16 v[32:35], v[112:115], v[96:99], v[32:35]
	ds_read_b128 v[128:131], v18
	v_mfma_f32_16x16x32_f16 v[36:39], v[116:119], v[96:99], v[36:39]
	ds_read_b128 v[144:147], v19 offset:32768
	v_mfma_f32_16x16x32_f16 v[40:43], v[120:123], v[96:99], v[40:43]
	ds_read_b128 v[148:151], v19 offset:34816
	v_mfma_f32_16x16x32_f16 v[44:47], v[124:127], v[96:99], v[44:47]
	ds_read_b128 v[152:155], v19 offset:36864
	v_mfma_f32_16x16x32_f16 v[48:51], v[112:115], v[100:103], v[48:51]
	ds_read_b128 v[156:159], v19 offset:38912
	v_mfma_f32_16x16x32_f16 v[52:55], v[116:119], v[100:103], v[52:55]
	ds_read_b128 v[132:135], v18 offset:2048
	v_mfma_f32_16x16x32_f16 v[56:59], v[120:123], v[100:103], v[56:59]
	ds_read_b128 v[136:139], v18 offset:4096
	v_mfma_f32_16x16x32_f16 v[60:63], v[124:127], v[100:103], v[60:63]
	ds_read_b128 v[140:143], v18 offset:6144
	v_mfma_f32_16x16x32_f16 v[64:67], v[112:115], v[104:107], v[64:67]
	v_mfma_f32_16x16x32_f16 v[68:71], v[116:119], v[104:107], v[68:71]
	v_mfma_f32_16x16x32_f16 v[72:75], v[120:123], v[104:107], v[72:75]
	s_add_u32 m0, s14, 0x12000
	s_nop 0
	global_load_lds_dwordx4 v5, s[28:29]
	v_mfma_f32_16x16x32_f16 v[76:79], v[124:127], v[104:107], v[76:79]
	v_mfma_f32_16x16x32_f16 v[80:83], v[112:115], v[108:111], v[80:83]
	s_add_u32 m0, s14, 0x14000
	s_nop 0
	global_load_lds_dwordx4 v6, s[30:31]
	v_mfma_f32_16x16x32_f16 v[84:87], v[116:119], v[108:111], v[84:87]
	v_mfma_f32_16x16x32_f16 v[88:91], v[120:123], v[108:111], v[88:91]
	s_add_u32 m0, s14, 0x16000
	s_nop 0
	global_load_lds_dwordx4 v7, s[30:31]
	v_mfma_f32_16x16x32_f16 v[92:95], v[124:127], v[108:111], v[92:95]
	s_waitcnt vmcnt(6) lgkmcnt(0)
	s_barrier
	s_add_u32 s28, s28, 0x80
	s_addc_u32 s29, s29, 0
	s_add_u32 s30, s30, 0x80
	s_addc_u32 s31, s31, 0
	s_waitcnt lgkmcnt(0)
	v_mfma_f32_16x16x32_f16 v[32:35], v[144:147], v[128:131], v[32:35]
	ds_read_b128 v[96:99], v8
	v_mfma_f32_16x16x32_f16 v[36:39], v[148:151], v[128:131], v[36:39]
	ds_read_b128 v[112:115], v9 offset:32768
	v_mfma_f32_16x16x32_f16 v[40:43], v[152:155], v[128:131], v[40:43]
	ds_read_b128 v[116:119], v9 offset:34816
	v_mfma_f32_16x16x32_f16 v[44:47], v[156:159], v[128:131], v[44:47]
	ds_read_b128 v[120:123], v9 offset:36864
	v_mfma_f32_16x16x32_f16 v[48:51], v[144:147], v[132:135], v[48:51]
	ds_read_b128 v[124:127], v9 offset:38912
	v_mfma_f32_16x16x32_f16 v[52:55], v[148:151], v[132:135], v[52:55]
	ds_read_b128 v[100:103], v8 offset:2048
	v_mfma_f32_16x16x32_f16 v[56:59], v[152:155], v[132:135], v[56:59]
	ds_read_b128 v[104:107], v8 offset:4096
	v_mfma_f32_16x16x32_f16 v[60:63], v[156:159], v[132:135], v[60:63]
	ds_read_b128 v[108:111], v8 offset:6144
	v_mfma_f32_16x16x32_f16 v[64:67], v[144:147], v[136:139], v[64:67]
	v_mfma_f32_16x16x32_f16 v[68:71], v[148:151], v[136:139], v[68:71]
	v_mfma_f32_16x16x32_f16 v[72:75], v[152:155], v[136:139], v[72:75]
	s_add_u32 m0, s14, 0x18000
	s_nop 0
	global_load_lds_dwordx4 v2, s[28:29]
	v_mfma_f32_16x16x32_f16 v[76:79], v[156:159], v[136:139], v[76:79]
	v_mfma_f32_16x16x32_f16 v[80:83], v[144:147], v[140:143], v[80:83]
	s_add_u32 m0, s14, 0x1a000
	s_nop 0
	global_load_lds_dwordx4 v3, s[28:29]
	v_mfma_f32_16x16x32_f16 v[84:87], v[148:151], v[140:143], v[84:87]
	v_mfma_f32_16x16x32_f16 v[88:91], v[152:155], v[140:143], v[88:91]
	s_add_u32 m0, s14, 0x1c000
	s_nop 0
	global_load_lds_dwordx4 v4, s[28:29]
	v_mfma_f32_16x16x32_f16 v[92:95], v[156:159], v[140:143], v[92:95]
	s_waitcnt lgkmcnt(0)
	v_mfma_f32_16x16x32_f16 v[32:35], v[112:115], v[96:99], v[32:35]
	ds_read_b128 v[128:131], v10
	v_mfma_f32_16x16x32_f16 v[36:39], v[116:119], v[96:99], v[36:39]
	ds_read_b128 v[144:147], v11 offset:32768
	v_mfma_f32_16x16x32_f16 v[40:43], v[120:123], v[96:99], v[40:43]
	ds_read_b128 v[148:151], v11 offset:34816
	v_mfma_f32_16x16x32_f16 v[44:47], v[124:127], v[96:99], v[44:47]
	ds_read_b128 v[152:155], v11 offset:36864
	v_mfma_f32_16x16x32_f16 v[48:51], v[112:115], v[100:103], v[48:51]
	ds_read_b128 v[156:159], v11 offset:38912
	v_mfma_f32_16x16x32_f16 v[52:55], v[116:119], v[100:103], v[52:55]
	ds_read_b128 v[132:135], v10 offset:2048
	v_mfma_f32_16x16x32_f16 v[56:59], v[120:123], v[100:103], v[56:59]
	ds_read_b128 v[136:139], v10 offset:4096
	v_mfma_f32_16x16x32_f16 v[60:63], v[124:127], v[100:103], v[60:63]
	ds_read_b128 v[140:143], v10 offset:6144
	v_mfma_f32_16x16x32_f16 v[64:67], v[112:115], v[104:107], v[64:67]
	v_mfma_f32_16x16x32_f16 v[68:71], v[116:119], v[104:107], v[68:71]
	v_mfma_f32_16x16x32_f16 v[72:75], v[120:123], v[104:107], v[72:75]
	s_add_u32 m0, s14, 0x1e000
	s_nop 0
	global_load_lds_dwordx4 v5, s[28:29]
	v_mfma_f32_16x16x32_f16 v[76:79], v[124:127], v[104:107], v[76:79]
	v_mfma_f32_16x16x32_f16 v[80:83], v[112:115], v[108:111], v[80:83]
	s_add_u32 m0, s14, 0x20000
	s_nop 0
	global_load_lds_dwordx4 v6, s[30:31]
	v_mfma_f32_16x16x32_f16 v[84:87], v[116:119], v[108:111], v[84:87]
	v_mfma_f32_16x16x32_f16 v[88:91], v[120:123], v[108:111], v[88:91]
	s_add_u32 m0, s14, 0x22000
	s_nop 0
	global_load_lds_dwordx4 v7, s[30:31]
	v_mfma_f32_16x16x32_f16 v[92:95], v[124:127], v[108:111], v[92:95]
	s_waitcnt vmcnt(6) lgkmcnt(0)
	s_barrier
	s_add_u32 s28, s28, 0x80
	s_addc_u32 s29, s29, 0
	s_add_u32 s30, s30, 0x80
	s_addc_u32 s31, s31, 0
	s_waitcnt lgkmcnt(0)
	v_mfma_f32_16x16x32_f16 v[32:35], v[144:147], v[128:131], v[32:35]
	ds_read_b128 v[96:99], v12
	v_mfma_f32_16x16x32_f16 v[36:39], v[148:151], v[128:131], v[36:39]
	ds_read_b128 v[112:115], v13 offset:32768
	v_mfma_f32_16x16x32_f16 v[40:43], v[152:155], v[128:131], v[40:43]
	ds_read_b128 v[116:119], v13 offset:34816
	v_mfma_f32_16x16x32_f16 v[44:47], v[156:159], v[128:131], v[44:47]
	ds_read_b128 v[120:123], v13 offset:36864
	v_mfma_f32_16x16x32_f16 v[48:51], v[144:147], v[132:135], v[48:51]
	ds_read_b128 v[124:127], v13 offset:38912
	v_mfma_f32_16x16x32_f16 v[52:55], v[148:151], v[132:135], v[52:55]
	ds_read_b128 v[100:103], v12 offset:2048
	v_mfma_f32_16x16x32_f16 v[56:59], v[152:155], v[132:135], v[56:59]
	ds_read_b128 v[104:107], v12 offset:4096
	v_mfma_f32_16x16x32_f16 v[60:63], v[156:159], v[132:135], v[60:63]
	ds_read_b128 v[108:111], v12 offset:6144
	v_mfma_f32_16x16x32_f16 v[64:67], v[144:147], v[136:139], v[64:67]
	v_mfma_f32_16x16x32_f16 v[68:71], v[148:151], v[136:139], v[68:71]
	v_mfma_f32_16x16x32_f16 v[72:75], v[152:155], v[136:139], v[72:75]
	s_add_u32 m0, s14, 0x0
	s_nop 0
	global_load_lds_dwordx4 v2, s[28:29]
	v_mfma_f32_16x16x32_f16 v[76:79], v[156:159], v[136:139], v[76:79]
	v_mfma_f32_16x16x32_f16 v[80:83], v[144:147], v[140:143], v[80:83]
	s_add_u32 m0, s14, 0x2000
	s_nop 0
	global_load_lds_dwordx4 v3, s[28:29]
	v_mfma_f32_16x16x32_f16 v[84:87], v[148:151], v[140:143], v[84:87]
	v_mfma_f32_16x16x32_f16 v[88:91], v[152:155], v[140:143], v[88:91]
	s_add_u32 m0, s14, 0x4000
	s_nop 0
	global_load_lds_dwordx4 v4, s[28:29]
	v_mfma_f32_16x16x32_f16 v[92:95], v[156:159], v[140:143], v[92:95]
	s_waitcnt lgkmcnt(0)
	v_mfma_f32_16x16x32_f16 v[32:35], v[112:115], v[96:99], v[32:35]
	ds_read_b128 v[128:131], v14
	v_mfma_f32_16x16x32_f16 v[36:39], v[116:119], v[96:99], v[36:39]
	ds_read_b128 v[144:147], v15 offset:32768
	v_mfma_f32_16x16x32_f16 v[40:43], v[120:123], v[96:99], v[40:43]
	ds_read_b128 v[148:151], v15 offset:34816
	v_mfma_f32_16x16x32_f16 v[44:47], v[124:127], v[96:99], v[44:47]
	ds_read_b128 v[152:155], v15 offset:36864
	v_mfma_f32_16x16x32_f16 v[48:51], v[112:115], v[100:103], v[48:51]
	ds_read_b128 v[156:159], v15 offset:38912
	v_mfma_f32_16x16x32_f16 v[52:55], v[116:119], v[100:103], v[52:55]
	ds_read_b128 v[132:135], v14 offset:2048
	v_mfma_f32_16x16x32_f16 v[56:59], v[120:123], v[100:103], v[56:59]
	ds_read_b128 v[136:139], v14 offset:4096
	v_mfma_f32_16x16x32_f16 v[60:63], v[124:127], v[100:103], v[60:63]
	ds_read_b128 v[140:143], v14 offset:6144
	v_mfma_f32_16x16x32_f16 v[64:67], v[112:115], v[104:107], v[64:67]
	v_mfma_f32_16x16x32_f16 v[68:71], v[116:119], v[104:107], v[68:71]
	v_mfma_f32_16x16x32_f16 v[72:75], v[120:123], v[104:107], v[72:75]
	s_add_u32 m0, s14, 0x6000
	s_nop 0
	global_load_lds_dwordx4 v5, s[28:29]
	v_mfma_f32_16x16x32_f16 v[76:79], v[124:127], v[104:107], v[76:79]
	v_mfma_f32_16x16x32_f16 v[80:83], v[112:115], v[108:111], v[80:83]
	s_add_u32 m0, s14, 0x8000
	s_nop 0
	global_load_lds_dwordx4 v6, s[30:31]
	v_mfma_f32_16x16x32_f16 v[84:87], v[116:119], v[108:111], v[84:87]
	v_mfma_f32_16x16x32_f16 v[88:91], v[120:123], v[108:111], v[88:91]
	s_add_u32 m0, s14, 0xa000
	s_nop 0
	global_load_lds_dwordx4 v7, s[30:31]
	v_mfma_f32_16x16x32_f16 v[92:95], v[124:127], v[108:111], v[92:95]
	s_waitcnt vmcnt(6) lgkmcnt(0)
	s_barrier
	s_add_u32 s28, s28, 0x80
	s_addc_u32 s29, s29, 0
	s_add_u32 s30, s30, 0x80
	s_addc_u32 s31, s31, 0
	s_waitcnt lgkmcnt(0)
	v_mfma_f32_16x16x32_f16 v[32:35], v[144:147], v[128:131], v[32:35]
	ds_read_b128 v[96:99], v16
	v_mfma_f32_16x16x32_f16 v[36:39], v[148:151], v[128:131], v[36:39]
	ds_read_b128 v[112:115], v17 offset:32768
	v_mfma_f32_16x16x32_f16 v[40:43], v[152:155], v[128:131], v[40:43]
	ds_read_b128 v[116:119], v17 offset:34816
	v_mfma_f32_16x16x32_f16 v[44:47], v[156:159], v[128:131], v[44:47]
	ds_read_b128 v[120:123], v17 offset:36864
	v_mfma_f32_16x16x32_f16 v[48:51], v[144:147], v[132:135], v[48:51]
	ds_read_b128 v[124:127], v17 offset:38912
	v_mfma_f32_16x16x32_f16 v[52:55], v[148:151], v[132:135], v[52:55]
	ds_read_b128 v[100:103], v16 offset:2048
	v_mfma_f32_16x16x32_f16 v[56:59], v[152:155], v[132:135], v[56:59]
	ds_read_b128 v[104:107], v16 offset:4096
	v_mfma_f32_16x16x32_f16 v[60:63], v[156:159], v[132:135], v[60:63]
	ds_read_b128 v[108:111], v16 offset:6144
	v_mfma_f32_16x16x32_f16 v[64:67], v[144:147], v[136:139], v[64:67]
	v_mfma_f32_16x16x32_f16 v[68:71], v[148:151], v[136:139], v[68:71]
	v_mfma_f32_16x16x32_f16 v[72:75], v[152:155], v[136:139], v[72:75]
	s_add_u32 m0, s14, 0xc000
	s_nop 0
	global_load_lds_dwordx4 v2, s[28:29]
	v_mfma_f32_16x16x32_f16 v[76:79], v[156:159], v[136:139], v[76:79]
	v_mfma_f32_16x16x32_f16 v[80:83], v[144:147], v[140:143], v[80:83]
	s_add_u32 m0, s14, 0xe000
	s_nop 0
	global_load_lds_dwordx4 v3, s[28:29]
	v_mfma_f32_16x16x32_f16 v[84:87], v[148:151], v[140:143], v[84:87]
	v_mfma_f32_16x16x32_f16 v[88:91], v[152:155], v[140:143], v[88:91]
	s_add_u32 m0, s14, 0x10000
	s_nop 0
	global_load_lds_dwordx4 v4, s[28:29]
	v_mfma_f32_16x16x32_f16 v[92:95], v[156:159], v[140:143], v[92:95]
	s_waitcnt lgkmcnt(0)
	v_mfma_f32_16x16x32_f16 v[32:35], v[112:115], v[96:99], v[32:35]
	ds_read_b128 v[128:131], v18
	v_mfma_f32_16x16x32_f16 v[36:39], v[116:119], v[96:99], v[36:39]
	ds_read_b128 v[144:147], v19 offset:32768
	v_mfma_f32_16x16x32_f16 v[40:43], v[120:123], v[96:99], v[40:43]
	ds_read_b128 v[148:151], v19 offset:34816
	v_mfma_f32_16x16x32_f16 v[44:47], v[124:127], v[96:99], v[44:47]
	ds_read_b128 v[152:155], v19 offset:36864
	v_mfma_f32_16x16x32_f16 v[48:51], v[112:115], v[100:103], v[48:51]
	ds_read_b128 v[156:159], v19 offset:38912
	v_mfma_f32_16x16x32_f16 v[52:55], v[116:119], v[100:103], v[52:55]
	ds_read_b128 v[132:135], v18 offset:2048
	v_mfma_f32_16x16x32_f16 v[56:59], v[120:123], v[100:103], v[56:59]
	ds_read_b128 v[136:139], v18 offset:4096
	v_mfma_f32_16x16x32_f16 v[60:63], v[124:127], v[100:103], v[60:63]
	ds_read_b128 v[140:143], v18 offset:6144
	v_mfma_f32_16x16x32_f16 v[64:67], v[112:115], v[104:107], v[64:67]
	v_mfma_f32_16x16x32_f16 v[68:71], v[116:119], v[104:107], v[68:71]
	v_mfma_f32_16x16x32_f16 v[72:75], v[120:123], v[104:107], v[72:75]
	s_add_u32 m0, s14, 0x12000
	s_nop 0
	global_load_lds_dwordx4 v5, s[28:29]
	v_mfma_f32_16x16x32_f16 v[76:79], v[124:127], v[104:107], v[76:79]
	v_mfma_f32_16x16x32_f16 v[80:83], v[112:115], v[108:111], v[80:83]
	s_add_u32 m0, s14, 0x14000
	s_nop 0
	global_load_lds_dwordx4 v6, s[30:31]
	v_mfma_f32_16x16x32_f16 v[84:87], v[116:119], v[108:111], v[84:87]
	v_mfma_f32_16x16x32_f16 v[88:91], v[120:123], v[108:111], v[88:91]
	s_add_u32 m0, s14, 0x16000
	s_nop 0
	global_load_lds_dwordx4 v7, s[30:31]
	v_mfma_f32_16x16x32_f16 v[92:95], v[124:127], v[108:111], v[92:95]
	s_waitcnt vmcnt(6) lgkmcnt(0)
	s_barrier
	s_add_u32 s28, s28, 0x80
	s_addc_u32 s29, s29, 0
	s_add_u32 s30, s30, 0x80
	s_addc_u32 s31, s31, 0
	s_waitcnt lgkmcnt(0)
	v_mfma_f32_16x16x32_f16 v[32:35], v[144:147], v[128:131], v[32:35]
	ds_read_b128 v[96:99], v8
	v_mfma_f32_16x16x32_f16 v[36:39], v[148:151], v[128:131], v[36:39]
	ds_read_b128 v[112:115], v9 offset:32768
	v_mfma_f32_16x16x32_f16 v[40:43], v[152:155], v[128:131], v[40:43]
	ds_read_b128 v[116:119], v9 offset:34816
	v_mfma_f32_16x16x32_f16 v[44:47], v[156:159], v[128:131], v[44:47]
	ds_read_b128 v[120:123], v9 offset:36864
	v_mfma_f32_16x16x32_f16 v[48:51], v[144:147], v[132:135], v[48:51]
	ds_read_b128 v[124:127], v9 offset:38912
	v_mfma_f32_16x16x32_f16 v[52:55], v[148:151], v[132:135], v[52:55]
	ds_read_b128 v[100:103], v8 offset:2048
	v_mfma_f32_16x16x32_f16 v[56:59], v[152:155], v[132:135], v[56:59]
	ds_read_b128 v[104:107], v8 offset:4096
	v_mfma_f32_16x16x32_f16 v[60:63], v[156:159], v[132:135], v[60:63]
	ds_read_b128 v[108:111], v8 offset:6144
	v_mfma_f32_16x16x32_f16 v[64:67], v[144:147], v[136:139], v[64:67]
	v_mfma_f32_16x16x32_f16 v[68:71], v[148:151], v[136:139], v[68:71]
	v_mfma_f32_16x16x32_f16 v[72:75], v[152:155], v[136:139], v[72:75]
	s_add_u32 m0, s14, 0x18000
	s_nop 0
	global_load_lds_dwordx4 v2, s[28:29]
	v_mfma_f32_16x16x32_f16 v[76:79], v[156:159], v[136:139], v[76:79]
	v_mfma_f32_16x16x32_f16 v[80:83], v[144:147], v[140:143], v[80:83]
	s_add_u32 m0, s14, 0x1a000
	s_nop 0
	global_load_lds_dwordx4 v3, s[28:29]
	v_mfma_f32_16x16x32_f16 v[84:87], v[148:151], v[140:143], v[84:87]
	v_mfma_f32_16x16x32_f16 v[88:91], v[152:155], v[140:143], v[88:91]
	s_add_u32 m0, s14, 0x1c000
	s_nop 0
	global_load_lds_dwordx4 v4, s[28:29]
	v_mfma_f32_16x16x32_f16 v[92:95], v[156:159], v[140:143], v[92:95]
	s_waitcnt lgkmcnt(0)
	v_mfma_f32_16x16x32_f16 v[32:35], v[112:115], v[96:99], v[32:35]
	ds_read_b128 v[128:131], v10
	v_mfma_f32_16x16x32_f16 v[36:39], v[116:119], v[96:99], v[36:39]
	ds_read_b128 v[144:147], v11 offset:32768
	v_mfma_f32_16x16x32_f16 v[40:43], v[120:123], v[96:99], v[40:43]
	ds_read_b128 v[148:151], v11 offset:34816
	v_mfma_f32_16x16x32_f16 v[44:47], v[124:127], v[96:99], v[44:47]
	ds_read_b128 v[152:155], v11 offset:36864
	v_mfma_f32_16x16x32_f16 v[48:51], v[112:115], v[100:103], v[48:51]
	ds_read_b128 v[156:159], v11 offset:38912
	v_mfma_f32_16x16x32_f16 v[52:55], v[116:119], v[100:103], v[52:55]
	ds_read_b128 v[132:135], v10 offset:2048
	v_mfma_f32_16x16x32_f16 v[56:59], v[120:123], v[100:103], v[56:59]
	ds_read_b128 v[136:139], v10 offset:4096
	v_mfma_f32_16x16x32_f16 v[60:63], v[124:127], v[100:103], v[60:63]
	ds_read_b128 v[140:143], v10 offset:6144
	v_mfma_f32_16x16x32_f16 v[64:67], v[112:115], v[104:107], v[64:67]
	v_mfma_f32_16x16x32_f16 v[68:71], v[116:119], v[104:107], v[68:71]
	v_mfma_f32_16x16x32_f16 v[72:75], v[120:123], v[104:107], v[72:75]
	s_add_u32 m0, s14, 0x1e000
	s_nop 0
	global_load_lds_dwordx4 v5, s[28:29]
	v_mfma_f32_16x16x32_f16 v[76:79], v[124:127], v[104:107], v[76:79]
	v_mfma_f32_16x16x32_f16 v[80:83], v[112:115], v[108:111], v[80:83]
	s_add_u32 m0, s14, 0x20000
	s_nop 0
	global_load_lds_dwordx4 v6, s[30:31]
	v_mfma_f32_16x16x32_f16 v[84:87], v[116:119], v[108:111], v[84:87]
	v_mfma_f32_16x16x32_f16 v[88:91], v[120:123], v[108:111], v[88:91]
	s_add_u32 m0, s14, 0x22000
	s_nop 0
	global_load_lds_dwordx4 v7, s[30:31]
	v_mfma_f32_16x16x32_f16 v[92:95], v[124:127], v[108:111], v[92:95]
	s_waitcnt vmcnt(6) lgkmcnt(0)
	s_barrier
	s_add_u32 s28, s28, 0x80
	s_addc_u32 s29, s29, 0
	s_add_u32 s30, s30, 0x80
	s_addc_u32 s31, s31, 0
	s_waitcnt lgkmcnt(0)
	v_mfma_f32_16x16x32_f16 v[32:35], v[144:147], v[128:131], v[32:35]
	ds_read_b128 v[96:99], v12
	v_mfma_f32_16x16x32_f16 v[36:39], v[148:151], v[128:131], v[36:39]
	ds_read_b128 v[112:115], v13 offset:32768
	v_mfma_f32_16x16x32_f16 v[40:43], v[152:155], v[128:131], v[40:43]
	ds_read_b128 v[116:119], v13 offset:34816
	v_mfma_f32_16x16x32_f16 v[44:47], v[156:159], v[128:131], v[44:47]
	ds_read_b128 v[120:123], v13 offset:36864
	v_mfma_f32_16x16x32_f16 v[48:51], v[144:147], v[132:135], v[48:51]
	ds_read_b128 v[124:127], v13 offset:38912
	v_mfma_f32_16x16x32_f16 v[52:55], v[148:151], v[132:135], v[52:55]
	ds_read_b128 v[100:103], v12 offset:2048
	v_mfma_f32_16x16x32_f16 v[56:59], v[152:155], v[132:135], v[56:59]
	ds_read_b128 v[104:107], v12 offset:4096
	v_mfma_f32_16x16x32_f16 v[60:63], v[156:159], v[132:135], v[60:63]
	ds_read_b128 v[108:111], v12 offset:6144
	v_mfma_f32_16x16x32_f16 v[64:67], v[144:147], v[136:139], v[64:67]
	v_mfma_f32_16x16x32_f16 v[68:71], v[148:151], v[136:139], v[68:71]
	v_mfma_f32_16x16x32_f16 v[72:75], v[152:155], v[136:139], v[72:75]
	s_add_u32 m0, s14, 0x0
	s_nop 0
	global_load_lds_dwordx4 v2, s[28:29]
	v_mfma_f32_16x16x32_f16 v[76:79], v[156:159], v[136:139], v[76:79]
	v_mfma_f32_16x16x32_f16 v[80:83], v[144:147], v[140:143], v[80:83]
	s_add_u32 m0, s14, 0x2000
	s_nop 0
	global_load_lds_dwordx4 v3, s[28:29]
	v_mfma_f32_16x16x32_f16 v[84:87], v[148:151], v[140:143], v[84:87]
	v_mfma_f32_16x16x32_f16 v[88:91], v[152:155], v[140:143], v[88:91]
	s_add_u32 m0, s14, 0x4000
	s_nop 0
	global_load_lds_dwordx4 v4, s[28:29]
	v_mfma_f32_16x16x32_f16 v[92:95], v[156:159], v[140:143], v[92:95]
	s_waitcnt lgkmcnt(0)
	v_mfma_f32_16x16x32_f16 v[32:35], v[112:115], v[96:99], v[32:35]
	ds_read_b128 v[128:131], v14
	v_mfma_f32_16x16x32_f16 v[36:39], v[116:119], v[96:99], v[36:39]
	ds_read_b128 v[144:147], v15 offset:32768
	v_mfma_f32_16x16x32_f16 v[40:43], v[120:123], v[96:99], v[40:43]
	ds_read_b128 v[148:151], v15 offset:34816
	v_mfma_f32_16x16x32_f16 v[44:47], v[124:127], v[96:99], v[44:47]
	ds_read_b128 v[152:155], v15 offset:36864
	v_mfma_f32_16x16x32_f16 v[48:51], v[112:115], v[100:103], v[48:51]
	ds_read_b128 v[156:159], v15 offset:38912
	v_mfma_f32_16x16x32_f16 v[52:55], v[116:119], v[100:103], v[52:55]
	ds_read_b128 v[132:135], v14 offset:2048
	v_mfma_f32_16x16x32_f16 v[56:59], v[120:123], v[100:103], v[56:59]
	ds_read_b128 v[136:139], v14 offset:4096
	v_mfma_f32_16x16x32_f16 v[60:63], v[124:127], v[100:103], v[60:63]
	ds_read_b128 v[140:143], v14 offset:6144
	v_mfma_f32_16x16x32_f16 v[64:67], v[112:115], v[104:107], v[64:67]
	v_mfma_f32_16x16x32_f16 v[68:71], v[116:119], v[104:107], v[68:71]
	v_mfma_f32_16x16x32_f16 v[72:75], v[120:123], v[104:107], v[72:75]
	s_add_u32 m0, s14, 0x6000
	s_nop 0
	global_load_lds_dwordx4 v5, s[28:29]
	v_mfma_f32_16x16x32_f16 v[76:79], v[124:127], v[104:107], v[76:79]
	v_mfma_f32_16x16x32_f16 v[80:83], v[112:115], v[108:111], v[80:83]
	s_add_u32 m0, s14, 0x8000
	s_nop 0
	global_load_lds_dwordx4 v6, s[30:31]
	v_mfma_f32_16x16x32_f16 v[84:87], v[116:119], v[108:111], v[84:87]
	v_mfma_f32_16x16x32_f16 v[88:91], v[120:123], v[108:111], v[88:91]
	s_add_u32 m0, s14, 0xa000
	s_nop 0
	global_load_lds_dwordx4 v7, s[30:31]
	v_mfma_f32_16x16x32_f16 v[92:95], v[124:127], v[108:111], v[92:95]
	s_waitcnt vmcnt(6) lgkmcnt(0)
	s_barrier
	s_add_u32 s28, s28, 0x80
	s_addc_u32 s29, s29, 0
	s_add_u32 s30, s30, 0x80
	s_addc_u32 s31, s31, 0
	s_waitcnt lgkmcnt(0)
	v_mfma_f32_16x16x32_f16 v[32:35], v[144:147], v[128:131], v[32:35]
	ds_read_b128 v[96:99], v16
	v_mfma_f32_16x16x32_f16 v[36:39], v[148:151], v[128:131], v[36:39]
	ds_read_b128 v[112:115], v17 offset:32768
	v_mfma_f32_16x16x32_f16 v[40:43], v[152:155], v[128:131], v[40:43]
	ds_read_b128 v[116:119], v17 offset:34816
	v_mfma_f32_16x16x32_f16 v[44:47], v[156:159], v[128:131], v[44:47]
	ds_read_b128 v[120:123], v17 offset:36864
	v_mfma_f32_16x16x32_f16 v[48:51], v[144:147], v[132:135], v[48:51]
	ds_read_b128 v[124:127], v17 offset:38912
	v_mfma_f32_16x16x32_f16 v[52:55], v[148:151], v[132:135], v[52:55]
	ds_read_b128 v[100:103], v16 offset:2048
	v_mfma_f32_16x16x32_f16 v[56:59], v[152:155], v[132:135], v[56:59]
	ds_read_b128 v[104:107], v16 offset:4096
	v_mfma_f32_16x16x32_f16 v[60:63], v[156:159], v[132:135], v[60:63]
	ds_read_b128 v[108:111], v16 offset:6144
	v_mfma_f32_16x16x32_f16 v[64:67], v[144:147], v[136:139], v[64:67]
	v_mfma_f32_16x16x32_f16 v[68:71], v[148:151], v[136:139], v[68:71]
	v_mfma_f32_16x16x32_f16 v[72:75], v[152:155], v[136:139], v[72:75]
	s_add_u32 m0, s14, 0xc000
	s_nop 0
	global_load_lds_dwordx4 v2, s[28:29]
	v_mfma_f32_16x16x32_f16 v[76:79], v[156:159], v[136:139], v[76:79]
	v_mfma_f32_16x16x32_f16 v[80:83], v[144:147], v[140:143], v[80:83]
	s_add_u32 m0, s14, 0xe000
	s_nop 0
	global_load_lds_dwordx4 v3, s[28:29]
	v_mfma_f32_16x16x32_f16 v[84:87], v[148:151], v[140:143], v[84:87]
	v_mfma_f32_16x16x32_f16 v[88:91], v[152:155], v[140:143], v[88:91]
	s_add_u32 m0, s14, 0x10000
	s_nop 0
	global_load_lds_dwordx4 v4, s[28:29]
	v_mfma_f32_16x16x32_f16 v[92:95], v[156:159], v[140:143], v[92:95]
	s_waitcnt lgkmcnt(0)
	v_mfma_f32_16x16x32_f16 v[32:35], v[112:115], v[96:99], v[32:35]
	ds_read_b128 v[128:131], v18
	v_mfma_f32_16x16x32_f16 v[36:39], v[116:119], v[96:99], v[36:39]
	ds_read_b128 v[144:147], v19 offset:32768
	v_mfma_f32_16x16x32_f16 v[40:43], v[120:123], v[96:99], v[40:43]
	ds_read_b128 v[148:151], v19 offset:34816
	v_mfma_f32_16x16x32_f16 v[44:47], v[124:127], v[96:99], v[44:47]
	ds_read_b128 v[152:155], v19 offset:36864
	v_mfma_f32_16x16x32_f16 v[48:51], v[112:115], v[100:103], v[48:51]
	ds_read_b128 v[156:159], v19 offset:38912
	v_mfma_f32_16x16x32_f16 v[52:55], v[116:119], v[100:103], v[52:55]
	ds_read_b128 v[132:135], v18 offset:2048
	v_mfma_f32_16x16x32_f16 v[56:59], v[120:123], v[100:103], v[56:59]
	ds_read_b128 v[136:139], v18 offset:4096
	v_mfma_f32_16x16x32_f16 v[60:63], v[124:127], v[100:103], v[60:63]
	ds_read_b128 v[140:143], v18 offset:6144
	v_mfma_f32_16x16x32_f16 v[64:67], v[112:115], v[104:107], v[64:67]
	v_mfma_f32_16x16x32_f16 v[68:71], v[116:119], v[104:107], v[68:71]
	v_mfma_f32_16x16x32_f16 v[72:75], v[120:123], v[104:107], v[72:75]
	s_add_u32 m0, s14, 0x12000
	s_nop 0
	global_load_lds_dwordx4 v5, s[28:29]
	v_mfma_f32_16x16x32_f16 v[76:79], v[124:127], v[104:107], v[76:79]
	v_mfma_f32_16x16x32_f16 v[80:83], v[112:115], v[108:111], v[80:83]
	s_add_u32 m0, s14, 0x14000
	s_nop 0
	global_load_lds_dwordx4 v6, s[30:31]
	v_mfma_f32_16x16x32_f16 v[84:87], v[116:119], v[108:111], v[84:87]
	v_mfma_f32_16x16x32_f16 v[88:91], v[120:123], v[108:111], v[88:91]
	s_add_u32 m0, s14, 0x16000
	s_nop 0
	global_load_lds_dwordx4 v7, s[30:31]
	v_mfma_f32_16x16x32_f16 v[92:95], v[124:127], v[108:111], v[92:95]
	s_waitcnt vmcnt(6) lgkmcnt(0)
	s_barrier
	s_add_u32 s28, s28, 0x80
	s_addc_u32 s29, s29, 0
	s_add_u32 s30, s30, 0x80
	s_addc_u32 s31, s31, 0
	s_waitcnt lgkmcnt(0)
	v_mfma_f32_16x16x32_f16 v[32:35], v[144:147], v[128:131], v[32:35]
	ds_read_b128 v[96:99], v8
	v_mfma_f32_16x16x32_f16 v[36:39], v[148:151], v[128:131], v[36:39]
	ds_read_b128 v[112:115], v9 offset:32768
	v_mfma_f32_16x16x32_f16 v[40:43], v[152:155], v[128:131], v[40:43]
	ds_read_b128 v[116:119], v9 offset:34816
	v_mfma_f32_16x16x32_f16 v[44:47], v[156:159], v[128:131], v[44:47]
	ds_read_b128 v[120:123], v9 offset:36864
	v_mfma_f32_16x16x32_f16 v[48:51], v[144:147], v[132:135], v[48:51]
	ds_read_b128 v[124:127], v9 offset:38912
	v_mfma_f32_16x16x32_f16 v[52:55], v[148:151], v[132:135], v[52:55]
	ds_read_b128 v[100:103], v8 offset:2048
	v_mfma_f32_16x16x32_f16 v[56:59], v[152:155], v[132:135], v[56:59]
	ds_read_b128 v[104:107], v8 offset:4096
	v_mfma_f32_16x16x32_f16 v[60:63], v[156:159], v[132:135], v[60:63]
	ds_read_b128 v[108:111], v8 offset:6144
	v_mfma_f32_16x16x32_f16 v[64:67], v[144:147], v[136:139], v[64:67]
	v_mfma_f32_16x16x32_f16 v[68:71], v[148:151], v[136:139], v[68:71]
	v_mfma_f32_16x16x32_f16 v[72:75], v[152:155], v[136:139], v[72:75]
	s_add_u32 m0, s14, 0x18000
	s_nop 0
	global_load_lds_dwordx4 v2, s[28:29]
	v_mfma_f32_16x16x32_f16 v[76:79], v[156:159], v[136:139], v[76:79]
	v_mfma_f32_16x16x32_f16 v[80:83], v[144:147], v[140:143], v[80:83]
	s_add_u32 m0, s14, 0x1a000
	s_nop 0
	global_load_lds_dwordx4 v3, s[28:29]
	v_mfma_f32_16x16x32_f16 v[84:87], v[148:151], v[140:143], v[84:87]
	v_mfma_f32_16x16x32_f16 v[88:91], v[152:155], v[140:143], v[88:91]
	s_add_u32 m0, s14, 0x1c000
	s_nop 0
	global_load_lds_dwordx4 v4, s[28:29]
	v_mfma_f32_16x16x32_f16 v[92:95], v[156:159], v[140:143], v[92:95]
	s_waitcnt lgkmcnt(0)
	v_mfma_f32_16x16x32_f16 v[32:35], v[112:115], v[96:99], v[32:35]
	ds_read_b128 v[128:131], v10
	v_mfma_f32_16x16x32_f16 v[36:39], v[116:119], v[96:99], v[36:39]
	ds_read_b128 v[144:147], v11 offset:32768
	v_mfma_f32_16x16x32_f16 v[40:43], v[120:123], v[96:99], v[40:43]
	ds_read_b128 v[148:151], v11 offset:34816
	v_mfma_f32_16x16x32_f16 v[44:47], v[124:127], v[96:99], v[44:47]
	ds_read_b128 v[152:155], v11 offset:36864
	v_mfma_f32_16x16x32_f16 v[48:51], v[112:115], v[100:103], v[48:51]
	ds_read_b128 v[156:159], v11 offset:38912
	v_mfma_f32_16x16x32_f16 v[52:55], v[116:119], v[100:103], v[52:55]
	ds_read_b128 v[132:135], v10 offset:2048
	v_mfma_f32_16x16x32_f16 v[56:59], v[120:123], v[100:103], v[56:59]
	ds_read_b128 v[136:139], v10 offset:4096
	v_mfma_f32_16x16x32_f16 v[60:63], v[124:127], v[100:103], v[60:63]
	ds_read_b128 v[140:143], v10 offset:6144
	v_mfma_f32_16x16x32_f16 v[64:67], v[112:115], v[104:107], v[64:67]
	v_mfma_f32_16x16x32_f16 v[68:71], v[116:119], v[104:107], v[68:71]
	v_mfma_f32_16x16x32_f16 v[72:75], v[120:123], v[104:107], v[72:75]
	s_add_u32 m0, s14, 0x1e000
	s_nop 0
	global_load_lds_dwordx4 v5, s[28:29]
	v_mfma_f32_16x16x32_f16 v[76:79], v[124:127], v[104:107], v[76:79]
	v_mfma_f32_16x16x32_f16 v[80:83], v[112:115], v[108:111], v[80:83]
	s_add_u32 m0, s14, 0x20000
	s_nop 0
	global_load_lds_dwordx4 v6, s[30:31]
	v_mfma_f32_16x16x32_f16 v[84:87], v[116:119], v[108:111], v[84:87]
	v_mfma_f32_16x16x32_f16 v[88:91], v[120:123], v[108:111], v[88:91]
	s_add_u32 m0, s14, 0x22000
	s_nop 0
	global_load_lds_dwordx4 v7, s[30:31]
	v_mfma_f32_16x16x32_f16 v[92:95], v[124:127], v[108:111], v[92:95]
	s_waitcnt vmcnt(6) lgkmcnt(0)
	s_barrier
	s_add_u32 s28, s28, 0x80
	s_addc_u32 s29, s29, 0
	s_add_u32 s30, s30, 0x80
	s_addc_u32 s31, s31, 0
	s_waitcnt lgkmcnt(0)
	v_mfma_f32_16x16x32_f16 v[32:35], v[144:147], v[128:131], v[32:35]
	ds_read_b128 v[96:99], v12
	v_mfma_f32_16x16x32_f16 v[36:39], v[148:151], v[128:131], v[36:39]
	ds_read_b128 v[112:115], v13 offset:32768
	v_mfma_f32_16x16x32_f16 v[40:43], v[152:155], v[128:131], v[40:43]
	ds_read_b128 v[116:119], v13 offset:34816
	v_mfma_f32_16x16x32_f16 v[44:47], v[156:159], v[128:131], v[44:47]
	ds_read_b128 v[120:123], v13 offset:36864
	v_mfma_f32_16x16x32_f16 v[48:51], v[144:147], v[132:135], v[48:51]
	ds_read_b128 v[124:127], v13 offset:38912
	v_mfma_f32_16x16x32_f16 v[52:55], v[148:151], v[132:135], v[52:55]
	ds_read_b128 v[100:103], v12 offset:2048
	v_mfma_f32_16x16x32_f16 v[56:59], v[152:155], v[132:135], v[56:59]
	ds_read_b128 v[104:107], v12 offset:4096
	v_mfma_f32_16x16x32_f16 v[60:63], v[156:159], v[132:135], v[60:63]
	ds_read_b128 v[108:111], v12 offset:6144
	v_mfma_f32_16x16x32_f16 v[64:67], v[144:147], v[136:139], v[64:67]
	v_mfma_f32_16x16x32_f16 v[68:71], v[148:151], v[136:139], v[68:71]
	v_mfma_f32_16x16x32_f16 v[72:75], v[152:155], v[136:139], v[72:75]
	s_add_u32 m0, s14, 0x0
	s_nop 0
	global_load_lds_dwordx4 v2, s[28:29]
	v_mfma_f32_16x16x32_f16 v[76:79], v[156:159], v[136:139], v[76:79]
	v_mfma_f32_16x16x32_f16 v[80:83], v[144:147], v[140:143], v[80:83]
	s_add_u32 m0, s14, 0x2000
	s_nop 0
	global_load_lds_dwordx4 v3, s[28:29]
	v_mfma_f32_16x16x32_f16 v[84:87], v[148:151], v[140:143], v[84:87]
	v_mfma_f32_16x16x32_f16 v[88:91], v[152:155], v[140:143], v[88:91]
	s_add_u32 m0, s14, 0x4000
	s_nop 0
	global_load_lds_dwordx4 v4, s[28:29]
	v_mfma_f32_16x16x32_f16 v[92:95], v[156:159], v[140:143], v[92:95]
	s_waitcnt lgkmcnt(0)
	v_mfma_f32_16x16x32_f16 v[32:35], v[112:115], v[96:99], v[32:35]
	ds_read_b128 v[128:131], v14
	v_mfma_f32_16x16x32_f16 v[36:39], v[116:119], v[96:99], v[36:39]
	ds_read_b128 v[144:147], v15 offset:32768
	v_mfma_f32_16x16x32_f16 v[40:43], v[120:123], v[96:99], v[40:43]
	ds_read_b128 v[148:151], v15 offset:34816
	v_mfma_f32_16x16x32_f16 v[44:47], v[124:127], v[96:99], v[44:47]
	ds_read_b128 v[152:155], v15 offset:36864
	v_mfma_f32_16x16x32_f16 v[48:51], v[112:115], v[100:103], v[48:51]
	ds_read_b128 v[156:159], v15 offset:38912
	v_mfma_f32_16x16x32_f16 v[52:55], v[116:119], v[100:103], v[52:55]
	ds_read_b128 v[132:135], v14 offset:2048
	v_mfma_f32_16x16x32_f16 v[56:59], v[120:123], v[100:103], v[56:59]
	ds_read_b128 v[136:139], v14 offset:4096
	v_mfma_f32_16x16x32_f16 v[60:63], v[124:127], v[100:103], v[60:63]
	ds_read_b128 v[140:143], v14 offset:6144
	v_mfma_f32_16x16x32_f16 v[64:67], v[112:115], v[104:107], v[64:67]
	v_mfma_f32_16x16x32_f16 v[68:71], v[116:119], v[104:107], v[68:71]
	v_mfma_f32_16x16x32_f16 v[72:75], v[120:123], v[104:107], v[72:75]
	s_add_u32 m0, s14, 0x6000
	s_nop 0
	global_load_lds_dwordx4 v5, s[28:29]
	v_mfma_f32_16x16x32_f16 v[76:79], v[124:127], v[104:107], v[76:79]
	v_mfma_f32_16x16x32_f16 v[80:83], v[112:115], v[108:111], v[80:83]
	s_add_u32 m0, s14, 0x8000
	s_nop 0
	global_load_lds_dwordx4 v6, s[30:31]
	v_mfma_f32_16x16x32_f16 v[84:87], v[116:119], v[108:111], v[84:87]
	v_mfma_f32_16x16x32_f16 v[88:91], v[120:123], v[108:111], v[88:91]
	s_add_u32 m0, s14, 0xa000
	s_nop 0
	global_load_lds_dwordx4 v7, s[30:31]
	v_mfma_f32_16x16x32_f16 v[92:95], v[124:127], v[108:111], v[92:95]
	s_waitcnt vmcnt(6) lgkmcnt(0)
	s_barrier
	s_add_u32 s28, s28, 0x80
	s_addc_u32 s29, s29, 0
	s_add_u32 s30, s30, 0x80
	s_addc_u32 s31, s31, 0
	s_waitcnt lgkmcnt(0)
	v_mfma_f32_16x16x32_f16 v[32:35], v[144:147], v[128:131], v[32:35]
	ds_read_b128 v[96:99], v16
	v_mfma_f32_16x16x32_f16 v[36:39], v[148:151], v[128:131], v[36:39]
	ds_read_b128 v[112:115], v17 offset:32768
	v_mfma_f32_16x16x32_f16 v[40:43], v[152:155], v[128:131], v[40:43]
	ds_read_b128 v[116:119], v17 offset:34816
	v_mfma_f32_16x16x32_f16 v[44:47], v[156:159], v[128:131], v[44:47]
	ds_read_b128 v[120:123], v17 offset:36864
	v_mfma_f32_16x16x32_f16 v[48:51], v[144:147], v[132:135], v[48:51]
	ds_read_b128 v[124:127], v17 offset:38912
	v_mfma_f32_16x16x32_f16 v[52:55], v[148:151], v[132:135], v[52:55]
	ds_read_b128 v[100:103], v16 offset:2048
	v_mfma_f32_16x16x32_f16 v[56:59], v[152:155], v[132:135], v[56:59]
	ds_read_b128 v[104:107], v16 offset:4096
	v_mfma_f32_16x16x32_f16 v[60:63], v[156:159], v[132:135], v[60:63]
	ds_read_b128 v[108:111], v16 offset:6144
	v_mfma_f32_16x16x32_f16 v[64:67], v[144:147], v[136:139], v[64:67]
	v_mfma_f32_16x16x32_f16 v[68:71], v[148:151], v[136:139], v[68:71]
	v_mfma_f32_16x16x32_f16 v[72:75], v[152:155], v[136:139], v[72:75]
	s_add_u32 m0, s14, 0xc000
	s_nop 0
	global_load_lds_dwordx4 v2, s[28:29]
	v_mfma_f32_16x16x32_f16 v[76:79], v[156:159], v[136:139], v[76:79]
	v_mfma_f32_16x16x32_f16 v[80:83], v[144:147], v[140:143], v[80:83]
	s_add_u32 m0, s14, 0xe000
	s_nop 0
	global_load_lds_dwordx4 v3, s[28:29]
	v_mfma_f32_16x16x32_f16 v[84:87], v[148:151], v[140:143], v[84:87]
	v_mfma_f32_16x16x32_f16 v[88:91], v[152:155], v[140:143], v[88:91]
	s_add_u32 m0, s14, 0x10000
	s_nop 0
	global_load_lds_dwordx4 v4, s[28:29]
	v_mfma_f32_16x16x32_f16 v[92:95], v[156:159], v[140:143], v[92:95]
	s_waitcnt lgkmcnt(0)
	v_mfma_f32_16x16x32_f16 v[32:35], v[112:115], v[96:99], v[32:35]
	ds_read_b128 v[128:131], v18
	v_mfma_f32_16x16x32_f16 v[36:39], v[116:119], v[96:99], v[36:39]
	ds_read_b128 v[144:147], v19 offset:32768
	v_mfma_f32_16x16x32_f16 v[40:43], v[120:123], v[96:99], v[40:43]
	ds_read_b128 v[148:151], v19 offset:34816
	v_mfma_f32_16x16x32_f16 v[44:47], v[124:127], v[96:99], v[44:47]
	ds_read_b128 v[152:155], v19 offset:36864
	v_mfma_f32_16x16x32_f16 v[48:51], v[112:115], v[100:103], v[48:51]
	ds_read_b128 v[156:159], v19 offset:38912
	v_mfma_f32_16x16x32_f16 v[52:55], v[116:119], v[100:103], v[52:55]
	ds_read_b128 v[132:135], v18 offset:2048
	v_mfma_f32_16x16x32_f16 v[56:59], v[120:123], v[100:103], v[56:59]
	ds_read_b128 v[136:139], v18 offset:4096
	v_mfma_f32_16x16x32_f16 v[60:63], v[124:127], v[100:103], v[60:63]
	ds_read_b128 v[140:143], v18 offset:6144
	v_mfma_f32_16x16x32_f16 v[64:67], v[112:115], v[104:107], v[64:67]
	v_mfma_f32_16x16x32_f16 v[68:71], v[116:119], v[104:107], v[68:71]
	v_mfma_f32_16x16x32_f16 v[72:75], v[120:123], v[104:107], v[72:75]
	s_add_u32 m0, s14, 0x12000
	s_nop 0
	global_load_lds_dwordx4 v5, s[28:29]
	v_mfma_f32_16x16x32_f16 v[76:79], v[124:127], v[104:107], v[76:79]
	v_mfma_f32_16x16x32_f16 v[80:83], v[112:115], v[108:111], v[80:83]
	s_add_u32 m0, s14, 0x14000
	s_nop 0
	global_load_lds_dwordx4 v6, s[30:31]
	v_mfma_f32_16x16x32_f16 v[84:87], v[116:119], v[108:111], v[84:87]
	v_mfma_f32_16x16x32_f16 v[88:91], v[120:123], v[108:111], v[88:91]
	s_add_u32 m0, s14, 0x16000
	s_nop 0
	global_load_lds_dwordx4 v7, s[30:31]
	v_mfma_f32_16x16x32_f16 v[92:95], v[124:127], v[108:111], v[92:95]
	s_waitcnt vmcnt(6) lgkmcnt(0)
	s_barrier
	s_add_u32 s28, s28, 0x80
	s_addc_u32 s29, s29, 0
	s_add_u32 s30, s30, 0x80
	s_addc_u32 s31, s31, 0
	s_waitcnt lgkmcnt(0)
	v_mfma_f32_16x16x32_f16 v[32:35], v[144:147], v[128:131], v[32:35]
	ds_read_b128 v[96:99], v8
	v_mfma_f32_16x16x32_f16 v[36:39], v[148:151], v[128:131], v[36:39]
	ds_read_b128 v[112:115], v9 offset:32768
	v_mfma_f32_16x16x32_f16 v[40:43], v[152:155], v[128:131], v[40:43]
	ds_read_b128 v[116:119], v9 offset:34816
	v_mfma_f32_16x16x32_f16 v[44:47], v[156:159], v[128:131], v[44:47]
	ds_read_b128 v[120:123], v9 offset:36864
	v_mfma_f32_16x16x32_f16 v[48:51], v[144:147], v[132:135], v[48:51]
	ds_read_b128 v[124:127], v9 offset:38912
	v_mfma_f32_16x16x32_f16 v[52:55], v[148:151], v[132:135], v[52:55]
	ds_read_b128 v[100:103], v8 offset:2048
	v_mfma_f32_16x16x32_f16 v[56:59], v[152:155], v[132:135], v[56:59]
	ds_read_b128 v[104:107], v8 offset:4096
	v_mfma_f32_16x16x32_f16 v[60:63], v[156:159], v[132:135], v[60:63]
	ds_read_b128 v[108:111], v8 offset:6144
	v_mfma_f32_16x16x32_f16 v[64:67], v[144:147], v[136:139], v[64:67]
	v_mfma_f32_16x16x32_f16 v[68:71], v[148:151], v[136:139], v[68:71]
	v_mfma_f32_16x16x32_f16 v[72:75], v[152:155], v[136:139], v[72:75]
	s_add_u32 m0, s14, 0x18000
	s_nop 0
	global_load_lds_dwordx4 v2, s[28:29]
	v_mfma_f32_16x16x32_f16 v[76:79], v[156:159], v[136:139], v[76:79]
	v_mfma_f32_16x16x32_f16 v[80:83], v[144:147], v[140:143], v[80:83]
	s_add_u32 m0, s14, 0x1a000
	s_nop 0
	global_load_lds_dwordx4 v3, s[28:29]
	v_mfma_f32_16x16x32_f16 v[84:87], v[148:151], v[140:143], v[84:87]
	v_mfma_f32_16x16x32_f16 v[88:91], v[152:155], v[140:143], v[88:91]
	s_add_u32 m0, s14, 0x1c000
	s_nop 0
	global_load_lds_dwordx4 v4, s[28:29]
	v_mfma_f32_16x16x32_f16 v[92:95], v[156:159], v[140:143], v[92:95]
	s_waitcnt lgkmcnt(0)
	v_mfma_f32_16x16x32_f16 v[32:35], v[112:115], v[96:99], v[32:35]
	ds_read_b128 v[128:131], v10
	v_mfma_f32_16x16x32_f16 v[36:39], v[116:119], v[96:99], v[36:39]
	ds_read_b128 v[144:147], v11 offset:32768
	v_mfma_f32_16x16x32_f16 v[40:43], v[120:123], v[96:99], v[40:43]
	ds_read_b128 v[148:151], v11 offset:34816
	v_mfma_f32_16x16x32_f16 v[44:47], v[124:127], v[96:99], v[44:47]
	ds_read_b128 v[152:155], v11 offset:36864
	v_mfma_f32_16x16x32_f16 v[48:51], v[112:115], v[100:103], v[48:51]
	ds_read_b128 v[156:159], v11 offset:38912
	v_mfma_f32_16x16x32_f16 v[52:55], v[116:119], v[100:103], v[52:55]
	ds_read_b128 v[132:135], v10 offset:2048
	v_mfma_f32_16x16x32_f16 v[56:59], v[120:123], v[100:103], v[56:59]
	ds_read_b128 v[136:139], v10 offset:4096
	v_mfma_f32_16x16x32_f16 v[60:63], v[124:127], v[100:103], v[60:63]
	ds_read_b128 v[140:143], v10 offset:6144
	v_mfma_f32_16x16x32_f16 v[64:67], v[112:115], v[104:107], v[64:67]
	v_mfma_f32_16x16x32_f16 v[68:71], v[116:119], v[104:107], v[68:71]
	v_mfma_f32_16x16x32_f16 v[72:75], v[120:123], v[104:107], v[72:75]
	s_add_u32 m0, s14, 0x1e000
	s_nop 0
	global_load_lds_dwordx4 v5, s[28:29]
	v_mfma_f32_16x16x32_f16 v[76:79], v[124:127], v[104:107], v[76:79]
	v_mfma_f32_16x16x32_f16 v[80:83], v[112:115], v[108:111], v[80:83]
	s_add_u32 m0, s14, 0x20000
	s_nop 0
	global_load_lds_dwordx4 v6, s[30:31]
	v_mfma_f32_16x16x32_f16 v[84:87], v[116:119], v[108:111], v[84:87]
	v_mfma_f32_16x16x32_f16 v[88:91], v[120:123], v[108:111], v[88:91]
	s_add_u32 m0, s14, 0x22000
	s_nop 0
	global_load_lds_dwordx4 v7, s[30:31]
	v_mfma_f32_16x16x32_f16 v[92:95], v[124:127], v[108:111], v[92:95]
	s_waitcnt vmcnt(6) lgkmcnt(0)
	s_barrier
	s_add_u32 s28, s28, 0x80
	s_addc_u32 s29, s29, 0
	s_add_u32 s30, s30, 0x80
	s_addc_u32 s31, s31, 0
	s_waitcnt lgkmcnt(0)
	v_mfma_f32_16x16x32_f16 v[32:35], v[144:147], v[128:131], v[32:35]
	ds_read_b128 v[96:99], v12
	v_mfma_f32_16x16x32_f16 v[36:39], v[148:151], v[128:131], v[36:39]
	ds_read_b128 v[112:115], v13 offset:32768
	v_mfma_f32_16x16x32_f16 v[40:43], v[152:155], v[128:131], v[40:43]
	ds_read_b128 v[116:119], v13 offset:34816
	v_mfma_f32_16x16x32_f16 v[44:47], v[156:159], v[128:131], v[44:47]
	ds_read_b128 v[120:123], v13 offset:36864
	v_mfma_f32_16x16x32_f16 v[48:51], v[144:147], v[132:135], v[48:51]
	ds_read_b128 v[124:127], v13 offset:38912
	v_mfma_f32_16x16x32_f16 v[52:55], v[148:151], v[132:135], v[52:55]
	ds_read_b128 v[100:103], v12 offset:2048
	v_mfma_f32_16x16x32_f16 v[56:59], v[152:155], v[132:135], v[56:59]
	ds_read_b128 v[104:107], v12 offset:4096
	v_mfma_f32_16x16x32_f16 v[60:63], v[156:159], v[132:135], v[60:63]
	ds_read_b128 v[108:111], v12 offset:6144
	v_mfma_f32_16x16x32_f16 v[64:67], v[144:147], v[136:139], v[64:67]
	v_mfma_f32_16x16x32_f16 v[68:71], v[148:151], v[136:139], v[68:71]
	v_mfma_f32_16x16x32_f16 v[72:75], v[152:155], v[136:139], v[72:75]
	s_add_u32 m0, s14, 0x0
	s_nop 0
	global_load_lds_dwordx4 v2, s[28:29]
	v_mfma_f32_16x16x32_f16 v[76:79], v[156:159], v[136:139], v[76:79]
	v_mfma_f32_16x16x32_f16 v[80:83], v[144:147], v[140:143], v[80:83]
	s_add_u32 m0, s14, 0x2000
	s_nop 0
	global_load_lds_dwordx4 v3, s[28:29]
	v_mfma_f32_16x16x32_f16 v[84:87], v[148:151], v[140:143], v[84:87]
	v_mfma_f32_16x16x32_f16 v[88:91], v[152:155], v[140:143], v[88:91]
	s_add_u32 m0, s14, 0x4000
	s_nop 0
	global_load_lds_dwordx4 v4, s[28:29]
	v_mfma_f32_16x16x32_f16 v[92:95], v[156:159], v[140:143], v[92:95]
	s_waitcnt lgkmcnt(0)
	v_mfma_f32_16x16x32_f16 v[32:35], v[112:115], v[96:99], v[32:35]
	ds_read_b128 v[128:131], v14
	v_mfma_f32_16x16x32_f16 v[36:39], v[116:119], v[96:99], v[36:39]
	ds_read_b128 v[144:147], v15 offset:32768
	v_mfma_f32_16x16x32_f16 v[40:43], v[120:123], v[96:99], v[40:43]
	ds_read_b128 v[148:151], v15 offset:34816
	v_mfma_f32_16x16x32_f16 v[44:47], v[124:127], v[96:99], v[44:47]
	ds_read_b128 v[152:155], v15 offset:36864
	v_mfma_f32_16x16x32_f16 v[48:51], v[112:115], v[100:103], v[48:51]
	ds_read_b128 v[156:159], v15 offset:38912
	v_mfma_f32_16x16x32_f16 v[52:55], v[116:119], v[100:103], v[52:55]
	ds_read_b128 v[132:135], v14 offset:2048
	v_mfma_f32_16x16x32_f16 v[56:59], v[120:123], v[100:103], v[56:59]
	ds_read_b128 v[136:139], v14 offset:4096
	v_mfma_f32_16x16x32_f16 v[60:63], v[124:127], v[100:103], v[60:63]
	ds_read_b128 v[140:143], v14 offset:6144
	v_mfma_f32_16x16x32_f16 v[64:67], v[112:115], v[104:107], v[64:67]
	v_mfma_f32_16x16x32_f16 v[68:71], v[116:119], v[104:107], v[68:71]
	v_mfma_f32_16x16x32_f16 v[72:75], v[120:123], v[104:107], v[72:75]
	s_add_u32 m0, s14, 0x6000
	s_nop 0
	global_load_lds_dwordx4 v5, s[28:29]
	v_mfma_f32_16x16x32_f16 v[76:79], v[124:127], v[104:107], v[76:79]
	v_mfma_f32_16x16x32_f16 v[80:83], v[112:115], v[108:111], v[80:83]
	s_add_u32 m0, s14, 0x8000
	s_nop 0
	global_load_lds_dwordx4 v6, s[30:31]
	v_mfma_f32_16x16x32_f16 v[84:87], v[116:119], v[108:111], v[84:87]
	v_mfma_f32_16x16x32_f16 v[88:91], v[120:123], v[108:111], v[88:91]
	s_add_u32 m0, s14, 0xa000
	s_nop 0
	global_load_lds_dwordx4 v7, s[30:31]
	v_mfma_f32_16x16x32_f16 v[92:95], v[124:127], v[108:111], v[92:95]
	s_waitcnt vmcnt(6) lgkmcnt(0)
	s_barrier
	s_add_u32 s28, s28, 0x80
	s_addc_u32 s29, s29, 0
	s_add_u32 s30, s30, 0x80
	s_addc_u32 s31, s31, 0
	s_waitcnt lgkmcnt(0)
	v_mfma_f32_16x16x32_f16 v[32:35], v[144:147], v[128:131], v[32:35]
	ds_read_b128 v[96:99], v16
	v_mfma_f32_16x16x32_f16 v[36:39], v[148:151], v[128:131], v[36:39]
	ds_read_b128 v[112:115], v17 offset:32768
	v_mfma_f32_16x16x32_f16 v[40:43], v[152:155], v[128:131], v[40:43]
	ds_read_b128 v[116:119], v17 offset:34816
	v_mfma_f32_16x16x32_f16 v[44:47], v[156:159], v[128:131], v[44:47]
	ds_read_b128 v[120:123], v17 offset:36864
	v_mfma_f32_16x16x32_f16 v[48:51], v[144:147], v[132:135], v[48:51]
	ds_read_b128 v[124:127], v17 offset:38912
	v_mfma_f32_16x16x32_f16 v[52:55], v[148:151], v[132:135], v[52:55]
	ds_read_b128 v[100:103], v16 offset:2048
	v_mfma_f32_16x16x32_f16 v[56:59], v[152:155], v[132:135], v[56:59]
	ds_read_b128 v[104:107], v16 offset:4096
	v_mfma_f32_16x16x32_f16 v[60:63], v[156:159], v[132:135], v[60:63]
	ds_read_b128 v[108:111], v16 offset:6144
	v_mfma_f32_16x16x32_f16 v[64:67], v[144:147], v[136:139], v[64:67]
	v_mfma_f32_16x16x32_f16 v[68:71], v[148:151], v[136:139], v[68:71]
	v_mfma_f32_16x16x32_f16 v[72:75], v[152:155], v[136:139], v[72:75]
	s_add_u32 m0, s14, 0xc000
	s_nop 0
	global_load_lds_dwordx4 v2, s[28:29]
	v_mfma_f32_16x16x32_f16 v[76:79], v[156:159], v[136:139], v[76:79]
	v_mfma_f32_16x16x32_f16 v[80:83], v[144:147], v[140:143], v[80:83]
	s_add_u32 m0, s14, 0xe000
	s_nop 0
	global_load_lds_dwordx4 v3, s[28:29]
	v_mfma_f32_16x16x32_f16 v[84:87], v[148:151], v[140:143], v[84:87]
	v_mfma_f32_16x16x32_f16 v[88:91], v[152:155], v[140:143], v[88:91]
	s_add_u32 m0, s14, 0x10000
	s_nop 0
	global_load_lds_dwordx4 v4, s[28:29]
	v_mfma_f32_16x16x32_f16 v[92:95], v[156:159], v[140:143], v[92:95]
	s_waitcnt lgkmcnt(0)
	v_mfma_f32_16x16x32_f16 v[32:35], v[112:115], v[96:99], v[32:35]
	ds_read_b128 v[128:131], v18
	v_mfma_f32_16x16x32_f16 v[36:39], v[116:119], v[96:99], v[36:39]
	ds_read_b128 v[144:147], v19 offset:32768
	v_mfma_f32_16x16x32_f16 v[40:43], v[120:123], v[96:99], v[40:43]
	ds_read_b128 v[148:151], v19 offset:34816
	v_mfma_f32_16x16x32_f16 v[44:47], v[124:127], v[96:99], v[44:47]
	ds_read_b128 v[152:155], v19 offset:36864
	v_mfma_f32_16x16x32_f16 v[48:51], v[112:115], v[100:103], v[48:51]
	ds_read_b128 v[156:159], v19 offset:38912
	v_mfma_f32_16x16x32_f16 v[52:55], v[116:119], v[100:103], v[52:55]
	ds_read_b128 v[132:135], v18 offset:2048
	v_mfma_f32_16x16x32_f16 v[56:59], v[120:123], v[100:103], v[56:59]
	ds_read_b128 v[136:139], v18 offset:4096
	v_mfma_f32_16x16x32_f16 v[60:63], v[124:127], v[100:103], v[60:63]
	ds_read_b128 v[140:143], v18 offset:6144
	v_mfma_f32_16x16x32_f16 v[64:67], v[112:115], v[104:107], v[64:67]
	v_mfma_f32_16x16x32_f16 v[68:71], v[116:119], v[104:107], v[68:71]
	v_mfma_f32_16x16x32_f16 v[72:75], v[120:123], v[104:107], v[72:75]
	s_add_u32 m0, s14, 0x12000
	s_nop 0
	global_load_lds_dwordx4 v5, s[28:29]
	v_mfma_f32_16x16x32_f16 v[76:79], v[124:127], v[104:107], v[76:79]
	v_mfma_f32_16x16x32_f16 v[80:83], v[112:115], v[108:111], v[80:83]
	s_add_u32 m0, s14, 0x14000
	s_nop 0
	global_load_lds_dwordx4 v6, s[30:31]
	v_mfma_f32_16x16x32_f16 v[84:87], v[116:119], v[108:111], v[84:87]
	v_mfma_f32_16x16x32_f16 v[88:91], v[120:123], v[108:111], v[88:91]
	s_add_u32 m0, s14, 0x16000
	s_nop 0
	global_load_lds_dwordx4 v7, s[30:31]
	v_mfma_f32_16x16x32_f16 v[92:95], v[124:127], v[108:111], v[92:95]
	s_waitcnt vmcnt(6) lgkmcnt(0)
	s_barrier
	s_mov_b64 s[28:29], s[18:19]
	s_mov_b64 s[30:31], s[24:25]
	s_waitcnt lgkmcnt(0)
	v_mfma_f32_16x16x32_f16 v[32:35], v[144:147], v[128:131], v[32:35]
	ds_read_b128 v[96:99], v8
	v_mfma_f32_16x16x32_f16 v[36:39], v[148:151], v[128:131], v[36:39]
	ds_read_b128 v[112:115], v9 offset:32768
	v_mfma_f32_16x16x32_f16 v[40:43], v[152:155], v[128:131], v[40:43]
	ds_read_b128 v[116:119], v9 offset:34816
	v_mfma_f32_16x16x32_f16 v[44:47], v[156:159], v[128:131], v[44:47]
	ds_read_b128 v[120:123], v9 offset:36864
	v_mfma_f32_16x16x32_f16 v[48:51], v[144:147], v[132:135], v[48:51]
	ds_read_b128 v[124:127], v9 offset:38912
	v_mfma_f32_16x16x32_f16 v[52:55], v[148:151], v[132:135], v[52:55]
	ds_read_b128 v[100:103], v8 offset:2048
	v_mfma_f32_16x16x32_f16 v[56:59], v[152:155], v[132:135], v[56:59]
	ds_read_b128 v[104:107], v8 offset:4096
	v_mfma_f32_16x16x32_f16 v[60:63], v[156:159], v[132:135], v[60:63]
	ds_read_b128 v[108:111], v8 offset:6144
	v_mfma_f32_16x16x32_f16 v[64:67], v[144:147], v[136:139], v[64:67]
	v_mfma_f32_16x16x32_f16 v[68:71], v[148:151], v[136:139], v[68:71]
	v_mfma_f32_16x16x32_f16 v[72:75], v[152:155], v[136:139], v[72:75]
	s_add_u32 m0, s14, 0x18000
	s_nop 0
	global_load_lds_dwordx4 v2, s[28:29]
	v_mfma_f32_16x16x32_f16 v[76:79], v[156:159], v[136:139], v[76:79]
	v_mfma_f32_16x16x32_f16 v[80:83], v[144:147], v[140:143], v[80:83]
	s_add_u32 m0, s14, 0x1a000
	s_nop 0
	global_load_lds_dwordx4 v3, s[28:29]
	v_mfma_f32_16x16x32_f16 v[84:87], v[148:151], v[140:143], v[84:87]
	v_mfma_f32_16x16x32_f16 v[88:91], v[152:155], v[140:143], v[88:91]
	s_add_u32 m0, s14, 0x1c000
	s_nop 0
	global_load_lds_dwordx4 v4, s[28:29]
	v_mfma_f32_16x16x32_f16 v[92:95], v[156:159], v[140:143], v[92:95]
	s_waitcnt lgkmcnt(0)
	v_mfma_f32_16x16x32_f16 v[32:35], v[112:115], v[96:99], v[32:35]
	ds_read_b128 v[128:131], v10
	v_mfma_f32_16x16x32_f16 v[36:39], v[116:119], v[96:99], v[36:39]
	ds_read_b128 v[144:147], v11 offset:32768
	v_mfma_f32_16x16x32_f16 v[40:43], v[120:123], v[96:99], v[40:43]
	ds_read_b128 v[148:151], v11 offset:34816
	v_mfma_f32_16x16x32_f16 v[44:47], v[124:127], v[96:99], v[44:47]
	ds_read_b128 v[152:155], v11 offset:36864
	v_mfma_f32_16x16x32_f16 v[48:51], v[112:115], v[100:103], v[48:51]
	ds_read_b128 v[156:159], v11 offset:38912
	v_mfma_f32_16x16x32_f16 v[52:55], v[116:119], v[100:103], v[52:55]
	ds_read_b128 v[132:135], v10 offset:2048
	v_mfma_f32_16x16x32_f16 v[56:59], v[120:123], v[100:103], v[56:59]
	ds_read_b128 v[136:139], v10 offset:4096
	v_mfma_f32_16x16x32_f16 v[60:63], v[124:127], v[100:103], v[60:63]
	ds_read_b128 v[140:143], v10 offset:6144
	v_mfma_f32_16x16x32_f16 v[64:67], v[112:115], v[104:107], v[64:67]
	v_mfma_f32_16x16x32_f16 v[68:71], v[116:119], v[104:107], v[68:71]
	v_mfma_f32_16x16x32_f16 v[72:75], v[120:123], v[104:107], v[72:75]
	s_add_u32 m0, s14, 0x1e000
	s_nop 0
	global_load_lds_dwordx4 v5, s[28:29]
	v_mfma_f32_16x16x32_f16 v[76:79], v[124:127], v[104:107], v[76:79]
	v_mfma_f32_16x16x32_f16 v[80:83], v[112:115], v[108:111], v[80:83]
	s_add_u32 m0, s14, 0x20000
	s_nop 0
	global_load_lds_dwordx4 v6, s[30:31]
	v_mfma_f32_16x16x32_f16 v[84:87], v[116:119], v[108:111], v[84:87]
	v_mfma_f32_16x16x32_f16 v[88:91], v[120:123], v[108:111], v[88:91]
	s_add_u32 m0, s14, 0x22000
	s_nop 0
	global_load_lds_dwordx4 v7, s[30:31]
	v_mfma_f32_16x16x32_f16 v[92:95], v[124:127], v[108:111], v[92:95]
	s_waitcnt vmcnt(6) lgkmcnt(0)
	s_barrier
	s_add_u32 s28, s28, 0x80
	s_addc_u32 s29, s29, 0
	s_add_u32 s30, s30, 0x80
	s_addc_u32 s31, s31, 0
	s_waitcnt lgkmcnt(0)
	v_mfma_f32_16x16x32_f16 v[32:35], v[144:147], v[128:131], v[32:35]
	ds_read_b128 v[96:99], v12
	v_mfma_f32_16x16x32_f16 v[36:39], v[148:151], v[128:131], v[36:39]
	ds_read_b128 v[112:115], v13 offset:32768
	v_mfma_f32_16x16x32_f16 v[40:43], v[152:155], v[128:131], v[40:43]
	ds_read_b128 v[116:119], v13 offset:34816
	v_mfma_f32_16x16x32_f16 v[44:47], v[156:159], v[128:131], v[44:47]
	ds_read_b128 v[120:123], v13 offset:36864
	v_mfma_f32_16x16x32_f16 v[48:51], v[144:147], v[132:135], v[48:51]
	ds_read_b128 v[124:127], v13 offset:38912
	v_mfma_f32_16x16x32_f16 v[52:55], v[148:151], v[132:135], v[52:55]
	ds_read_b128 v[100:103], v12 offset:2048
	v_mfma_f32_16x16x32_f16 v[56:59], v[152:155], v[132:135], v[56:59]
	ds_read_b128 v[104:107], v12 offset:4096
	v_mfma_f32_16x16x32_f16 v[60:63], v[156:159], v[132:135], v[60:63]
	ds_read_b128 v[108:111], v12 offset:6144
	v_mfma_f32_16x16x32_f16 v[64:67], v[144:147], v[136:139], v[64:67]
	v_mfma_f32_16x16x32_f16 v[68:71], v[148:151], v[136:139], v[68:71]
	v_mfma_f32_16x16x32_f16 v[72:75], v[152:155], v[136:139], v[72:75]
	s_add_u32 m0, s14, 0x0
	s_nop 0
	global_load_lds_dwordx4 v2, s[28:29]
	v_mfma_f32_16x16x32_f16 v[76:79], v[156:159], v[136:139], v[76:79]
	v_mfma_f32_16x16x32_f16 v[80:83], v[144:147], v[140:143], v[80:83]
	s_add_u32 m0, s14, 0x2000
	s_nop 0
	global_load_lds_dwordx4 v3, s[28:29]
	v_mfma_f32_16x16x32_f16 v[84:87], v[148:151], v[140:143], v[84:87]
	v_mfma_f32_16x16x32_f16 v[88:91], v[152:155], v[140:143], v[88:91]
	s_add_u32 m0, s14, 0x4000
	s_nop 0
	global_load_lds_dwordx4 v4, s[28:29]
	v_mfma_f32_16x16x32_f16 v[92:95], v[156:159], v[140:143], v[92:95]
	s_waitcnt lgkmcnt(0)
	v_mfma_f32_16x16x32_f16 v[32:35], v[112:115], v[96:99], v[32:35]
	ds_read_b128 v[128:131], v14
	v_mfma_f32_16x16x32_f16 v[36:39], v[116:119], v[96:99], v[36:39]
	ds_read_b128 v[144:147], v15 offset:32768
	v_mfma_f32_16x16x32_f16 v[40:43], v[120:123], v[96:99], v[40:43]
	ds_read_b128 v[148:151], v15 offset:34816
	v_mfma_f32_16x16x32_f16 v[44:47], v[124:127], v[96:99], v[44:47]
	ds_read_b128 v[152:155], v15 offset:36864
	v_mfma_f32_16x16x32_f16 v[48:51], v[112:115], v[100:103], v[48:51]
	ds_read_b128 v[156:159], v15 offset:38912
	v_mfma_f32_16x16x32_f16 v[52:55], v[116:119], v[100:103], v[52:55]
	ds_read_b128 v[132:135], v14 offset:2048
	v_mfma_f32_16x16x32_f16 v[56:59], v[120:123], v[100:103], v[56:59]
	ds_read_b128 v[136:139], v14 offset:4096
	v_mfma_f32_16x16x32_f16 v[60:63], v[124:127], v[100:103], v[60:63]
	ds_read_b128 v[140:143], v14 offset:6144
	v_mfma_f32_16x16x32_f16 v[64:67], v[112:115], v[104:107], v[64:67]
	v_mfma_f32_16x16x32_f16 v[68:71], v[116:119], v[104:107], v[68:71]
	v_mfma_f32_16x16x32_f16 v[72:75], v[120:123], v[104:107], v[72:75]
	s_add_u32 m0, s14, 0x6000
	s_nop 0
	global_load_lds_dwordx4 v5, s[28:29]
	v_mfma_f32_16x16x32_f16 v[76:79], v[124:127], v[104:107], v[76:79]
	v_mfma_f32_16x16x32_f16 v[80:83], v[112:115], v[108:111], v[80:83]
	s_add_u32 m0, s14, 0x8000
	s_nop 0
	global_load_lds_dwordx4 v6, s[30:31]
	v_mfma_f32_16x16x32_f16 v[84:87], v[116:119], v[108:111], v[84:87]
	v_mfma_f32_16x16x32_f16 v[88:91], v[120:123], v[108:111], v[88:91]
	s_add_u32 m0, s14, 0xa000
	s_nop 0
	global_load_lds_dwordx4 v7, s[30:31]
	v_mfma_f32_16x16x32_f16 v[92:95], v[124:127], v[108:111], v[92:95]
	s_waitcnt vmcnt(6) lgkmcnt(0)
	s_barrier
	s_add_u32 s28, s28, 0x80
	s_addc_u32 s29, s29, 0
	s_add_u32 s30, s30, 0x80
	s_addc_u32 s31, s31, 0
	s_waitcnt lgkmcnt(0)
	v_mfma_f32_16x16x32_f16 v[32:35], v[144:147], v[128:131], v[32:35]
	ds_read_b128 v[96:99], v16
	v_mfma_f32_16x16x32_f16 v[36:39], v[148:151], v[128:131], v[36:39]
	ds_read_b128 v[112:115], v17 offset:32768
	v_mfma_f32_16x16x32_f16 v[40:43], v[152:155], v[128:131], v[40:43]
	ds_read_b128 v[116:119], v17 offset:34816
	v_mfma_f32_16x16x32_f16 v[44:47], v[156:159], v[128:131], v[44:47]
	ds_read_b128 v[120:123], v17 offset:36864
	v_mfma_f32_16x16x32_f16 v[48:51], v[144:147], v[132:135], v[48:51]
	ds_read_b128 v[124:127], v17 offset:38912
	v_mfma_f32_16x16x32_f16 v[52:55], v[148:151], v[132:135], v[52:55]
	ds_read_b128 v[100:103], v16 offset:2048
	v_mfma_f32_16x16x32_f16 v[56:59], v[152:155], v[132:135], v[56:59]
	ds_read_b128 v[104:107], v16 offset:4096
	v_mfma_f32_16x16x32_f16 v[60:63], v[156:159], v[132:135], v[60:63]
	ds_read_b128 v[108:111], v16 offset:6144
	v_mfma_f32_16x16x32_f16 v[64:67], v[144:147], v[136:139], v[64:67]
	v_mfma_f32_16x16x32_f16 v[68:71], v[148:151], v[136:139], v[68:71]
	v_mfma_f32_16x16x32_f16 v[72:75], v[152:155], v[136:139], v[72:75]
	s_add_u32 m0, s14, 0xc000
	s_nop 0
	global_load_lds_dwordx4 v2, s[28:29]
	v_mfma_f32_16x16x32_f16 v[76:79], v[156:159], v[136:139], v[76:79]
	v_mfma_f32_16x16x32_f16 v[80:83], v[144:147], v[140:143], v[80:83]
	s_add_u32 m0, s14, 0xe000
	s_nop 0
	global_load_lds_dwordx4 v3, s[28:29]
	v_mfma_f32_16x16x32_f16 v[84:87], v[148:151], v[140:143], v[84:87]
	v_mfma_f32_16x16x32_f16 v[88:91], v[152:155], v[140:143], v[88:91]
	s_add_u32 m0, s14, 0x10000
	s_nop 0
	global_load_lds_dwordx4 v4, s[28:29]
	v_mfma_f32_16x16x32_f16 v[92:95], v[156:159], v[140:143], v[92:95]
	s_nop 7
	s_nop 1
	v_pk_mul_f32 v[160:161], v[32:33], s[50:51] op_sel_hi:[1,0]
	v_pk_mul_f32 v[162:163], v[34:35], s[50:51] op_sel_hi:[1,0]
	v_pk_mul_f32 v[164:165], v[36:37], s[50:51] op_sel_hi:[1,0]
	v_pk_mul_f32 v[166:167], v[38:39], s[50:51] op_sel_hi:[1,0]
	v_pk_mul_f32 v[176:177], v[160:161], s[52:53] op_sel_hi:[1,0]
	v_pk_mul_f32 v[178:179], v[162:163], s[52:53] op_sel_hi:[1,0]
	v_pk_mul_f32 v[180:181], v[164:165], s[52:53] op_sel_hi:[1,0]
	v_pk_mul_f32 v[182:183], v[166:167], s[52:53] op_sel_hi:[1,0]
	v_exp_f32_e32 v176, v176
	v_exp_f32_e32 v177, v177
	v_exp_f32_e32 v178, v178
	v_exp_f32_e32 v179, v179
	v_exp_f32_e32 v180, v180
	v_exp_f32_e32 v181, v181
	v_exp_f32_e32 v182, v182
	v_exp_f32_e32 v183, v183
	v_pk_add_f32 v[176:177], v[176:177], 1.0 op_sel_hi:[1,0]
	v_pk_add_f32 v[178:179], v[178:179], 1.0 op_sel_hi:[1,0]
	v_pk_add_f32 v[180:181], v[180:181], 1.0 op_sel_hi:[1,0]
	v_pk_add_f32 v[182:183], v[182:183], 1.0 op_sel_hi:[1,0]
	v_rcp_f32_e32 v176, v176
	v_rcp_f32_e32 v177, v177
	v_rcp_f32_e32 v178, v178
	v_rcp_f32_e32 v179, v179
	v_rcp_f32_e32 v180, v180
	v_rcp_f32_e32 v181, v181
	v_rcp_f32_e32 v182, v182
	v_rcp_f32_e32 v183, v183
	v_pk_mul_f32 v[160:161], v[160:161], v[176:177]
	v_pk_mul_f32 v[162:163], v[162:163], v[178:179]
	v_pk_mul_f32 v[164:165], v[164:165], v[180:181]
	v_pk_mul_f32 v[166:167], v[166:167], v[182:183]
	v_cvt_pk_f16_f32 v168, v160, v161
	v_cvt_pk_f16_f32 v169, v162, v163
	v_cvt_pk_f16_f32 v170, v164, v165
	v_cvt_pk_f16_f32 v171, v166, v167
	global_store_dwordx4 v20, v[168:171], s[32:33] offset:256
	v_pk_mul_f32 v[160:161], v[40:41], s[50:51] op_sel_hi:[1,0]
	v_pk_mul_f32 v[162:163], v[42:43], s[50:51] op_sel_hi:[1,0]
	v_pk_mul_f32 v[164:165], v[44:45], s[50:51] op_sel_hi:[1,0]
	v_pk_mul_f32 v[166:167], v[46:47], s[50:51] op_sel_hi:[1,0]
	v_pk_mul_f32 v[176:177], v[160:161], s[52:53] op_sel_hi:[1,0]
	v_pk_mul_f32 v[178:179], v[162:163], s[52:53] op_sel_hi:[1,0]
	v_pk_mul_f32 v[180:181], v[164:165], s[52:53] op_sel_hi:[1,0]
	v_pk_mul_f32 v[182:183], v[166:167], s[52:53] op_sel_hi:[1,0]
	v_exp_f32_e32 v176, v176
	v_exp_f32_e32 v177, v177
	v_exp_f32_e32 v178, v178
	v_exp_f32_e32 v179, v179
	v_exp_f32_e32 v180, v180
	v_exp_f32_e32 v181, v181
	v_exp_f32_e32 v182, v182
	v_exp_f32_e32 v183, v183
	v_pk_add_f32 v[176:177], v[176:177], 1.0 op_sel_hi:[1,0]
	v_pk_add_f32 v[178:179], v[178:179], 1.0 op_sel_hi:[1,0]
	v_pk_add_f32 v[180:181], v[180:181], 1.0 op_sel_hi:[1,0]
	v_pk_add_f32 v[182:183], v[182:183], 1.0 op_sel_hi:[1,0]
	v_rcp_f32_e32 v176, v176
	v_rcp_f32_e32 v177, v177
	v_rcp_f32_e32 v178, v178
	v_rcp_f32_e32 v179, v179
	v_rcp_f32_e32 v180, v180
	v_rcp_f32_e32 v181, v181
	v_rcp_f32_e32 v182, v182
	v_rcp_f32_e32 v183, v183
	v_pk_mul_f32 v[160:161], v[160:161], v[176:177]
	v_pk_mul_f32 v[162:163], v[162:163], v[178:179]
	v_pk_mul_f32 v[164:165], v[164:165], v[180:181]
	v_pk_mul_f32 v[166:167], v[166:167], v[182:183]
	v_cvt_pk_f16_f32 v172, v160, v161
	v_cvt_pk_f16_f32 v173, v162, v163
	v_cvt_pk_f16_f32 v174, v164, v165
	v_cvt_pk_f16_f32 v175, v166, v167
	global_store_dwordx4 v20, v[172:175], s[32:33] offset:320
	v_pk_mul_f32 v[160:161], v[48:49], s[50:51] op_sel_hi:[1,0]
	v_pk_mul_f32 v[162:163], v[50:51], s[50:51] op_sel_hi:[1,0]
	v_pk_mul_f32 v[164:165], v[52:53], s[50:51] op_sel_hi:[1,0]
	v_pk_mul_f32 v[166:167], v[54:55], s[50:51] op_sel_hi:[1,0]
	v_pk_mul_f32 v[176:177], v[160:161], s[52:53] op_sel_hi:[1,0]
	v_pk_mul_f32 v[178:179], v[162:163], s[52:53] op_sel_hi:[1,0]
	v_pk_mul_f32 v[180:181], v[164:165], s[52:53] op_sel_hi:[1,0]
	v_pk_mul_f32 v[182:183], v[166:167], s[52:53] op_sel_hi:[1,0]
	v_exp_f32_e32 v176, v176
	v_exp_f32_e32 v177, v177
	v_exp_f32_e32 v178, v178
	v_exp_f32_e32 v179, v179
	v_exp_f32_e32 v180, v180
	v_exp_f32_e32 v181, v181
	v_exp_f32_e32 v182, v182
	v_exp_f32_e32 v183, v183
	v_pk_add_f32 v[176:177], v[176:177], 1.0 op_sel_hi:[1,0]
	v_pk_add_f32 v[178:179], v[178:179], 1.0 op_sel_hi:[1,0]
	v_pk_add_f32 v[180:181], v[180:181], 1.0 op_sel_hi:[1,0]
	v_pk_add_f32 v[182:183], v[182:183], 1.0 op_sel_hi:[1,0]
	v_rcp_f32_e32 v176, v176
	v_rcp_f32_e32 v177, v177
	v_rcp_f32_e32 v178, v178
	v_rcp_f32_e32 v179, v179
	v_rcp_f32_e32 v180, v180
	v_rcp_f32_e32 v181, v181
	v_rcp_f32_e32 v182, v182
	v_rcp_f32_e32 v183, v183
	v_pk_mul_f32 v[160:161], v[160:161], v[176:177]
	v_pk_mul_f32 v[162:163], v[162:163], v[178:179]
	v_pk_mul_f32 v[164:165], v[164:165], v[180:181]
	v_pk_mul_f32 v[166:167], v[166:167], v[182:183]
	v_cvt_pk_f16_f32 v168, v160, v161
	v_cvt_pk_f16_f32 v169, v162, v163
	v_cvt_pk_f16_f32 v170, v164, v165
	v_cvt_pk_f16_f32 v171, v166, v167
	global_store_dwordx4 v21, v[168:171], s[32:33] offset:256
	v_pk_mul_f32 v[160:161], v[56:57], s[50:51] op_sel_hi:[1,0]
	v_pk_mul_f32 v[162:163], v[58:59], s[50:51] op_sel_hi:[1,0]
	v_pk_mul_f32 v[164:165], v[60:61], s[50:51] op_sel_hi:[1,0]
	v_pk_mul_f32 v[166:167], v[62:63], s[50:51] op_sel_hi:[1,0]
	v_pk_mul_f32 v[176:177], v[160:161], s[52:53] op_sel_hi:[1,0]
	v_pk_mul_f32 v[178:179], v[162:163], s[52:53] op_sel_hi:[1,0]
	v_pk_mul_f32 v[180:181], v[164:165], s[52:53] op_sel_hi:[1,0]
	v_pk_mul_f32 v[182:183], v[166:167], s[52:53] op_sel_hi:[1,0]
	v_exp_f32_e32 v176, v176
	v_exp_f32_e32 v177, v177
	v_exp_f32_e32 v178, v178
	v_exp_f32_e32 v179, v179
	v_exp_f32_e32 v180, v180
	v_exp_f32_e32 v181, v181
	v_exp_f32_e32 v182, v182
	v_exp_f32_e32 v183, v183
	v_pk_add_f32 v[176:177], v[176:177], 1.0 op_sel_hi:[1,0]
	v_pk_add_f32 v[178:179], v[178:179], 1.0 op_sel_hi:[1,0]
	v_pk_add_f32 v[180:181], v[180:181], 1.0 op_sel_hi:[1,0]
	v_pk_add_f32 v[182:183], v[182:183], 1.0 op_sel_hi:[1,0]
	v_rcp_f32_e32 v176, v176
	v_rcp_f32_e32 v177, v177
	v_rcp_f32_e32 v178, v178
	v_rcp_f32_e32 v179, v179
	v_rcp_f32_e32 v180, v180
	v_rcp_f32_e32 v181, v181
	v_rcp_f32_e32 v182, v182
	v_rcp_f32_e32 v183, v183
	v_pk_mul_f32 v[160:161], v[160:161], v[176:177]
	v_pk_mul_f32 v[162:163], v[162:163], v[178:179]
	v_pk_mul_f32 v[164:165], v[164:165], v[180:181]
	v_pk_mul_f32 v[166:167], v[166:167], v[182:183]
	v_cvt_pk_f16_f32 v172, v160, v161
	v_cvt_pk_f16_f32 v173, v162, v163
	v_cvt_pk_f16_f32 v174, v164, v165
	v_cvt_pk_f16_f32 v175, v166, v167
	global_store_dwordx4 v21, v[172:175], s[32:33] offset:320
	v_pk_mul_f32 v[160:161], v[64:65], s[50:51] op_sel_hi:[1,0]
	v_pk_mul_f32 v[162:163], v[66:67], s[50:51] op_sel_hi:[1,0]
	v_pk_mul_f32 v[164:165], v[68:69], s[50:51] op_sel_hi:[1,0]
	v_pk_mul_f32 v[166:167], v[70:71], s[50:51] op_sel_hi:[1,0]
	v_pk_mul_f32 v[176:177], v[160:161], s[52:53] op_sel_hi:[1,0]
	v_pk_mul_f32 v[178:179], v[162:163], s[52:53] op_sel_hi:[1,0]
	v_pk_mul_f32 v[180:181], v[164:165], s[52:53] op_sel_hi:[1,0]
	v_pk_mul_f32 v[182:183], v[166:167], s[52:53] op_sel_hi:[1,0]
	v_exp_f32_e32 v176, v176
	v_exp_f32_e32 v177, v177
	v_exp_f32_e32 v178, v178
	v_exp_f32_e32 v179, v179
	v_exp_f32_e32 v180, v180
	v_exp_f32_e32 v181, v181
	v_exp_f32_e32 v182, v182
	v_exp_f32_e32 v183, v183
	v_pk_add_f32 v[176:177], v[176:177], 1.0 op_sel_hi:[1,0]
	v_pk_add_f32 v[178:179], v[178:179], 1.0 op_sel_hi:[1,0]
	v_pk_add_f32 v[180:181], v[180:181], 1.0 op_sel_hi:[1,0]
	v_pk_add_f32 v[182:183], v[182:183], 1.0 op_sel_hi:[1,0]
	v_rcp_f32_e32 v176, v176
	v_rcp_f32_e32 v177, v177
	v_rcp_f32_e32 v178, v178
	v_rcp_f32_e32 v179, v179
	v_rcp_f32_e32 v180, v180
	v_rcp_f32_e32 v181, v181
	v_rcp_f32_e32 v182, v182
	v_rcp_f32_e32 v183, v183
	v_pk_mul_f32 v[160:161], v[160:161], v[176:177]
	v_pk_mul_f32 v[162:163], v[162:163], v[178:179]
	v_pk_mul_f32 v[164:165], v[164:165], v[180:181]
	v_pk_mul_f32 v[166:167], v[166:167], v[182:183]
	v_cvt_pk_f16_f32 v168, v160, v161
	v_cvt_pk_f16_f32 v169, v162, v163
	v_cvt_pk_f16_f32 v170, v164, v165
	v_cvt_pk_f16_f32 v171, v166, v167
	global_store_dwordx4 v22, v[168:171], s[32:33] offset:256
	v_pk_mul_f32 v[160:161], v[72:73], s[50:51] op_sel_hi:[1,0]
	v_pk_mul_f32 v[162:163], v[74:75], s[50:51] op_sel_hi:[1,0]
	v_pk_mul_f32 v[164:165], v[76:77], s[50:51] op_sel_hi:[1,0]
	v_pk_mul_f32 v[166:167], v[78:79], s[50:51] op_sel_hi:[1,0]
	v_pk_mul_f32 v[176:177], v[160:161], s[52:53] op_sel_hi:[1,0]
	v_pk_mul_f32 v[178:179], v[162:163], s[52:53] op_sel_hi:[1,0]
	v_pk_mul_f32 v[180:181], v[164:165], s[52:53] op_sel_hi:[1,0]
	v_pk_mul_f32 v[182:183], v[166:167], s[52:53] op_sel_hi:[1,0]
	v_exp_f32_e32 v176, v176
	v_exp_f32_e32 v177, v177
	v_exp_f32_e32 v178, v178
	v_exp_f32_e32 v179, v179
	v_exp_f32_e32 v180, v180
	v_exp_f32_e32 v181, v181
	v_exp_f32_e32 v182, v182
	v_exp_f32_e32 v183, v183
	v_pk_add_f32 v[176:177], v[176:177], 1.0 op_sel_hi:[1,0]
	v_pk_add_f32 v[178:179], v[178:179], 1.0 op_sel_hi:[1,0]
	v_pk_add_f32 v[180:181], v[180:181], 1.0 op_sel_hi:[1,0]
	v_pk_add_f32 v[182:183], v[182:183], 1.0 op_sel_hi:[1,0]
	v_rcp_f32_e32 v176, v176
	v_rcp_f32_e32 v177, v177
	v_rcp_f32_e32 v178, v178
	v_rcp_f32_e32 v179, v179
	v_rcp_f32_e32 v180, v180
	v_rcp_f32_e32 v181, v181
	v_rcp_f32_e32 v182, v182
	v_rcp_f32_e32 v183, v183
	v_pk_mul_f32 v[160:161], v[160:161], v[176:177]
	v_pk_mul_f32 v[162:163], v[162:163], v[178:179]
	v_pk_mul_f32 v[164:165], v[164:165], v[180:181]
	v_pk_mul_f32 v[166:167], v[166:167], v[182:183]
	v_cvt_pk_f16_f32 v172, v160, v161
	v_cvt_pk_f16_f32 v173, v162, v163
	v_cvt_pk_f16_f32 v174, v164, v165
	v_cvt_pk_f16_f32 v175, v166, v167
	global_store_dwordx4 v22, v[172:175], s[32:33] offset:320
	v_pk_mul_f32 v[160:161], v[80:81], s[50:51] op_sel_hi:[1,0]
	v_pk_mul_f32 v[162:163], v[82:83], s[50:51] op_sel_hi:[1,0]
	v_pk_mul_f32 v[164:165], v[84:85], s[50:51] op_sel_hi:[1,0]
	v_pk_mul_f32 v[166:167], v[86:87], s[50:51] op_sel_hi:[1,0]
	v_pk_mul_f32 v[176:177], v[160:161], s[52:53] op_sel_hi:[1,0]
	v_pk_mul_f32 v[178:179], v[162:163], s[52:53] op_sel_hi:[1,0]
	v_pk_mul_f32 v[180:181], v[164:165], s[52:53] op_sel_hi:[1,0]
	v_pk_mul_f32 v[182:183], v[166:167], s[52:53] op_sel_hi:[1,0]
	v_exp_f32_e32 v176, v176
	v_exp_f32_e32 v177, v177
	v_exp_f32_e32 v178, v178
	v_exp_f32_e32 v179, v179
	v_exp_f32_e32 v180, v180
	v_exp_f32_e32 v181, v181
	v_exp_f32_e32 v182, v182
	v_exp_f32_e32 v183, v183
	v_pk_add_f32 v[176:177], v[176:177], 1.0 op_sel_hi:[1,0]
	v_pk_add_f32 v[178:179], v[178:179], 1.0 op_sel_hi:[1,0]
	v_pk_add_f32 v[180:181], v[180:181], 1.0 op_sel_hi:[1,0]
	v_pk_add_f32 v[182:183], v[182:183], 1.0 op_sel_hi:[1,0]
	v_rcp_f32_e32 v176, v176
	v_rcp_f32_e32 v177, v177
	v_rcp_f32_e32 v178, v178
	v_rcp_f32_e32 v179, v179
	v_rcp_f32_e32 v180, v180
	v_rcp_f32_e32 v181, v181
	v_rcp_f32_e32 v182, v182
	v_rcp_f32_e32 v183, v183
	v_pk_mul_f32 v[160:161], v[160:161], v[176:177]
	v_pk_mul_f32 v[162:163], v[162:163], v[178:179]
	v_pk_mul_f32 v[164:165], v[164:165], v[180:181]
	v_pk_mul_f32 v[166:167], v[166:167], v[182:183]
	v_cvt_pk_f16_f32 v168, v160, v161
	v_cvt_pk_f16_f32 v169, v162, v163
	v_cvt_pk_f16_f32 v170, v164, v165
	v_cvt_pk_f16_f32 v171, v166, v167
	global_store_dwordx4 v23, v[168:171], s[32:33] offset:256
	v_pk_mul_f32 v[160:161], v[88:89], s[50:51] op_sel_hi:[1,0]
	v_pk_mul_f32 v[162:163], v[90:91], s[50:51] op_sel_hi:[1,0]
	v_pk_mul_f32 v[164:165], v[92:93], s[50:51] op_sel_hi:[1,0]
	v_pk_mul_f32 v[166:167], v[94:95], s[50:51] op_sel_hi:[1,0]
	v_pk_mul_f32 v[176:177], v[160:161], s[52:53] op_sel_hi:[1,0]
	v_pk_mul_f32 v[178:179], v[162:163], s[52:53] op_sel_hi:[1,0]
	v_pk_mul_f32 v[180:181], v[164:165], s[52:53] op_sel_hi:[1,0]
	v_pk_mul_f32 v[182:183], v[166:167], s[52:53] op_sel_hi:[1,0]
	v_exp_f32_e32 v176, v176
	v_exp_f32_e32 v177, v177
	v_exp_f32_e32 v178, v178
	v_exp_f32_e32 v179, v179
	v_exp_f32_e32 v180, v180
	v_exp_f32_e32 v181, v181
	v_exp_f32_e32 v182, v182
	v_exp_f32_e32 v183, v183
	v_pk_add_f32 v[176:177], v[176:177], 1.0 op_sel_hi:[1,0]
	v_pk_add_f32 v[178:179], v[178:179], 1.0 op_sel_hi:[1,0]
	v_pk_add_f32 v[180:181], v[180:181], 1.0 op_sel_hi:[1,0]
	v_pk_add_f32 v[182:183], v[182:183], 1.0 op_sel_hi:[1,0]
	v_rcp_f32_e32 v176, v176
	v_rcp_f32_e32 v177, v177
	v_rcp_f32_e32 v178, v178
	v_rcp_f32_e32 v179, v179
	v_rcp_f32_e32 v180, v180
	v_rcp_f32_e32 v181, v181
	v_rcp_f32_e32 v182, v182
	v_rcp_f32_e32 v183, v183
	v_pk_mul_f32 v[160:161], v[160:161], v[176:177]
	v_pk_mul_f32 v[162:163], v[162:163], v[178:179]
	v_pk_mul_f32 v[164:165], v[164:165], v[180:181]
	v_pk_mul_f32 v[166:167], v[166:167], v[182:183]
	v_cvt_pk_f16_f32 v172, v160, v161
	v_cvt_pk_f16_f32 v173, v162, v163
	v_cvt_pk_f16_f32 v174, v164, v165
	v_cvt_pk_f16_f32 v175, v166, v167
	global_store_dwordx4 v23, v[172:175], s[32:33] offset:320
	s_waitcnt lgkmcnt(0)
	v_mfma_f32_16x16x32_f16 v[32:35], v[112:115], v[96:99], 0
	ds_read_b128 v[128:131], v18
	v_mfma_f32_16x16x32_f16 v[36:39], v[116:119], v[96:99], 0
	ds_read_b128 v[144:147], v19 offset:32768
	v_mfma_f32_16x16x32_f16 v[40:43], v[120:123], v[96:99], 0
	ds_read_b128 v[148:151], v19 offset:34816
	v_mfma_f32_16x16x32_f16 v[44:47], v[124:127], v[96:99], 0
	ds_read_b128 v[152:155], v19 offset:36864
	v_mfma_f32_16x16x32_f16 v[48:51], v[112:115], v[100:103], 0
	ds_read_b128 v[156:159], v19 offset:38912
	v_mfma_f32_16x16x32_f16 v[52:55], v[116:119], v[100:103], 0
	ds_read_b128 v[132:135], v18 offset:2048
	v_mfma_f32_16x16x32_f16 v[56:59], v[120:123], v[100:103], 0
	ds_read_b128 v[136:139], v18 offset:4096
	v_mfma_f32_16x16x32_f16 v[60:63], v[124:127], v[100:103], 0
	ds_read_b128 v[140:143], v18 offset:6144
	v_mfma_f32_16x16x32_f16 v[64:67], v[112:115], v[104:107], 0
	v_mfma_f32_16x16x32_f16 v[68:71], v[116:119], v[104:107], 0
	v_mfma_f32_16x16x32_f16 v[72:75], v[120:123], v[104:107], 0
	s_add_u32 m0, s14, 0x12000
	s_nop 0
	global_load_lds_dwordx4 v5, s[28:29]
	v_mfma_f32_16x16x32_f16 v[76:79], v[124:127], v[104:107], 0
	v_mfma_f32_16x16x32_f16 v[80:83], v[112:115], v[108:111], 0
	s_add_u32 m0, s14, 0x14000
	s_nop 0
	global_load_lds_dwordx4 v6, s[30:31]
	v_mfma_f32_16x16x32_f16 v[84:87], v[116:119], v[108:111], 0
	v_mfma_f32_16x16x32_f16 v[88:91], v[120:123], v[108:111], 0
	s_add_u32 m0, s14, 0x16000
	s_nop 0
	global_load_lds_dwordx4 v7, s[30:31]
	v_mfma_f32_16x16x32_f16 v[92:95], v[124:127], v[108:111], 0
	s_waitcnt vmcnt(14) lgkmcnt(0)
	s_barrier
	s_add_u32 s28, s28, 0x80
	s_addc_u32 s29, s29, 0
	s_add_u32 s30, s30, 0x80
	s_addc_u32 s31, s31, 0
	s_waitcnt lgkmcnt(0)
	v_mfma_f32_16x16x32_f16 v[32:35], v[144:147], v[128:131], v[32:35]
	ds_read_b128 v[96:99], v8
	v_mfma_f32_16x16x32_f16 v[36:39], v[148:151], v[128:131], v[36:39]
	ds_read_b128 v[112:115], v9 offset:32768
	v_mfma_f32_16x16x32_f16 v[40:43], v[152:155], v[128:131], v[40:43]
	ds_read_b128 v[116:119], v9 offset:34816
	v_mfma_f32_16x16x32_f16 v[44:47], v[156:159], v[128:131], v[44:47]
	ds_read_b128 v[120:123], v9 offset:36864
	v_mfma_f32_16x16x32_f16 v[48:51], v[144:147], v[132:135], v[48:51]
	ds_read_b128 v[124:127], v9 offset:38912
	v_mfma_f32_16x16x32_f16 v[52:55], v[148:151], v[132:135], v[52:55]
	ds_read_b128 v[100:103], v8 offset:2048
	v_mfma_f32_16x16x32_f16 v[56:59], v[152:155], v[132:135], v[56:59]
	ds_read_b128 v[104:107], v8 offset:4096
	v_mfma_f32_16x16x32_f16 v[60:63], v[156:159], v[132:135], v[60:63]
	ds_read_b128 v[108:111], v8 offset:6144
	v_mfma_f32_16x16x32_f16 v[64:67], v[144:147], v[136:139], v[64:67]
	v_mfma_f32_16x16x32_f16 v[68:71], v[148:151], v[136:139], v[68:71]
	v_mfma_f32_16x16x32_f16 v[72:75], v[152:155], v[136:139], v[72:75]
	s_add_u32 m0, s14, 0x18000
	s_nop 0
	global_load_lds_dwordx4 v2, s[28:29]
	v_mfma_f32_16x16x32_f16 v[76:79], v[156:159], v[136:139], v[76:79]
	v_mfma_f32_16x16x32_f16 v[80:83], v[144:147], v[140:143], v[80:83]
	s_add_u32 m0, s14, 0x1a000
	s_nop 0
	global_load_lds_dwordx4 v3, s[28:29]
	v_mfma_f32_16x16x32_f16 v[84:87], v[148:151], v[140:143], v[84:87]
	v_mfma_f32_16x16x32_f16 v[88:91], v[152:155], v[140:143], v[88:91]
	s_add_u32 m0, s14, 0x1c000
	s_nop 0
	global_load_lds_dwordx4 v4, s[28:29]
	v_mfma_f32_16x16x32_f16 v[92:95], v[156:159], v[140:143], v[92:95]
	s_waitcnt lgkmcnt(0)
	v_mfma_f32_16x16x32_f16 v[32:35], v[112:115], v[96:99], v[32:35]
	ds_read_b128 v[128:131], v10
	v_mfma_f32_16x16x32_f16 v[36:39], v[116:119], v[96:99], v[36:39]
	ds_read_b128 v[144:147], v11 offset:32768
	v_mfma_f32_16x16x32_f16 v[40:43], v[120:123], v[96:99], v[40:43]
	ds_read_b128 v[148:151], v11 offset:34816
	v_mfma_f32_16x16x32_f16 v[44:47], v[124:127], v[96:99], v[44:47]
	ds_read_b128 v[152:155], v11 offset:36864
	v_mfma_f32_16x16x32_f16 v[48:51], v[112:115], v[100:103], v[48:51]
	ds_read_b128 v[156:159], v11 offset:38912
	v_mfma_f32_16x16x32_f16 v[52:55], v[116:119], v[100:103], v[52:55]
	ds_read_b128 v[132:135], v10 offset:2048
	v_mfma_f32_16x16x32_f16 v[56:59], v[120:123], v[100:103], v[56:59]
	ds_read_b128 v[136:139], v10 offset:4096
	v_mfma_f32_16x16x32_f16 v[60:63], v[124:127], v[100:103], v[60:63]
	ds_read_b128 v[140:143], v10 offset:6144
	v_mfma_f32_16x16x32_f16 v[64:67], v[112:115], v[104:107], v[64:67]
	v_mfma_f32_16x16x32_f16 v[68:71], v[116:119], v[104:107], v[68:71]
	v_mfma_f32_16x16x32_f16 v[72:75], v[120:123], v[104:107], v[72:75]
	s_add_u32 m0, s14, 0x1e000
	s_nop 0
	global_load_lds_dwordx4 v5, s[28:29]
	v_mfma_f32_16x16x32_f16 v[76:79], v[124:127], v[104:107], v[76:79]
	v_mfma_f32_16x16x32_f16 v[80:83], v[112:115], v[108:111], v[80:83]
	s_add_u32 m0, s14, 0x20000
	s_nop 0
	global_load_lds_dwordx4 v6, s[30:31]
	v_mfma_f32_16x16x32_f16 v[84:87], v[116:119], v[108:111], v[84:87]
	v_mfma_f32_16x16x32_f16 v[88:91], v[120:123], v[108:111], v[88:91]
	s_add_u32 m0, s14, 0x22000
	s_nop 0
	global_load_lds_dwordx4 v7, s[30:31]
	v_mfma_f32_16x16x32_f16 v[92:95], v[124:127], v[108:111], v[92:95]
	s_waitcnt vmcnt(6) lgkmcnt(0)
	s_barrier
	s_add_u32 s28, s28, 0x80
	s_addc_u32 s29, s29, 0
	s_add_u32 s30, s30, 0x80
	s_addc_u32 s31, s31, 0
	s_waitcnt lgkmcnt(0)
	v_mfma_f32_16x16x32_f16 v[32:35], v[144:147], v[128:131], v[32:35]
	ds_read_b128 v[96:99], v12
	v_mfma_f32_16x16x32_f16 v[36:39], v[148:151], v[128:131], v[36:39]
	ds_read_b128 v[112:115], v13 offset:32768
	v_mfma_f32_16x16x32_f16 v[40:43], v[152:155], v[128:131], v[40:43]
	ds_read_b128 v[116:119], v13 offset:34816
	v_mfma_f32_16x16x32_f16 v[44:47], v[156:159], v[128:131], v[44:47]
	ds_read_b128 v[120:123], v13 offset:36864
	v_mfma_f32_16x16x32_f16 v[48:51], v[144:147], v[132:135], v[48:51]
	ds_read_b128 v[124:127], v13 offset:38912
	v_mfma_f32_16x16x32_f16 v[52:55], v[148:151], v[132:135], v[52:55]
	ds_read_b128 v[100:103], v12 offset:2048
	v_mfma_f32_16x16x32_f16 v[56:59], v[152:155], v[132:135], v[56:59]
	ds_read_b128 v[104:107], v12 offset:4096
	v_mfma_f32_16x16x32_f16 v[60:63], v[156:159], v[132:135], v[60:63]
	ds_read_b128 v[108:111], v12 offset:6144
	v_mfma_f32_16x16x32_f16 v[64:67], v[144:147], v[136:139], v[64:67]
	v_mfma_f32_16x16x32_f16 v[68:71], v[148:151], v[136:139], v[68:71]
	v_mfma_f32_16x16x32_f16 v[72:75], v[152:155], v[136:139], v[72:75]
	s_add_u32 m0, s14, 0x0
	s_nop 0
	global_load_lds_dwordx4 v2, s[28:29]
	v_mfma_f32_16x16x32_f16 v[76:79], v[156:159], v[136:139], v[76:79]
	v_mfma_f32_16x16x32_f16 v[80:83], v[144:147], v[140:143], v[80:83]
	s_add_u32 m0, s14, 0x2000
	s_nop 0
	global_load_lds_dwordx4 v3, s[28:29]
	v_mfma_f32_16x16x32_f16 v[84:87], v[148:151], v[140:143], v[84:87]
	v_mfma_f32_16x16x32_f16 v[88:91], v[152:155], v[140:143], v[88:91]
	s_add_u32 m0, s14, 0x4000
	s_nop 0
	global_load_lds_dwordx4 v4, s[28:29]
	v_mfma_f32_16x16x32_f16 v[92:95], v[156:159], v[140:143], v[92:95]
	s_waitcnt lgkmcnt(0)
	v_mfma_f32_16x16x32_f16 v[32:35], v[112:115], v[96:99], v[32:35]
	ds_read_b128 v[128:131], v14
	v_mfma_f32_16x16x32_f16 v[36:39], v[116:119], v[96:99], v[36:39]
	ds_read_b128 v[144:147], v15 offset:32768
	v_mfma_f32_16x16x32_f16 v[40:43], v[120:123], v[96:99], v[40:43]
	ds_read_b128 v[148:151], v15 offset:34816
	v_mfma_f32_16x16x32_f16 v[44:47], v[124:127], v[96:99], v[44:47]
	ds_read_b128 v[152:155], v15 offset:36864
	v_mfma_f32_16x16x32_f16 v[48:51], v[112:115], v[100:103], v[48:51]
	ds_read_b128 v[156:159], v15 offset:38912
	v_mfma_f32_16x16x32_f16 v[52:55], v[116:119], v[100:103], v[52:55]
	ds_read_b128 v[132:135], v14 offset:2048
	v_mfma_f32_16x16x32_f16 v[56:59], v[120:123], v[100:103], v[56:59]
	ds_read_b128 v[136:139], v14 offset:4096
	v_mfma_f32_16x16x32_f16 v[60:63], v[124:127], v[100:103], v[60:63]
	ds_read_b128 v[140:143], v14 offset:6144
	v_mfma_f32_16x16x32_f16 v[64:67], v[112:115], v[104:107], v[64:67]
	v_mfma_f32_16x16x32_f16 v[68:71], v[116:119], v[104:107], v[68:71]
	v_mfma_f32_16x16x32_f16 v[72:75], v[120:123], v[104:107], v[72:75]
	s_add_u32 m0, s14, 0x6000
	s_nop 0
	global_load_lds_dwordx4 v5, s[28:29]
	v_mfma_f32_16x16x32_f16 v[76:79], v[124:127], v[104:107], v[76:79]
	v_mfma_f32_16x16x32_f16 v[80:83], v[112:115], v[108:111], v[80:83]
	s_add_u32 m0, s14, 0x8000
	s_nop 0
	global_load_lds_dwordx4 v6, s[30:31]
	v_mfma_f32_16x16x32_f16 v[84:87], v[116:119], v[108:111], v[84:87]
	v_mfma_f32_16x16x32_f16 v[88:91], v[120:123], v[108:111], v[88:91]
	s_add_u32 m0, s14, 0xa000
	s_nop 0
	global_load_lds_dwordx4 v7, s[30:31]
	v_mfma_f32_16x16x32_f16 v[92:95], v[124:127], v[108:111], v[92:95]
	s_waitcnt vmcnt(6) lgkmcnt(0)
	s_barrier
	s_add_u32 s28, s28, 0x80
	s_addc_u32 s29, s29, 0
	s_add_u32 s30, s30, 0x80
	s_addc_u32 s31, s31, 0
	s_waitcnt lgkmcnt(0)
	v_mfma_f32_16x16x32_f16 v[32:35], v[144:147], v[128:131], v[32:35]
	ds_read_b128 v[96:99], v16
	v_mfma_f32_16x16x32_f16 v[36:39], v[148:151], v[128:131], v[36:39]
	ds_read_b128 v[112:115], v17 offset:32768
	v_mfma_f32_16x16x32_f16 v[40:43], v[152:155], v[128:131], v[40:43]
	ds_read_b128 v[116:119], v17 offset:34816
	v_mfma_f32_16x16x32_f16 v[44:47], v[156:159], v[128:131], v[44:47]
	ds_read_b128 v[120:123], v17 offset:36864
	v_mfma_f32_16x16x32_f16 v[48:51], v[144:147], v[132:135], v[48:51]
	ds_read_b128 v[124:127], v17 offset:38912
	v_mfma_f32_16x16x32_f16 v[52:55], v[148:151], v[132:135], v[52:55]
	ds_read_b128 v[100:103], v16 offset:2048
	v_mfma_f32_16x16x32_f16 v[56:59], v[152:155], v[132:135], v[56:59]
	ds_read_b128 v[104:107], v16 offset:4096
	v_mfma_f32_16x16x32_f16 v[60:63], v[156:159], v[132:135], v[60:63]
	ds_read_b128 v[108:111], v16 offset:6144
	v_mfma_f32_16x16x32_f16 v[64:67], v[144:147], v[136:139], v[64:67]
	v_mfma_f32_16x16x32_f16 v[68:71], v[148:151], v[136:139], v[68:71]
	v_mfma_f32_16x16x32_f16 v[72:75], v[152:155], v[136:139], v[72:75]
	s_add_u32 m0, s14, 0xc000
	s_nop 0
	global_load_lds_dwordx4 v2, s[28:29]
	v_mfma_f32_16x16x32_f16 v[76:79], v[156:159], v[136:139], v[76:79]
	v_mfma_f32_16x16x32_f16 v[80:83], v[144:147], v[140:143], v[80:83]
	s_add_u32 m0, s14, 0xe000
	s_nop 0
	global_load_lds_dwordx4 v3, s[28:29]
	v_mfma_f32_16x16x32_f16 v[84:87], v[148:151], v[140:143], v[84:87]
	v_mfma_f32_16x16x32_f16 v[88:91], v[152:155], v[140:143], v[88:91]
	s_add_u32 m0, s14, 0x10000
	s_nop 0
	global_load_lds_dwordx4 v4, s[28:29]
	v_mfma_f32_16x16x32_f16 v[92:95], v[156:159], v[140:143], v[92:95]
	s_waitcnt lgkmcnt(0)
	v_mfma_f32_16x16x32_f16 v[32:35], v[112:115], v[96:99], v[32:35]
	ds_read_b128 v[128:131], v18
	v_mfma_f32_16x16x32_f16 v[36:39], v[116:119], v[96:99], v[36:39]
	ds_read_b128 v[144:147], v19 offset:32768
	v_mfma_f32_16x16x32_f16 v[40:43], v[120:123], v[96:99], v[40:43]
	ds_read_b128 v[148:151], v19 offset:34816
	v_mfma_f32_16x16x32_f16 v[44:47], v[124:127], v[96:99], v[44:47]
	ds_read_b128 v[152:155], v19 offset:36864
	v_mfma_f32_16x16x32_f16 v[48:51], v[112:115], v[100:103], v[48:51]
	ds_read_b128 v[156:159], v19 offset:38912
	v_mfma_f32_16x16x32_f16 v[52:55], v[116:119], v[100:103], v[52:55]
	ds_read_b128 v[132:135], v18 offset:2048
	v_mfma_f32_16x16x32_f16 v[56:59], v[120:123], v[100:103], v[56:59]
	ds_read_b128 v[136:139], v18 offset:4096
	v_mfma_f32_16x16x32_f16 v[60:63], v[124:127], v[100:103], v[60:63]
	ds_read_b128 v[140:143], v18 offset:6144
	v_mfma_f32_16x16x32_f16 v[64:67], v[112:115], v[104:107], v[64:67]
	v_mfma_f32_16x16x32_f16 v[68:71], v[116:119], v[104:107], v[68:71]
	v_mfma_f32_16x16x32_f16 v[72:75], v[120:123], v[104:107], v[72:75]
	s_add_u32 m0, s14, 0x12000
	s_nop 0
	global_load_lds_dwordx4 v5, s[28:29]
	v_mfma_f32_16x16x32_f16 v[76:79], v[124:127], v[104:107], v[76:79]
	v_mfma_f32_16x16x32_f16 v[80:83], v[112:115], v[108:111], v[80:83]
	s_add_u32 m0, s14, 0x14000
	s_nop 0
	global_load_lds_dwordx4 v6, s[30:31]
	v_mfma_f32_16x16x32_f16 v[84:87], v[116:119], v[108:111], v[84:87]
	v_mfma_f32_16x16x32_f16 v[88:91], v[120:123], v[108:111], v[88:91]
	s_add_u32 m0, s14, 0x16000
	s_nop 0
	global_load_lds_dwordx4 v7, s[30:31]
	v_mfma_f32_16x16x32_f16 v[92:95], v[124:127], v[108:111], v[92:95]
	s_waitcnt vmcnt(6) lgkmcnt(0)
	s_barrier
	s_add_u32 s28, s28, 0x80
	s_addc_u32 s29, s29, 0
	s_add_u32 s30, s30, 0x80
	s_addc_u32 s31, s31, 0
	s_waitcnt lgkmcnt(0)
	v_mfma_f32_16x16x32_f16 v[32:35], v[144:147], v[128:131], v[32:35]
	ds_read_b128 v[96:99], v8
	v_mfma_f32_16x16x32_f16 v[36:39], v[148:151], v[128:131], v[36:39]
	ds_read_b128 v[112:115], v9 offset:32768
	v_mfma_f32_16x16x32_f16 v[40:43], v[152:155], v[128:131], v[40:43]
	ds_read_b128 v[116:119], v9 offset:34816
	v_mfma_f32_16x16x32_f16 v[44:47], v[156:159], v[128:131], v[44:47]
	ds_read_b128 v[120:123], v9 offset:36864
	v_mfma_f32_16x16x32_f16 v[48:51], v[144:147], v[132:135], v[48:51]
	ds_read_b128 v[124:127], v9 offset:38912
	v_mfma_f32_16x16x32_f16 v[52:55], v[148:151], v[132:135], v[52:55]
	ds_read_b128 v[100:103], v8 offset:2048
	v_mfma_f32_16x16x32_f16 v[56:59], v[152:155], v[132:135], v[56:59]
	ds_read_b128 v[104:107], v8 offset:4096
	v_mfma_f32_16x16x32_f16 v[60:63], v[156:159], v[132:135], v[60:63]
	ds_read_b128 v[108:111], v8 offset:6144
	v_mfma_f32_16x16x32_f16 v[64:67], v[144:147], v[136:139], v[64:67]
	v_mfma_f32_16x16x32_f16 v[68:71], v[148:151], v[136:139], v[68:71]
	v_mfma_f32_16x16x32_f16 v[72:75], v[152:155], v[136:139], v[72:75]
	s_add_u32 m0, s14, 0x18000
	s_nop 0
	global_load_lds_dwordx4 v2, s[28:29]
	v_mfma_f32_16x16x32_f16 v[76:79], v[156:159], v[136:139], v[76:79]
	v_mfma_f32_16x16x32_f16 v[80:83], v[144:147], v[140:143], v[80:83]
	s_add_u32 m0, s14, 0x1a000
	s_nop 0
	global_load_lds_dwordx4 v3, s[28:29]
	v_mfma_f32_16x16x32_f16 v[84:87], v[148:151], v[140:143], v[84:87]
	v_mfma_f32_16x16x32_f16 v[88:91], v[152:155], v[140:143], v[88:91]
	s_add_u32 m0, s14, 0x1c000
	s_nop 0
	global_load_lds_dwordx4 v4, s[28:29]
	v_mfma_f32_16x16x32_f16 v[92:95], v[156:159], v[140:143], v[92:95]
	s_waitcnt lgkmcnt(0)
	v_mfma_f32_16x16x32_f16 v[32:35], v[112:115], v[96:99], v[32:35]
	ds_read_b128 v[128:131], v10
	v_mfma_f32_16x16x32_f16 v[36:39], v[116:119], v[96:99], v[36:39]
	ds_read_b128 v[144:147], v11 offset:32768
	v_mfma_f32_16x16x32_f16 v[40:43], v[120:123], v[96:99], v[40:43]
	ds_read_b128 v[148:151], v11 offset:34816
	v_mfma_f32_16x16x32_f16 v[44:47], v[124:127], v[96:99], v[44:47]
	ds_read_b128 v[152:155], v11 offset:36864
	v_mfma_f32_16x16x32_f16 v[48:51], v[112:115], v[100:103], v[48:51]
	ds_read_b128 v[156:159], v11 offset:38912
	v_mfma_f32_16x16x32_f16 v[52:55], v[116:119], v[100:103], v[52:55]
	ds_read_b128 v[132:135], v10 offset:2048
	v_mfma_f32_16x16x32_f16 v[56:59], v[120:123], v[100:103], v[56:59]
	ds_read_b128 v[136:139], v10 offset:4096
	v_mfma_f32_16x16x32_f16 v[60:63], v[124:127], v[100:103], v[60:63]
	ds_read_b128 v[140:143], v10 offset:6144
	v_mfma_f32_16x16x32_f16 v[64:67], v[112:115], v[104:107], v[64:67]
	v_mfma_f32_16x16x32_f16 v[68:71], v[116:119], v[104:107], v[68:71]
	v_mfma_f32_16x16x32_f16 v[72:75], v[120:123], v[104:107], v[72:75]
	s_add_u32 m0, s14, 0x1e000
	s_nop 0
	global_load_lds_dwordx4 v5, s[28:29]
	v_mfma_f32_16x16x32_f16 v[76:79], v[124:127], v[104:107], v[76:79]
	v_mfma_f32_16x16x32_f16 v[80:83], v[112:115], v[108:111], v[80:83]
	s_add_u32 m0, s14, 0x20000
	s_nop 0
	global_load_lds_dwordx4 v6, s[30:31]
	v_mfma_f32_16x16x32_f16 v[84:87], v[116:119], v[108:111], v[84:87]
	v_mfma_f32_16x16x32_f16 v[88:91], v[120:123], v[108:111], v[88:91]
	s_add_u32 m0, s14, 0x22000
	s_nop 0
	global_load_lds_dwordx4 v7, s[30:31]
	v_mfma_f32_16x16x32_f16 v[92:95], v[124:127], v[108:111], v[92:95]
	s_waitcnt vmcnt(6) lgkmcnt(0)
	s_barrier
	s_add_u32 s28, s28, 0x80
	s_addc_u32 s29, s29, 0
	s_add_u32 s30, s30, 0x80
	s_addc_u32 s31, s31, 0
	s_waitcnt lgkmcnt(0)
	v_mfma_f32_16x16x32_f16 v[32:35], v[144:147], v[128:131], v[32:35]
	ds_read_b128 v[96:99], v12
	v_mfma_f32_16x16x32_f16 v[36:39], v[148:151], v[128:131], v[36:39]
	ds_read_b128 v[112:115], v13 offset:32768
	v_mfma_f32_16x16x32_f16 v[40:43], v[152:155], v[128:131], v[40:43]
	ds_read_b128 v[116:119], v13 offset:34816
	v_mfma_f32_16x16x32_f16 v[44:47], v[156:159], v[128:131], v[44:47]
	ds_read_b128 v[120:123], v13 offset:36864
	v_mfma_f32_16x16x32_f16 v[48:51], v[144:147], v[132:135], v[48:51]
	ds_read_b128 v[124:127], v13 offset:38912
	v_mfma_f32_16x16x32_f16 v[52:55], v[148:151], v[132:135], v[52:55]
	ds_read_b128 v[100:103], v12 offset:2048
	v_mfma_f32_16x16x32_f16 v[56:59], v[152:155], v[132:135], v[56:59]
	ds_read_b128 v[104:107], v12 offset:4096
	v_mfma_f32_16x16x32_f16 v[60:63], v[156:159], v[132:135], v[60:63]
	ds_read_b128 v[108:111], v12 offset:6144
	v_mfma_f32_16x16x32_f16 v[64:67], v[144:147], v[136:139], v[64:67]
	v_mfma_f32_16x16x32_f16 v[68:71], v[148:151], v[136:139], v[68:71]
	v_mfma_f32_16x16x32_f16 v[72:75], v[152:155], v[136:139], v[72:75]
	s_add_u32 m0, s14, 0x0
	s_nop 0
	global_load_lds_dwordx4 v2, s[28:29]
	v_mfma_f32_16x16x32_f16 v[76:79], v[156:159], v[136:139], v[76:79]
	v_mfma_f32_16x16x32_f16 v[80:83], v[144:147], v[140:143], v[80:83]
	s_add_u32 m0, s14, 0x2000
	s_nop 0
	global_load_lds_dwordx4 v3, s[28:29]
	v_mfma_f32_16x16x32_f16 v[84:87], v[148:151], v[140:143], v[84:87]
	v_mfma_f32_16x16x32_f16 v[88:91], v[152:155], v[140:143], v[88:91]
	s_add_u32 m0, s14, 0x4000
	s_nop 0
	global_load_lds_dwordx4 v4, s[28:29]
	v_mfma_f32_16x16x32_f16 v[92:95], v[156:159], v[140:143], v[92:95]
	s_waitcnt lgkmcnt(0)
	v_mfma_f32_16x16x32_f16 v[32:35], v[112:115], v[96:99], v[32:35]
	ds_read_b128 v[128:131], v14
	v_mfma_f32_16x16x32_f16 v[36:39], v[116:119], v[96:99], v[36:39]
	ds_read_b128 v[144:147], v15 offset:32768
	v_mfma_f32_16x16x32_f16 v[40:43], v[120:123], v[96:99], v[40:43]
	ds_read_b128 v[148:151], v15 offset:34816
	v_mfma_f32_16x16x32_f16 v[44:47], v[124:127], v[96:99], v[44:47]
	ds_read_b128 v[152:155], v15 offset:36864
	v_mfma_f32_16x16x32_f16 v[48:51], v[112:115], v[100:103], v[48:51]
	ds_read_b128 v[156:159], v15 offset:38912
	v_mfma_f32_16x16x32_f16 v[52:55], v[116:119], v[100:103], v[52:55]
	ds_read_b128 v[132:135], v14 offset:2048
	v_mfma_f32_16x16x32_f16 v[56:59], v[120:123], v[100:103], v[56:59]
	ds_read_b128 v[136:139], v14 offset:4096
	v_mfma_f32_16x16x32_f16 v[60:63], v[124:127], v[100:103], v[60:63]
	ds_read_b128 v[140:143], v14 offset:6144
	v_mfma_f32_16x16x32_f16 v[64:67], v[112:115], v[104:107], v[64:67]
	v_mfma_f32_16x16x32_f16 v[68:71], v[116:119], v[104:107], v[68:71]
	v_mfma_f32_16x16x32_f16 v[72:75], v[120:123], v[104:107], v[72:75]
	s_add_u32 m0, s14, 0x6000
	s_nop 0
	global_load_lds_dwordx4 v5, s[28:29]
	v_mfma_f32_16x16x32_f16 v[76:79], v[124:127], v[104:107], v[76:79]
	v_mfma_f32_16x16x32_f16 v[80:83], v[112:115], v[108:111], v[80:83]
	s_add_u32 m0, s14, 0x8000
	s_nop 0
	global_load_lds_dwordx4 v6, s[30:31]
	v_mfma_f32_16x16x32_f16 v[84:87], v[116:119], v[108:111], v[84:87]
	v_mfma_f32_16x16x32_f16 v[88:91], v[120:123], v[108:111], v[88:91]
	s_add_u32 m0, s14, 0xa000
	s_nop 0
	global_load_lds_dwordx4 v7, s[30:31]
	v_mfma_f32_16x16x32_f16 v[92:95], v[124:127], v[108:111], v[92:95]
	s_waitcnt vmcnt(6) lgkmcnt(0)
	s_barrier
	s_add_u32 s28, s28, 0x80
	s_addc_u32 s29, s29, 0
	s_add_u32 s30, s30, 0x80
	s_addc_u32 s31, s31, 0
	s_waitcnt lgkmcnt(0)
	v_mfma_f32_16x16x32_f16 v[32:35], v[144:147], v[128:131], v[32:35]
	ds_read_b128 v[96:99], v16
	v_mfma_f32_16x16x32_f16 v[36:39], v[148:151], v[128:131], v[36:39]
	ds_read_b128 v[112:115], v17 offset:32768
	v_mfma_f32_16x16x32_f16 v[40:43], v[152:155], v[128:131], v[40:43]
	ds_read_b128 v[116:119], v17 offset:34816
	v_mfma_f32_16x16x32_f16 v[44:47], v[156:159], v[128:131], v[44:47]
	ds_read_b128 v[120:123], v17 offset:36864
	v_mfma_f32_16x16x32_f16 v[48:51], v[144:147], v[132:135], v[48:51]
	ds_read_b128 v[124:127], v17 offset:38912
	v_mfma_f32_16x16x32_f16 v[52:55], v[148:151], v[132:135], v[52:55]
	ds_read_b128 v[100:103], v16 offset:2048
	v_mfma_f32_16x16x32_f16 v[56:59], v[152:155], v[132:135], v[56:59]
	ds_read_b128 v[104:107], v16 offset:4096
	v_mfma_f32_16x16x32_f16 v[60:63], v[156:159], v[132:135], v[60:63]
	ds_read_b128 v[108:111], v16 offset:6144
	v_mfma_f32_16x16x32_f16 v[64:67], v[144:147], v[136:139], v[64:67]
	v_mfma_f32_16x16x32_f16 v[68:71], v[148:151], v[136:139], v[68:71]
	v_mfma_f32_16x16x32_f16 v[72:75], v[152:155], v[136:139], v[72:75]
	s_add_u32 m0, s14, 0xc000
	s_nop 0
	global_load_lds_dwordx4 v2, s[28:29]
	v_mfma_f32_16x16x32_f16 v[76:79], v[156:159], v[136:139], v[76:79]
	v_mfma_f32_16x16x32_f16 v[80:83], v[144:147], v[140:143], v[80:83]
	s_add_u32 m0, s14, 0xe000
	s_nop 0
	global_load_lds_dwordx4 v3, s[28:29]
	v_mfma_f32_16x16x32_f16 v[84:87], v[148:151], v[140:143], v[84:87]
	v_mfma_f32_16x16x32_f16 v[88:91], v[152:155], v[140:143], v[88:91]
	s_add_u32 m0, s14, 0x10000
	s_nop 0
	global_load_lds_dwordx4 v4, s[28:29]
	v_mfma_f32_16x16x32_f16 v[92:95], v[156:159], v[140:143], v[92:95]
	s_waitcnt lgkmcnt(0)
	v_mfma_f32_16x16x32_f16 v[32:35], v[112:115], v[96:99], v[32:35]
	ds_read_b128 v[128:131], v18
	v_mfma_f32_16x16x32_f16 v[36:39], v[116:119], v[96:99], v[36:39]
	ds_read_b128 v[144:147], v19 offset:32768
	v_mfma_f32_16x16x32_f16 v[40:43], v[120:123], v[96:99], v[40:43]
	ds_read_b128 v[148:151], v19 offset:34816
	v_mfma_f32_16x16x32_f16 v[44:47], v[124:127], v[96:99], v[44:47]
	ds_read_b128 v[152:155], v19 offset:36864
	v_mfma_f32_16x16x32_f16 v[48:51], v[112:115], v[100:103], v[48:51]
	ds_read_b128 v[156:159], v19 offset:38912
	v_mfma_f32_16x16x32_f16 v[52:55], v[116:119], v[100:103], v[52:55]
	ds_read_b128 v[132:135], v18 offset:2048
	v_mfma_f32_16x16x32_f16 v[56:59], v[120:123], v[100:103], v[56:59]
	ds_read_b128 v[136:139], v18 offset:4096
	v_mfma_f32_16x16x32_f16 v[60:63], v[124:127], v[100:103], v[60:63]
	ds_read_b128 v[140:143], v18 offset:6144
	v_mfma_f32_16x16x32_f16 v[64:67], v[112:115], v[104:107], v[64:67]
	v_mfma_f32_16x16x32_f16 v[68:71], v[116:119], v[104:107], v[68:71]
	v_mfma_f32_16x16x32_f16 v[72:75], v[120:123], v[104:107], v[72:75]
	s_add_u32 m0, s14, 0x12000
	s_nop 0
	global_load_lds_dwordx4 v5, s[28:29]
	v_mfma_f32_16x16x32_f16 v[76:79], v[124:127], v[104:107], v[76:79]
	v_mfma_f32_16x16x32_f16 v[80:83], v[112:115], v[108:111], v[80:83]
	s_add_u32 m0, s14, 0x14000
	s_nop 0
	global_load_lds_dwordx4 v6, s[30:31]
	v_mfma_f32_16x16x32_f16 v[84:87], v[116:119], v[108:111], v[84:87]
	v_mfma_f32_16x16x32_f16 v[88:91], v[120:123], v[108:111], v[88:91]
	s_add_u32 m0, s14, 0x16000
	s_nop 0
	global_load_lds_dwordx4 v7, s[30:31]
	v_mfma_f32_16x16x32_f16 v[92:95], v[124:127], v[108:111], v[92:95]
	s_waitcnt vmcnt(6) lgkmcnt(0)
	s_barrier
	s_add_u32 s28, s28, 0x80
	s_addc_u32 s29, s29, 0
	s_add_u32 s30, s30, 0x80
	s_addc_u32 s31, s31, 0
	s_waitcnt lgkmcnt(0)
	v_mfma_f32_16x16x32_f16 v[32:35], v[144:147], v[128:131], v[32:35]
	ds_read_b128 v[96:99], v8
	v_mfma_f32_16x16x32_f16 v[36:39], v[148:151], v[128:131], v[36:39]
	ds_read_b128 v[112:115], v9 offset:32768
	v_mfma_f32_16x16x32_f16 v[40:43], v[152:155], v[128:131], v[40:43]
	ds_read_b128 v[116:119], v9 offset:34816
	v_mfma_f32_16x16x32_f16 v[44:47], v[156:159], v[128:131], v[44:47]
	ds_read_b128 v[120:123], v9 offset:36864
	v_mfma_f32_16x16x32_f16 v[48:51], v[144:147], v[132:135], v[48:51]
	ds_read_b128 v[124:127], v9 offset:38912
	v_mfma_f32_16x16x32_f16 v[52:55], v[148:151], v[132:135], v[52:55]
	ds_read_b128 v[100:103], v8 offset:2048
	v_mfma_f32_16x16x32_f16 v[56:59], v[152:155], v[132:135], v[56:59]
	ds_read_b128 v[104:107], v8 offset:4096
	v_mfma_f32_16x16x32_f16 v[60:63], v[156:159], v[132:135], v[60:63]
	ds_read_b128 v[108:111], v8 offset:6144
	v_mfma_f32_16x16x32_f16 v[64:67], v[144:147], v[136:139], v[64:67]
	v_mfma_f32_16x16x32_f16 v[68:71], v[148:151], v[136:139], v[68:71]
	v_mfma_f32_16x16x32_f16 v[72:75], v[152:155], v[136:139], v[72:75]
	s_add_u32 m0, s14, 0x18000
	s_nop 0
	global_load_lds_dwordx4 v2, s[28:29]
	v_mfma_f32_16x16x32_f16 v[76:79], v[156:159], v[136:139], v[76:79]
	v_mfma_f32_16x16x32_f16 v[80:83], v[144:147], v[140:143], v[80:83]
	s_add_u32 m0, s14, 0x1a000
	s_nop 0
	global_load_lds_dwordx4 v3, s[28:29]
	v_mfma_f32_16x16x32_f16 v[84:87], v[148:151], v[140:143], v[84:87]
	v_mfma_f32_16x16x32_f16 v[88:91], v[152:155], v[140:143], v[88:91]
	s_add_u32 m0, s14, 0x1c000
	s_nop 0
	global_load_lds_dwordx4 v4, s[28:29]
	v_mfma_f32_16x16x32_f16 v[92:95], v[156:159], v[140:143], v[92:95]
	s_waitcnt lgkmcnt(0)
	v_mfma_f32_16x16x32_f16 v[32:35], v[112:115], v[96:99], v[32:35]
	ds_read_b128 v[128:131], v10
	v_mfma_f32_16x16x32_f16 v[36:39], v[116:119], v[96:99], v[36:39]
	ds_read_b128 v[144:147], v11 offset:32768
	v_mfma_f32_16x16x32_f16 v[40:43], v[120:123], v[96:99], v[40:43]
	ds_read_b128 v[148:151], v11 offset:34816
	v_mfma_f32_16x16x32_f16 v[44:47], v[124:127], v[96:99], v[44:47]
	ds_read_b128 v[152:155], v11 offset:36864
	v_mfma_f32_16x16x32_f16 v[48:51], v[112:115], v[100:103], v[48:51]
	ds_read_b128 v[156:159], v11 offset:38912
	v_mfma_f32_16x16x32_f16 v[52:55], v[116:119], v[100:103], v[52:55]
	ds_read_b128 v[132:135], v10 offset:2048
	v_mfma_f32_16x16x32_f16 v[56:59], v[120:123], v[100:103], v[56:59]
	ds_read_b128 v[136:139], v10 offset:4096
	v_mfma_f32_16x16x32_f16 v[60:63], v[124:127], v[100:103], v[60:63]
	ds_read_b128 v[140:143], v10 offset:6144
	v_mfma_f32_16x16x32_f16 v[64:67], v[112:115], v[104:107], v[64:67]
	v_mfma_f32_16x16x32_f16 v[68:71], v[116:119], v[104:107], v[68:71]
	v_mfma_f32_16x16x32_f16 v[72:75], v[120:123], v[104:107], v[72:75]
	s_add_u32 m0, s14, 0x1e000
	s_nop 0
	global_load_lds_dwordx4 v5, s[28:29]
	v_mfma_f32_16x16x32_f16 v[76:79], v[124:127], v[104:107], v[76:79]
	v_mfma_f32_16x16x32_f16 v[80:83], v[112:115], v[108:111], v[80:83]
	s_add_u32 m0, s14, 0x20000
	s_nop 0
	global_load_lds_dwordx4 v6, s[30:31]
	v_mfma_f32_16x16x32_f16 v[84:87], v[116:119], v[108:111], v[84:87]
	v_mfma_f32_16x16x32_f16 v[88:91], v[120:123], v[108:111], v[88:91]
	s_add_u32 m0, s14, 0x22000
	s_nop 0
	global_load_lds_dwordx4 v7, s[30:31]
	v_mfma_f32_16x16x32_f16 v[92:95], v[124:127], v[108:111], v[92:95]
	s_waitcnt vmcnt(6) lgkmcnt(0)
	s_barrier
	s_add_u32 s28, s28, 0x80
	s_addc_u32 s29, s29, 0
	s_add_u32 s30, s30, 0x80
	s_addc_u32 s31, s31, 0
	s_waitcnt lgkmcnt(0)
	v_mfma_f32_16x16x32_f16 v[32:35], v[144:147], v[128:131], v[32:35]
	ds_read_b128 v[96:99], v12
	v_mfma_f32_16x16x32_f16 v[36:39], v[148:151], v[128:131], v[36:39]
	ds_read_b128 v[112:115], v13 offset:32768
	v_mfma_f32_16x16x32_f16 v[40:43], v[152:155], v[128:131], v[40:43]
	ds_read_b128 v[116:119], v13 offset:34816
	v_mfma_f32_16x16x32_f16 v[44:47], v[156:159], v[128:131], v[44:47]
	ds_read_b128 v[120:123], v13 offset:36864
	v_mfma_f32_16x16x32_f16 v[48:51], v[144:147], v[132:135], v[48:51]
	ds_read_b128 v[124:127], v13 offset:38912
	v_mfma_f32_16x16x32_f16 v[52:55], v[148:151], v[132:135], v[52:55]
	ds_read_b128 v[100:103], v12 offset:2048
	v_mfma_f32_16x16x32_f16 v[56:59], v[152:155], v[132:135], v[56:59]
	ds_read_b128 v[104:107], v12 offset:4096
	v_mfma_f32_16x16x32_f16 v[60:63], v[156:159], v[132:135], v[60:63]
	ds_read_b128 v[108:111], v12 offset:6144
	v_mfma_f32_16x16x32_f16 v[64:67], v[144:147], v[136:139], v[64:67]
	v_mfma_f32_16x16x32_f16 v[68:71], v[148:151], v[136:139], v[68:71]
	v_mfma_f32_16x16x32_f16 v[72:75], v[152:155], v[136:139], v[72:75]
	s_add_u32 m0, s14, 0x0
	s_nop 0
	global_load_lds_dwordx4 v2, s[28:29]
	v_mfma_f32_16x16x32_f16 v[76:79], v[156:159], v[136:139], v[76:79]
	v_mfma_f32_16x16x32_f16 v[80:83], v[144:147], v[140:143], v[80:83]
	s_add_u32 m0, s14, 0x2000
	s_nop 0
	global_load_lds_dwordx4 v3, s[28:29]
	v_mfma_f32_16x16x32_f16 v[84:87], v[148:151], v[140:143], v[84:87]
	v_mfma_f32_16x16x32_f16 v[88:91], v[152:155], v[140:143], v[88:91]
	s_add_u32 m0, s14, 0x4000
	s_nop 0
	global_load_lds_dwordx4 v4, s[28:29]
	v_mfma_f32_16x16x32_f16 v[92:95], v[156:159], v[140:143], v[92:95]
	s_waitcnt lgkmcnt(0)
	v_mfma_f32_16x16x32_f16 v[32:35], v[112:115], v[96:99], v[32:35]
	ds_read_b128 v[128:131], v14
	v_mfma_f32_16x16x32_f16 v[36:39], v[116:119], v[96:99], v[36:39]
	ds_read_b128 v[144:147], v15 offset:32768
	v_mfma_f32_16x16x32_f16 v[40:43], v[120:123], v[96:99], v[40:43]
	ds_read_b128 v[148:151], v15 offset:34816
	v_mfma_f32_16x16x32_f16 v[44:47], v[124:127], v[96:99], v[44:47]
	ds_read_b128 v[152:155], v15 offset:36864
	v_mfma_f32_16x16x32_f16 v[48:51], v[112:115], v[100:103], v[48:51]
	ds_read_b128 v[156:159], v15 offset:38912
	v_mfma_f32_16x16x32_f16 v[52:55], v[116:119], v[100:103], v[52:55]
	ds_read_b128 v[132:135], v14 offset:2048
	v_mfma_f32_16x16x32_f16 v[56:59], v[120:123], v[100:103], v[56:59]
	ds_read_b128 v[136:139], v14 offset:4096
	v_mfma_f32_16x16x32_f16 v[60:63], v[124:127], v[100:103], v[60:63]
	ds_read_b128 v[140:143], v14 offset:6144
	v_mfma_f32_16x16x32_f16 v[64:67], v[112:115], v[104:107], v[64:67]
	v_mfma_f32_16x16x32_f16 v[68:71], v[116:119], v[104:107], v[68:71]
	v_mfma_f32_16x16x32_f16 v[72:75], v[120:123], v[104:107], v[72:75]
	s_add_u32 m0, s14, 0x6000
	s_nop 0
	global_load_lds_dwordx4 v5, s[28:29]
	v_mfma_f32_16x16x32_f16 v[76:79], v[124:127], v[104:107], v[76:79]
	v_mfma_f32_16x16x32_f16 v[80:83], v[112:115], v[108:111], v[80:83]
	s_add_u32 m0, s14, 0x8000
	s_nop 0
	global_load_lds_dwordx4 v6, s[30:31]
	v_mfma_f32_16x16x32_f16 v[84:87], v[116:119], v[108:111], v[84:87]
	v_mfma_f32_16x16x32_f16 v[88:91], v[120:123], v[108:111], v[88:91]
	s_add_u32 m0, s14, 0xa000
	s_nop 0
	global_load_lds_dwordx4 v7, s[30:31]
	v_mfma_f32_16x16x32_f16 v[92:95], v[124:127], v[108:111], v[92:95]
	s_waitcnt vmcnt(6) lgkmcnt(0)
	s_barrier
	s_add_u32 s28, s28, 0x80
	s_addc_u32 s29, s29, 0
	s_add_u32 s30, s30, 0x80
	s_addc_u32 s31, s31, 0
	s_waitcnt lgkmcnt(0)
	v_mfma_f32_16x16x32_f16 v[32:35], v[144:147], v[128:131], v[32:35]
	ds_read_b128 v[96:99], v16
	v_mfma_f32_16x16x32_f16 v[36:39], v[148:151], v[128:131], v[36:39]
	ds_read_b128 v[112:115], v17 offset:32768
	v_mfma_f32_16x16x32_f16 v[40:43], v[152:155], v[128:131], v[40:43]
	ds_read_b128 v[116:119], v17 offset:34816
	v_mfma_f32_16x16x32_f16 v[44:47], v[156:159], v[128:131], v[44:47]
	ds_read_b128 v[120:123], v17 offset:36864
	v_mfma_f32_16x16x32_f16 v[48:51], v[144:147], v[132:135], v[48:51]
	ds_read_b128 v[124:127], v17 offset:38912
	v_mfma_f32_16x16x32_f16 v[52:55], v[148:151], v[132:135], v[52:55]
	ds_read_b128 v[100:103], v16 offset:2048
	v_mfma_f32_16x16x32_f16 v[56:59], v[152:155], v[132:135], v[56:59]
	ds_read_b128 v[104:107], v16 offset:4096
	v_mfma_f32_16x16x32_f16 v[60:63], v[156:159], v[132:135], v[60:63]
	ds_read_b128 v[108:111], v16 offset:6144
	v_mfma_f32_16x16x32_f16 v[64:67], v[144:147], v[136:139], v[64:67]
	v_mfma_f32_16x16x32_f16 v[68:71], v[148:151], v[136:139], v[68:71]
	v_mfma_f32_16x16x32_f16 v[72:75], v[152:155], v[136:139], v[72:75]
	s_add_u32 m0, s14, 0xc000
	s_nop 0
	global_load_lds_dwordx4 v2, s[28:29]
	v_mfma_f32_16x16x32_f16 v[76:79], v[156:159], v[136:139], v[76:79]
	v_mfma_f32_16x16x32_f16 v[80:83], v[144:147], v[140:143], v[80:83]
	s_add_u32 m0, s14, 0xe000
	s_nop 0
	global_load_lds_dwordx4 v3, s[28:29]
	v_mfma_f32_16x16x32_f16 v[84:87], v[148:151], v[140:143], v[84:87]
	v_mfma_f32_16x16x32_f16 v[88:91], v[152:155], v[140:143], v[88:91]
	s_add_u32 m0, s14, 0x10000
	s_nop 0
	global_load_lds_dwordx4 v4, s[28:29]
	v_mfma_f32_16x16x32_f16 v[92:95], v[156:159], v[140:143], v[92:95]
	s_waitcnt lgkmcnt(0)
	v_mfma_f32_16x16x32_f16 v[32:35], v[112:115], v[96:99], v[32:35]
	ds_read_b128 v[128:131], v18
	v_mfma_f32_16x16x32_f16 v[36:39], v[116:119], v[96:99], v[36:39]
	ds_read_b128 v[144:147], v19 offset:32768
	v_mfma_f32_16x16x32_f16 v[40:43], v[120:123], v[96:99], v[40:43]
	ds_read_b128 v[148:151], v19 offset:34816
	v_mfma_f32_16x16x32_f16 v[44:47], v[124:127], v[96:99], v[44:47]
	ds_read_b128 v[152:155], v19 offset:36864
	v_mfma_f32_16x16x32_f16 v[48:51], v[112:115], v[100:103], v[48:51]
	ds_read_b128 v[156:159], v19 offset:38912
	v_mfma_f32_16x16x32_f16 v[52:55], v[116:119], v[100:103], v[52:55]
	ds_read_b128 v[132:135], v18 offset:2048
	v_mfma_f32_16x16x32_f16 v[56:59], v[120:123], v[100:103], v[56:59]
	ds_read_b128 v[136:139], v18 offset:4096
	v_mfma_f32_16x16x32_f16 v[60:63], v[124:127], v[100:103], v[60:63]
	ds_read_b128 v[140:143], v18 offset:6144
	v_mfma_f32_16x16x32_f16 v[64:67], v[112:115], v[104:107], v[64:67]
	v_mfma_f32_16x16x32_f16 v[68:71], v[116:119], v[104:107], v[68:71]
	v_mfma_f32_16x16x32_f16 v[72:75], v[120:123], v[104:107], v[72:75]
	s_add_u32 m0, s14, 0x12000
	s_nop 0
	global_load_lds_dwordx4 v5, s[28:29]
	v_mfma_f32_16x16x32_f16 v[76:79], v[124:127], v[104:107], v[76:79]
	v_mfma_f32_16x16x32_f16 v[80:83], v[112:115], v[108:111], v[80:83]
	s_add_u32 m0, s14, 0x14000
	s_nop 0
	global_load_lds_dwordx4 v6, s[30:31]
	v_mfma_f32_16x16x32_f16 v[84:87], v[116:119], v[108:111], v[84:87]
	v_mfma_f32_16x16x32_f16 v[88:91], v[120:123], v[108:111], v[88:91]
	s_add_u32 m0, s14, 0x16000
	s_nop 0
	global_load_lds_dwordx4 v7, s[30:31]
	v_mfma_f32_16x16x32_f16 v[92:95], v[124:127], v[108:111], v[92:95]
	s_waitcnt vmcnt(6) lgkmcnt(0)
	s_barrier
	s_add_u32 s28, s28, 0x80
	s_addc_u32 s29, s29, 0
	s_add_u32 s30, s30, 0x80
	s_addc_u32 s31, s31, 0
	s_waitcnt lgkmcnt(0)
	v_mfma_f32_16x16x32_f16 v[32:35], v[144:147], v[128:131], v[32:35]
	ds_read_b128 v[96:99], v8
	v_mfma_f32_16x16x32_f16 v[36:39], v[148:151], v[128:131], v[36:39]
	ds_read_b128 v[112:115], v9 offset:32768
	v_mfma_f32_16x16x32_f16 v[40:43], v[152:155], v[128:131], v[40:43]
	ds_read_b128 v[116:119], v9 offset:34816
	v_mfma_f32_16x16x32_f16 v[44:47], v[156:159], v[128:131], v[44:47]
	ds_read_b128 v[120:123], v9 offset:36864
	v_mfma_f32_16x16x32_f16 v[48:51], v[144:147], v[132:135], v[48:51]
	ds_read_b128 v[124:127], v9 offset:38912
	v_mfma_f32_16x16x32_f16 v[52:55], v[148:151], v[132:135], v[52:55]
	ds_read_b128 v[100:103], v8 offset:2048
	v_mfma_f32_16x16x32_f16 v[56:59], v[152:155], v[132:135], v[56:59]
	ds_read_b128 v[104:107], v8 offset:4096
	v_mfma_f32_16x16x32_f16 v[60:63], v[156:159], v[132:135], v[60:63]
	ds_read_b128 v[108:111], v8 offset:6144
	v_mfma_f32_16x16x32_f16 v[64:67], v[144:147], v[136:139], v[64:67]
	v_mfma_f32_16x16x32_f16 v[68:71], v[148:151], v[136:139], v[68:71]
	v_mfma_f32_16x16x32_f16 v[72:75], v[152:155], v[136:139], v[72:75]
	s_add_u32 m0, s14, 0x18000
	s_nop 0
	global_load_lds_dwordx4 v2, s[28:29]
	v_mfma_f32_16x16x32_f16 v[76:79], v[156:159], v[136:139], v[76:79]
	v_mfma_f32_16x16x32_f16 v[80:83], v[144:147], v[140:143], v[80:83]
	s_add_u32 m0, s14, 0x1a000
	s_nop 0
	global_load_lds_dwordx4 v3, s[28:29]
	v_mfma_f32_16x16x32_f16 v[84:87], v[148:151], v[140:143], v[84:87]
	v_mfma_f32_16x16x32_f16 v[88:91], v[152:155], v[140:143], v[88:91]
	s_add_u32 m0, s14, 0x1c000
	s_nop 0
	global_load_lds_dwordx4 v4, s[28:29]
	v_mfma_f32_16x16x32_f16 v[92:95], v[156:159], v[140:143], v[92:95]
	s_waitcnt lgkmcnt(0)
	v_mfma_f32_16x16x32_f16 v[32:35], v[112:115], v[96:99], v[32:35]
	ds_read_b128 v[128:131], v10
	v_mfma_f32_16x16x32_f16 v[36:39], v[116:119], v[96:99], v[36:39]
	ds_read_b128 v[144:147], v11 offset:32768
	v_mfma_f32_16x16x32_f16 v[40:43], v[120:123], v[96:99], v[40:43]
	ds_read_b128 v[148:151], v11 offset:34816
	v_mfma_f32_16x16x32_f16 v[44:47], v[124:127], v[96:99], v[44:47]
	ds_read_b128 v[152:155], v11 offset:36864
	v_mfma_f32_16x16x32_f16 v[48:51], v[112:115], v[100:103], v[48:51]
	ds_read_b128 v[156:159], v11 offset:38912
	v_mfma_f32_16x16x32_f16 v[52:55], v[116:119], v[100:103], v[52:55]
	ds_read_b128 v[132:135], v10 offset:2048
	v_mfma_f32_16x16x32_f16 v[56:59], v[120:123], v[100:103], v[56:59]
	ds_read_b128 v[136:139], v10 offset:4096
	v_mfma_f32_16x16x32_f16 v[60:63], v[124:127], v[100:103], v[60:63]
	ds_read_b128 v[140:143], v10 offset:6144
	v_mfma_f32_16x16x32_f16 v[64:67], v[112:115], v[104:107], v[64:67]
	v_mfma_f32_16x16x32_f16 v[68:71], v[116:119], v[104:107], v[68:71]
	v_mfma_f32_16x16x32_f16 v[72:75], v[120:123], v[104:107], v[72:75]
	s_add_u32 m0, s14, 0x1e000
	s_nop 0
	global_load_lds_dwordx4 v5, s[28:29]
	v_mfma_f32_16x16x32_f16 v[76:79], v[124:127], v[104:107], v[76:79]
	v_mfma_f32_16x16x32_f16 v[80:83], v[112:115], v[108:111], v[80:83]
	s_add_u32 m0, s14, 0x20000
	s_nop 0
	global_load_lds_dwordx4 v6, s[30:31]
	v_mfma_f32_16x16x32_f16 v[84:87], v[116:119], v[108:111], v[84:87]
	v_mfma_f32_16x16x32_f16 v[88:91], v[120:123], v[108:111], v[88:91]
	s_add_u32 m0, s14, 0x22000
	s_nop 0
	global_load_lds_dwordx4 v7, s[30:31]
	v_mfma_f32_16x16x32_f16 v[92:95], v[124:127], v[108:111], v[92:95]
	s_waitcnt vmcnt(6) lgkmcnt(0)
	s_barrier
	s_add_u32 s28, s28, 0x80
	s_addc_u32 s29, s29, 0
	s_add_u32 s30, s30, 0x80
	s_addc_u32 s31, s31, 0
	s_waitcnt lgkmcnt(0)
	v_mfma_f32_16x16x32_f16 v[32:35], v[144:147], v[128:131], v[32:35]
	ds_read_b128 v[96:99], v12
	v_mfma_f32_16x16x32_f16 v[36:39], v[148:151], v[128:131], v[36:39]
	ds_read_b128 v[112:115], v13 offset:32768
	v_mfma_f32_16x16x32_f16 v[40:43], v[152:155], v[128:131], v[40:43]
	ds_read_b128 v[116:119], v13 offset:34816
	v_mfma_f32_16x16x32_f16 v[44:47], v[156:159], v[128:131], v[44:47]
	ds_read_b128 v[120:123], v13 offset:36864
	v_mfma_f32_16x16x32_f16 v[48:51], v[144:147], v[132:135], v[48:51]
	ds_read_b128 v[124:127], v13 offset:38912
	v_mfma_f32_16x16x32_f16 v[52:55], v[148:151], v[132:135], v[52:55]
	ds_read_b128 v[100:103], v12 offset:2048
	v_mfma_f32_16x16x32_f16 v[56:59], v[152:155], v[132:135], v[56:59]
	ds_read_b128 v[104:107], v12 offset:4096
	v_mfma_f32_16x16x32_f16 v[60:63], v[156:159], v[132:135], v[60:63]
	ds_read_b128 v[108:111], v12 offset:6144
	v_mfma_f32_16x16x32_f16 v[64:67], v[144:147], v[136:139], v[64:67]
	v_mfma_f32_16x16x32_f16 v[68:71], v[148:151], v[136:139], v[68:71]
	v_mfma_f32_16x16x32_f16 v[72:75], v[152:155], v[136:139], v[72:75]
	s_add_u32 m0, s14, 0x0
	s_nop 0
	global_load_lds_dwordx4 v2, s[28:29]
	v_mfma_f32_16x16x32_f16 v[76:79], v[156:159], v[136:139], v[76:79]
	v_mfma_f32_16x16x32_f16 v[80:83], v[144:147], v[140:143], v[80:83]
	s_add_u32 m0, s14, 0x2000
	s_nop 0
	global_load_lds_dwordx4 v3, s[28:29]
	v_mfma_f32_16x16x32_f16 v[84:87], v[148:151], v[140:143], v[84:87]
	v_mfma_f32_16x16x32_f16 v[88:91], v[152:155], v[140:143], v[88:91]
	s_add_u32 m0, s14, 0x4000
	s_nop 0
	global_load_lds_dwordx4 v4, s[28:29]
	v_mfma_f32_16x16x32_f16 v[92:95], v[156:159], v[140:143], v[92:95]
	s_waitcnt lgkmcnt(0)
	v_mfma_f32_16x16x32_f16 v[32:35], v[112:115], v[96:99], v[32:35]
	ds_read_b128 v[128:131], v14
	v_mfma_f32_16x16x32_f16 v[36:39], v[116:119], v[96:99], v[36:39]
	ds_read_b128 v[144:147], v15 offset:32768
	v_mfma_f32_16x16x32_f16 v[40:43], v[120:123], v[96:99], v[40:43]
	ds_read_b128 v[148:151], v15 offset:34816
	v_mfma_f32_16x16x32_f16 v[44:47], v[124:127], v[96:99], v[44:47]
	ds_read_b128 v[152:155], v15 offset:36864
	v_mfma_f32_16x16x32_f16 v[48:51], v[112:115], v[100:103], v[48:51]
	ds_read_b128 v[156:159], v15 offset:38912
	v_mfma_f32_16x16x32_f16 v[52:55], v[116:119], v[100:103], v[52:55]
	ds_read_b128 v[132:135], v14 offset:2048
	v_mfma_f32_16x16x32_f16 v[56:59], v[120:123], v[100:103], v[56:59]
	ds_read_b128 v[136:139], v14 offset:4096
	v_mfma_f32_16x16x32_f16 v[60:63], v[124:127], v[100:103], v[60:63]
	ds_read_b128 v[140:143], v14 offset:6144
	v_mfma_f32_16x16x32_f16 v[64:67], v[112:115], v[104:107], v[64:67]
	v_mfma_f32_16x16x32_f16 v[68:71], v[116:119], v[104:107], v[68:71]
	v_mfma_f32_16x16x32_f16 v[72:75], v[120:123], v[104:107], v[72:75]
	s_add_u32 m0, s14, 0x6000
	s_nop 0
	global_load_lds_dwordx4 v5, s[28:29]
	v_mfma_f32_16x16x32_f16 v[76:79], v[124:127], v[104:107], v[76:79]
	v_mfma_f32_16x16x32_f16 v[80:83], v[112:115], v[108:111], v[80:83]
	s_add_u32 m0, s14, 0x8000
	s_nop 0
	global_load_lds_dwordx4 v6, s[30:31]
	v_mfma_f32_16x16x32_f16 v[84:87], v[116:119], v[108:111], v[84:87]
	v_mfma_f32_16x16x32_f16 v[88:91], v[120:123], v[108:111], v[88:91]
	s_add_u32 m0, s14, 0xa000
	s_nop 0
	global_load_lds_dwordx4 v7, s[30:31]
	v_mfma_f32_16x16x32_f16 v[92:95], v[124:127], v[108:111], v[92:95]
	s_waitcnt vmcnt(6) lgkmcnt(0)
	s_barrier
	s_add_u32 s28, s28, 0x80
	s_addc_u32 s29, s29, 0
	s_add_u32 s30, s30, 0x80
	s_addc_u32 s31, s31, 0
	s_waitcnt lgkmcnt(0)
	v_mfma_f32_16x16x32_f16 v[32:35], v[144:147], v[128:131], v[32:35]
	ds_read_b128 v[96:99], v16
	v_mfma_f32_16x16x32_f16 v[36:39], v[148:151], v[128:131], v[36:39]
	ds_read_b128 v[112:115], v17 offset:32768
	v_mfma_f32_16x16x32_f16 v[40:43], v[152:155], v[128:131], v[40:43]
	ds_read_b128 v[116:119], v17 offset:34816
	v_mfma_f32_16x16x32_f16 v[44:47], v[156:159], v[128:131], v[44:47]
	ds_read_b128 v[120:123], v17 offset:36864
	v_mfma_f32_16x16x32_f16 v[48:51], v[144:147], v[132:135], v[48:51]
	ds_read_b128 v[124:127], v17 offset:38912
	v_mfma_f32_16x16x32_f16 v[52:55], v[148:151], v[132:135], v[52:55]
	ds_read_b128 v[100:103], v16 offset:2048
	v_mfma_f32_16x16x32_f16 v[56:59], v[152:155], v[132:135], v[56:59]
	ds_read_b128 v[104:107], v16 offset:4096
	v_mfma_f32_16x16x32_f16 v[60:63], v[156:159], v[132:135], v[60:63]
	ds_read_b128 v[108:111], v16 offset:6144
	v_mfma_f32_16x16x32_f16 v[64:67], v[144:147], v[136:139], v[64:67]
	v_mfma_f32_16x16x32_f16 v[68:71], v[148:151], v[136:139], v[68:71]
	v_mfma_f32_16x16x32_f16 v[72:75], v[152:155], v[136:139], v[72:75]
	s_add_u32 m0, s14, 0xc000
	s_nop 0
	global_load_lds_dwordx4 v2, s[28:29]
	v_mfma_f32_16x16x32_f16 v[76:79], v[156:159], v[136:139], v[76:79]
	v_mfma_f32_16x16x32_f16 v[80:83], v[144:147], v[140:143], v[80:83]
	s_add_u32 m0, s14, 0xe000
	s_nop 0
	global_load_lds_dwordx4 v3, s[28:29]
	v_mfma_f32_16x16x32_f16 v[84:87], v[148:151], v[140:143], v[84:87]
	v_mfma_f32_16x16x32_f16 v[88:91], v[152:155], v[140:143], v[88:91]
	s_add_u32 m0, s14, 0x10000
	s_nop 0
	global_load_lds_dwordx4 v4, s[28:29]
	v_mfma_f32_16x16x32_f16 v[92:95], v[156:159], v[140:143], v[92:95]
	s_waitcnt lgkmcnt(0)
	v_mfma_f32_16x16x32_f16 v[32:35], v[112:115], v[96:99], v[32:35]
	ds_read_b128 v[128:131], v18
	v_mfma_f32_16x16x32_f16 v[36:39], v[116:119], v[96:99], v[36:39]
	ds_read_b128 v[144:147], v19 offset:32768
	v_mfma_f32_16x16x32_f16 v[40:43], v[120:123], v[96:99], v[40:43]
	ds_read_b128 v[148:151], v19 offset:34816
	v_mfma_f32_16x16x32_f16 v[44:47], v[124:127], v[96:99], v[44:47]
	ds_read_b128 v[152:155], v19 offset:36864
	v_mfma_f32_16x16x32_f16 v[48:51], v[112:115], v[100:103], v[48:51]
	ds_read_b128 v[156:159], v19 offset:38912
	v_mfma_f32_16x16x32_f16 v[52:55], v[116:119], v[100:103], v[52:55]
	ds_read_b128 v[132:135], v18 offset:2048
	v_mfma_f32_16x16x32_f16 v[56:59], v[120:123], v[100:103], v[56:59]
	ds_read_b128 v[136:139], v18 offset:4096
	v_mfma_f32_16x16x32_f16 v[60:63], v[124:127], v[100:103], v[60:63]
	ds_read_b128 v[140:143], v18 offset:6144
	v_mfma_f32_16x16x32_f16 v[64:67], v[112:115], v[104:107], v[64:67]
	v_mfma_f32_16x16x32_f16 v[68:71], v[116:119], v[104:107], v[68:71]
	v_mfma_f32_16x16x32_f16 v[72:75], v[120:123], v[104:107], v[72:75]
	s_add_u32 m0, s14, 0x12000
	s_nop 0
	global_load_lds_dwordx4 v5, s[28:29]
	v_mfma_f32_16x16x32_f16 v[76:79], v[124:127], v[104:107], v[76:79]
	v_mfma_f32_16x16x32_f16 v[80:83], v[112:115], v[108:111], v[80:83]
	s_add_u32 m0, s14, 0x14000
	s_nop 0
	global_load_lds_dwordx4 v6, s[30:31]
	v_mfma_f32_16x16x32_f16 v[84:87], v[116:119], v[108:111], v[84:87]
	v_mfma_f32_16x16x32_f16 v[88:91], v[120:123], v[108:111], v[88:91]
	s_add_u32 m0, s14, 0x16000
	s_nop 0
	global_load_lds_dwordx4 v7, s[30:31]
	v_mfma_f32_16x16x32_f16 v[92:95], v[124:127], v[108:111], v[92:95]
	s_waitcnt vmcnt(6) lgkmcnt(0)
	s_barrier
	s_add_u32 s28, s28, 0x80
	s_addc_u32 s29, s29, 0
	s_add_u32 s30, s30, 0x80
	s_addc_u32 s31, s31, 0
	s_waitcnt lgkmcnt(0)
	v_mfma_f32_16x16x32_f16 v[32:35], v[144:147], v[128:131], v[32:35]
	ds_read_b128 v[96:99], v8
	v_mfma_f32_16x16x32_f16 v[36:39], v[148:151], v[128:131], v[36:39]
	ds_read_b128 v[112:115], v9 offset:32768
	v_mfma_f32_16x16x32_f16 v[40:43], v[152:155], v[128:131], v[40:43]
	ds_read_b128 v[116:119], v9 offset:34816
	v_mfma_f32_16x16x32_f16 v[44:47], v[156:159], v[128:131], v[44:47]
	ds_read_b128 v[120:123], v9 offset:36864
	v_mfma_f32_16x16x32_f16 v[48:51], v[144:147], v[132:135], v[48:51]
	ds_read_b128 v[124:127], v9 offset:38912
	v_mfma_f32_16x16x32_f16 v[52:55], v[148:151], v[132:135], v[52:55]
	ds_read_b128 v[100:103], v8 offset:2048
	v_mfma_f32_16x16x32_f16 v[56:59], v[152:155], v[132:135], v[56:59]
	ds_read_b128 v[104:107], v8 offset:4096
	v_mfma_f32_16x16x32_f16 v[60:63], v[156:159], v[132:135], v[60:63]
	ds_read_b128 v[108:111], v8 offset:6144
	v_mfma_f32_16x16x32_f16 v[64:67], v[144:147], v[136:139], v[64:67]
	v_mfma_f32_16x16x32_f16 v[68:71], v[148:151], v[136:139], v[68:71]
	v_mfma_f32_16x16x32_f16 v[72:75], v[152:155], v[136:139], v[72:75]
	s_add_u32 m0, s14, 0x18000
	s_nop 0
	global_load_lds_dwordx4 v2, s[28:29]
	v_mfma_f32_16x16x32_f16 v[76:79], v[156:159], v[136:139], v[76:79]
	v_mfma_f32_16x16x32_f16 v[80:83], v[144:147], v[140:143], v[80:83]
	s_add_u32 m0, s14, 0x1a000
	s_nop 0
	global_load_lds_dwordx4 v3, s[28:29]
	v_mfma_f32_16x16x32_f16 v[84:87], v[148:151], v[140:143], v[84:87]
	v_mfma_f32_16x16x32_f16 v[88:91], v[152:155], v[140:143], v[88:91]
	s_add_u32 m0, s14, 0x1c000
	s_nop 0
	global_load_lds_dwordx4 v4, s[28:29]
	v_mfma_f32_16x16x32_f16 v[92:95], v[156:159], v[140:143], v[92:95]
	s_waitcnt lgkmcnt(0)
	v_mfma_f32_16x16x32_f16 v[32:35], v[112:115], v[96:99], v[32:35]
	ds_read_b128 v[128:131], v10
	v_mfma_f32_16x16x32_f16 v[36:39], v[116:119], v[96:99], v[36:39]
	ds_read_b128 v[144:147], v11 offset:32768
	v_mfma_f32_16x16x32_f16 v[40:43], v[120:123], v[96:99], v[40:43]
	ds_read_b128 v[148:151], v11 offset:34816
	v_mfma_f32_16x16x32_f16 v[44:47], v[124:127], v[96:99], v[44:47]
	ds_read_b128 v[152:155], v11 offset:36864
	v_mfma_f32_16x16x32_f16 v[48:51], v[112:115], v[100:103], v[48:51]
	ds_read_b128 v[156:159], v11 offset:38912
	v_mfma_f32_16x16x32_f16 v[52:55], v[116:119], v[100:103], v[52:55]
	ds_read_b128 v[132:135], v10 offset:2048
	v_mfma_f32_16x16x32_f16 v[56:59], v[120:123], v[100:103], v[56:59]
	ds_read_b128 v[136:139], v10 offset:4096
	v_mfma_f32_16x16x32_f16 v[60:63], v[124:127], v[100:103], v[60:63]
	ds_read_b128 v[140:143], v10 offset:6144
	v_mfma_f32_16x16x32_f16 v[64:67], v[112:115], v[104:107], v[64:67]
	v_mfma_f32_16x16x32_f16 v[68:71], v[116:119], v[104:107], v[68:71]
	v_mfma_f32_16x16x32_f16 v[72:75], v[120:123], v[104:107], v[72:75]
	s_add_u32 m0, s14, 0x1e000
	s_nop 0
	global_load_lds_dwordx4 v5, s[28:29]
	v_mfma_f32_16x16x32_f16 v[76:79], v[124:127], v[104:107], v[76:79]
	v_mfma_f32_16x16x32_f16 v[80:83], v[112:115], v[108:111], v[80:83]
	s_add_u32 m0, s14, 0x20000
	s_nop 0
	global_load_lds_dwordx4 v6, s[30:31]
	v_mfma_f32_16x16x32_f16 v[84:87], v[116:119], v[108:111], v[84:87]
	v_mfma_f32_16x16x32_f16 v[88:91], v[120:123], v[108:111], v[88:91]
	s_add_u32 m0, s14, 0x22000
	s_nop 0
	global_load_lds_dwordx4 v7, s[30:31]
	v_mfma_f32_16x16x32_f16 v[92:95], v[124:127], v[108:111], v[92:95]
	s_waitcnt vmcnt(6) lgkmcnt(0)
	s_barrier
	s_mov_b64 s[28:29], s[18:19]
	s_mov_b64 s[30:31], s[26:27]
	s_waitcnt lgkmcnt(0)
	v_mfma_f32_16x16x32_f16 v[32:35], v[144:147], v[128:131], v[32:35]
	ds_read_b128 v[96:99], v12
	v_mfma_f32_16x16x32_f16 v[36:39], v[148:151], v[128:131], v[36:39]
	ds_read_b128 v[112:115], v13 offset:32768
	v_mfma_f32_16x16x32_f16 v[40:43], v[152:155], v[128:131], v[40:43]
	ds_read_b128 v[116:119], v13 offset:34816
	v_mfma_f32_16x16x32_f16 v[44:47], v[156:159], v[128:131], v[44:47]
	ds_read_b128 v[120:123], v13 offset:36864
	v_mfma_f32_16x16x32_f16 v[48:51], v[144:147], v[132:135], v[48:51]
	ds_read_b128 v[124:127], v13 offset:38912
	v_mfma_f32_16x16x32_f16 v[52:55], v[148:151], v[132:135], v[52:55]
	ds_read_b128 v[100:103], v12 offset:2048
	v_mfma_f32_16x16x32_f16 v[56:59], v[152:155], v[132:135], v[56:59]
	ds_read_b128 v[104:107], v12 offset:4096
	v_mfma_f32_16x16x32_f16 v[60:63], v[156:159], v[132:135], v[60:63]
	ds_read_b128 v[108:111], v12 offset:6144
	v_mfma_f32_16x16x32_f16 v[64:67], v[144:147], v[136:139], v[64:67]
	v_mfma_f32_16x16x32_f16 v[68:71], v[148:151], v[136:139], v[68:71]
	v_mfma_f32_16x16x32_f16 v[72:75], v[152:155], v[136:139], v[72:75]
	s_add_u32 m0, s14, 0x0
	s_nop 0
	global_load_lds_dwordx4 v2, s[28:29]
	v_mfma_f32_16x16x32_f16 v[76:79], v[156:159], v[136:139], v[76:79]
	v_mfma_f32_16x16x32_f16 v[80:83], v[144:147], v[140:143], v[80:83]
	s_add_u32 m0, s14, 0x2000
	s_nop 0
	global_load_lds_dwordx4 v3, s[28:29]
	v_mfma_f32_16x16x32_f16 v[84:87], v[148:151], v[140:143], v[84:87]
	v_mfma_f32_16x16x32_f16 v[88:91], v[152:155], v[140:143], v[88:91]
	s_add_u32 m0, s14, 0x4000
	s_nop 0
	global_load_lds_dwordx4 v4, s[28:29]
	v_mfma_f32_16x16x32_f16 v[92:95], v[156:159], v[140:143], v[92:95]
	s_waitcnt lgkmcnt(0)
	v_mfma_f32_16x16x32_f16 v[32:35], v[112:115], v[96:99], v[32:35]
	ds_read_b128 v[128:131], v14
	v_mfma_f32_16x16x32_f16 v[36:39], v[116:119], v[96:99], v[36:39]
	ds_read_b128 v[144:147], v15 offset:32768
	v_mfma_f32_16x16x32_f16 v[40:43], v[120:123], v[96:99], v[40:43]
	ds_read_b128 v[148:151], v15 offset:34816
	v_mfma_f32_16x16x32_f16 v[44:47], v[124:127], v[96:99], v[44:47]
	ds_read_b128 v[152:155], v15 offset:36864
	v_mfma_f32_16x16x32_f16 v[48:51], v[112:115], v[100:103], v[48:51]
	ds_read_b128 v[156:159], v15 offset:38912
	v_mfma_f32_16x16x32_f16 v[52:55], v[116:119], v[100:103], v[52:55]
	ds_read_b128 v[132:135], v14 offset:2048
	v_mfma_f32_16x16x32_f16 v[56:59], v[120:123], v[100:103], v[56:59]
	ds_read_b128 v[136:139], v14 offset:4096
	v_mfma_f32_16x16x32_f16 v[60:63], v[124:127], v[100:103], v[60:63]
	ds_read_b128 v[140:143], v14 offset:6144
	v_mfma_f32_16x16x32_f16 v[64:67], v[112:115], v[104:107], v[64:67]
	v_mfma_f32_16x16x32_f16 v[68:71], v[116:119], v[104:107], v[68:71]
	v_mfma_f32_16x16x32_f16 v[72:75], v[120:123], v[104:107], v[72:75]
	s_add_u32 m0, s14, 0x6000
	s_nop 0
	global_load_lds_dwordx4 v5, s[28:29]
	v_mfma_f32_16x16x32_f16 v[76:79], v[124:127], v[104:107], v[76:79]
	v_mfma_f32_16x16x32_f16 v[80:83], v[112:115], v[108:111], v[80:83]
	s_add_u32 m0, s14, 0x8000
	s_nop 0
	global_load_lds_dwordx4 v6, s[30:31]
	v_mfma_f32_16x16x32_f16 v[84:87], v[116:119], v[108:111], v[84:87]
	v_mfma_f32_16x16x32_f16 v[88:91], v[120:123], v[108:111], v[88:91]
	s_add_u32 m0, s14, 0xa000
	s_nop 0
	global_load_lds_dwordx4 v7, s[30:31]
	v_mfma_f32_16x16x32_f16 v[92:95], v[124:127], v[108:111], v[92:95]
	s_waitcnt vmcnt(6) lgkmcnt(0)
	s_barrier
	s_add_u32 s28, s28, 0x80
	s_addc_u32 s29, s29, 0
	s_add_u32 s30, s30, 0x80
	s_addc_u32 s31, s31, 0
	s_waitcnt lgkmcnt(0)
	v_mfma_f32_16x16x32_f16 v[32:35], v[144:147], v[128:131], v[32:35]
	ds_read_b128 v[96:99], v16
	v_mfma_f32_16x16x32_f16 v[36:39], v[148:151], v[128:131], v[36:39]
	ds_read_b128 v[112:115], v17 offset:32768
	v_mfma_f32_16x16x32_f16 v[40:43], v[152:155], v[128:131], v[40:43]
	ds_read_b128 v[116:119], v17 offset:34816
	v_mfma_f32_16x16x32_f16 v[44:47], v[156:159], v[128:131], v[44:47]
	ds_read_b128 v[120:123], v17 offset:36864
	v_mfma_f32_16x16x32_f16 v[48:51], v[144:147], v[132:135], v[48:51]
	ds_read_b128 v[124:127], v17 offset:38912
	v_mfma_f32_16x16x32_f16 v[52:55], v[148:151], v[132:135], v[52:55]
	ds_read_b128 v[100:103], v16 offset:2048
	v_mfma_f32_16x16x32_f16 v[56:59], v[152:155], v[132:135], v[56:59]
	ds_read_b128 v[104:107], v16 offset:4096
	v_mfma_f32_16x16x32_f16 v[60:63], v[156:159], v[132:135], v[60:63]
	ds_read_b128 v[108:111], v16 offset:6144
	v_mfma_f32_16x16x32_f16 v[64:67], v[144:147], v[136:139], v[64:67]
	v_mfma_f32_16x16x32_f16 v[68:71], v[148:151], v[136:139], v[68:71]
	v_mfma_f32_16x16x32_f16 v[72:75], v[152:155], v[136:139], v[72:75]
	s_add_u32 m0, s14, 0xc000
	s_nop 0
	global_load_lds_dwordx4 v2, s[28:29]
	v_mfma_f32_16x16x32_f16 v[76:79], v[156:159], v[136:139], v[76:79]
	v_mfma_f32_16x16x32_f16 v[80:83], v[144:147], v[140:143], v[80:83]
	s_add_u32 m0, s14, 0xe000
	s_nop 0
	global_load_lds_dwordx4 v3, s[28:29]
	v_mfma_f32_16x16x32_f16 v[84:87], v[148:151], v[140:143], v[84:87]
	v_mfma_f32_16x16x32_f16 v[88:91], v[152:155], v[140:143], v[88:91]
	s_add_u32 m0, s14, 0x10000
	s_nop 0
	global_load_lds_dwordx4 v4, s[28:29]
	v_mfma_f32_16x16x32_f16 v[92:95], v[156:159], v[140:143], v[92:95]
	s_waitcnt lgkmcnt(0)
	v_mfma_f32_16x16x32_f16 v[32:35], v[112:115], v[96:99], v[32:35]
	ds_read_b128 v[128:131], v18
	v_mfma_f32_16x16x32_f16 v[36:39], v[116:119], v[96:99], v[36:39]
	ds_read_b128 v[144:147], v19 offset:32768
	v_mfma_f32_16x16x32_f16 v[40:43], v[120:123], v[96:99], v[40:43]
	ds_read_b128 v[148:151], v19 offset:34816
	v_mfma_f32_16x16x32_f16 v[44:47], v[124:127], v[96:99], v[44:47]
	ds_read_b128 v[152:155], v19 offset:36864
	v_mfma_f32_16x16x32_f16 v[48:51], v[112:115], v[100:103], v[48:51]
	ds_read_b128 v[156:159], v19 offset:38912
	v_mfma_f32_16x16x32_f16 v[52:55], v[116:119], v[100:103], v[52:55]
	ds_read_b128 v[132:135], v18 offset:2048
	v_mfma_f32_16x16x32_f16 v[56:59], v[120:123], v[100:103], v[56:59]
	ds_read_b128 v[136:139], v18 offset:4096
	v_mfma_f32_16x16x32_f16 v[60:63], v[124:127], v[100:103], v[60:63]
	ds_read_b128 v[140:143], v18 offset:6144
	v_mfma_f32_16x16x32_f16 v[64:67], v[112:115], v[104:107], v[64:67]
	v_mfma_f32_16x16x32_f16 v[68:71], v[116:119], v[104:107], v[68:71]
	v_mfma_f32_16x16x32_f16 v[72:75], v[120:123], v[104:107], v[72:75]
	s_add_u32 m0, s14, 0x12000
	s_nop 0
	global_load_lds_dwordx4 v5, s[28:29]
	v_mfma_f32_16x16x32_f16 v[76:79], v[124:127], v[104:107], v[76:79]
	v_mfma_f32_16x16x32_f16 v[80:83], v[112:115], v[108:111], v[80:83]
	s_add_u32 m0, s14, 0x14000
	s_nop 0
	global_load_lds_dwordx4 v6, s[30:31]
	v_mfma_f32_16x16x32_f16 v[84:87], v[116:119], v[108:111], v[84:87]
	v_mfma_f32_16x16x32_f16 v[88:91], v[120:123], v[108:111], v[88:91]
	s_add_u32 m0, s14, 0x16000
	s_nop 0
	global_load_lds_dwordx4 v7, s[30:31]
	v_mfma_f32_16x16x32_f16 v[92:95], v[124:127], v[108:111], v[92:95]
	s_waitcnt vmcnt(6) lgkmcnt(0)
	s_barrier
	s_add_u32 s28, s28, 0x80
	s_addc_u32 s29, s29, 0
	s_add_u32 s30, s30, 0x80
	s_addc_u32 s31, s31, 0
	s_waitcnt lgkmcnt(0)
	v_mfma_f32_16x16x32_f16 v[32:35], v[144:147], v[128:131], v[32:35]
	ds_read_b128 v[96:99], v8
	v_mfma_f32_16x16x32_f16 v[36:39], v[148:151], v[128:131], v[36:39]
	ds_read_b128 v[112:115], v9 offset:32768
	v_mfma_f32_16x16x32_f16 v[40:43], v[152:155], v[128:131], v[40:43]
	ds_read_b128 v[116:119], v9 offset:34816
	v_mfma_f32_16x16x32_f16 v[44:47], v[156:159], v[128:131], v[44:47]
	ds_read_b128 v[120:123], v9 offset:36864
	v_mfma_f32_16x16x32_f16 v[48:51], v[144:147], v[132:135], v[48:51]
	ds_read_b128 v[124:127], v9 offset:38912
	v_mfma_f32_16x16x32_f16 v[52:55], v[148:151], v[132:135], v[52:55]
	ds_read_b128 v[100:103], v8 offset:2048
	v_mfma_f32_16x16x32_f16 v[56:59], v[152:155], v[132:135], v[56:59]
	ds_read_b128 v[104:107], v8 offset:4096
	v_mfma_f32_16x16x32_f16 v[60:63], v[156:159], v[132:135], v[60:63]
	ds_read_b128 v[108:111], v8 offset:6144
	v_mfma_f32_16x16x32_f16 v[64:67], v[144:147], v[136:139], v[64:67]
	v_mfma_f32_16x16x32_f16 v[68:71], v[148:151], v[136:139], v[68:71]
	v_mfma_f32_16x16x32_f16 v[72:75], v[152:155], v[136:139], v[72:75]
	s_add_u32 m0, s14, 0x18000
	s_nop 0
	global_load_lds_dwordx4 v2, s[28:29]
	v_mfma_f32_16x16x32_f16 v[76:79], v[156:159], v[136:139], v[76:79]
	v_mfma_f32_16x16x32_f16 v[80:83], v[144:147], v[140:143], v[80:83]
	s_add_u32 m0, s14, 0x1a000
	s_nop 0
	global_load_lds_dwordx4 v3, s[28:29]
	v_mfma_f32_16x16x32_f16 v[84:87], v[148:151], v[140:143], v[84:87]
	v_mfma_f32_16x16x32_f16 v[88:91], v[152:155], v[140:143], v[88:91]
	s_add_u32 m0, s14, 0x1c000
	s_nop 0
	global_load_lds_dwordx4 v4, s[28:29]
	v_mfma_f32_16x16x32_f16 v[92:95], v[156:159], v[140:143], v[92:95]
	s_nop 7
	s_nop 1
	v_pk_mul_f32 v[160:161], v[32:33], s[50:51] op_sel_hi:[1,0]
	v_pk_mul_f32 v[162:163], v[34:35], s[50:51] op_sel_hi:[1,0]
	v_pk_mul_f32 v[164:165], v[36:37], s[50:51] op_sel_hi:[1,0]
	v_pk_mul_f32 v[166:167], v[38:39], s[50:51] op_sel_hi:[1,0]
	v_cvt_pk_f16_f32 v168, v160, v161
	v_cvt_pk_f16_f32 v169, v162, v163
	v_cvt_pk_f16_f32 v170, v164, v165
	v_cvt_pk_f16_f32 v171, v166, v167
	global_store_dwordx4 v24, v[168:171], s[34:35]
	v_pk_mul_f32 v[160:161], v[40:41], s[50:51] op_sel_hi:[1,0]
	v_pk_mul_f32 v[162:163], v[42:43], s[50:51] op_sel_hi:[1,0]
	v_pk_mul_f32 v[164:165], v[44:45], s[50:51] op_sel_hi:[1,0]
	v_pk_mul_f32 v[166:167], v[46:47], s[50:51] op_sel_hi:[1,0]
	v_cvt_pk_f16_f32 v172, v160, v161
	v_cvt_pk_f16_f32 v173, v162, v163
	v_cvt_pk_f16_f32 v174, v164, v165
	v_cvt_pk_f16_f32 v175, v166, v167
	global_store_dwordx4 v24, v[172:175], s[34:35] offset:64
	v_pk_mul_f32 v[160:161], v[48:49], s[50:51] op_sel_hi:[1,0]
	v_pk_mul_f32 v[162:163], v[50:51], s[50:51] op_sel_hi:[1,0]
	v_pk_mul_f32 v[164:165], v[52:53], s[50:51] op_sel_hi:[1,0]
	v_pk_mul_f32 v[166:167], v[54:55], s[50:51] op_sel_hi:[1,0]
	v_cvt_pk_f16_f32 v168, v160, v161
	v_cvt_pk_f16_f32 v169, v162, v163
	v_cvt_pk_f16_f32 v170, v164, v165
	v_cvt_pk_f16_f32 v171, v166, v167
	global_store_dwordx4 v25, v[168:171], s[34:35]
	v_pk_mul_f32 v[160:161], v[56:57], s[50:51] op_sel_hi:[1,0]
	v_pk_mul_f32 v[162:163], v[58:59], s[50:51] op_sel_hi:[1,0]
	v_pk_mul_f32 v[164:165], v[60:61], s[50:51] op_sel_hi:[1,0]
	v_pk_mul_f32 v[166:167], v[62:63], s[50:51] op_sel_hi:[1,0]
	v_cvt_pk_f16_f32 v172, v160, v161
	v_cvt_pk_f16_f32 v173, v162, v163
	v_cvt_pk_f16_f32 v174, v164, v165
	v_cvt_pk_f16_f32 v175, v166, v167
	global_store_dwordx4 v25, v[172:175], s[34:35] offset:64
	v_pk_mul_f32 v[160:161], v[64:65], s[50:51] op_sel_hi:[1,0]
	v_pk_mul_f32 v[162:163], v[66:67], s[50:51] op_sel_hi:[1,0]
	v_pk_mul_f32 v[164:165], v[68:69], s[50:51] op_sel_hi:[1,0]
	v_pk_mul_f32 v[166:167], v[70:71], s[50:51] op_sel_hi:[1,0]
	v_cvt_pk_f16_f32 v168, v160, v161
	v_cvt_pk_f16_f32 v169, v162, v163
	v_cvt_pk_f16_f32 v170, v164, v165
	v_cvt_pk_f16_f32 v171, v166, v167
	global_store_dwordx4 v26, v[168:171], s[34:35]
	v_pk_mul_f32 v[160:161], v[72:73], s[50:51] op_sel_hi:[1,0]
	v_pk_mul_f32 v[162:163], v[74:75], s[50:51] op_sel_hi:[1,0]
	v_pk_mul_f32 v[164:165], v[76:77], s[50:51] op_sel_hi:[1,0]
	v_pk_mul_f32 v[166:167], v[78:79], s[50:51] op_sel_hi:[1,0]
	v_cvt_pk_f16_f32 v172, v160, v161
	v_cvt_pk_f16_f32 v173, v162, v163
	v_cvt_pk_f16_f32 v174, v164, v165
	v_cvt_pk_f16_f32 v175, v166, v167
	global_store_dwordx4 v26, v[172:175], s[34:35] offset:64
	v_pk_mul_f32 v[160:161], v[80:81], s[50:51] op_sel_hi:[1,0]
	v_pk_mul_f32 v[162:163], v[82:83], s[50:51] op_sel_hi:[1,0]
	v_pk_mul_f32 v[164:165], v[84:85], s[50:51] op_sel_hi:[1,0]
	v_pk_mul_f32 v[166:167], v[86:87], s[50:51] op_sel_hi:[1,0]
	v_cvt_pk_f16_f32 v168, v160, v161
	v_cvt_pk_f16_f32 v169, v162, v163
	v_cvt_pk_f16_f32 v170, v164, v165
	v_cvt_pk_f16_f32 v171, v166, v167
	global_store_dwordx4 v27, v[168:171], s[34:35]
	v_pk_mul_f32 v[160:161], v[88:89], s[50:51] op_sel_hi:[1,0]
	v_pk_mul_f32 v[162:163], v[90:91], s[50:51] op_sel_hi:[1,0]
	v_pk_mul_f32 v[164:165], v[92:93], s[50:51] op_sel_hi:[1,0]
	v_pk_mul_f32 v[166:167], v[94:95], s[50:51] op_sel_hi:[1,0]
	v_cvt_pk_f16_f32 v172, v160, v161
	v_cvt_pk_f16_f32 v173, v162, v163
	v_cvt_pk_f16_f32 v174, v164, v165
	v_cvt_pk_f16_f32 v175, v166, v167
	global_store_dwordx4 v27, v[172:175], s[34:35] offset:64
	s_waitcnt lgkmcnt(0)
	v_mfma_f32_16x16x32_f16 v[32:35], v[112:115], v[96:99], 0
	ds_read_b128 v[128:131], v10
	v_mfma_f32_16x16x32_f16 v[36:39], v[116:119], v[96:99], 0
	ds_read_b128 v[144:147], v11 offset:32768
	v_mfma_f32_16x16x32_f16 v[40:43], v[120:123], v[96:99], 0
	ds_read_b128 v[148:151], v11 offset:34816
	v_mfma_f32_16x16x32_f16 v[44:47], v[124:127], v[96:99], 0
	ds_read_b128 v[152:155], v11 offset:36864
	v_mfma_f32_16x16x32_f16 v[48:51], v[112:115], v[100:103], 0
	ds_read_b128 v[156:159], v11 offset:38912
	v_mfma_f32_16x16x32_f16 v[52:55], v[116:119], v[100:103], 0
	ds_read_b128 v[132:135], v10 offset:2048
	v_mfma_f32_16x16x32_f16 v[56:59], v[120:123], v[100:103], 0
	ds_read_b128 v[136:139], v10 offset:4096
	v_mfma_f32_16x16x32_f16 v[60:63], v[124:127], v[100:103], 0
	ds_read_b128 v[140:143], v10 offset:6144
	v_mfma_f32_16x16x32_f16 v[64:67], v[112:115], v[104:107], 0
	v_mfma_f32_16x16x32_f16 v[68:71], v[116:119], v[104:107], 0
	v_mfma_f32_16x16x32_f16 v[72:75], v[120:123], v[104:107], 0
	s_add_u32 m0, s14, 0x1e000
	s_nop 0
	global_load_lds_dwordx4 v5, s[28:29]
	v_mfma_f32_16x16x32_f16 v[76:79], v[124:127], v[104:107], 0
	v_mfma_f32_16x16x32_f16 v[80:83], v[112:115], v[108:111], 0
	s_add_u32 m0, s14, 0x20000
	s_nop 0
	global_load_lds_dwordx4 v6, s[30:31]
	v_mfma_f32_16x16x32_f16 v[84:87], v[116:119], v[108:111], 0
	v_mfma_f32_16x16x32_f16 v[88:91], v[120:123], v[108:111], 0
	s_add_u32 m0, s14, 0x22000
	s_nop 0
	global_load_lds_dwordx4 v7, s[30:31]
	v_mfma_f32_16x16x32_f16 v[92:95], v[124:127], v[108:111], 0
	s_waitcnt vmcnt(14) lgkmcnt(0)
	s_barrier
	s_add_u32 s28, s28, 0x80
	s_addc_u32 s29, s29, 0
	s_add_u32 s30, s30, 0x80
	s_addc_u32 s31, s31, 0
	s_waitcnt lgkmcnt(0)
	v_mfma_f32_16x16x32_f16 v[32:35], v[144:147], v[128:131], v[32:35]
	ds_read_b128 v[96:99], v12
	v_mfma_f32_16x16x32_f16 v[36:39], v[148:151], v[128:131], v[36:39]
	ds_read_b128 v[112:115], v13 offset:32768
	v_mfma_f32_16x16x32_f16 v[40:43], v[152:155], v[128:131], v[40:43]
	ds_read_b128 v[116:119], v13 offset:34816
	v_mfma_f32_16x16x32_f16 v[44:47], v[156:159], v[128:131], v[44:47]
	ds_read_b128 v[120:123], v13 offset:36864
	v_mfma_f32_16x16x32_f16 v[48:51], v[144:147], v[132:135], v[48:51]
	ds_read_b128 v[124:127], v13 offset:38912
	v_mfma_f32_16x16x32_f16 v[52:55], v[148:151], v[132:135], v[52:55]
	ds_read_b128 v[100:103], v12 offset:2048
	v_mfma_f32_16x16x32_f16 v[56:59], v[152:155], v[132:135], v[56:59]
	ds_read_b128 v[104:107], v12 offset:4096
	v_mfma_f32_16x16x32_f16 v[60:63], v[156:159], v[132:135], v[60:63]
	ds_read_b128 v[108:111], v12 offset:6144
	v_mfma_f32_16x16x32_f16 v[64:67], v[144:147], v[136:139], v[64:67]
	v_mfma_f32_16x16x32_f16 v[68:71], v[148:151], v[136:139], v[68:71]
	v_mfma_f32_16x16x32_f16 v[72:75], v[152:155], v[136:139], v[72:75]
	s_add_u32 m0, s14, 0x0
	s_nop 0
	global_load_lds_dwordx4 v2, s[28:29]
	v_mfma_f32_16x16x32_f16 v[76:79], v[156:159], v[136:139], v[76:79]
	v_mfma_f32_16x16x32_f16 v[80:83], v[144:147], v[140:143], v[80:83]
	s_add_u32 m0, s14, 0x2000
	s_nop 0
	global_load_lds_dwordx4 v3, s[28:29]
	v_mfma_f32_16x16x32_f16 v[84:87], v[148:151], v[140:143], v[84:87]
	v_mfma_f32_16x16x32_f16 v[88:91], v[152:155], v[140:143], v[88:91]
	s_add_u32 m0, s14, 0x4000
	s_nop 0
	global_load_lds_dwordx4 v4, s[28:29]
	v_mfma_f32_16x16x32_f16 v[92:95], v[156:159], v[140:143], v[92:95]
	s_waitcnt lgkmcnt(0)
	v_mfma_f32_16x16x32_f16 v[32:35], v[112:115], v[96:99], v[32:35]
	ds_read_b128 v[128:131], v14
	v_mfma_f32_16x16x32_f16 v[36:39], v[116:119], v[96:99], v[36:39]
	ds_read_b128 v[144:147], v15 offset:32768
	v_mfma_f32_16x16x32_f16 v[40:43], v[120:123], v[96:99], v[40:43]
	ds_read_b128 v[148:151], v15 offset:34816
	v_mfma_f32_16x16x32_f16 v[44:47], v[124:127], v[96:99], v[44:47]
	ds_read_b128 v[152:155], v15 offset:36864
	v_mfma_f32_16x16x32_f16 v[48:51], v[112:115], v[100:103], v[48:51]
	ds_read_b128 v[156:159], v15 offset:38912
	v_mfma_f32_16x16x32_f16 v[52:55], v[116:119], v[100:103], v[52:55]
	ds_read_b128 v[132:135], v14 offset:2048
	v_mfma_f32_16x16x32_f16 v[56:59], v[120:123], v[100:103], v[56:59]
	ds_read_b128 v[136:139], v14 offset:4096
	v_mfma_f32_16x16x32_f16 v[60:63], v[124:127], v[100:103], v[60:63]
	ds_read_b128 v[140:143], v14 offset:6144
	v_mfma_f32_16x16x32_f16 v[64:67], v[112:115], v[104:107], v[64:67]
	v_mfma_f32_16x16x32_f16 v[68:71], v[116:119], v[104:107], v[68:71]
	v_mfma_f32_16x16x32_f16 v[72:75], v[120:123], v[104:107], v[72:75]
	s_add_u32 m0, s14, 0x6000
	s_nop 0
	global_load_lds_dwordx4 v5, s[28:29]
	v_mfma_f32_16x16x32_f16 v[76:79], v[124:127], v[104:107], v[76:79]
	v_mfma_f32_16x16x32_f16 v[80:83], v[112:115], v[108:111], v[80:83]
	s_add_u32 m0, s14, 0x8000
	s_nop 0
	global_load_lds_dwordx4 v6, s[30:31]
	v_mfma_f32_16x16x32_f16 v[84:87], v[116:119], v[108:111], v[84:87]
	v_mfma_f32_16x16x32_f16 v[88:91], v[120:123], v[108:111], v[88:91]
	s_add_u32 m0, s14, 0xa000
	s_nop 0
	global_load_lds_dwordx4 v7, s[30:31]
	v_mfma_f32_16x16x32_f16 v[92:95], v[124:127], v[108:111], v[92:95]
	s_waitcnt vmcnt(6) lgkmcnt(0)
	s_barrier
	s_add_u32 s28, s28, 0x80
	s_addc_u32 s29, s29, 0
	s_add_u32 s30, s30, 0x80
	s_addc_u32 s31, s31, 0
	s_waitcnt lgkmcnt(0)
	v_mfma_f32_16x16x32_f16 v[32:35], v[144:147], v[128:131], v[32:35]
	ds_read_b128 v[96:99], v16
	v_mfma_f32_16x16x32_f16 v[36:39], v[148:151], v[128:131], v[36:39]
	ds_read_b128 v[112:115], v17 offset:32768
	v_mfma_f32_16x16x32_f16 v[40:43], v[152:155], v[128:131], v[40:43]
	ds_read_b128 v[116:119], v17 offset:34816
	v_mfma_f32_16x16x32_f16 v[44:47], v[156:159], v[128:131], v[44:47]
	ds_read_b128 v[120:123], v17 offset:36864
	v_mfma_f32_16x16x32_f16 v[48:51], v[144:147], v[132:135], v[48:51]
	ds_read_b128 v[124:127], v17 offset:38912
	v_mfma_f32_16x16x32_f16 v[52:55], v[148:151], v[132:135], v[52:55]
	ds_read_b128 v[100:103], v16 offset:2048
	v_mfma_f32_16x16x32_f16 v[56:59], v[152:155], v[132:135], v[56:59]
	ds_read_b128 v[104:107], v16 offset:4096
	v_mfma_f32_16x16x32_f16 v[60:63], v[156:159], v[132:135], v[60:63]
	ds_read_b128 v[108:111], v16 offset:6144
	v_mfma_f32_16x16x32_f16 v[64:67], v[144:147], v[136:139], v[64:67]
	v_mfma_f32_16x16x32_f16 v[68:71], v[148:151], v[136:139], v[68:71]
	v_mfma_f32_16x16x32_f16 v[72:75], v[152:155], v[136:139], v[72:75]
	s_add_u32 m0, s14, 0xc000
	s_nop 0
	global_load_lds_dwordx4 v2, s[28:29]
	v_mfma_f32_16x16x32_f16 v[76:79], v[156:159], v[136:139], v[76:79]
	v_mfma_f32_16x16x32_f16 v[80:83], v[144:147], v[140:143], v[80:83]
	s_add_u32 m0, s14, 0xe000
	s_nop 0
	global_load_lds_dwordx4 v3, s[28:29]
	v_mfma_f32_16x16x32_f16 v[84:87], v[148:151], v[140:143], v[84:87]
	v_mfma_f32_16x16x32_f16 v[88:91], v[152:155], v[140:143], v[88:91]
	s_add_u32 m0, s14, 0x10000
	s_nop 0
	global_load_lds_dwordx4 v4, s[28:29]
	v_mfma_f32_16x16x32_f16 v[92:95], v[156:159], v[140:143], v[92:95]
	s_waitcnt lgkmcnt(0)
	v_mfma_f32_16x16x32_f16 v[32:35], v[112:115], v[96:99], v[32:35]
	ds_read_b128 v[128:131], v18
	v_mfma_f32_16x16x32_f16 v[36:39], v[116:119], v[96:99], v[36:39]
	ds_read_b128 v[144:147], v19 offset:32768
	v_mfma_f32_16x16x32_f16 v[40:43], v[120:123], v[96:99], v[40:43]
	ds_read_b128 v[148:151], v19 offset:34816
	v_mfma_f32_16x16x32_f16 v[44:47], v[124:127], v[96:99], v[44:47]
	ds_read_b128 v[152:155], v19 offset:36864
	v_mfma_f32_16x16x32_f16 v[48:51], v[112:115], v[100:103], v[48:51]
	ds_read_b128 v[156:159], v19 offset:38912
	v_mfma_f32_16x16x32_f16 v[52:55], v[116:119], v[100:103], v[52:55]
	ds_read_b128 v[132:135], v18 offset:2048
	v_mfma_f32_16x16x32_f16 v[56:59], v[120:123], v[100:103], v[56:59]
	ds_read_b128 v[136:139], v18 offset:4096
	v_mfma_f32_16x16x32_f16 v[60:63], v[124:127], v[100:103], v[60:63]
	ds_read_b128 v[140:143], v18 offset:6144
	v_mfma_f32_16x16x32_f16 v[64:67], v[112:115], v[104:107], v[64:67]
	v_mfma_f32_16x16x32_f16 v[68:71], v[116:119], v[104:107], v[68:71]
	v_mfma_f32_16x16x32_f16 v[72:75], v[120:123], v[104:107], v[72:75]
	s_add_u32 m0, s14, 0x12000
	s_nop 0
	global_load_lds_dwordx4 v5, s[28:29]
	v_mfma_f32_16x16x32_f16 v[76:79], v[124:127], v[104:107], v[76:79]
	v_mfma_f32_16x16x32_f16 v[80:83], v[112:115], v[108:111], v[80:83]
	s_add_u32 m0, s14, 0x14000
	s_nop 0
	global_load_lds_dwordx4 v6, s[30:31]
	v_mfma_f32_16x16x32_f16 v[84:87], v[116:119], v[108:111], v[84:87]
	v_mfma_f32_16x16x32_f16 v[88:91], v[120:123], v[108:111], v[88:91]
	s_add_u32 m0, s14, 0x16000
	s_nop 0
	global_load_lds_dwordx4 v7, s[30:31]
	v_mfma_f32_16x16x32_f16 v[92:95], v[124:127], v[108:111], v[92:95]
	s_waitcnt vmcnt(6) lgkmcnt(0)
	s_barrier
	s_add_u32 s28, s28, 0x80
	s_addc_u32 s29, s29, 0
	s_add_u32 s30, s30, 0x80
	s_addc_u32 s31, s31, 0
	s_waitcnt lgkmcnt(0)
	v_mfma_f32_16x16x32_f16 v[32:35], v[144:147], v[128:131], v[32:35]
	ds_read_b128 v[96:99], v8
	v_mfma_f32_16x16x32_f16 v[36:39], v[148:151], v[128:131], v[36:39]
	ds_read_b128 v[112:115], v9 offset:32768
	v_mfma_f32_16x16x32_f16 v[40:43], v[152:155], v[128:131], v[40:43]
	ds_read_b128 v[116:119], v9 offset:34816
	v_mfma_f32_16x16x32_f16 v[44:47], v[156:159], v[128:131], v[44:47]
	ds_read_b128 v[120:123], v9 offset:36864
	v_mfma_f32_16x16x32_f16 v[48:51], v[144:147], v[132:135], v[48:51]
	ds_read_b128 v[124:127], v9 offset:38912
	v_mfma_f32_16x16x32_f16 v[52:55], v[148:151], v[132:135], v[52:55]
	ds_read_b128 v[100:103], v8 offset:2048
	v_mfma_f32_16x16x32_f16 v[56:59], v[152:155], v[132:135], v[56:59]
	ds_read_b128 v[104:107], v8 offset:4096
	v_mfma_f32_16x16x32_f16 v[60:63], v[156:159], v[132:135], v[60:63]
	ds_read_b128 v[108:111], v8 offset:6144
	v_mfma_f32_16x16x32_f16 v[64:67], v[144:147], v[136:139], v[64:67]
	v_mfma_f32_16x16x32_f16 v[68:71], v[148:151], v[136:139], v[68:71]
	v_mfma_f32_16x16x32_f16 v[72:75], v[152:155], v[136:139], v[72:75]
	s_add_u32 m0, s14, 0x18000
	s_nop 0
	global_load_lds_dwordx4 v2, s[28:29]
	v_mfma_f32_16x16x32_f16 v[76:79], v[156:159], v[136:139], v[76:79]
	v_mfma_f32_16x16x32_f16 v[80:83], v[144:147], v[140:143], v[80:83]
	s_add_u32 m0, s14, 0x1a000
	s_nop 0
	global_load_lds_dwordx4 v3, s[28:29]
	v_mfma_f32_16x16x32_f16 v[84:87], v[148:151], v[140:143], v[84:87]
	v_mfma_f32_16x16x32_f16 v[88:91], v[152:155], v[140:143], v[88:91]
	s_add_u32 m0, s14, 0x1c000
	s_nop 0
	global_load_lds_dwordx4 v4, s[28:29]
	v_mfma_f32_16x16x32_f16 v[92:95], v[156:159], v[140:143], v[92:95]
	s_waitcnt lgkmcnt(0)
	v_mfma_f32_16x16x32_f16 v[32:35], v[112:115], v[96:99], v[32:35]
	ds_read_b128 v[128:131], v10
	v_mfma_f32_16x16x32_f16 v[36:39], v[116:119], v[96:99], v[36:39]
	ds_read_b128 v[144:147], v11 offset:32768
	v_mfma_f32_16x16x32_f16 v[40:43], v[120:123], v[96:99], v[40:43]
	ds_read_b128 v[148:151], v11 offset:34816
	v_mfma_f32_16x16x32_f16 v[44:47], v[124:127], v[96:99], v[44:47]
	ds_read_b128 v[152:155], v11 offset:36864
	v_mfma_f32_16x16x32_f16 v[48:51], v[112:115], v[100:103], v[48:51]
	ds_read_b128 v[156:159], v11 offset:38912
	v_mfma_f32_16x16x32_f16 v[52:55], v[116:119], v[100:103], v[52:55]
	ds_read_b128 v[132:135], v10 offset:2048
	v_mfma_f32_16x16x32_f16 v[56:59], v[120:123], v[100:103], v[56:59]
	ds_read_b128 v[136:139], v10 offset:4096
	v_mfma_f32_16x16x32_f16 v[60:63], v[124:127], v[100:103], v[60:63]
	ds_read_b128 v[140:143], v10 offset:6144
	v_mfma_f32_16x16x32_f16 v[64:67], v[112:115], v[104:107], v[64:67]
	v_mfma_f32_16x16x32_f16 v[68:71], v[116:119], v[104:107], v[68:71]
	v_mfma_f32_16x16x32_f16 v[72:75], v[120:123], v[104:107], v[72:75]
	s_add_u32 m0, s14, 0x1e000
	s_nop 0
	global_load_lds_dwordx4 v5, s[28:29]
	v_mfma_f32_16x16x32_f16 v[76:79], v[124:127], v[104:107], v[76:79]
	v_mfma_f32_16x16x32_f16 v[80:83], v[112:115], v[108:111], v[80:83]
	s_add_u32 m0, s14, 0x20000
	s_nop 0
	global_load_lds_dwordx4 v6, s[30:31]
	v_mfma_f32_16x16x32_f16 v[84:87], v[116:119], v[108:111], v[84:87]
	v_mfma_f32_16x16x32_f16 v[88:91], v[120:123], v[108:111], v[88:91]
	s_add_u32 m0, s14, 0x22000
	s_nop 0
	global_load_lds_dwordx4 v7, s[30:31]
	v_mfma_f32_16x16x32_f16 v[92:95], v[124:127], v[108:111], v[92:95]
	s_waitcnt vmcnt(6) lgkmcnt(0)
	s_barrier
	s_add_u32 s28, s28, 0x80
	s_addc_u32 s29, s29, 0
	s_add_u32 s30, s30, 0x80
	s_addc_u32 s31, s31, 0
	s_waitcnt lgkmcnt(0)
	v_mfma_f32_16x16x32_f16 v[32:35], v[144:147], v[128:131], v[32:35]
	ds_read_b128 v[96:99], v12
	v_mfma_f32_16x16x32_f16 v[36:39], v[148:151], v[128:131], v[36:39]
	ds_read_b128 v[112:115], v13 offset:32768
	v_mfma_f32_16x16x32_f16 v[40:43], v[152:155], v[128:131], v[40:43]
	ds_read_b128 v[116:119], v13 offset:34816
	v_mfma_f32_16x16x32_f16 v[44:47], v[156:159], v[128:131], v[44:47]
	ds_read_b128 v[120:123], v13 offset:36864
	v_mfma_f32_16x16x32_f16 v[48:51], v[144:147], v[132:135], v[48:51]
	ds_read_b128 v[124:127], v13 offset:38912
	v_mfma_f32_16x16x32_f16 v[52:55], v[148:151], v[132:135], v[52:55]
	ds_read_b128 v[100:103], v12 offset:2048
	v_mfma_f32_16x16x32_f16 v[56:59], v[152:155], v[132:135], v[56:59]
	ds_read_b128 v[104:107], v12 offset:4096
	v_mfma_f32_16x16x32_f16 v[60:63], v[156:159], v[132:135], v[60:63]
	ds_read_b128 v[108:111], v12 offset:6144
	v_mfma_f32_16x16x32_f16 v[64:67], v[144:147], v[136:139], v[64:67]
	v_mfma_f32_16x16x32_f16 v[68:71], v[148:151], v[136:139], v[68:71]
	v_mfma_f32_16x16x32_f16 v[72:75], v[152:155], v[136:139], v[72:75]
	s_add_u32 m0, s14, 0x0
	s_nop 0
	global_load_lds_dwordx4 v2, s[28:29]
	v_mfma_f32_16x16x32_f16 v[76:79], v[156:159], v[136:139], v[76:79]
	v_mfma_f32_16x16x32_f16 v[80:83], v[144:147], v[140:143], v[80:83]
	s_add_u32 m0, s14, 0x2000
	s_nop 0
	global_load_lds_dwordx4 v3, s[28:29]
	v_mfma_f32_16x16x32_f16 v[84:87], v[148:151], v[140:143], v[84:87]
	v_mfma_f32_16x16x32_f16 v[88:91], v[152:155], v[140:143], v[88:91]
	s_add_u32 m0, s14, 0x4000
	s_nop 0
	global_load_lds_dwordx4 v4, s[28:29]
	v_mfma_f32_16x16x32_f16 v[92:95], v[156:159], v[140:143], v[92:95]
	s_waitcnt lgkmcnt(0)
	v_mfma_f32_16x16x32_f16 v[32:35], v[112:115], v[96:99], v[32:35]
	ds_read_b128 v[128:131], v14
	v_mfma_f32_16x16x32_f16 v[36:39], v[116:119], v[96:99], v[36:39]
	ds_read_b128 v[144:147], v15 offset:32768
	v_mfma_f32_16x16x32_f16 v[40:43], v[120:123], v[96:99], v[40:43]
	ds_read_b128 v[148:151], v15 offset:34816
	v_mfma_f32_16x16x32_f16 v[44:47], v[124:127], v[96:99], v[44:47]
	ds_read_b128 v[152:155], v15 offset:36864
	v_mfma_f32_16x16x32_f16 v[48:51], v[112:115], v[100:103], v[48:51]
	ds_read_b128 v[156:159], v15 offset:38912
	v_mfma_f32_16x16x32_f16 v[52:55], v[116:119], v[100:103], v[52:55]
	ds_read_b128 v[132:135], v14 offset:2048
	v_mfma_f32_16x16x32_f16 v[56:59], v[120:123], v[100:103], v[56:59]
	ds_read_b128 v[136:139], v14 offset:4096
	v_mfma_f32_16x16x32_f16 v[60:63], v[124:127], v[100:103], v[60:63]
	ds_read_b128 v[140:143], v14 offset:6144
	v_mfma_f32_16x16x32_f16 v[64:67], v[112:115], v[104:107], v[64:67]
	v_mfma_f32_16x16x32_f16 v[68:71], v[116:119], v[104:107], v[68:71]
	v_mfma_f32_16x16x32_f16 v[72:75], v[120:123], v[104:107], v[72:75]
	s_add_u32 m0, s14, 0x6000
	s_nop 0
	global_load_lds_dwordx4 v5, s[28:29]
	v_mfma_f32_16x16x32_f16 v[76:79], v[124:127], v[104:107], v[76:79]
	v_mfma_f32_16x16x32_f16 v[80:83], v[112:115], v[108:111], v[80:83]
	s_add_u32 m0, s14, 0x8000
	s_nop 0
	global_load_lds_dwordx4 v6, s[30:31]
	v_mfma_f32_16x16x32_f16 v[84:87], v[116:119], v[108:111], v[84:87]
	v_mfma_f32_16x16x32_f16 v[88:91], v[120:123], v[108:111], v[88:91]
	s_add_u32 m0, s14, 0xa000
	s_nop 0
	global_load_lds_dwordx4 v7, s[30:31]
	v_mfma_f32_16x16x32_f16 v[92:95], v[124:127], v[108:111], v[92:95]
	s_waitcnt vmcnt(6) lgkmcnt(0)
	s_barrier
	s_add_u32 s28, s28, 0x80
	s_addc_u32 s29, s29, 0
	s_add_u32 s30, s30, 0x80
	s_addc_u32 s31, s31, 0
	s_waitcnt lgkmcnt(0)
	v_mfma_f32_16x16x32_f16 v[32:35], v[144:147], v[128:131], v[32:35]
	ds_read_b128 v[96:99], v16
	v_mfma_f32_16x16x32_f16 v[36:39], v[148:151], v[128:131], v[36:39]
	ds_read_b128 v[112:115], v17 offset:32768
	v_mfma_f32_16x16x32_f16 v[40:43], v[152:155], v[128:131], v[40:43]
	ds_read_b128 v[116:119], v17 offset:34816
	v_mfma_f32_16x16x32_f16 v[44:47], v[156:159], v[128:131], v[44:47]
	ds_read_b128 v[120:123], v17 offset:36864
	v_mfma_f32_16x16x32_f16 v[48:51], v[144:147], v[132:135], v[48:51]
	ds_read_b128 v[124:127], v17 offset:38912
	v_mfma_f32_16x16x32_f16 v[52:55], v[148:151], v[132:135], v[52:55]
	ds_read_b128 v[100:103], v16 offset:2048
	v_mfma_f32_16x16x32_f16 v[56:59], v[152:155], v[132:135], v[56:59]
	ds_read_b128 v[104:107], v16 offset:4096
	v_mfma_f32_16x16x32_f16 v[60:63], v[156:159], v[132:135], v[60:63]
	ds_read_b128 v[108:111], v16 offset:6144
	v_mfma_f32_16x16x32_f16 v[64:67], v[144:147], v[136:139], v[64:67]
	v_mfma_f32_16x16x32_f16 v[68:71], v[148:151], v[136:139], v[68:71]
	v_mfma_f32_16x16x32_f16 v[72:75], v[152:155], v[136:139], v[72:75]
	s_add_u32 m0, s14, 0xc000
	s_nop 0
	global_load_lds_dwordx4 v2, s[28:29]
	v_mfma_f32_16x16x32_f16 v[76:79], v[156:159], v[136:139], v[76:79]
	v_mfma_f32_16x16x32_f16 v[80:83], v[144:147], v[140:143], v[80:83]
	s_add_u32 m0, s14, 0xe000
	s_nop 0
	global_load_lds_dwordx4 v3, s[28:29]
	v_mfma_f32_16x16x32_f16 v[84:87], v[148:151], v[140:143], v[84:87]
	v_mfma_f32_16x16x32_f16 v[88:91], v[152:155], v[140:143], v[88:91]
	s_add_u32 m0, s14, 0x10000
	s_nop 0
	global_load_lds_dwordx4 v4, s[28:29]
	v_mfma_f32_16x16x32_f16 v[92:95], v[156:159], v[140:143], v[92:95]
	s_waitcnt lgkmcnt(0)
	v_mfma_f32_16x16x32_f16 v[32:35], v[112:115], v[96:99], v[32:35]
	ds_read_b128 v[128:131], v18
	v_mfma_f32_16x16x32_f16 v[36:39], v[116:119], v[96:99], v[36:39]
	ds_read_b128 v[144:147], v19 offset:32768
	v_mfma_f32_16x16x32_f16 v[40:43], v[120:123], v[96:99], v[40:43]
	ds_read_b128 v[148:151], v19 offset:34816
	v_mfma_f32_16x16x32_f16 v[44:47], v[124:127], v[96:99], v[44:47]
	ds_read_b128 v[152:155], v19 offset:36864
	v_mfma_f32_16x16x32_f16 v[48:51], v[112:115], v[100:103], v[48:51]
	ds_read_b128 v[156:159], v19 offset:38912
	v_mfma_f32_16x16x32_f16 v[52:55], v[116:119], v[100:103], v[52:55]
	ds_read_b128 v[132:135], v18 offset:2048
	v_mfma_f32_16x16x32_f16 v[56:59], v[120:123], v[100:103], v[56:59]
	ds_read_b128 v[136:139], v18 offset:4096
	v_mfma_f32_16x16x32_f16 v[60:63], v[124:127], v[100:103], v[60:63]
	ds_read_b128 v[140:143], v18 offset:6144
	v_mfma_f32_16x16x32_f16 v[64:67], v[112:115], v[104:107], v[64:67]
	v_mfma_f32_16x16x32_f16 v[68:71], v[116:119], v[104:107], v[68:71]
	v_mfma_f32_16x16x32_f16 v[72:75], v[120:123], v[104:107], v[72:75]
	s_add_u32 m0, s14, 0x12000
	s_nop 0
	global_load_lds_dwordx4 v5, s[28:29]
	v_mfma_f32_16x16x32_f16 v[76:79], v[124:127], v[104:107], v[76:79]
	v_mfma_f32_16x16x32_f16 v[80:83], v[112:115], v[108:111], v[80:83]
	s_add_u32 m0, s14, 0x14000
	s_nop 0
	global_load_lds_dwordx4 v6, s[30:31]
	v_mfma_f32_16x16x32_f16 v[84:87], v[116:119], v[108:111], v[84:87]
	v_mfma_f32_16x16x32_f16 v[88:91], v[120:123], v[108:111], v[88:91]
	s_add_u32 m0, s14, 0x16000
	s_nop 0
	global_load_lds_dwordx4 v7, s[30:31]
	v_mfma_f32_16x16x32_f16 v[92:95], v[124:127], v[108:111], v[92:95]
	s_waitcnt vmcnt(6) lgkmcnt(0)
	s_barrier
	s_add_u32 s28, s28, 0x80
	s_addc_u32 s29, s29, 0
	s_add_u32 s30, s30, 0x80
	s_addc_u32 s31, s31, 0
	s_waitcnt lgkmcnt(0)
	v_mfma_f32_16x16x32_f16 v[32:35], v[144:147], v[128:131], v[32:35]
	ds_read_b128 v[96:99], v8
	v_mfma_f32_16x16x32_f16 v[36:39], v[148:151], v[128:131], v[36:39]
	ds_read_b128 v[112:115], v9 offset:32768
	v_mfma_f32_16x16x32_f16 v[40:43], v[152:155], v[128:131], v[40:43]
	ds_read_b128 v[116:119], v9 offset:34816
	v_mfma_f32_16x16x32_f16 v[44:47], v[156:159], v[128:131], v[44:47]
	ds_read_b128 v[120:123], v9 offset:36864
	v_mfma_f32_16x16x32_f16 v[48:51], v[144:147], v[132:135], v[48:51]
	ds_read_b128 v[124:127], v9 offset:38912
	v_mfma_f32_16x16x32_f16 v[52:55], v[148:151], v[132:135], v[52:55]
	ds_read_b128 v[100:103], v8 offset:2048
	v_mfma_f32_16x16x32_f16 v[56:59], v[152:155], v[132:135], v[56:59]
	ds_read_b128 v[104:107], v8 offset:4096
	v_mfma_f32_16x16x32_f16 v[60:63], v[156:159], v[132:135], v[60:63]
	ds_read_b128 v[108:111], v8 offset:6144
	v_mfma_f32_16x16x32_f16 v[64:67], v[144:147], v[136:139], v[64:67]
	v_mfma_f32_16x16x32_f16 v[68:71], v[148:151], v[136:139], v[68:71]
	v_mfma_f32_16x16x32_f16 v[72:75], v[152:155], v[136:139], v[72:75]
	s_add_u32 m0, s14, 0x18000
	s_nop 0
	global_load_lds_dwordx4 v2, s[28:29]
	v_mfma_f32_16x16x32_f16 v[76:79], v[156:159], v[136:139], v[76:79]
	v_mfma_f32_16x16x32_f16 v[80:83], v[144:147], v[140:143], v[80:83]
	s_add_u32 m0, s14, 0x1a000
	s_nop 0
	global_load_lds_dwordx4 v3, s[28:29]
	v_mfma_f32_16x16x32_f16 v[84:87], v[148:151], v[140:143], v[84:87]
	v_mfma_f32_16x16x32_f16 v[88:91], v[152:155], v[140:143], v[88:91]
	s_add_u32 m0, s14, 0x1c000
	s_nop 0
	global_load_lds_dwordx4 v4, s[28:29]
	v_mfma_f32_16x16x32_f16 v[92:95], v[156:159], v[140:143], v[92:95]
	s_waitcnt lgkmcnt(0)
	v_mfma_f32_16x16x32_f16 v[32:35], v[112:115], v[96:99], v[32:35]
	ds_read_b128 v[128:131], v10
	v_mfma_f32_16x16x32_f16 v[36:39], v[116:119], v[96:99], v[36:39]
	ds_read_b128 v[144:147], v11 offset:32768
	v_mfma_f32_16x16x32_f16 v[40:43], v[120:123], v[96:99], v[40:43]
	ds_read_b128 v[148:151], v11 offset:34816
	v_mfma_f32_16x16x32_f16 v[44:47], v[124:127], v[96:99], v[44:47]
	ds_read_b128 v[152:155], v11 offset:36864
	v_mfma_f32_16x16x32_f16 v[48:51], v[112:115], v[100:103], v[48:51]
	ds_read_b128 v[156:159], v11 offset:38912
	v_mfma_f32_16x16x32_f16 v[52:55], v[116:119], v[100:103], v[52:55]
	ds_read_b128 v[132:135], v10 offset:2048
	v_mfma_f32_16x16x32_f16 v[56:59], v[120:123], v[100:103], v[56:59]
	ds_read_b128 v[136:139], v10 offset:4096
	v_mfma_f32_16x16x32_f16 v[60:63], v[124:127], v[100:103], v[60:63]
	ds_read_b128 v[140:143], v10 offset:6144
	v_mfma_f32_16x16x32_f16 v[64:67], v[112:115], v[104:107], v[64:67]
	v_mfma_f32_16x16x32_f16 v[68:71], v[116:119], v[104:107], v[68:71]
	v_mfma_f32_16x16x32_f16 v[72:75], v[120:123], v[104:107], v[72:75]
	s_add_u32 m0, s14, 0x1e000
	s_nop 0
	global_load_lds_dwordx4 v5, s[28:29]
	v_mfma_f32_16x16x32_f16 v[76:79], v[124:127], v[104:107], v[76:79]
	v_mfma_f32_16x16x32_f16 v[80:83], v[112:115], v[108:111], v[80:83]
	s_add_u32 m0, s14, 0x20000
	s_nop 0
	global_load_lds_dwordx4 v6, s[30:31]
	v_mfma_f32_16x16x32_f16 v[84:87], v[116:119], v[108:111], v[84:87]
	v_mfma_f32_16x16x32_f16 v[88:91], v[120:123], v[108:111], v[88:91]
	s_add_u32 m0, s14, 0x22000
	s_nop 0
	global_load_lds_dwordx4 v7, s[30:31]
	v_mfma_f32_16x16x32_f16 v[92:95], v[124:127], v[108:111], v[92:95]
	s_waitcnt vmcnt(6) lgkmcnt(0)
	s_barrier
	s_add_u32 s28, s28, 0x80
	s_addc_u32 s29, s29, 0
	s_add_u32 s30, s30, 0x80
	s_addc_u32 s31, s31, 0
	s_waitcnt lgkmcnt(0)
	v_mfma_f32_16x16x32_f16 v[32:35], v[144:147], v[128:131], v[32:35]
	ds_read_b128 v[96:99], v12
	v_mfma_f32_16x16x32_f16 v[36:39], v[148:151], v[128:131], v[36:39]
	ds_read_b128 v[112:115], v13 offset:32768
	v_mfma_f32_16x16x32_f16 v[40:43], v[152:155], v[128:131], v[40:43]
	ds_read_b128 v[116:119], v13 offset:34816
	v_mfma_f32_16x16x32_f16 v[44:47], v[156:159], v[128:131], v[44:47]
	ds_read_b128 v[120:123], v13 offset:36864
	v_mfma_f32_16x16x32_f16 v[48:51], v[144:147], v[132:135], v[48:51]
	ds_read_b128 v[124:127], v13 offset:38912
	v_mfma_f32_16x16x32_f16 v[52:55], v[148:151], v[132:135], v[52:55]
	ds_read_b128 v[100:103], v12 offset:2048
	v_mfma_f32_16x16x32_f16 v[56:59], v[152:155], v[132:135], v[56:59]
	ds_read_b128 v[104:107], v12 offset:4096
	v_mfma_f32_16x16x32_f16 v[60:63], v[156:159], v[132:135], v[60:63]
	ds_read_b128 v[108:111], v12 offset:6144
	v_mfma_f32_16x16x32_f16 v[64:67], v[144:147], v[136:139], v[64:67]
	v_mfma_f32_16x16x32_f16 v[68:71], v[148:151], v[136:139], v[68:71]
	v_mfma_f32_16x16x32_f16 v[72:75], v[152:155], v[136:139], v[72:75]
	s_add_u32 m0, s14, 0x0
	s_nop 0
	global_load_lds_dwordx4 v2, s[28:29]
	v_mfma_f32_16x16x32_f16 v[76:79], v[156:159], v[136:139], v[76:79]
	v_mfma_f32_16x16x32_f16 v[80:83], v[144:147], v[140:143], v[80:83]
	s_add_u32 m0, s14, 0x2000
	s_nop 0
	global_load_lds_dwordx4 v3, s[28:29]
	v_mfma_f32_16x16x32_f16 v[84:87], v[148:151], v[140:143], v[84:87]
	v_mfma_f32_16x16x32_f16 v[88:91], v[152:155], v[140:143], v[88:91]
	s_add_u32 m0, s14, 0x4000
	s_nop 0
	global_load_lds_dwordx4 v4, s[28:29]
	v_mfma_f32_16x16x32_f16 v[92:95], v[156:159], v[140:143], v[92:95]
	s_waitcnt lgkmcnt(0)
	v_mfma_f32_16x16x32_f16 v[32:35], v[112:115], v[96:99], v[32:35]
	ds_read_b128 v[128:131], v14
	v_mfma_f32_16x16x32_f16 v[36:39], v[116:119], v[96:99], v[36:39]
	ds_read_b128 v[144:147], v15 offset:32768
	v_mfma_f32_16x16x32_f16 v[40:43], v[120:123], v[96:99], v[40:43]
	ds_read_b128 v[148:151], v15 offset:34816
	v_mfma_f32_16x16x32_f16 v[44:47], v[124:127], v[96:99], v[44:47]
	ds_read_b128 v[152:155], v15 offset:36864
	v_mfma_f32_16x16x32_f16 v[48:51], v[112:115], v[100:103], v[48:51]
	ds_read_b128 v[156:159], v15 offset:38912
	v_mfma_f32_16x16x32_f16 v[52:55], v[116:119], v[100:103], v[52:55]
	ds_read_b128 v[132:135], v14 offset:2048
	v_mfma_f32_16x16x32_f16 v[56:59], v[120:123], v[100:103], v[56:59]
	ds_read_b128 v[136:139], v14 offset:4096
	v_mfma_f32_16x16x32_f16 v[60:63], v[124:127], v[100:103], v[60:63]
	ds_read_b128 v[140:143], v14 offset:6144
	v_mfma_f32_16x16x32_f16 v[64:67], v[112:115], v[104:107], v[64:67]
	v_mfma_f32_16x16x32_f16 v[68:71], v[116:119], v[104:107], v[68:71]
	v_mfma_f32_16x16x32_f16 v[72:75], v[120:123], v[104:107], v[72:75]
	s_add_u32 m0, s14, 0x6000
	s_nop 0
	global_load_lds_dwordx4 v5, s[28:29]
	v_mfma_f32_16x16x32_f16 v[76:79], v[124:127], v[104:107], v[76:79]
	v_mfma_f32_16x16x32_f16 v[80:83], v[112:115], v[108:111], v[80:83]
	s_add_u32 m0, s14, 0x8000
	s_nop 0
	global_load_lds_dwordx4 v6, s[30:31]
	v_mfma_f32_16x16x32_f16 v[84:87], v[116:119], v[108:111], v[84:87]
	v_mfma_f32_16x16x32_f16 v[88:91], v[120:123], v[108:111], v[88:91]
	s_add_u32 m0, s14, 0xa000
	s_nop 0
	global_load_lds_dwordx4 v7, s[30:31]
	v_mfma_f32_16x16x32_f16 v[92:95], v[124:127], v[108:111], v[92:95]
	s_waitcnt vmcnt(6) lgkmcnt(0)
	s_barrier
	s_add_u32 s28, s28, 0x80
	s_addc_u32 s29, s29, 0
	s_add_u32 s30, s30, 0x80
	s_addc_u32 s31, s31, 0
	s_waitcnt lgkmcnt(0)
	v_mfma_f32_16x16x32_f16 v[32:35], v[144:147], v[128:131], v[32:35]
	ds_read_b128 v[96:99], v16
	v_mfma_f32_16x16x32_f16 v[36:39], v[148:151], v[128:131], v[36:39]
	ds_read_b128 v[112:115], v17 offset:32768
	v_mfma_f32_16x16x32_f16 v[40:43], v[152:155], v[128:131], v[40:43]
	ds_read_b128 v[116:119], v17 offset:34816
	v_mfma_f32_16x16x32_f16 v[44:47], v[156:159], v[128:131], v[44:47]
	ds_read_b128 v[120:123], v17 offset:36864
	v_mfma_f32_16x16x32_f16 v[48:51], v[144:147], v[132:135], v[48:51]
	ds_read_b128 v[124:127], v17 offset:38912
	v_mfma_f32_16x16x32_f16 v[52:55], v[148:151], v[132:135], v[52:55]
	ds_read_b128 v[100:103], v16 offset:2048
	v_mfma_f32_16x16x32_f16 v[56:59], v[152:155], v[132:135], v[56:59]
	ds_read_b128 v[104:107], v16 offset:4096
	v_mfma_f32_16x16x32_f16 v[60:63], v[156:159], v[132:135], v[60:63]
	ds_read_b128 v[108:111], v16 offset:6144
	v_mfma_f32_16x16x32_f16 v[64:67], v[144:147], v[136:139], v[64:67]
	v_mfma_f32_16x16x32_f16 v[68:71], v[148:151], v[136:139], v[68:71]
	v_mfma_f32_16x16x32_f16 v[72:75], v[152:155], v[136:139], v[72:75]
	s_add_u32 m0, s14, 0xc000
	s_nop 0
	global_load_lds_dwordx4 v2, s[28:29]
	v_mfma_f32_16x16x32_f16 v[76:79], v[156:159], v[136:139], v[76:79]
	v_mfma_f32_16x16x32_f16 v[80:83], v[144:147], v[140:143], v[80:83]
	s_add_u32 m0, s14, 0xe000
	s_nop 0
	global_load_lds_dwordx4 v3, s[28:29]
	v_mfma_f32_16x16x32_f16 v[84:87], v[148:151], v[140:143], v[84:87]
	v_mfma_f32_16x16x32_f16 v[88:91], v[152:155], v[140:143], v[88:91]
	s_add_u32 m0, s14, 0x10000
	s_nop 0
	global_load_lds_dwordx4 v4, s[28:29]
	v_mfma_f32_16x16x32_f16 v[92:95], v[156:159], v[140:143], v[92:95]
	s_waitcnt lgkmcnt(0)
	v_mfma_f32_16x16x32_f16 v[32:35], v[112:115], v[96:99], v[32:35]
	ds_read_b128 v[128:131], v18
	v_mfma_f32_16x16x32_f16 v[36:39], v[116:119], v[96:99], v[36:39]
	ds_read_b128 v[144:147], v19 offset:32768
	v_mfma_f32_16x16x32_f16 v[40:43], v[120:123], v[96:99], v[40:43]
	ds_read_b128 v[148:151], v19 offset:34816
	v_mfma_f32_16x16x32_f16 v[44:47], v[124:127], v[96:99], v[44:47]
	ds_read_b128 v[152:155], v19 offset:36864
	v_mfma_f32_16x16x32_f16 v[48:51], v[112:115], v[100:103], v[48:51]
	ds_read_b128 v[156:159], v19 offset:38912
	v_mfma_f32_16x16x32_f16 v[52:55], v[116:119], v[100:103], v[52:55]
	ds_read_b128 v[132:135], v18 offset:2048
	v_mfma_f32_16x16x32_f16 v[56:59], v[120:123], v[100:103], v[56:59]
	ds_read_b128 v[136:139], v18 offset:4096
	v_mfma_f32_16x16x32_f16 v[60:63], v[124:127], v[100:103], v[60:63]
	ds_read_b128 v[140:143], v18 offset:6144
	v_mfma_f32_16x16x32_f16 v[64:67], v[112:115], v[104:107], v[64:67]
	v_mfma_f32_16x16x32_f16 v[68:71], v[116:119], v[104:107], v[68:71]
	v_mfma_f32_16x16x32_f16 v[72:75], v[120:123], v[104:107], v[72:75]
	s_add_u32 m0, s14, 0x12000
	s_nop 0
	global_load_lds_dwordx4 v5, s[28:29]
	v_mfma_f32_16x16x32_f16 v[76:79], v[124:127], v[104:107], v[76:79]
	v_mfma_f32_16x16x32_f16 v[80:83], v[112:115], v[108:111], v[80:83]
	s_add_u32 m0, s14, 0x14000
	s_nop 0
	global_load_lds_dwordx4 v6, s[30:31]
	v_mfma_f32_16x16x32_f16 v[84:87], v[116:119], v[108:111], v[84:87]
	v_mfma_f32_16x16x32_f16 v[88:91], v[120:123], v[108:111], v[88:91]
	s_add_u32 m0, s14, 0x16000
	s_nop 0
	global_load_lds_dwordx4 v7, s[30:31]
	v_mfma_f32_16x16x32_f16 v[92:95], v[124:127], v[108:111], v[92:95]
	s_waitcnt vmcnt(6) lgkmcnt(0)
	s_barrier
	s_add_u32 s28, s28, 0x80
	s_addc_u32 s29, s29, 0
	s_add_u32 s30, s30, 0x80
	s_addc_u32 s31, s31, 0
	s_waitcnt lgkmcnt(0)
	v_mfma_f32_16x16x32_f16 v[32:35], v[144:147], v[128:131], v[32:35]
	ds_read_b128 v[96:99], v8
	v_mfma_f32_16x16x32_f16 v[36:39], v[148:151], v[128:131], v[36:39]
	ds_read_b128 v[112:115], v9 offset:32768
	v_mfma_f32_16x16x32_f16 v[40:43], v[152:155], v[128:131], v[40:43]
	ds_read_b128 v[116:119], v9 offset:34816
	v_mfma_f32_16x16x32_f16 v[44:47], v[156:159], v[128:131], v[44:47]
	ds_read_b128 v[120:123], v9 offset:36864
	v_mfma_f32_16x16x32_f16 v[48:51], v[144:147], v[132:135], v[48:51]
	ds_read_b128 v[124:127], v9 offset:38912
	v_mfma_f32_16x16x32_f16 v[52:55], v[148:151], v[132:135], v[52:55]
	ds_read_b128 v[100:103], v8 offset:2048
	v_mfma_f32_16x16x32_f16 v[56:59], v[152:155], v[132:135], v[56:59]
	ds_read_b128 v[104:107], v8 offset:4096
	v_mfma_f32_16x16x32_f16 v[60:63], v[156:159], v[132:135], v[60:63]
	ds_read_b128 v[108:111], v8 offset:6144
	v_mfma_f32_16x16x32_f16 v[64:67], v[144:147], v[136:139], v[64:67]
	v_mfma_f32_16x16x32_f16 v[68:71], v[148:151], v[136:139], v[68:71]
	v_mfma_f32_16x16x32_f16 v[72:75], v[152:155], v[136:139], v[72:75]
	s_add_u32 m0, s14, 0x18000
	s_nop 0
	global_load_lds_dwordx4 v2, s[28:29]
	v_mfma_f32_16x16x32_f16 v[76:79], v[156:159], v[136:139], v[76:79]
	v_mfma_f32_16x16x32_f16 v[80:83], v[144:147], v[140:143], v[80:83]
	s_add_u32 m0, s14, 0x1a000
	s_nop 0
	global_load_lds_dwordx4 v3, s[28:29]
	v_mfma_f32_16x16x32_f16 v[84:87], v[148:151], v[140:143], v[84:87]
	v_mfma_f32_16x16x32_f16 v[88:91], v[152:155], v[140:143], v[88:91]
	s_add_u32 m0, s14, 0x1c000
	s_nop 0
	global_load_lds_dwordx4 v4, s[28:29]
	v_mfma_f32_16x16x32_f16 v[92:95], v[156:159], v[140:143], v[92:95]
	s_waitcnt lgkmcnt(0)
	v_mfma_f32_16x16x32_f16 v[32:35], v[112:115], v[96:99], v[32:35]
	ds_read_b128 v[128:131], v10
	v_mfma_f32_16x16x32_f16 v[36:39], v[116:119], v[96:99], v[36:39]
	ds_read_b128 v[144:147], v11 offset:32768
	v_mfma_f32_16x16x32_f16 v[40:43], v[120:123], v[96:99], v[40:43]
	ds_read_b128 v[148:151], v11 offset:34816
	v_mfma_f32_16x16x32_f16 v[44:47], v[124:127], v[96:99], v[44:47]
	ds_read_b128 v[152:155], v11 offset:36864
	v_mfma_f32_16x16x32_f16 v[48:51], v[112:115], v[100:103], v[48:51]
	ds_read_b128 v[156:159], v11 offset:38912
	v_mfma_f32_16x16x32_f16 v[52:55], v[116:119], v[100:103], v[52:55]
	ds_read_b128 v[132:135], v10 offset:2048
	v_mfma_f32_16x16x32_f16 v[56:59], v[120:123], v[100:103], v[56:59]
	ds_read_b128 v[136:139], v10 offset:4096
	v_mfma_f32_16x16x32_f16 v[60:63], v[124:127], v[100:103], v[60:63]
	ds_read_b128 v[140:143], v10 offset:6144
	v_mfma_f32_16x16x32_f16 v[64:67], v[112:115], v[104:107], v[64:67]
	v_mfma_f32_16x16x32_f16 v[68:71], v[116:119], v[104:107], v[68:71]
	v_mfma_f32_16x16x32_f16 v[72:75], v[120:123], v[104:107], v[72:75]
	s_add_u32 m0, s14, 0x1e000
	s_nop 0
	global_load_lds_dwordx4 v5, s[28:29]
	v_mfma_f32_16x16x32_f16 v[76:79], v[124:127], v[104:107], v[76:79]
	v_mfma_f32_16x16x32_f16 v[80:83], v[112:115], v[108:111], v[80:83]
	s_add_u32 m0, s14, 0x20000
	s_nop 0
	global_load_lds_dwordx4 v6, s[30:31]
	v_mfma_f32_16x16x32_f16 v[84:87], v[116:119], v[108:111], v[84:87]
	v_mfma_f32_16x16x32_f16 v[88:91], v[120:123], v[108:111], v[88:91]
	s_add_u32 m0, s14, 0x22000
	s_nop 0
	global_load_lds_dwordx4 v7, s[30:31]
	v_mfma_f32_16x16x32_f16 v[92:95], v[124:127], v[108:111], v[92:95]
	s_waitcnt vmcnt(6) lgkmcnt(0)
	s_barrier
	s_add_u32 s28, s28, 0x80
	s_addc_u32 s29, s29, 0
	s_add_u32 s30, s30, 0x80
	s_addc_u32 s31, s31, 0
	s_waitcnt lgkmcnt(0)
	v_mfma_f32_16x16x32_f16 v[32:35], v[144:147], v[128:131], v[32:35]
	ds_read_b128 v[96:99], v12
	v_mfma_f32_16x16x32_f16 v[36:39], v[148:151], v[128:131], v[36:39]
	ds_read_b128 v[112:115], v13 offset:32768
	v_mfma_f32_16x16x32_f16 v[40:43], v[152:155], v[128:131], v[40:43]
	ds_read_b128 v[116:119], v13 offset:34816
	v_mfma_f32_16x16x32_f16 v[44:47], v[156:159], v[128:131], v[44:47]
	ds_read_b128 v[120:123], v13 offset:36864
	v_mfma_f32_16x16x32_f16 v[48:51], v[144:147], v[132:135], v[48:51]
	ds_read_b128 v[124:127], v13 offset:38912
	v_mfma_f32_16x16x32_f16 v[52:55], v[148:151], v[132:135], v[52:55]
	ds_read_b128 v[100:103], v12 offset:2048
	v_mfma_f32_16x16x32_f16 v[56:59], v[152:155], v[132:135], v[56:59]
	ds_read_b128 v[104:107], v12 offset:4096
	v_mfma_f32_16x16x32_f16 v[60:63], v[156:159], v[132:135], v[60:63]
	ds_read_b128 v[108:111], v12 offset:6144
	v_mfma_f32_16x16x32_f16 v[64:67], v[144:147], v[136:139], v[64:67]
	v_mfma_f32_16x16x32_f16 v[68:71], v[148:151], v[136:139], v[68:71]
	v_mfma_f32_16x16x32_f16 v[72:75], v[152:155], v[136:139], v[72:75]
	s_add_u32 m0, s14, 0x0
	s_nop 0
	global_load_lds_dwordx4 v2, s[28:29]
	v_mfma_f32_16x16x32_f16 v[76:79], v[156:159], v[136:139], v[76:79]
	v_mfma_f32_16x16x32_f16 v[80:83], v[144:147], v[140:143], v[80:83]
	s_add_u32 m0, s14, 0x2000
	s_nop 0
	global_load_lds_dwordx4 v3, s[28:29]
	v_mfma_f32_16x16x32_f16 v[84:87], v[148:151], v[140:143], v[84:87]
	v_mfma_f32_16x16x32_f16 v[88:91], v[152:155], v[140:143], v[88:91]
	s_add_u32 m0, s14, 0x4000
	s_nop 0
	global_load_lds_dwordx4 v4, s[28:29]
	v_mfma_f32_16x16x32_f16 v[92:95], v[156:159], v[140:143], v[92:95]
	s_waitcnt lgkmcnt(0)
	v_mfma_f32_16x16x32_f16 v[32:35], v[112:115], v[96:99], v[32:35]
	ds_read_b128 v[128:131], v14
	v_mfma_f32_16x16x32_f16 v[36:39], v[116:119], v[96:99], v[36:39]
	ds_read_b128 v[144:147], v15 offset:32768
	v_mfma_f32_16x16x32_f16 v[40:43], v[120:123], v[96:99], v[40:43]
	ds_read_b128 v[148:151], v15 offset:34816
	v_mfma_f32_16x16x32_f16 v[44:47], v[124:127], v[96:99], v[44:47]
	ds_read_b128 v[152:155], v15 offset:36864
	v_mfma_f32_16x16x32_f16 v[48:51], v[112:115], v[100:103], v[48:51]
	ds_read_b128 v[156:159], v15 offset:38912
	v_mfma_f32_16x16x32_f16 v[52:55], v[116:119], v[100:103], v[52:55]
	ds_read_b128 v[132:135], v14 offset:2048
	v_mfma_f32_16x16x32_f16 v[56:59], v[120:123], v[100:103], v[56:59]
	ds_read_b128 v[136:139], v14 offset:4096
	v_mfma_f32_16x16x32_f16 v[60:63], v[124:127], v[100:103], v[60:63]
	ds_read_b128 v[140:143], v14 offset:6144
	v_mfma_f32_16x16x32_f16 v[64:67], v[112:115], v[104:107], v[64:67]
	v_mfma_f32_16x16x32_f16 v[68:71], v[116:119], v[104:107], v[68:71]
	v_mfma_f32_16x16x32_f16 v[72:75], v[120:123], v[104:107], v[72:75]
	s_add_u32 m0, s14, 0x6000
	s_nop 0
	global_load_lds_dwordx4 v5, s[28:29]
	v_mfma_f32_16x16x32_f16 v[76:79], v[124:127], v[104:107], v[76:79]
	v_mfma_f32_16x16x32_f16 v[80:83], v[112:115], v[108:111], v[80:83]
	s_add_u32 m0, s14, 0x8000
	s_nop 0
	global_load_lds_dwordx4 v6, s[30:31]
	v_mfma_f32_16x16x32_f16 v[84:87], v[116:119], v[108:111], v[84:87]
	v_mfma_f32_16x16x32_f16 v[88:91], v[120:123], v[108:111], v[88:91]
	s_add_u32 m0, s14, 0xa000
	s_nop 0
	global_load_lds_dwordx4 v7, s[30:31]
	v_mfma_f32_16x16x32_f16 v[92:95], v[124:127], v[108:111], v[92:95]
	s_waitcnt vmcnt(6) lgkmcnt(0)
	s_barrier
	s_add_u32 s28, s28, 0x80
	s_addc_u32 s29, s29, 0
	s_add_u32 s30, s30, 0x80
	s_addc_u32 s31, s31, 0
	s_waitcnt lgkmcnt(0)
	v_mfma_f32_16x16x32_f16 v[32:35], v[144:147], v[128:131], v[32:35]
	ds_read_b128 v[96:99], v16
	v_mfma_f32_16x16x32_f16 v[36:39], v[148:151], v[128:131], v[36:39]
	ds_read_b128 v[112:115], v17 offset:32768
	v_mfma_f32_16x16x32_f16 v[40:43], v[152:155], v[128:131], v[40:43]
	ds_read_b128 v[116:119], v17 offset:34816
	v_mfma_f32_16x16x32_f16 v[44:47], v[156:159], v[128:131], v[44:47]
	ds_read_b128 v[120:123], v17 offset:36864
	v_mfma_f32_16x16x32_f16 v[48:51], v[144:147], v[132:135], v[48:51]
	ds_read_b128 v[124:127], v17 offset:38912
	v_mfma_f32_16x16x32_f16 v[52:55], v[148:151], v[132:135], v[52:55]
	ds_read_b128 v[100:103], v16 offset:2048
	v_mfma_f32_16x16x32_f16 v[56:59], v[152:155], v[132:135], v[56:59]
	ds_read_b128 v[104:107], v16 offset:4096
	v_mfma_f32_16x16x32_f16 v[60:63], v[156:159], v[132:135], v[60:63]
	ds_read_b128 v[108:111], v16 offset:6144
	v_mfma_f32_16x16x32_f16 v[64:67], v[144:147], v[136:139], v[64:67]
	v_mfma_f32_16x16x32_f16 v[68:71], v[148:151], v[136:139], v[68:71]
	v_mfma_f32_16x16x32_f16 v[72:75], v[152:155], v[136:139], v[72:75]
	s_add_u32 m0, s14, 0xc000
	s_nop 0
	global_load_lds_dwordx4 v2, s[28:29]
	v_mfma_f32_16x16x32_f16 v[76:79], v[156:159], v[136:139], v[76:79]
	v_mfma_f32_16x16x32_f16 v[80:83], v[144:147], v[140:143], v[80:83]
	s_add_u32 m0, s14, 0xe000
	s_nop 0
	global_load_lds_dwordx4 v3, s[28:29]
	v_mfma_f32_16x16x32_f16 v[84:87], v[148:151], v[140:143], v[84:87]
	v_mfma_f32_16x16x32_f16 v[88:91], v[152:155], v[140:143], v[88:91]
	s_add_u32 m0, s14, 0x10000
	s_nop 0
	global_load_lds_dwordx4 v4, s[28:29]
	v_mfma_f32_16x16x32_f16 v[92:95], v[156:159], v[140:143], v[92:95]
	s_waitcnt lgkmcnt(0)
	v_mfma_f32_16x16x32_f16 v[32:35], v[112:115], v[96:99], v[32:35]
	ds_read_b128 v[128:131], v18
	v_mfma_f32_16x16x32_f16 v[36:39], v[116:119], v[96:99], v[36:39]
	ds_read_b128 v[144:147], v19 offset:32768
	v_mfma_f32_16x16x32_f16 v[40:43], v[120:123], v[96:99], v[40:43]
	ds_read_b128 v[148:151], v19 offset:34816
	v_mfma_f32_16x16x32_f16 v[44:47], v[124:127], v[96:99], v[44:47]
	ds_read_b128 v[152:155], v19 offset:36864
	v_mfma_f32_16x16x32_f16 v[48:51], v[112:115], v[100:103], v[48:51]
	ds_read_b128 v[156:159], v19 offset:38912
	v_mfma_f32_16x16x32_f16 v[52:55], v[116:119], v[100:103], v[52:55]
	ds_read_b128 v[132:135], v18 offset:2048
	v_mfma_f32_16x16x32_f16 v[56:59], v[120:123], v[100:103], v[56:59]
	ds_read_b128 v[136:139], v18 offset:4096
	v_mfma_f32_16x16x32_f16 v[60:63], v[124:127], v[100:103], v[60:63]
	ds_read_b128 v[140:143], v18 offset:6144
	v_mfma_f32_16x16x32_f16 v[64:67], v[112:115], v[104:107], v[64:67]
	v_mfma_f32_16x16x32_f16 v[68:71], v[116:119], v[104:107], v[68:71]
	v_mfma_f32_16x16x32_f16 v[72:75], v[120:123], v[104:107], v[72:75]
	s_add_u32 m0, s14, 0x12000
	s_nop 0
	global_load_lds_dwordx4 v5, s[28:29]
	v_mfma_f32_16x16x32_f16 v[76:79], v[124:127], v[104:107], v[76:79]
	v_mfma_f32_16x16x32_f16 v[80:83], v[112:115], v[108:111], v[80:83]
	s_add_u32 m0, s14, 0x14000
	s_nop 0
	global_load_lds_dwordx4 v6, s[30:31]
	v_mfma_f32_16x16x32_f16 v[84:87], v[116:119], v[108:111], v[84:87]
	v_mfma_f32_16x16x32_f16 v[88:91], v[120:123], v[108:111], v[88:91]
	s_add_u32 m0, s14, 0x16000
	s_nop 0
	global_load_lds_dwordx4 v7, s[30:31]
	v_mfma_f32_16x16x32_f16 v[92:95], v[124:127], v[108:111], v[92:95]
	s_waitcnt vmcnt(6) lgkmcnt(0)
	s_barrier
	s_add_u32 s28, s28, 0x80
	s_addc_u32 s29, s29, 0
	s_add_u32 s30, s30, 0x80
	s_addc_u32 s31, s31, 0
	s_waitcnt lgkmcnt(0)
	v_mfma_f32_16x16x32_f16 v[32:35], v[144:147], v[128:131], v[32:35]
	ds_read_b128 v[96:99], v8
	v_mfma_f32_16x16x32_f16 v[36:39], v[148:151], v[128:131], v[36:39]
	ds_read_b128 v[112:115], v9 offset:32768
	v_mfma_f32_16x16x32_f16 v[40:43], v[152:155], v[128:131], v[40:43]
	ds_read_b128 v[116:119], v9 offset:34816
	v_mfma_f32_16x16x32_f16 v[44:47], v[156:159], v[128:131], v[44:47]
	ds_read_b128 v[120:123], v9 offset:36864
	v_mfma_f32_16x16x32_f16 v[48:51], v[144:147], v[132:135], v[48:51]
	ds_read_b128 v[124:127], v9 offset:38912
	v_mfma_f32_16x16x32_f16 v[52:55], v[148:151], v[132:135], v[52:55]
	ds_read_b128 v[100:103], v8 offset:2048
	v_mfma_f32_16x16x32_f16 v[56:59], v[152:155], v[132:135], v[56:59]
	ds_read_b128 v[104:107], v8 offset:4096
	v_mfma_f32_16x16x32_f16 v[60:63], v[156:159], v[132:135], v[60:63]
	ds_read_b128 v[108:111], v8 offset:6144
	v_mfma_f32_16x16x32_f16 v[64:67], v[144:147], v[136:139], v[64:67]
	v_mfma_f32_16x16x32_f16 v[68:71], v[148:151], v[136:139], v[68:71]
	v_mfma_f32_16x16x32_f16 v[72:75], v[152:155], v[136:139], v[72:75]
	s_add_u32 m0, s14, 0x18000
	s_nop 0
	global_load_lds_dwordx4 v2, s[28:29]
	v_mfma_f32_16x16x32_f16 v[76:79], v[156:159], v[136:139], v[76:79]
	v_mfma_f32_16x16x32_f16 v[80:83], v[144:147], v[140:143], v[80:83]
	s_add_u32 m0, s14, 0x1a000
	s_nop 0
	global_load_lds_dwordx4 v3, s[28:29]
	v_mfma_f32_16x16x32_f16 v[84:87], v[148:151], v[140:143], v[84:87]
	v_mfma_f32_16x16x32_f16 v[88:91], v[152:155], v[140:143], v[88:91]
	s_add_u32 m0, s14, 0x1c000
	s_nop 0
	global_load_lds_dwordx4 v4, s[28:29]
	v_mfma_f32_16x16x32_f16 v[92:95], v[156:159], v[140:143], v[92:95]
	s_waitcnt lgkmcnt(0)
	v_mfma_f32_16x16x32_f16 v[32:35], v[112:115], v[96:99], v[32:35]
	ds_read_b128 v[128:131], v10
	v_mfma_f32_16x16x32_f16 v[36:39], v[116:119], v[96:99], v[36:39]
	ds_read_b128 v[144:147], v11 offset:32768
	v_mfma_f32_16x16x32_f16 v[40:43], v[120:123], v[96:99], v[40:43]
	ds_read_b128 v[148:151], v11 offset:34816
	v_mfma_f32_16x16x32_f16 v[44:47], v[124:127], v[96:99], v[44:47]
	ds_read_b128 v[152:155], v11 offset:36864
	v_mfma_f32_16x16x32_f16 v[48:51], v[112:115], v[100:103], v[48:51]
	ds_read_b128 v[156:159], v11 offset:38912
	v_mfma_f32_16x16x32_f16 v[52:55], v[116:119], v[100:103], v[52:55]
	ds_read_b128 v[132:135], v10 offset:2048
	v_mfma_f32_16x16x32_f16 v[56:59], v[120:123], v[100:103], v[56:59]
	ds_read_b128 v[136:139], v10 offset:4096
	v_mfma_f32_16x16x32_f16 v[60:63], v[124:127], v[100:103], v[60:63]
	ds_read_b128 v[140:143], v10 offset:6144
	v_mfma_f32_16x16x32_f16 v[64:67], v[112:115], v[104:107], v[64:67]
	v_mfma_f32_16x16x32_f16 v[68:71], v[116:119], v[104:107], v[68:71]
	v_mfma_f32_16x16x32_f16 v[72:75], v[120:123], v[104:107], v[72:75]
	s_add_u32 m0, s14, 0x1e000
	s_nop 0
	global_load_lds_dwordx4 v5, s[28:29]
	v_mfma_f32_16x16x32_f16 v[76:79], v[124:127], v[104:107], v[76:79]
	v_mfma_f32_16x16x32_f16 v[80:83], v[112:115], v[108:111], v[80:83]
	s_add_u32 m0, s14, 0x20000
	s_nop 0
	global_load_lds_dwordx4 v6, s[30:31]
	v_mfma_f32_16x16x32_f16 v[84:87], v[116:119], v[108:111], v[84:87]
	v_mfma_f32_16x16x32_f16 v[88:91], v[120:123], v[108:111], v[88:91]
	s_add_u32 m0, s14, 0x22000
	s_nop 0
	global_load_lds_dwordx4 v7, s[30:31]
	v_mfma_f32_16x16x32_f16 v[92:95], v[124:127], v[108:111], v[92:95]
	s_waitcnt vmcnt(6) lgkmcnt(0)
	s_barrier
	s_add_u32 s28, s28, 0x80
	s_addc_u32 s29, s29, 0
	s_add_u32 s30, s30, 0x80
	s_addc_u32 s31, s31, 0
	s_waitcnt lgkmcnt(0)
	v_mfma_f32_16x16x32_f16 v[32:35], v[144:147], v[128:131], v[32:35]
	ds_read_b128 v[96:99], v12
	v_mfma_f32_16x16x32_f16 v[36:39], v[148:151], v[128:131], v[36:39]
	ds_read_b128 v[112:115], v13 offset:32768
	v_mfma_f32_16x16x32_f16 v[40:43], v[152:155], v[128:131], v[40:43]
	ds_read_b128 v[116:119], v13 offset:34816
	v_mfma_f32_16x16x32_f16 v[44:47], v[156:159], v[128:131], v[44:47]
	ds_read_b128 v[120:123], v13 offset:36864
	v_mfma_f32_16x16x32_f16 v[48:51], v[144:147], v[132:135], v[48:51]
	ds_read_b128 v[124:127], v13 offset:38912
	v_mfma_f32_16x16x32_f16 v[52:55], v[148:151], v[132:135], v[52:55]
	ds_read_b128 v[100:103], v12 offset:2048
	v_mfma_f32_16x16x32_f16 v[56:59], v[152:155], v[132:135], v[56:59]
	ds_read_b128 v[104:107], v12 offset:4096
	v_mfma_f32_16x16x32_f16 v[60:63], v[156:159], v[132:135], v[60:63]
	ds_read_b128 v[108:111], v12 offset:6144
	v_mfma_f32_16x16x32_f16 v[64:67], v[144:147], v[136:139], v[64:67]
	v_mfma_f32_16x16x32_f16 v[68:71], v[148:151], v[136:139], v[68:71]
	v_mfma_f32_16x16x32_f16 v[72:75], v[152:155], v[136:139], v[72:75]
	s_add_u32 m0, s14, 0x0
	s_nop 0
	global_load_lds_dwordx4 v2, s[28:29]
	v_mfma_f32_16x16x32_f16 v[76:79], v[156:159], v[136:139], v[76:79]
	v_mfma_f32_16x16x32_f16 v[80:83], v[144:147], v[140:143], v[80:83]
	s_add_u32 m0, s14, 0x2000
	s_nop 0
	global_load_lds_dwordx4 v3, s[28:29]
	v_mfma_f32_16x16x32_f16 v[84:87], v[148:151], v[140:143], v[84:87]
	v_mfma_f32_16x16x32_f16 v[88:91], v[152:155], v[140:143], v[88:91]
	s_add_u32 m0, s14, 0x4000
	s_nop 0
	global_load_lds_dwordx4 v4, s[28:29]
	v_mfma_f32_16x16x32_f16 v[92:95], v[156:159], v[140:143], v[92:95]
	s_waitcnt lgkmcnt(0)
	v_mfma_f32_16x16x32_f16 v[32:35], v[112:115], v[96:99], v[32:35]
	ds_read_b128 v[128:131], v14
	v_mfma_f32_16x16x32_f16 v[36:39], v[116:119], v[96:99], v[36:39]
	ds_read_b128 v[144:147], v15 offset:32768
	v_mfma_f32_16x16x32_f16 v[40:43], v[120:123], v[96:99], v[40:43]
	ds_read_b128 v[148:151], v15 offset:34816
	v_mfma_f32_16x16x32_f16 v[44:47], v[124:127], v[96:99], v[44:47]
	ds_read_b128 v[152:155], v15 offset:36864
	v_mfma_f32_16x16x32_f16 v[48:51], v[112:115], v[100:103], v[48:51]
	ds_read_b128 v[156:159], v15 offset:38912
	v_mfma_f32_16x16x32_f16 v[52:55], v[116:119], v[100:103], v[52:55]
	ds_read_b128 v[132:135], v14 offset:2048
	v_mfma_f32_16x16x32_f16 v[56:59], v[120:123], v[100:103], v[56:59]
	ds_read_b128 v[136:139], v14 offset:4096
	v_mfma_f32_16x16x32_f16 v[60:63], v[124:127], v[100:103], v[60:63]
	ds_read_b128 v[140:143], v14 offset:6144
	v_mfma_f32_16x16x32_f16 v[64:67], v[112:115], v[104:107], v[64:67]
	v_mfma_f32_16x16x32_f16 v[68:71], v[116:119], v[104:107], v[68:71]
	v_mfma_f32_16x16x32_f16 v[72:75], v[120:123], v[104:107], v[72:75]
	s_add_u32 m0, s14, 0x6000
	s_nop 0
	global_load_lds_dwordx4 v5, s[28:29]
	v_mfma_f32_16x16x32_f16 v[76:79], v[124:127], v[104:107], v[76:79]
	v_mfma_f32_16x16x32_f16 v[80:83], v[112:115], v[108:111], v[80:83]
	s_add_u32 m0, s14, 0x8000
	s_nop 0
	global_load_lds_dwordx4 v6, s[30:31]
	v_mfma_f32_16x16x32_f16 v[84:87], v[116:119], v[108:111], v[84:87]
	v_mfma_f32_16x16x32_f16 v[88:91], v[120:123], v[108:111], v[88:91]
	s_add_u32 m0, s14, 0xa000
	s_nop 0
	global_load_lds_dwordx4 v7, s[30:31]
	v_mfma_f32_16x16x32_f16 v[92:95], v[124:127], v[108:111], v[92:95]
	s_waitcnt vmcnt(6) lgkmcnt(0)
	s_barrier
	s_waitcnt lgkmcnt(0)
	v_mfma_f32_16x16x32_f16 v[32:35], v[144:147], v[128:131], v[32:35]
	ds_read_b128 v[96:99], v16
	v_mfma_f32_16x16x32_f16 v[36:39], v[148:151], v[128:131], v[36:39]
	ds_read_b128 v[112:115], v17 offset:32768
	v_mfma_f32_16x16x32_f16 v[40:43], v[152:155], v[128:131], v[40:43]
	ds_read_b128 v[116:119], v17 offset:34816
	v_mfma_f32_16x16x32_f16 v[44:47], v[156:159], v[128:131], v[44:47]
	ds_read_b128 v[120:123], v17 offset:36864
	v_mfma_f32_16x16x32_f16 v[48:51], v[144:147], v[132:135], v[48:51]
	ds_read_b128 v[124:127], v17 offset:38912
	v_mfma_f32_16x16x32_f16 v[52:55], v[148:151], v[132:135], v[52:55]
	ds_read_b128 v[100:103], v16 offset:2048
	v_mfma_f32_16x16x32_f16 v[56:59], v[152:155], v[132:135], v[56:59]
	ds_read_b128 v[104:107], v16 offset:4096
	v_mfma_f32_16x16x32_f16 v[60:63], v[156:159], v[132:135], v[60:63]
	ds_read_b128 v[108:111], v16 offset:6144
	v_mfma_f32_16x16x32_f16 v[64:67], v[144:147], v[136:139], v[64:67]
	v_mfma_f32_16x16x32_f16 v[68:71], v[148:151], v[136:139], v[68:71]
	v_mfma_f32_16x16x32_f16 v[72:75], v[152:155], v[136:139], v[72:75]
	v_mfma_f32_16x16x32_f16 v[76:79], v[156:159], v[136:139], v[76:79]
	v_mfma_f32_16x16x32_f16 v[80:83], v[144:147], v[140:143], v[80:83]
	v_mfma_f32_16x16x32_f16 v[84:87], v[148:151], v[140:143], v[84:87]
	v_mfma_f32_16x16x32_f16 v[88:91], v[152:155], v[140:143], v[88:91]
	v_mfma_f32_16x16x32_f16 v[92:95], v[156:159], v[140:143], v[92:95]
	s_waitcnt lgkmcnt(0)
	v_mfma_f32_16x16x32_f16 v[32:35], v[112:115], v[96:99], v[32:35]
	ds_read_b128 v[128:131], v18
	v_mfma_f32_16x16x32_f16 v[36:39], v[116:119], v[96:99], v[36:39]
	ds_read_b128 v[144:147], v19 offset:32768
	v_mfma_f32_16x16x32_f16 v[40:43], v[120:123], v[96:99], v[40:43]
	ds_read_b128 v[148:151], v19 offset:34816
	v_mfma_f32_16x16x32_f16 v[44:47], v[124:127], v[96:99], v[44:47]
	ds_read_b128 v[152:155], v19 offset:36864
	v_mfma_f32_16x16x32_f16 v[48:51], v[112:115], v[100:103], v[48:51]
	ds_read_b128 v[156:159], v19 offset:38912
	v_mfma_f32_16x16x32_f16 v[52:55], v[116:119], v[100:103], v[52:55]
	ds_read_b128 v[132:135], v18 offset:2048
	v_mfma_f32_16x16x32_f16 v[56:59], v[120:123], v[100:103], v[56:59]
	ds_read_b128 v[136:139], v18 offset:4096
	v_mfma_f32_16x16x32_f16 v[60:63], v[124:127], v[100:103], v[60:63]
	ds_read_b128 v[140:143], v18 offset:6144
	v_mfma_f32_16x16x32_f16 v[64:67], v[112:115], v[104:107], v[64:67]
	v_mfma_f32_16x16x32_f16 v[68:71], v[116:119], v[104:107], v[68:71]
	v_mfma_f32_16x16x32_f16 v[72:75], v[120:123], v[104:107], v[72:75]
	v_mfma_f32_16x16x32_f16 v[76:79], v[124:127], v[104:107], v[76:79]
	v_mfma_f32_16x16x32_f16 v[80:83], v[112:115], v[108:111], v[80:83]
	v_mfma_f32_16x16x32_f16 v[84:87], v[116:119], v[108:111], v[84:87]
	v_mfma_f32_16x16x32_f16 v[88:91], v[120:123], v[108:111], v[88:91]
	v_mfma_f32_16x16x32_f16 v[92:95], v[124:127], v[108:111], v[92:95]
	s_waitcnt vmcnt(0) lgkmcnt(0)
	s_barrier
	s_waitcnt lgkmcnt(0)
	v_mfma_f32_16x16x32_f16 v[32:35], v[144:147], v[128:131], v[32:35]
	ds_read_b128 v[96:99], v8
	v_mfma_f32_16x16x32_f16 v[36:39], v[148:151], v[128:131], v[36:39]
	ds_read_b128 v[112:115], v9 offset:32768
	v_mfma_f32_16x16x32_f16 v[40:43], v[152:155], v[128:131], v[40:43]
	ds_read_b128 v[116:119], v9 offset:34816
	v_mfma_f32_16x16x32_f16 v[44:47], v[156:159], v[128:131], v[44:47]
	ds_read_b128 v[120:123], v9 offset:36864
	v_mfma_f32_16x16x32_f16 v[48:51], v[144:147], v[132:135], v[48:51]
	ds_read_b128 v[124:127], v9 offset:38912
	v_mfma_f32_16x16x32_f16 v[52:55], v[148:151], v[132:135], v[52:55]
	ds_read_b128 v[100:103], v8 offset:2048
	v_mfma_f32_16x16x32_f16 v[56:59], v[152:155], v[132:135], v[56:59]
	ds_read_b128 v[104:107], v8 offset:4096
	v_mfma_f32_16x16x32_f16 v[60:63], v[156:159], v[132:135], v[60:63]
	ds_read_b128 v[108:111], v8 offset:6144
	v_mfma_f32_16x16x32_f16 v[64:67], v[144:147], v[136:139], v[64:67]
	v_mfma_f32_16x16x32_f16 v[68:71], v[148:151], v[136:139], v[68:71]
	v_mfma_f32_16x16x32_f16 v[72:75], v[152:155], v[136:139], v[72:75]
	v_mfma_f32_16x16x32_f16 v[76:79], v[156:159], v[136:139], v[76:79]
	v_mfma_f32_16x16x32_f16 v[80:83], v[144:147], v[140:143], v[80:83]
	v_mfma_f32_16x16x32_f16 v[84:87], v[148:151], v[140:143], v[84:87]
	v_mfma_f32_16x16x32_f16 v[88:91], v[152:155], v[140:143], v[88:91]
	v_mfma_f32_16x16x32_f16 v[92:95], v[156:159], v[140:143], v[92:95]
	s_waitcnt lgkmcnt(0)
	v_mfma_f32_16x16x32_f16 v[32:35], v[112:115], v[96:99], v[32:35]
	ds_read_b128 v[128:131], v10
	v_mfma_f32_16x16x32_f16 v[36:39], v[116:119], v[96:99], v[36:39]
	ds_read_b128 v[144:147], v11 offset:32768
	v_mfma_f32_16x16x32_f16 v[40:43], v[120:123], v[96:99], v[40:43]
	ds_read_b128 v[148:151], v11 offset:34816
	v_mfma_f32_16x16x32_f16 v[44:47], v[124:127], v[96:99], v[44:47]
	ds_read_b128 v[152:155], v11 offset:36864
	v_mfma_f32_16x16x32_f16 v[48:51], v[112:115], v[100:103], v[48:51]
	ds_read_b128 v[156:159], v11 offset:38912
	v_mfma_f32_16x16x32_f16 v[52:55], v[116:119], v[100:103], v[52:55]
	ds_read_b128 v[132:135], v10 offset:2048
	v_mfma_f32_16x16x32_f16 v[56:59], v[120:123], v[100:103], v[56:59]
	ds_read_b128 v[136:139], v10 offset:4096
	v_mfma_f32_16x16x32_f16 v[60:63], v[124:127], v[100:103], v[60:63]
	ds_read_b128 v[140:143], v10 offset:6144
	v_mfma_f32_16x16x32_f16 v[64:67], v[112:115], v[104:107], v[64:67]
	v_mfma_f32_16x16x32_f16 v[68:71], v[116:119], v[104:107], v[68:71]
	v_mfma_f32_16x16x32_f16 v[72:75], v[120:123], v[104:107], v[72:75]
	v_mfma_f32_16x16x32_f16 v[76:79], v[124:127], v[104:107], v[76:79]
	v_mfma_f32_16x16x32_f16 v[80:83], v[112:115], v[108:111], v[80:83]
	v_mfma_f32_16x16x32_f16 v[84:87], v[116:119], v[108:111], v[84:87]
	v_mfma_f32_16x16x32_f16 v[88:91], v[120:123], v[108:111], v[88:91]
	v_mfma_f32_16x16x32_f16 v[92:95], v[124:127], v[108:111], v[92:95]
	s_waitcnt lgkmcnt(0)
	v_mfma_f32_16x16x32_f16 v[32:35], v[144:147], v[128:131], v[32:35]
	v_mfma_f32_16x16x32_f16 v[36:39], v[148:151], v[128:131], v[36:39]
	v_mfma_f32_16x16x32_f16 v[40:43], v[152:155], v[128:131], v[40:43]
	v_mfma_f32_16x16x32_f16 v[44:47], v[156:159], v[128:131], v[44:47]
	v_mfma_f32_16x16x32_f16 v[48:51], v[144:147], v[132:135], v[48:51]
	v_mfma_f32_16x16x32_f16 v[52:55], v[148:151], v[132:135], v[52:55]
	v_mfma_f32_16x16x32_f16 v[56:59], v[152:155], v[132:135], v[56:59]
	v_mfma_f32_16x16x32_f16 v[60:63], v[156:159], v[132:135], v[60:63]
	v_mfma_f32_16x16x32_f16 v[64:67], v[144:147], v[136:139], v[64:67]
	v_mfma_f32_16x16x32_f16 v[68:71], v[148:151], v[136:139], v[68:71]
	v_mfma_f32_16x16x32_f16 v[72:75], v[152:155], v[136:139], v[72:75]
	v_mfma_f32_16x16x32_f16 v[76:79], v[156:159], v[136:139], v[76:79]
	v_mfma_f32_16x16x32_f16 v[80:83], v[144:147], v[140:143], v[80:83]
	v_mfma_f32_16x16x32_f16 v[84:87], v[148:151], v[140:143], v[84:87]
	v_mfma_f32_16x16x32_f16 v[88:91], v[152:155], v[140:143], v[88:91]
	v_mfma_f32_16x16x32_f16 v[92:95], v[156:159], v[140:143], v[92:95]
	s_nop 7
	s_nop 1
	v_pk_mul_f32 v[160:161], v[32:33], s[50:51] op_sel_hi:[1,0]
	v_pk_mul_f32 v[162:163], v[34:35], s[50:51] op_sel_hi:[1,0]
	v_pk_mul_f32 v[164:165], v[36:37], s[50:51] op_sel_hi:[1,0]
	v_pk_mul_f32 v[166:167], v[38:39], s[50:51] op_sel_hi:[1,0]
	v_cvt_pk_f16_f32 v168, v160, v161
	v_cvt_pk_f16_f32 v169, v162, v163
	v_cvt_pk_f16_f32 v170, v164, v165
	v_cvt_pk_f16_f32 v171, v166, v167
	global_store_dwordx4 v24, v[168:171], s[34:35] offset:256
	v_pk_mul_f32 v[160:161], v[40:41], s[50:51] op_sel_hi:[1,0]
	v_pk_mul_f32 v[162:163], v[42:43], s[50:51] op_sel_hi:[1,0]
	v_pk_mul_f32 v[164:165], v[44:45], s[50:51] op_sel_hi:[1,0]
	v_pk_mul_f32 v[166:167], v[46:47], s[50:51] op_sel_hi:[1,0]
	v_cvt_pk_f16_f32 v172, v160, v161
	v_cvt_pk_f16_f32 v173, v162, v163
	v_cvt_pk_f16_f32 v174, v164, v165
	v_cvt_pk_f16_f32 v175, v166, v167
	global_store_dwordx4 v24, v[172:175], s[34:35] offset:320
	v_pk_mul_f32 v[160:161], v[48:49], s[50:51] op_sel_hi:[1,0]
	v_pk_mul_f32 v[162:163], v[50:51], s[50:51] op_sel_hi:[1,0]
	v_pk_mul_f32 v[164:165], v[52:53], s[50:51] op_sel_hi:[1,0]
	v_pk_mul_f32 v[166:167], v[54:55], s[50:51] op_sel_hi:[1,0]
	v_cvt_pk_f16_f32 v168, v160, v161
	v_cvt_pk_f16_f32 v169, v162, v163
	v_cvt_pk_f16_f32 v170, v164, v165
	v_cvt_pk_f16_f32 v171, v166, v167
	global_store_dwordx4 v25, v[168:171], s[34:35] offset:256
	v_pk_mul_f32 v[160:161], v[56:57], s[50:51] op_sel_hi:[1,0]
	v_pk_mul_f32 v[162:163], v[58:59], s[50:51] op_sel_hi:[1,0]
	v_pk_mul_f32 v[164:165], v[60:61], s[50:51] op_sel_hi:[1,0]
	v_pk_mul_f32 v[166:167], v[62:63], s[50:51] op_sel_hi:[1,0]
	v_cvt_pk_f16_f32 v172, v160, v161
	v_cvt_pk_f16_f32 v173, v162, v163
	v_cvt_pk_f16_f32 v174, v164, v165
	v_cvt_pk_f16_f32 v175, v166, v167
	global_store_dwordx4 v25, v[172:175], s[34:35] offset:320
	v_pk_mul_f32 v[160:161], v[64:65], s[50:51] op_sel_hi:[1,0]
	v_pk_mul_f32 v[162:163], v[66:67], s[50:51] op_sel_hi:[1,0]
	v_pk_mul_f32 v[164:165], v[68:69], s[50:51] op_sel_hi:[1,0]
	v_pk_mul_f32 v[166:167], v[70:71], s[50:51] op_sel_hi:[1,0]
	v_cvt_pk_f16_f32 v168, v160, v161
	v_cvt_pk_f16_f32 v169, v162, v163
	v_cvt_pk_f16_f32 v170, v164, v165
	v_cvt_pk_f16_f32 v171, v166, v167
	global_store_dwordx4 v26, v[168:171], s[34:35] offset:256
	v_pk_mul_f32 v[160:161], v[72:73], s[50:51] op_sel_hi:[1,0]
	v_pk_mul_f32 v[162:163], v[74:75], s[50:51] op_sel_hi:[1,0]
	v_pk_mul_f32 v[164:165], v[76:77], s[50:51] op_sel_hi:[1,0]
	v_pk_mul_f32 v[166:167], v[78:79], s[50:51] op_sel_hi:[1,0]
	v_cvt_pk_f16_f32 v172, v160, v161
	v_cvt_pk_f16_f32 v173, v162, v163
	v_cvt_pk_f16_f32 v174, v164, v165
	v_cvt_pk_f16_f32 v175, v166, v167
	global_store_dwordx4 v26, v[172:175], s[34:35] offset:320
	v_pk_mul_f32 v[160:161], v[80:81], s[50:51] op_sel_hi:[1,0]
	v_pk_mul_f32 v[162:163], v[82:83], s[50:51] op_sel_hi:[1,0]
	v_pk_mul_f32 v[164:165], v[84:85], s[50:51] op_sel_hi:[1,0]
	v_pk_mul_f32 v[166:167], v[86:87], s[50:51] op_sel_hi:[1,0]
	v_cvt_pk_f16_f32 v168, v160, v161
	v_cvt_pk_f16_f32 v169, v162, v163
	v_cvt_pk_f16_f32 v170, v164, v165
	v_cvt_pk_f16_f32 v171, v166, v167
	global_store_dwordx4 v27, v[168:171], s[34:35] offset:256
	v_pk_mul_f32 v[160:161], v[88:89], s[50:51] op_sel_hi:[1,0]
	v_pk_mul_f32 v[162:163], v[90:91], s[50:51] op_sel_hi:[1,0]
	v_pk_mul_f32 v[164:165], v[92:93], s[50:51] op_sel_hi:[1,0]
	v_pk_mul_f32 v[166:167], v[94:95], s[50:51] op_sel_hi:[1,0]
	v_cvt_pk_f16_f32 v172, v160, v161
	v_cvt_pk_f16_f32 v173, v162, v163
	v_cvt_pk_f16_f32 v174, v164, v165
	v_cvt_pk_f16_f32 v175, v166, v167
	global_store_dwordx4 v27, v[172:175], s[34:35] offset:320
	s_endpgm

	.amdhsa_kernel _Z12gemm8_kernelPKDF16_S0_PDF16_S1_
		.amdhsa_group_segment_fixed_size 16384
		.amdhsa_private_segment_fixed_size 0
		.amdhsa_kernarg_size 32
		.amdhsa_user_sgpr_count 2
		.amdhsa_user_sgpr_dispatch_ptr 0
		.amdhsa_user_sgpr_queue_ptr 0
		.amdhsa_user_sgpr_kernarg_segment_ptr 1
		.amdhsa_user_sgpr_dispatch_id 0
		.amdhsa_user_sgpr_kernarg_preload_length 0
		.amdhsa_user_sgpr_kernarg_preload_offset 0
		.amdhsa_user_sgpr_private_segment_size 0
		.amdhsa_uses_dynamic_stack 0
		.amdhsa_enable_private_segment 0
		.amdhsa_system_sgpr_workgroup_id_x 1
		.amdhsa_system_sgpr_workgroup_id_y 0
		.amdhsa_system_sgpr_workgroup_id_z 0
		.amdhsa_system_sgpr_workgroup_info 0
		.amdhsa_system_vgpr_workitem_id 0
		.amdhsa_next_free_vgpr 184
		.amdhsa_next_free_sgpr 54
		.amdhsa_accum_offset 184
		.amdhsa_reserve_vcc 1
		.amdhsa_float_round_mode_32 0
		.amdhsa_float_round_mode_16_64 0
		.amdhsa_float_denorm_mode_32 3
		.amdhsa_float_denorm_mode_16_64 3
		.amdhsa_dx10_clamp 1
		.amdhsa_ieee_mode 1
		.amdhsa_fp16_overflow 0
		.amdhsa_tg_split 0
		.amdhsa_exception_fp_ieee_invalid_op 0
		.amdhsa_exception_fp_denorm_src 0
		.amdhsa_exception_fp_ieee_div_zero 0
		.amdhsa_exception_fp_ieee_overflow 0
		.amdhsa_exception_fp_ieee_underflow 0
		.amdhsa_exception_fp_ieee_inexact 0
		.amdhsa_exception_int_div_zero 0
	.end_amdhsa_kernel

amdhsa.kernels:
  - .agpr_count:     0
    .args:
      - .actual_access:  read_only
        .address_space:  global
        .offset:         0
        .size:           8
        .value_kind:     global_buffer
      - .actual_access:  read_only
        .address_space:  global
        .offset:         8
        .size:           8
        .value_kind:     global_buffer
      - .actual_access:  read_only
        .address_space:  global
        .offset:         16
        .size:           8
        .value_kind:     global_buffer
      - .actual_access:  read_only
        .address_space:  global
        .offset:         24
        .size:           8
        .value_kind:     global_buffer
      - .actual_access:  write_only
        .address_space:  global
        .offset:         32
        .size:           8
        .value_kind:     global_buffer
      - .actual_access:  write_only
        .address_space:  global
        .offset:         40
        .size:           8
        .value_kind:     global_buffer
      - .actual_access:  write_only
        .address_space:  global
        .offset:         48
        .size:           8
        .value_kind:     global_buffer
      - .actual_access:  write_only
        .address_space:  global
        .offset:         56
        .size:           8
        .value_kind:     global_buffer
    .group_segment_fixed_size: 16640
    .kernarg_segment_align: 8
    .kernarg_segment_size: 64
    .language:       OpenCL C
    .language_version:
      - 2
      - 0
    .max_flat_workgroup_size: 256
    .name:           _Z11prep_kernelPKfS0_S0_S0_PDF16_S1_S1_Pf
    .private_segment_fixed_size: 0
    .sgpr_count:     18
    .sgpr_spill_count: 0
    .symbol:         _Z11prep_kernelPKfS0_S0_S0_PDF16_S1_S1_Pf.kd
    .uniform_work_group_size: 1
    .uses_dynamic_stack: false
    .vgpr_count:     42
    .vgpr_spill_count: 0
    .wavefront_size: 64
  - .agpr_count:     0
    .args:
      - .address_space:  global
        .offset:         0
        .size:           8
        .value_kind:     global_buffer
      - .address_space:  global
        .offset:         8
        .size:           8
        .value_kind:     global_buffer
      - .actual_access:  write_only
        .address_space:  global
        .offset:         16
        .size:           8
        .value_kind:     global_buffer
      - .actual_access:  read_only
        .address_space:  global
        .offset:         24
        .size:           8
        .value_kind:     global_buffer
    .group_segment_fixed_size: 49152
    .kernarg_segment_align: 8
    .kernarg_segment_size: 32
    .language:       OpenCL C
    .language_version:
      - 2
      - 0
    .max_flat_workgroup_size: 512
    .name:           _Z13gemm2b_kernelPKDF16_S0_PfPKf
    .private_segment_fixed_size: 0
    .sgpr_count:     24
    .sgpr_spill_count: 0
    .symbol:         _Z13gemm2b_kernelPKDF16_S0_PfPKf.kd
    .uniform_work_group_size: 1
    .uses_dynamic_stack: false
    .vgpr_count:     176
    .vgpr_spill_count: 0
    .wavefront_size: 64
  - .agpr_count:     0
    .args:
      - .address_space:  global
        .offset:         0
        .size:           8
        .value_kind:     global_buffer
      - .address_space:  global
        .offset:         8
        .size:           8
        .value_kind:     global_buffer
      - .actual_access:  write_only
        .address_space:  global
        .offset:         16
        .size:           8
        .value_kind:     global_buffer
      - .actual_access:  write_only
        .address_space:  global
        .offset:         24
        .size:           8
        .value_kind:     global_buffer
    .group_segment_fixed_size: 16384
    .kernarg_segment_align: 8
    .kernarg_segment_size: 32
    .language:       OpenCL C
    .language_version:
      - 2
      - 0
    .max_flat_workgroup_size: 512
    .name:           _Z12gemm8_kernelPKDF16_S0_PDF16_S1_
    .private_segment_fixed_size: 0
    .sgpr_count:     60
    .sgpr_spill_count: 0
    .symbol:         _Z12gemm8_kernelPKDF16_S0_PDF16_S1_.kd
    .uniform_work_group_size: 1
    .uses_dynamic_stack: false
    .vgpr_count:     184
    .vgpr_spill_count: 0
    .wavefront_size: 64
  - .agpr_count:     0
    .args:
      - .actual_access:  read_only
        .address_space:  global
        .offset:         0
        .size:           8
        .value_kind:     global_buffer
      - .actual_access:  read_only
        .address_space:  global
        .offset:         8
        .size:           8
        .value_kind:     global_buffer
      - .actual_access:  read_only
        .address_space:  global
        .offset:         16
        .size:           8
        .value_kind:     global_buffer
      - .actual_access:  read_only
        .address_space:  global
        .offset:         24
        .size:           8
        .value_kind:     global_buffer
      - .actual_access:  write_only
        .address_space:  global
        .offset:         32
        .size:           8
        .value_kind:     global_buffer
      - .actual_access:  write_only
        .address_space:  global
        .offset:         40
        .size:           8
        .value_kind:     global_buffer
      - .actual_access:  read_only
        .address_space:  global
        .offset:         48
        .size:           8
        .value_kind:     global_buffer
      - .actual_access:  read_only
        .address_space:  global
        .offset:         56
        .size:           8
        .value_kind:     global_buffer
      - .actual_access:  read_only
        .address_space:  global
        .offset:         64
        .size:           8
        .value_kind:     global_buffer
      - .actual_access:  write_only
        .address_space:  global
        .offset:         72
        .size:           8
        .value_kind:     global_buffer
      - .actual_access:  write_only
        .address_space:  global
        .offset:         80
        .size:           8
        .value_kind:     global_buffer
      - .actual_access:  write_only
        .address_space:  global
        .offset:         88
        .size:           8
        .value_kind:     global_buffer
      - .actual_access:  write_only
        .address_space:  global
        .offset:         96
        .size:           8
        .value_kind:     global_buffer
    .group_segment_fixed_size: 17952
    .kernarg_segment_align: 8
    .kernarg_segment_size: 104
    .language:       OpenCL C
    .language_version:
      - 2
      - 0
    .max_flat_workgroup_size: 256
    .name:           _Z13convdt_kernelPKDF16_S0_PKfS2_PDF16_S3_S2_S2_S2_PfS4_S4_S4_
    .private_segment_fixed_size: 0
    .sgpr_count:     26
    .sgpr_spill_count: 0
    .symbol:         _Z13convdt_kernelPKDF16_S0_PKfS2_PDF16_S3_S2_S2_S2_PfS4_S4_S4_.kd
    .uniform_work_group_size: 1
    .uses_dynamic_stack: false
    .vgpr_count:     88
    .vgpr_spill_count: 0
    .wavefront_size: 64
  - .agpr_count:     0
    .args:
      - .actual_access:  read_only
        .address_space:  global
        .offset:         0
        .size:           8
        .value_kind:     global_buffer
      - .actual_access:  read_only
        .address_space:  global
        .offset:         8
        .size:           8
        .value_kind:     global_buffer
      - .actual_access:  read_only
        .address_space:  global
        .offset:         16
        .size:           8
        .value_kind:     global_buffer
      - .actual_access:  write_only
        .address_space:  global
        .offset:         24
        .size:           8
        .value_kind:     global_buffer
    .group_segment_fixed_size: 34816
    .kernarg_segment_align: 8
    .kernarg_segment_size: 32
    .language:       OpenCL C
    .language_version:
      - 2
      - 0
    .max_flat_workgroup_size: 256
    .name:           _Z11sloc_kernelPKDF16_PKfS2_PDF16_
    .private_segment_fixed_size: 0
    .sgpr_count:     28
    .sgpr_spill_count: 0
    .symbol:         _Z11sloc_kernelPKDF16_PKfS2_PDF16_.kd
    .uniform_work_group_size: 1
    .uses_dynamic_stack: false
    .vgpr_count:     120
    .vgpr_spill_count: 0
    .wavefront_size: 64
  - .agpr_count:     64
    .args:
      - .actual_access:  read_only
        .address_space:  global
        .offset:         0
        .size:           8
        .value_kind:     global_buffer
      - .address_space:  global
        .offset:         8
        .size:           8
        .value_kind:     global_buffer
      - .actual_access:  read_only
        .address_space:  global
        .offset:         16
        .size:           8
        .value_kind:     global_buffer
      - .actual_access:  write_only
        .address_space:  global
        .offset:         24
        .size:           8
        .value_kind:     global_buffer
    .group_segment_fixed_size: 0
    .kernarg_segment_align: 8
    .kernarg_segment_size: 32
    .language:       OpenCL C
    .language_version:
      - 2
      - 0
    .max_flat_workgroup_size: 256
    .name:           _Z12spass_kernelPKfPDF16_PKDF16_S1_
    .private_segment_fixed_size: 0
    .sgpr_count:     21
    .sgpr_spill_count: 0
    .symbol:         _Z12spass_kernelPKfPDF16_PKDF16_S1_.kd
    .uniform_work_group_size: 1
    .uses_dynamic_stack: false
    .vgpr_count:     180
    .vgpr_spill_count: 0
    .wavefront_size: 64
  - .agpr_count:     0
    .args:
      - .actual_access:  read_only
        .address_space:  global
        .offset:         0
        .size:           8
        .value_kind:     global_buffer
      - .actual_access:  read_only
        .address_space:  global
        .offset:         8
        .size:           8
        .value_kind:     global_buffer
      - .actual_access:  read_only
        .address_space:  global
        .offset:         16
        .size:           8
        .value_kind:     global_buffer
      - .actual_access:  read_only
        .address_space:  global
        .offset:         24
        .size:           8
        .value_kind:     global_buffer
      - .actual_access:  read_only
        .address_space:  global
        .offset:         32
        .size:           8
        .value_kind:     global_buffer
      - .actual_access:  read_only
        .address_space:  global
        .offset:         40
        .size:           8
        .value_kind:     global_buffer
      - .actual_access:  read_only
        .address_space:  global
        .offset:         48
        .size:           8
        .value_kind:     global_buffer
      - .actual_access:  read_only
        .address_space:  global
        .offset:         56
        .size:           8
        .value_kind:     global_buffer
      - .actual_access:  read_only
        .address_space:  global
        .offset:         64
        .size:           8
        .value_kind:     global_buffer
      - .actual_access:  write_only
        .address_space:  global
        .offset:         72
        .size:           8
        .value_kind:     global_buffer
      - .address_space:  global
        .offset:         80
        .size:           8
        .value_kind:     global_buffer
      - .actual_access:  read_only
        .address_space:  global
        .offset:         88
        .size:           8
        .value_kind:     global_buffer
    .group_segment_fixed_size: 54272
    .kernarg_segment_align: 8
    .kernarg_segment_size: 96
    .language:       OpenCL C
    .language_version:
      - 2
      - 0
    .max_flat_workgroup_size: 256
    .name:           _Z11scan_kernelPKDF16_S0_S0_S0_S0_PKfS2_S2_S2_PDF16_PfS4_
    .private_segment_fixed_size: 0
    .sgpr_count:     106
    .sgpr_spill_count: 56
    .symbol:         _Z11scan_kernelPKDF16_S0_S0_S0_S0_PKfS2_S2_S2_PDF16_PfS4_.kd
    .uniform_work_group_size: 1
    .uses_dynamic_stack: false
    .vgpr_count:     243
    .vgpr_spill_count: 0
    .wavefront_size: 64
  - .agpr_count:     0
    .args:
      - .actual_access:  read_only
        .address_space:  global
        .offset:         0
        .size:           8
        .value_kind:     global_buffer
      - .address_space:  global
        .offset:         8
        .size:           8
        .value_kind:     global_buffer
      - .address_space:  global
        .offset:         16
        .size:           8
        .value_kind:     global_buffer
      - .actual_access:  read_only
        .address_space:  global
        .offset:         24
        .size:           8
        .value_kind:     global_buffer
      - .address_space:  global
        .offset:         32
        .size:           8
        .value_kind:     global_buffer
      - .address_space:  global
        .offset:         40
        .size:           8
        .value_kind:     global_buffer
      - .address_space:  global
        .offset:         48
        .size:           8
        .value_kind:     global_buffer
      - .actual_access:  read_only
        .address_space:  global
        .offset:         56
        .size:           8
        .value_kind:     global_buffer
      - .actual_access:  read_only
        .address_space:  global
        .offset:         64
        .size:           8
        .value_kind:     global_buffer
      - .actual_access:  write_only
        .address_space:  global
        .offset:         72
        .size:           8
        .value_kind:     global_buffer
      - .address_space:  global
        .offset:         80
        .size:           8
        .value_kind:     global_buffer
      - .actual_access:  read_only
        .address_space:  global
        .offset:         88
        .size:           8
        .value_kind:     global_buffer
    .group_segment_fixed_size: 34816
    .kernarg_segment_align: 8
    .kernarg_segment_size: 96
    .language:       OpenCL C
    .language_version:
      - 2
      - 0
    .max_flat_workgroup_size: 512
    .name:           _Z12scan2_kernelPKDF16_S0_S0_S0_S0_PKfS2_S2_S2_PDF16_PfS4_
    .private_segment_fixed_size: 0
    .sgpr_count:     74
    .sgpr_spill_count: 0
    .symbol:         _Z12scan2_kernelPKDF16_S0_S0_S0_S0_PKfS2_S2_S2_PDF16_PfS4_.kd
    .uniform_work_group_size: 1
    .uses_dynamic_stack: false
    .vgpr_count:     252
    .vgpr_spill_count: 0
    .wavefront_size: 64
  - .agpr_count:     64
    .args:
      - .address_space:  global
        .offset:         0
        .size:           8
        .value_kind:     global_buffer
      - .address_space:  global
        .offset:         8
        .size:           8
        .value_kind:     global_buffer
      - .offset:         16
        .size:           4
        .value_kind:     by_value
      - .offset:         20
        .size:           4
        .value_kind:     by_value
      - .offset:         24
        .size:           4
        .value_kind:     by_value
      - .actual_access:  write_only
        .address_space:  global
        .offset:         32
        .size:           8
        .value_kind:     global_buffer
      - .actual_access:  write_only
        .address_space:  global
        .offset:         40
        .size:           8
        .value_kind:     global_buffer
      - .actual_access:  read_only
        .address_space:  global
        .offset:         48
        .size:           8
        .value_kind:     global_buffer
      - .offset:         56
        .size:           4
        .value_kind:     by_value
    .group_segment_fixed_size: 131072
    .kernarg_segment_align: 8
    .kernarg_segment_size: 60
    .language:       OpenCL C
    .language_version:
      - 2
      - 0
    .max_flat_workgroup_size: 256
    .name:           _Z11gemm_kernelILi1EEvPKDF16_S1_iiiPDF16_PfPKfi
    .private_segment_fixed_size: 0
    .sgpr_count:     27
    .sgpr_spill_count: 0
    .symbol:         _Z11gemm_kernelILi1EEvPKDF16_S1_iiiPDF16_PfPKfi.kd
    .uniform_work_group_size: 1
    .uses_dynamic_stack: false
    .vgpr_count:     208
    .vgpr_spill_count: 0
    .wavefront_size: 64
